# speedup vs baseline: 1.0094x; 1.0023x over previous
.LE_cdone1:
	s_waitcnt lgkmcnt(0)
	s_barrier
	v_mov_b32_e32 v252, 0x20800
	ds_read_b32 v200, v252
	ds_read_b32 v201, v252 offset:4
	ds_read_b32 v202, v252 offset:8
	s_waitcnt lgkmcnt(0)
	s_nop 1
	v_readfirstlane_b32 s31, v200
	v_readfirstlane_b32 s29, v201
	v_readfirstlane_b32 s30, v202
	s_nop 3
	s_barrier
	s_lshl_b32 s49, s29, 19
	s_lshl_b32 s64, s32, 13
	s_add_u32 s49, s49, s64
	s_mov_b32 s51, s64
	s_add_u32 s52, s51, 0x0
	s_add_u32 s53, s51, 0x1000
	s_add_u32 s54, s51, 0x8000
	s_add_u32 s55, s51, 0x9000
	s_add_u32 s56, s51, 0x10000
	s_add_u32 s57, s51, 0x11000
	s_add_u32 s58, s51, 0x18000
	s_add_u32 s59, s51, 0x19000
	s_lshl_b32 s64, s29, 8
	s_lshl_b32 s65, s30, 1
	s_add_u32 s64, s64, s65
	s_lshr_b32 s65, s32, 1
	s_add_u32 s64, s64, s65
	s_lshl_b32 s64, s64, 11
	s_and_b32 s65, s32, 1
	s_lshl_b32 s65, s65, 9
	s_add_u32 s50, s64, s65
	s_sub_u32 s60, s28, 1
	s_lshl_b32 s64, s30, 2
	s_add_u32 s64, s64, s32
	s_lshl_b32 s64, s64, 16
	s_add_u32 s44, s4, s64
	s_addc_u32 s45, s5, 0
	global_load_dwordx4 a[0:3], v192, s[44:45] offset:0
	global_load_dwordx4 a[4:7], v192, s[44:45] offset:1024
	global_load_dwordx4 a[8:11], v192, s[44:45] offset:2048
	global_load_dwordx4 a[12:15], v192, s[44:45] offset:3072
	s_add_u32 s44, s44, 0x1000
	s_addc_u32 s45, s45, 0
	global_load_dwordx4 a[16:19], v192, s[44:45] offset:0
	global_load_dwordx4 a[20:23], v192, s[44:45] offset:1024
	global_load_dwordx4 a[24:27], v192, s[44:45] offset:2048
	global_load_dwordx4 a[28:31], v192, s[44:45] offset:3072
	s_add_u32 s44, s44, 0x1000
	s_addc_u32 s45, s45, 0
	global_load_dwordx4 a[32:35], v192, s[44:45] offset:0
	global_load_dwordx4 a[36:39], v192, s[44:45] offset:1024
	global_load_dwordx4 a[40:43], v192, s[44:45] offset:2048
	global_load_dwordx4 a[44:47], v192, s[44:45] offset:3072
	s_add_u32 s44, s44, 0x1000
	s_addc_u32 s45, s45, 0
	global_load_dwordx4 a[48:51], v192, s[44:45] offset:0
	global_load_dwordx4 a[52:55], v192, s[44:45] offset:1024
	global_load_dwordx4 a[56:59], v192, s[44:45] offset:2048
	global_load_dwordx4 a[60:63], v192, s[44:45] offset:3072
	s_add_u32 s44, s44, 0x1000
	s_addc_u32 s45, s45, 0
	global_load_dwordx4 a[64:67], v192, s[44:45] offset:0
	global_load_dwordx4 a[68:71], v192, s[44:45] offset:1024
	global_load_dwordx4 a[72:75], v192, s[44:45] offset:2048
	global_load_dwordx4 a[76:79], v192, s[44:45] offset:3072
	s_add_u32 s44, s44, 0x1000
	s_addc_u32 s45, s45, 0
	global_load_dwordx4 a[80:83], v192, s[44:45] offset:0
	global_load_dwordx4 a[84:87], v192, s[44:45] offset:1024
	global_load_dwordx4 a[88:91], v192, s[44:45] offset:2048
	global_load_dwordx4 a[92:95], v192, s[44:45] offset:3072
	s_add_u32 s44, s44, 0x1000
	s_addc_u32 s45, s45, 0
	global_load_dwordx4 a[96:99], v192, s[44:45] offset:0
	global_load_dwordx4 a[100:103], v192, s[44:45] offset:1024
	global_load_dwordx4 a[104:107], v192, s[44:45] offset:2048
	global_load_dwordx4 a[108:111], v192, s[44:45] offset:3072
	s_add_u32 s44, s44, 0x1000
	s_addc_u32 s45, s45, 0
	global_load_dwordx4 a[112:115], v192, s[44:45] offset:0
	global_load_dwordx4 a[116:119], v192, s[44:45] offset:1024
	global_load_dwordx4 a[120:123], v192, s[44:45] offset:2048
	global_load_dwordx4 a[124:127], v192, s[44:45] offset:3072
	s_add_u32 s44, s44, 0x1000
	s_addc_u32 s45, s45, 0
	s_waitcnt vmcnt(16)
	global_load_dwordx4 a[128:131], v192, s[44:45] offset:0
	global_load_dwordx4 a[132:135], v192, s[44:45] offset:1024
	global_load_dwordx4 a[136:139], v192, s[44:45] offset:2048
	global_load_dwordx4 a[140:143], v192, s[44:45] offset:3072
	s_add_u32 s44, s44, 0x1000
	s_addc_u32 s45, s45, 0
	global_load_dwordx4 a[144:147], v192, s[44:45] offset:0
	global_load_dwordx4 a[148:151], v192, s[44:45] offset:1024
	global_load_dwordx4 a[152:155], v192, s[44:45] offset:2048
	global_load_dwordx4 a[156:159], v192, s[44:45] offset:3072
	s_add_u32 s44, s44, 0x1000
	s_addc_u32 s45, s45, 0
	global_load_dwordx4 a[160:163], v192, s[44:45] offset:0
	global_load_dwordx4 a[164:167], v192, s[44:45] offset:1024
	global_load_dwordx4 a[168:171], v192, s[44:45] offset:2048
	global_load_dwordx4 a[172:175], v192, s[44:45] offset:3072
	s_add_u32 s44, s44, 0x1000
	s_addc_u32 s45, s45, 0
	global_load_dwordx4 a[176:179], v192, s[44:45] offset:0
	global_load_dwordx4 a[180:183], v192, s[44:45] offset:1024
	global_load_dwordx4 a[184:187], v192, s[44:45] offset:2048
	global_load_dwordx4 a[188:191], v192, s[44:45] offset:3072
	s_add_u32 s44, s44, 0x1000
	s_addc_u32 s45, s45, 0
	global_load_dwordx4 a[192:195], v192, s[44:45] offset:0
	global_load_dwordx4 a[196:199], v192, s[44:45] offset:1024
	global_load_dwordx4 a[200:203], v192, s[44:45] offset:2048
	global_load_dwordx4 a[204:207], v192, s[44:45] offset:3072
	s_add_u32 s44, s44, 0x1000
	s_addc_u32 s45, s45, 0
	global_load_dwordx4 a[208:211], v192, s[44:45] offset:0
	global_load_dwordx4 a[212:215], v192, s[44:45] offset:1024
	global_load_dwordx4 a[216:219], v192, s[44:45] offset:2048
	global_load_dwordx4 a[220:223], v192, s[44:45] offset:3072
	s_add_u32 s44, s44, 0x1000
	s_addc_u32 s45, s45, 0
	global_load_dwordx4 a[224:227], v192, s[44:45] offset:0
	global_load_dwordx4 a[228:231], v192, s[44:45] offset:1024
	global_load_dwordx4 a[232:235], v192, s[44:45] offset:2048
	global_load_dwordx4 a[236:239], v192, s[44:45] offset:3072
	s_add_u32 s44, s44, 0x1000
	s_addc_u32 s45, s45, 0
	global_load_dwordx4 a[240:243], v192, s[44:45] offset:0
	global_load_dwordx4 a[244:247], v192, s[44:45] offset:1024
	global_load_dwordx4 a[248:251], v192, s[44:45] offset:2048
	global_load_dwordx4 a[252:255], v192, s[44:45] offset:3072
	s_add_u32 s44, s44, 0x1000
	s_addc_u32 s45, s45, 0
	v_mov_b32_e32 v128, 0
	v_mov_b32_e32 v129, 0
	v_mov_b32_e32 v130, 0
	v_mov_b32_e32 v131, 0
	v_mov_b32_e32 v132, 0
	v_mov_b32_e32 v133, 0
	v_mov_b32_e32 v134, 0
	v_mov_b32_e32 v135, 0
	v_mov_b32_e32 v136, 0
	v_mov_b32_e32 v137, 0
	v_mov_b32_e32 v138, 0
	v_mov_b32_e32 v139, 0
	v_mov_b32_e32 v140, 0
	v_mov_b32_e32 v141, 0
	v_mov_b32_e32 v142, 0
	v_mov_b32_e32 v143, 0
	v_mov_b32_e32 v144, 0
	v_mov_b32_e32 v145, 0
	v_mov_b32_e32 v146, 0
	v_mov_b32_e32 v147, 0
	v_mov_b32_e32 v148, 0
	v_mov_b32_e32 v149, 0
	v_mov_b32_e32 v150, 0
	v_mov_b32_e32 v151, 0
	v_mov_b32_e32 v152, 0
	v_mov_b32_e32 v153, 0
	v_mov_b32_e32 v154, 0
	v_mov_b32_e32 v155, 0
	v_mov_b32_e32 v156, 0
	v_mov_b32_e32 v157, 0
	v_mov_b32_e32 v158, 0
	v_mov_b32_e32 v159, 0
	s_lshl_b32 s64, s30, 5
	s_lshl_b32 s65, s32, 3
	s_add_u32 s64, s64, s65
	v_lshlrev_b32_e32 v255, 2, v254
	v_add_u32_e32 v255, s64, v255
	v_lshlrev_b32_e32 v249, 3, v253
	v_lshl_add_u32 v249, v254, 2, v249
	v_lshlrev_b32_e32 v250, 12, v253
	v_lshl_add_u32 v250, v254, 4, v250
	v_lshrrev_b32_e32 v200, 3, v253
	v_and_b32_e32 v201, 7, v253
	v_lshl_add_u32 v202, v200, 10, v201
	v_add_u32_e32 v202, s64, v202
	v_lshl_add_u32 v202, v202, 1, v254
	v_lshlrev_b32_e32 v202, 2, v202
	global_load_dword v248, v202, s[14:15]
	v_mov_b32_e32 v203, 0xbfb8aa3b
	v_mov_b32_e32 v204, 0xc038aa3b
	v_cmp_eq_u32_e32 vcc, 2, v200
	s_nop 1
	v_cndmask_b32_e32 v203, v203, v204, vcc
	v_lshlrev_b32_e32 v205, 2, v255
	v_add_u32_e32 v206, 0x0, v205
	global_load_dwordx4 v[232:235], v206, s[16:17]
	v_add_u32_e32 v206, 0x1000, v205
	global_load_dwordx4 v[236:239], v206, s[16:17]
	v_add_u32_e32 v206, 0x2000, v205
	global_load_dwordx4 v[240:243], v206, s[16:17]
	v_add_u32_e32 v206, 0x3000, v205
	global_load_dwordx4 v[244:247], v206, s[16:17]
	s_waitcnt vmcnt(0)
	v_mul_f32_e32 v248, v203, v248
	s_mov_b32 s65, 0xbfb8aa3b
	v_mul_f32_e32 v232, s65, v232
	v_mul_f32_e32 v233, s65, v233
	v_mul_f32_e32 v234, s65, v234
	v_mul_f32_e32 v235, s65, v235
	s_mov_b32 s65, 0xbfb8aa3b
	v_mul_f32_e32 v236, s65, v236
	v_mul_f32_e32 v237, s65, v237
	v_mul_f32_e32 v238, s65, v238
	v_mul_f32_e32 v239, s65, v239
	s_mov_b32 s65, 0xc038aa3b
	v_mul_f32_e32 v240, s65, v240
	v_mul_f32_e32 v241, s65, v241
	v_mul_f32_e32 v242, s65, v242
	v_mul_f32_e32 v243, s65, v243
	s_mov_b32 s65, 0xbfb8aa3b
	v_mul_f32_e32 v244, s65, v244
	v_mul_f32_e32 v245, s65, v245
	v_mul_f32_e32 v246, s65, v246
	v_mul_f32_e32 v247, s65, v247
	s_lshl_b32 s65, s29, 20
	s_lshl_b32 s66, s64, 2
	s_add_u32 s65, s65, s66
	s_add_u32 s62, s26, s65
	s_addc_u32 s63, s27, 0
	s_waitcnt vmcnt(0)
	s_mov_b32 s33, 0
	s_lshl_b32 s64, s33, 11
	s_lshl_b32 s65, s29, 8
	s_add_u32 s64, s64, s65
	s_lshl_b32 s64, s64, 3
	s_add_u32 s42, s12, s64
	s_addc_u32 s43, s13, 0
	global_load_dword v228, v249, s[42:43] offset:0
	global_load_dword v229, v249, s[42:43] offset:256
	s_waitcnt vmcnt(0)
	v_mfma_f32_32x32x2_f32 v[0:15], v248, v228, v[232:247]
	v_mfma_f32_32x32x2_f32 v[16:31], v248, v229, v[232:247]
	s_nop 15
	s_nop 3
	s_lshl_b32 s64, s33, 11
	s_lshl_b32 s65, s29, 8
	s_add_u32 s64, s64, s65
	s_add_u32 s64, s64, 64
	s_lshl_b32 s64, s64, 3
	s_add_u32 s42, s12, s64
	s_addc_u32 s43, s13, 0
	global_load_dword v228, v249, s[42:43] offset:0
	global_load_dword v229, v249, s[42:43] offset:256
	s_waitcnt vmcnt(0)
	v_mfma_f32_32x32x2_f32 v[32:47], v248, v228, v[232:247]
	v_mfma_f32_32x32x2_f32 v[48:63], v248, v229, v[232:247]
	s_nop 15
	s_nop 3
	s_lshl_b32 s64, s33, 11
	s_lshl_b32 s65, s29, 8
	s_add_u32 s64, s64, s65
	s_add_u32 s64, s64, 128
	s_lshl_b32 s64, s64, 3
	s_add_u32 s42, s12, s64
	s_addc_u32 s43, s13, 0
	global_load_dword v228, v249, s[42:43] offset:0
	global_load_dword v229, v249, s[42:43] offset:256
	s_waitcnt vmcnt(0)
	v_mfma_f32_32x32x2_f32 v[64:79], v248, v228, v[232:247]
	v_mfma_f32_32x32x2_f32 v[80:95], v248, v229, v[232:247]
	s_nop 15
	s_nop 3
	s_lshl_b32 s64, s33, 11
	s_lshl_b32 s65, s29, 8
	s_add_u32 s64, s64, s65
	s_add_u32 s64, s64, 192
	s_lshl_b32 s64, s64, 3
	s_add_u32 s42, s12, s64
	s_addc_u32 s43, s13, 0
	global_load_dword v228, v249, s[42:43] offset:0
	global_load_dword v229, v249, s[42:43] offset:256
	s_waitcnt vmcnt(0)
	v_mfma_f32_32x32x2_f32 v[96:111], v248, v228, v[232:247]
	v_mfma_f32_32x32x2_f32 v[112:127], v248, v229, v[232:247]
	s_nop 15
	s_nop 3
	s_waitcnt vmcnt(0)
	s_waitcnt lgkmcnt(0)
	s_lshl_b32 s64, s33, 3
	s_add_u32 s64, s64, s29
	s_lshl_b32 s64, s64, 5
	s_add_u32 s64, s64, s30
	s_lshl_b32 s64, s64, 2
	s_add_u32 s40, s8, s64
	s_addc_u32 s41, s9, 0
	s_and_b32 s64, s33, 1
	s_lshl_b32 s64, s64, 22
	s_add_u32 s64, s64, s50
	s_add_u32 s36, s6, s64
	s_addc_u32 s37, s7, 0
	v_exp_f32_e32 v200, v0
	v_exp_f32_e32 v201, v1
	v_exp_f32_e32 v202, v2
	v_exp_f32_e32 v203, v3
	v_exp_f32_e32 v204, v4
	v_exp_f32_e32 v205, v5
	v_exp_f32_e32 v206, v6
	v_exp_f32_e32 v207, v7
	v_exp_f32_e32 v208, v8
	v_exp_f32_e32 v209, v9
	v_exp_f32_e32 v210, v10
	v_exp_f32_e32 v211, v11
	v_exp_f32_e32 v212, v12
	v_exp_f32_e32 v213, v13
	v_exp_f32_e32 v214, v14
	v_exp_f32_e32 v215, v15
	v_add_f32_e32 v200, 1.0, v200
	v_add_f32_e32 v201, 1.0, v201
	v_add_f32_e32 v202, 1.0, v202
	v_add_f32_e32 v203, 1.0, v203
	v_add_f32_e32 v204, 1.0, v204
	v_add_f32_e32 v205, 1.0, v205
	v_add_f32_e32 v206, 1.0, v206
	v_add_f32_e32 v207, 1.0, v207
	v_add_f32_e32 v208, 1.0, v208
	v_add_f32_e32 v209, 1.0, v209
	v_add_f32_e32 v210, 1.0, v210
	v_add_f32_e32 v211, 1.0, v211
	v_add_f32_e32 v212, 1.0, v212
	v_add_f32_e32 v213, 1.0, v213
	v_add_f32_e32 v214, 1.0, v214
	v_add_f32_e32 v215, 1.0, v215
	v_rcp_f32_e32 v200, v200
	v_rcp_f32_e32 v201, v201
	v_rcp_f32_e32 v202, v202
	v_rcp_f32_e32 v203, v203
	v_rcp_f32_e32 v204, v204
	v_rcp_f32_e32 v205, v205
	v_rcp_f32_e32 v206, v206
	v_rcp_f32_e32 v207, v207
	v_rcp_f32_e32 v208, v208
	v_rcp_f32_e32 v209, v209
	v_rcp_f32_e32 v210, v210
	v_rcp_f32_e32 v211, v211
	v_rcp_f32_e32 v212, v212
	v_rcp_f32_e32 v213, v213
	v_rcp_f32_e32 v214, v214
	v_rcp_f32_e32 v215, v215
	v_fmamk_f32 v208, v208, 0xc0b8aa3b, v198
	v_fmamk_f32 v209, v209, 0xc0b8aa3b, v198
	v_fmamk_f32 v210, v210, 0xc0b8aa3b, v198
	v_fmamk_f32 v211, v211, 0xc0b8aa3b, v198
	v_mul_f32_e32 v204, v204, v128
	v_mul_f32_e32 v205, v205, v129
	v_mul_f32_e32 v206, v206, v130
	v_mul_f32_e32 v207, v207, v131
	v_fma_f32 v128, v200, v208, v204
	v_fma_f32 v129, v201, v209, v205
	v_fma_f32 v130, v202, v210, v206
	v_fma_f32 v131, v203, v211, v207
	v_exp_f32_e32 v200, v128
	v_exp_f32_e32 v201, v129
	v_exp_f32_e32 v202, v130
	v_exp_f32_e32 v203, v131
	v_add_f32_e32 v200, 1.0, v200
	v_add_f32_e32 v201, 1.0, v201
	v_add_f32_e32 v202, 1.0, v202
	v_add_f32_e32 v203, 1.0, v203
	v_rcp_f32_e32 v200, v200
	v_rcp_f32_e32 v201, v201
	v_rcp_f32_e32 v202, v202
	v_rcp_f32_e32 v203, v203
	v_fma_f32 v200, v200, 2.0, -1.0
	v_fma_f32 v201, v201, 2.0, -1.0
	v_fma_f32 v202, v202, 2.0, -1.0
	v_fma_f32 v203, v203, 2.0, -1.0
	v_mul_f32_e32 v216, v212, v200
	v_mul_f32_e32 v217, v213, v201
	v_mul_f32_e32 v218, v214, v202
	v_mul_f32_e32 v219, v215, v203
	v_cvt_pk_f16_f32 v220, v216, v217
	v_cvt_pk_f16_f32 v221, v218, v219
	v_exp_f32_e32 v200, v16
	v_exp_f32_e32 v201, v17
	v_exp_f32_e32 v202, v18
	v_exp_f32_e32 v203, v19
	v_exp_f32_e32 v204, v20
	v_exp_f32_e32 v205, v21
	v_exp_f32_e32 v206, v22
	v_exp_f32_e32 v207, v23
	v_exp_f32_e32 v208, v24
	v_exp_f32_e32 v209, v25
	v_exp_f32_e32 v210, v26
	v_exp_f32_e32 v211, v27
	v_exp_f32_e32 v212, v28
	v_exp_f32_e32 v213, v29
	v_exp_f32_e32 v214, v30
	v_exp_f32_e32 v215, v31
	v_add_f32_e32 v200, 1.0, v200
	v_add_f32_e32 v201, 1.0, v201
	v_add_f32_e32 v202, 1.0, v202
	v_add_f32_e32 v203, 1.0, v203
	v_add_f32_e32 v204, 1.0, v204
	v_add_f32_e32 v205, 1.0, v205
	v_add_f32_e32 v206, 1.0, v206
	v_add_f32_e32 v207, 1.0, v207
	v_add_f32_e32 v208, 1.0, v208
	v_add_f32_e32 v209, 1.0, v209
	v_add_f32_e32 v210, 1.0, v210
	v_add_f32_e32 v211, 1.0, v211
	v_add_f32_e32 v212, 1.0, v212
	v_add_f32_e32 v213, 1.0, v213
	v_add_f32_e32 v214, 1.0, v214
	v_add_f32_e32 v215, 1.0, v215
	v_rcp_f32_e32 v200, v200
	v_rcp_f32_e32 v201, v201
	v_rcp_f32_e32 v202, v202
	v_rcp_f32_e32 v203, v203
	v_rcp_f32_e32 v204, v204
	v_rcp_f32_e32 v205, v205
	v_rcp_f32_e32 v206, v206
	v_rcp_f32_e32 v207, v207
	v_rcp_f32_e32 v208, v208
	v_rcp_f32_e32 v209, v209
	v_rcp_f32_e32 v210, v210
	v_rcp_f32_e32 v211, v211
	v_rcp_f32_e32 v212, v212
	v_rcp_f32_e32 v213, v213
	v_rcp_f32_e32 v214, v214
	v_rcp_f32_e32 v215, v215
	v_fmamk_f32 v208, v208, 0xc0b8aa3b, v198
	v_fmamk_f32 v209, v209, 0xc0b8aa3b, v198
	v_fmamk_f32 v210, v210, 0xc0b8aa3b, v198
	v_fmamk_f32 v211, v211, 0xc0b8aa3b, v198
	v_mul_f32_e32 v204, v204, v132
	v_mul_f32_e32 v205, v205, v133
	v_mul_f32_e32 v206, v206, v134
	v_mul_f32_e32 v207, v207, v135
	v_fma_f32 v132, v200, v208, v204
	v_fma_f32 v133, v201, v209, v205
	v_fma_f32 v134, v202, v210, v206
	v_fma_f32 v135, v203, v211, v207
	v_exp_f32_e32 v200, v132
	v_exp_f32_e32 v201, v133
	v_exp_f32_e32 v202, v134
	v_exp_f32_e32 v203, v135
	v_add_f32_e32 v200, 1.0, v200
	v_add_f32_e32 v201, 1.0, v201
	v_add_f32_e32 v202, 1.0, v202
	v_add_f32_e32 v203, 1.0, v203
	v_rcp_f32_e32 v200, v200
	v_rcp_f32_e32 v201, v201
	v_rcp_f32_e32 v202, v202
	v_rcp_f32_e32 v203, v203
	v_fma_f32 v200, v200, 2.0, -1.0
	v_fma_f32 v201, v201, 2.0, -1.0
	v_fma_f32 v202, v202, 2.0, -1.0
	v_fma_f32 v203, v203, 2.0, -1.0
	v_mul_f32_e32 v216, v212, v200
	v_mul_f32_e32 v217, v213, v201
	v_mul_f32_e32 v218, v214, v202
	v_mul_f32_e32 v219, v215, v203
	v_cvt_pk_f16_f32 v222, v216, v217
	v_cvt_pk_f16_f32 v223, v218, v219
	s_nop 1
	v_permlane32_swap_b32_e32 v220, v222
	v_permlane32_swap_b32_e32 v221, v223
	s_cmp_eq_u32 s31, 0
	s_cbranch_scc1 .LE_slow4
	global_store_dwordx4 v195, v[220:223], s[36:37] offset:0
.LE_join5:
	s_waitcnt vmcnt(0)
	s_barrier
	v_mov_b32_e32 v199, 1
	s_cmp_eq_u32 s31, 0
	s_cbranch_scc1 .LE_slow6
	global_store_dword v197, v199, s[40:41]
.LE_join7:
	s_and_b32 s64, s33, 1
	s_lshl_b32 s64, s64, 22
	s_add_u32 s64, s64, s50
	s_add_u32 s64, s64, 0x20000
	s_add_u32 s36, s6, s64
	s_addc_u32 s37, s7, 0
	v_exp_f32_e32 v200, v32
	v_exp_f32_e32 v201, v33
	v_exp_f32_e32 v202, v34
	v_exp_f32_e32 v203, v35
	v_exp_f32_e32 v204, v36
	v_exp_f32_e32 v205, v37
	v_exp_f32_e32 v206, v38
	v_exp_f32_e32 v207, v39
	v_exp_f32_e32 v208, v40
	v_exp_f32_e32 v209, v41
	v_exp_f32_e32 v210, v42
	v_exp_f32_e32 v211, v43
	v_exp_f32_e32 v212, v44
	v_exp_f32_e32 v213, v45
	v_exp_f32_e32 v214, v46
	v_exp_f32_e32 v215, v47
	v_add_f32_e32 v200, 1.0, v200
	v_add_f32_e32 v201, 1.0, v201
	v_add_f32_e32 v202, 1.0, v202
	v_add_f32_e32 v203, 1.0, v203
	v_add_f32_e32 v204, 1.0, v204
	v_add_f32_e32 v205, 1.0, v205
	v_add_f32_e32 v206, 1.0, v206
	v_add_f32_e32 v207, 1.0, v207
	v_add_f32_e32 v208, 1.0, v208
	v_add_f32_e32 v209, 1.0, v209
	v_add_f32_e32 v210, 1.0, v210
	v_add_f32_e32 v211, 1.0, v211
	v_add_f32_e32 v212, 1.0, v212
	v_add_f32_e32 v213, 1.0, v213
	v_add_f32_e32 v214, 1.0, v214
	v_add_f32_e32 v215, 1.0, v215
	v_rcp_f32_e32 v200, v200
	v_rcp_f32_e32 v201, v201
	v_rcp_f32_e32 v202, v202
	v_rcp_f32_e32 v203, v203
	v_rcp_f32_e32 v204, v204
	v_rcp_f32_e32 v205, v205
	v_rcp_f32_e32 v206, v206
	v_rcp_f32_e32 v207, v207
	v_rcp_f32_e32 v208, v208
	v_rcp_f32_e32 v209, v209
	v_rcp_f32_e32 v210, v210
	v_rcp_f32_e32 v211, v211
	v_rcp_f32_e32 v212, v212
	v_rcp_f32_e32 v213, v213
	v_rcp_f32_e32 v214, v214
	v_rcp_f32_e32 v215, v215
	v_fmamk_f32 v208, v208, 0xc0b8aa3b, v198
	v_fmamk_f32 v209, v209, 0xc0b8aa3b, v198
	v_fmamk_f32 v210, v210, 0xc0b8aa3b, v198
	v_fmamk_f32 v211, v211, 0xc0b8aa3b, v198
	v_mul_f32_e32 v204, v204, v136
	v_mul_f32_e32 v205, v205, v137
	v_mul_f32_e32 v206, v206, v138
	v_mul_f32_e32 v207, v207, v139
	v_fma_f32 v136, v200, v208, v204
	v_fma_f32 v137, v201, v209, v205
	v_fma_f32 v138, v202, v210, v206
	v_fma_f32 v139, v203, v211, v207
	v_exp_f32_e32 v200, v136
	v_exp_f32_e32 v201, v137
	v_exp_f32_e32 v202, v138
	v_exp_f32_e32 v203, v139
	v_add_f32_e32 v200, 1.0, v200
	v_add_f32_e32 v201, 1.0, v201
	v_add_f32_e32 v202, 1.0, v202
	v_add_f32_e32 v203, 1.0, v203
	v_rcp_f32_e32 v200, v200
	v_rcp_f32_e32 v201, v201
	v_rcp_f32_e32 v202, v202
	v_rcp_f32_e32 v203, v203
	v_fma_f32 v200, v200, 2.0, -1.0
	v_fma_f32 v201, v201, 2.0, -1.0
	v_fma_f32 v202, v202, 2.0, -1.0
	v_fma_f32 v203, v203, 2.0, -1.0
	v_mul_f32_e32 v216, v212, v200
	v_mul_f32_e32 v217, v213, v201
	v_mul_f32_e32 v218, v214, v202
	v_mul_f32_e32 v219, v215, v203
	v_cvt_pk_f16_f32 v220, v216, v217
	v_cvt_pk_f16_f32 v221, v218, v219
	v_exp_f32_e32 v200, v48
	v_exp_f32_e32 v201, v49
	v_exp_f32_e32 v202, v50
	v_exp_f32_e32 v203, v51
	v_exp_f32_e32 v204, v52
	v_exp_f32_e32 v205, v53
	v_exp_f32_e32 v206, v54
	v_exp_f32_e32 v207, v55
	v_exp_f32_e32 v208, v56
	v_exp_f32_e32 v209, v57
	v_exp_f32_e32 v210, v58
	v_exp_f32_e32 v211, v59
	v_exp_f32_e32 v212, v60
	v_exp_f32_e32 v213, v61
	v_exp_f32_e32 v214, v62
	v_exp_f32_e32 v215, v63
	v_add_f32_e32 v200, 1.0, v200
	v_add_f32_e32 v201, 1.0, v201
	v_add_f32_e32 v202, 1.0, v202
	v_add_f32_e32 v203, 1.0, v203
	v_add_f32_e32 v204, 1.0, v204
	v_add_f32_e32 v205, 1.0, v205
	v_add_f32_e32 v206, 1.0, v206
	v_add_f32_e32 v207, 1.0, v207
	v_add_f32_e32 v208, 1.0, v208
	v_add_f32_e32 v209, 1.0, v209
	v_add_f32_e32 v210, 1.0, v210
	v_add_f32_e32 v211, 1.0, v211
	v_add_f32_e32 v212, 1.0, v212
	v_add_f32_e32 v213, 1.0, v213
	v_add_f32_e32 v214, 1.0, v214
	v_add_f32_e32 v215, 1.0, v215
	v_rcp_f32_e32 v200, v200
	v_rcp_f32_e32 v201, v201
	v_rcp_f32_e32 v202, v202
	v_rcp_f32_e32 v203, v203
	v_rcp_f32_e32 v204, v204
	v_rcp_f32_e32 v205, v205
	v_rcp_f32_e32 v206, v206
	v_rcp_f32_e32 v207, v207
	v_rcp_f32_e32 v208, v208
	v_rcp_f32_e32 v209, v209
	v_rcp_f32_e32 v210, v210
	v_rcp_f32_e32 v211, v211
	v_rcp_f32_e32 v212, v212
	v_rcp_f32_e32 v213, v213
	v_rcp_f32_e32 v214, v214
	v_rcp_f32_e32 v215, v215
	v_fmamk_f32 v208, v208, 0xc0b8aa3b, v198
	v_fmamk_f32 v209, v209, 0xc0b8aa3b, v198
	v_fmamk_f32 v210, v210, 0xc0b8aa3b, v198
	v_fmamk_f32 v211, v211, 0xc0b8aa3b, v198
	v_mul_f32_e32 v204, v204, v140
	v_mul_f32_e32 v205, v205, v141
	v_mul_f32_e32 v206, v206, v142
	v_mul_f32_e32 v207, v207, v143
	v_fma_f32 v140, v200, v208, v204
	v_fma_f32 v141, v201, v209, v205
	v_fma_f32 v142, v202, v210, v206
	v_fma_f32 v143, v203, v211, v207
	v_exp_f32_e32 v200, v140
	v_exp_f32_e32 v201, v141
	v_exp_f32_e32 v202, v142
	v_exp_f32_e32 v203, v143
	v_add_f32_e32 v200, 1.0, v200
	v_add_f32_e32 v201, 1.0, v201
	v_add_f32_e32 v202, 1.0, v202
	v_add_f32_e32 v203, 1.0, v203
	v_rcp_f32_e32 v200, v200
	v_rcp_f32_e32 v201, v201
	v_rcp_f32_e32 v202, v202
	v_rcp_f32_e32 v203, v203
	v_fma_f32 v200, v200, 2.0, -1.0
	v_fma_f32 v201, v201, 2.0, -1.0
	v_fma_f32 v202, v202, 2.0, -1.0
	v_fma_f32 v203, v203, 2.0, -1.0
	v_mul_f32_e32 v216, v212, v200
	v_mul_f32_e32 v217, v213, v201
	v_mul_f32_e32 v218, v214, v202
	v_mul_f32_e32 v219, v215, v203
	v_cvt_pk_f16_f32 v222, v216, v217
	v_cvt_pk_f16_f32 v223, v218, v219
	s_nop 1
	v_permlane32_swap_b32_e32 v220, v222
	v_permlane32_swap_b32_e32 v221, v223
	s_cmp_eq_u32 s31, 0
	s_cbranch_scc1 .LE_slow8
	global_store_dwordx4 v195, v[220:223], s[36:37] offset:0
.LE_join9:
	s_waitcnt vmcnt(0)
	s_barrier
	v_mov_b32_e32 v199, 2
	s_cmp_eq_u32 s31, 0
	s_cbranch_scc1 .LE_slow10
	global_store_dword v197, v199, s[40:41]
.LE_join11:
	s_and_b32 s64, s33, 1
	s_lshl_b32 s64, s64, 22
	s_add_u32 s64, s64, s50
	s_add_u32 s64, s64, 0x40000
	s_add_u32 s36, s6, s64
	s_addc_u32 s37, s7, 0
	v_exp_f32_e32 v200, v64
	v_exp_f32_e32 v201, v65
	v_exp_f32_e32 v202, v66
	v_exp_f32_e32 v203, v67
	v_exp_f32_e32 v204, v68
	v_exp_f32_e32 v205, v69
	v_exp_f32_e32 v206, v70
	v_exp_f32_e32 v207, v71
	v_exp_f32_e32 v208, v72
	v_exp_f32_e32 v209, v73
	v_exp_f32_e32 v210, v74
	v_exp_f32_e32 v211, v75
	v_exp_f32_e32 v212, v76
	v_exp_f32_e32 v213, v77
	v_exp_f32_e32 v214, v78
	v_exp_f32_e32 v215, v79
	v_add_f32_e32 v200, 1.0, v200
	v_add_f32_e32 v201, 1.0, v201
	v_add_f32_e32 v202, 1.0, v202
	v_add_f32_e32 v203, 1.0, v203
	v_add_f32_e32 v204, 1.0, v204
	v_add_f32_e32 v205, 1.0, v205
	v_add_f32_e32 v206, 1.0, v206
	v_add_f32_e32 v207, 1.0, v207
	v_add_f32_e32 v208, 1.0, v208
	v_add_f32_e32 v209, 1.0, v209
	v_add_f32_e32 v210, 1.0, v210
	v_add_f32_e32 v211, 1.0, v211
	v_add_f32_e32 v212, 1.0, v212
	v_add_f32_e32 v213, 1.0, v213
	v_add_f32_e32 v214, 1.0, v214
	v_add_f32_e32 v215, 1.0, v215
	v_rcp_f32_e32 v200, v200
	v_rcp_f32_e32 v201, v201
	v_rcp_f32_e32 v202, v202
	v_rcp_f32_e32 v203, v203
	v_rcp_f32_e32 v204, v204
	v_rcp_f32_e32 v205, v205
	v_rcp_f32_e32 v206, v206
	v_rcp_f32_e32 v207, v207
	v_rcp_f32_e32 v208, v208
	v_rcp_f32_e32 v209, v209
	v_rcp_f32_e32 v210, v210
	v_rcp_f32_e32 v211, v211
	v_rcp_f32_e32 v212, v212
	v_rcp_f32_e32 v213, v213
	v_rcp_f32_e32 v214, v214
	v_rcp_f32_e32 v215, v215
	v_fmamk_f32 v208, v208, 0xc0b8aa3b, v198
	v_fmamk_f32 v209, v209, 0xc0b8aa3b, v198
	v_fmamk_f32 v210, v210, 0xc0b8aa3b, v198
	v_fmamk_f32 v211, v211, 0xc0b8aa3b, v198
	v_mul_f32_e32 v204, v204, v144
	v_mul_f32_e32 v205, v205, v145
	v_mul_f32_e32 v206, v206, v146
	v_mul_f32_e32 v207, v207, v147
	v_fma_f32 v144, v200, v208, v204
	v_fma_f32 v145, v201, v209, v205
	v_fma_f32 v146, v202, v210, v206
	v_fma_f32 v147, v203, v211, v207
	v_exp_f32_e32 v200, v144
	v_exp_f32_e32 v201, v145
	v_exp_f32_e32 v202, v146
	v_exp_f32_e32 v203, v147
	v_add_f32_e32 v200, 1.0, v200
	v_add_f32_e32 v201, 1.0, v201
	v_add_f32_e32 v202, 1.0, v202
	v_add_f32_e32 v203, 1.0, v203
	v_rcp_f32_e32 v200, v200
	v_rcp_f32_e32 v201, v201
	v_rcp_f32_e32 v202, v202
	v_rcp_f32_e32 v203, v203
	v_fma_f32 v200, v200, 2.0, -1.0
	v_fma_f32 v201, v201, 2.0, -1.0
	v_fma_f32 v202, v202, 2.0, -1.0
	v_fma_f32 v203, v203, 2.0, -1.0
	v_mul_f32_e32 v216, v212, v200
	v_mul_f32_e32 v217, v213, v201
	v_mul_f32_e32 v218, v214, v202
	v_mul_f32_e32 v219, v215, v203
	v_cvt_pk_f16_f32 v220, v216, v217
	v_cvt_pk_f16_f32 v221, v218, v219
	v_exp_f32_e32 v200, v80
	v_exp_f32_e32 v201, v81
	v_exp_f32_e32 v202, v82
	v_exp_f32_e32 v203, v83
	v_exp_f32_e32 v204, v84
	v_exp_f32_e32 v205, v85
	v_exp_f32_e32 v206, v86
	v_exp_f32_e32 v207, v87
	v_exp_f32_e32 v208, v88
	v_exp_f32_e32 v209, v89
	v_exp_f32_e32 v210, v90
	v_exp_f32_e32 v211, v91
	v_exp_f32_e32 v212, v92
	v_exp_f32_e32 v213, v93
	v_exp_f32_e32 v214, v94
	v_exp_f32_e32 v215, v95
	v_add_f32_e32 v200, 1.0, v200
	v_add_f32_e32 v201, 1.0, v201
	v_add_f32_e32 v202, 1.0, v202
	v_add_f32_e32 v203, 1.0, v203
	v_add_f32_e32 v204, 1.0, v204
	v_add_f32_e32 v205, 1.0, v205
	v_add_f32_e32 v206, 1.0, v206
	v_add_f32_e32 v207, 1.0, v207
	v_add_f32_e32 v208, 1.0, v208
	v_add_f32_e32 v209, 1.0, v209
	v_add_f32_e32 v210, 1.0, v210
	v_add_f32_e32 v211, 1.0, v211
	v_add_f32_e32 v212, 1.0, v212
	v_add_f32_e32 v213, 1.0, v213
	v_add_f32_e32 v214, 1.0, v214
	v_add_f32_e32 v215, 1.0, v215
	v_rcp_f32_e32 v200, v200
	v_rcp_f32_e32 v201, v201
	v_rcp_f32_e32 v202, v202
	v_rcp_f32_e32 v203, v203
	v_rcp_f32_e32 v204, v204
	v_rcp_f32_e32 v205, v205
	v_rcp_f32_e32 v206, v206
	v_rcp_f32_e32 v207, v207
	v_rcp_f32_e32 v208, v208
	v_rcp_f32_e32 v209, v209
	v_rcp_f32_e32 v210, v210
	v_rcp_f32_e32 v211, v211
	v_rcp_f32_e32 v212, v212
	v_rcp_f32_e32 v213, v213
	v_rcp_f32_e32 v214, v214
	v_rcp_f32_e32 v215, v215
	v_fmamk_f32 v208, v208, 0xc0b8aa3b, v198
	v_fmamk_f32 v209, v209, 0xc0b8aa3b, v198
	v_fmamk_f32 v210, v210, 0xc0b8aa3b, v198
	v_fmamk_f32 v211, v211, 0xc0b8aa3b, v198
	v_mul_f32_e32 v204, v204, v148
	v_mul_f32_e32 v205, v205, v149
	v_mul_f32_e32 v206, v206, v150
	v_mul_f32_e32 v207, v207, v151
	v_fma_f32 v148, v200, v208, v204
	v_fma_f32 v149, v201, v209, v205
	v_fma_f32 v150, v202, v210, v206
	v_fma_f32 v151, v203, v211, v207
	v_exp_f32_e32 v200, v148
	v_exp_f32_e32 v201, v149
	v_exp_f32_e32 v202, v150
	v_exp_f32_e32 v203, v151
	v_add_f32_e32 v200, 1.0, v200
	v_add_f32_e32 v201, 1.0, v201
	v_add_f32_e32 v202, 1.0, v202
	v_add_f32_e32 v203, 1.0, v203
	v_rcp_f32_e32 v200, v200
	v_rcp_f32_e32 v201, v201
	v_rcp_f32_e32 v202, v202
	v_rcp_f32_e32 v203, v203
	v_fma_f32 v200, v200, 2.0, -1.0
	v_fma_f32 v201, v201, 2.0, -1.0
	v_fma_f32 v202, v202, 2.0, -1.0
	v_fma_f32 v203, v203, 2.0, -1.0
	v_mul_f32_e32 v216, v212, v200
	v_mul_f32_e32 v217, v213, v201
	v_mul_f32_e32 v218, v214, v202
	v_mul_f32_e32 v219, v215, v203
	v_cvt_pk_f16_f32 v222, v216, v217
	v_cvt_pk_f16_f32 v223, v218, v219
	s_nop 1
	v_permlane32_swap_b32_e32 v220, v222
	v_permlane32_swap_b32_e32 v221, v223
	s_cmp_eq_u32 s31, 0
	s_cbranch_scc1 .LE_slow12
	global_store_dwordx4 v195, v[220:223], s[36:37] offset:0
.LE_join13:
	s_waitcnt vmcnt(0)
	s_barrier
	v_mov_b32_e32 v199, 3
	s_cmp_eq_u32 s31, 0
	s_cbranch_scc1 .LE_slow14
	global_store_dword v197, v199, s[40:41]
.LE_join15:
	s_mov_b32 s33, 1
	s_lshl_b32 s64, s33, 11
	s_lshl_b32 s65, s29, 8
	s_add_u32 s64, s64, s65
	s_lshl_b32 s64, s64, 3
	s_add_u32 s42, s12, s64
	s_addc_u32 s43, s13, 0
	global_load_dword v228, v249, s[42:43] offset:0
	global_load_dword v229, v249, s[42:43] offset:256
	s_waitcnt vmcnt(0)
	v_mfma_f32_32x32x2_f32 v[0:15], v248, v228, v[232:247]
	v_mfma_f32_32x32x2_f32 v[16:31], v248, v229, v[232:247]
	s_nop 15
	s_nop 3
	s_lshl_b32 s64, s33, 11
	s_lshl_b32 s65, s29, 8
	s_add_u32 s64, s64, s65
	s_add_u32 s64, s64, 64
	s_lshl_b32 s64, s64, 3
	s_add_u32 s42, s12, s64
	s_addc_u32 s43, s13, 0
	global_load_dword v228, v249, s[42:43] offset:0
	global_load_dword v229, v249, s[42:43] offset:256
	s_waitcnt vmcnt(0)
	v_mfma_f32_32x32x2_f32 v[32:47], v248, v228, v[232:247]
	v_mfma_f32_32x32x2_f32 v[48:63], v248, v229, v[232:247]
	s_nop 15
	s_nop 3
	s_waitcnt vmcnt(0)
	s_waitcnt lgkmcnt(0)
	s_cmp_ge_u32 s33, s28
	s_cbranch_scc1 .LE_end17
	s_sub_u32 s71, s33, 1
	s_and_b32 s64, s71, 1
	s_lshl_b32 s64, s64, 22
	s_add_u32 s64, s64, s49
	s_add_u32 s34, s6, s64
	s_addc_u32 s35, s7, 0
	s_lshl_b32 s64, s71, 3
	s_add_u32 s64, s64, s29
	s_lshl_b32 s64, s64, 7
	s_add_u32 s38, s8, s64
	s_addc_u32 s39, s9, 0

.LE_loop16:
	s_sub_u32 s71, s33, 1
	s_add_u32 s61, s33, 1
	s_min_u32 s61, s61, s60
	s_and_b32 s64, s71, 1
	s_lshl_b32 s64, s64, 22
	s_add_u32 s64, s64, s50
	s_add_u32 s64, s64, 0x60000
	s_add_u32 s36, s6, s64
	s_addc_u32 s37, s7, 0
	s_lshl_b32 s64, s71, 3
	s_add_u32 s64, s64, s29
	s_lshl_b32 s64, s64, 5
	s_add_u32 s64, s64, s30
	s_lshl_b32 s64, s64, 2
	s_add_u32 s40, s8, s64
	s_addc_u32 s41, s9, 0
	s_lshl_b32 s64, s33, 11
	s_lshl_b32 s65, s29, 8
	s_add_u32 s64, s64, s65
	s_add_u32 s64, s64, 128
	s_lshl_b32 s64, s64, 3
	s_add_u32 s42, s12, s64
	s_addc_u32 s43, s13, 0
	s_nop 3
	global_load_dword v228, v249, s[42:43] offset:0
	global_load_dword v229, v249, s[42:43] offset:256
	s_waitcnt lgkmcnt(4)
	v_mfma_f32_32x32x16_f16 v[0:15], a[0:3], v[160:163], v[0:15]
	ds_read_b128 v[160:163], v192 offset:8192
	v_exp_f32_e32 v200, v96
	v_mfma_f32_32x32x16_f16 v[16:31], a[0:3], v[164:167], v[16:31]
	ds_read_b128 v[164:167], v192 offset:9216
	s_lshl_b32 s64, s71, 3
	s_add_u32 s64, s64, s29
	s_lshl_b32 s64, s64, 7
	s_add_u32 s38, s8, s64
	s_addc_u32 s39, s9, 0
	global_load_dword v251, v196, s[38:39] sc1
	v_exp_f32_e32 v201, v97
	v_add_f32_e32 v200, 1.0, v200
	v_mfma_f32_32x32x16_f16 v[0:15], a[4:7], v[168:171], v[0:15]
	ds_read_b128 v[168:171], v192 offset:10240
	v_exp_f32_e32 v202, v98
	v_add_f32_e32 v201, 1.0, v201
	v_mfma_f32_32x32x16_f16 v[16:31], a[4:7], v[172:175], v[16:31]
	ds_read_b128 v[172:175], v192 offset:11264
	global_load_lds_dwordx4 v192, s[44:45] offset:1024 sc1
	v_exp_f32_e32 v203, v99
	v_add_f32_e32 v202, 1.0, v202
	s_waitcnt lgkmcnt(4)
	v_mfma_f32_32x32x16_f16 v[0:15], a[8:11], v[176:179], v[0:15]
	ds_read_b128 v[176:179], v192 offset:12288
	v_exp_f32_e32 v204, v100
	v_add_f32_e32 v203, 1.0, v203
	v_mfma_f32_32x32x16_f16 v[16:31], a[8:11], v[180:183], v[16:31]
	ds_read_b128 v[180:183], v192 offset:13312
	v_exp_f32_e32 v205, v101
	v_add_f32_e32 v204, 1.0, v204
	v_mfma_f32_32x32x16_f16 v[0:15], a[12:15], v[184:187], v[0:15]
	ds_read_b128 v[184:187], v192 offset:14336
	v_exp_f32_e32 v206, v102
	v_add_f32_e32 v205, 1.0, v205
	v_mfma_f32_32x32x16_f16 v[16:31], a[12:15], v[188:191], v[16:31]
	ds_read_b128 v[188:191], v192 offset:15360
	global_load_lds_dwordx4 v192, s[44:45] offset:2048 sc1
	v_exp_f32_e32 v207, v103
	v_add_f32_e32 v206, 1.0, v206
	s_waitcnt lgkmcnt(4)
	v_mfma_f32_32x32x16_f16 v[0:15], a[16:19], v[160:163], v[0:15]
	ds_read_b128 v[160:163], v192 offset:16384
	v_exp_f32_e32 v208, v104
	v_add_f32_e32 v207, 1.0, v207
	v_mfma_f32_32x32x16_f16 v[16:31], a[16:19], v[164:167], v[16:31]
	ds_read_b128 v[164:167], v192 offset:17408
	v_exp_f32_e32 v209, v105
	v_add_f32_e32 v208, 1.0, v208
	v_mfma_f32_32x32x16_f16 v[0:15], a[20:23], v[168:171], v[0:15]
	ds_read_b128 v[168:171], v192 offset:18432
	v_exp_f32_e32 v210, v106
	v_add_f32_e32 v209, 1.0, v209
	v_mfma_f32_32x32x16_f16 v[16:31], a[20:23], v[172:175], v[16:31]
	ds_read_b128 v[172:175], v192 offset:19456
	global_load_lds_dwordx4 v192, s[44:45] offset:3072 sc1
	v_exp_f32_e32 v211, v107
	v_add_f32_e32 v210, 1.0, v210
	s_waitcnt lgkmcnt(4)
	v_mfma_f32_32x32x16_f16 v[0:15], a[24:27], v[176:179], v[0:15]
	ds_read_b128 v[176:179], v192 offset:20480
	v_exp_f32_e32 v212, v108
	v_add_f32_e32 v211, 1.0, v211
	v_mfma_f32_32x32x16_f16 v[16:31], a[24:27], v[180:183], v[16:31]
	ds_read_b128 v[180:183], v192 offset:21504
	v_exp_f32_e32 v213, v109
	v_add_f32_e32 v212, 1.0, v212
	v_mfma_f32_32x32x16_f16 v[0:15], a[28:31], v[184:187], v[0:15]
	ds_read_b128 v[184:187], v192 offset:22528
	v_exp_f32_e32 v214, v110
	v_add_f32_e32 v213, 1.0, v213
	v_mfma_f32_32x32x16_f16 v[16:31], a[28:31], v[188:191], v[16:31]
	ds_read_b128 v[188:191], v192 offset:23552
	s_add_u32 s44, s34, 0x11000
	s_addc_u32 s45, s35, 0
	s_mov_b32 m0, s57
	s_nop 0
	global_load_lds_dwordx4 v192, s[44:45] sc1
	v_exp_f32_e32 v215, v111
	v_add_f32_e32 v214, 1.0, v214
	s_waitcnt lgkmcnt(4)
	v_mfma_f32_32x32x16_f16 v[0:15], a[32:35], v[160:163], v[0:15]
	ds_read_b128 v[160:163], v192 offset:24576
	v_add_f32_e32 v215, 1.0, v215
	v_rcp_f32_e32 v200, v200
	v_mfma_f32_32x32x16_f16 v[16:31], a[32:35], v[164:167], v[16:31]
	ds_read_b128 v[164:167], v192 offset:25600
	v_rcp_f32_e32 v201, v201
	v_mfma_f32_32x32x16_f16 v[0:15], a[36:39], v[168:171], v[0:15]
	ds_read_b128 v[168:171], v192 offset:26624
	v_rcp_f32_e32 v202, v202
	v_mfma_f32_32x32x16_f16 v[16:31], a[36:39], v[172:175], v[16:31]
	ds_read_b128 v[172:175], v192 offset:27648
	global_load_lds_dwordx4 v192, s[44:45] offset:1024 sc1
	v_rcp_f32_e32 v203, v203
	s_waitcnt lgkmcnt(4)
	v_mfma_f32_32x32x16_f16 v[0:15], a[40:43], v[176:179], v[0:15]
	ds_read_b128 v[176:179], v192 offset:28672
	v_rcp_f32_e32 v204, v204
	v_mfma_f32_32x32x16_f16 v[16:31], a[40:43], v[180:183], v[16:31]
	ds_read_b128 v[180:183], v192 offset:29696
	v_rcp_f32_e32 v205, v205
	v_mul_f32_e32 v204, v204, v152
	v_mfma_f32_32x32x16_f16 v[0:15], a[44:47], v[184:187], v[0:15]
	ds_read_b128 v[184:187], v192 offset:30720
	v_rcp_f32_e32 v206, v206
	v_mul_f32_e32 v205, v205, v153
	v_mfma_f32_32x32x16_f16 v[16:31], a[44:47], v[188:191], v[16:31]
	ds_read_b128 v[188:191], v192 offset:31744
	global_load_lds_dwordx4 v192, s[44:45] offset:2048 sc1
	v_rcp_f32_e32 v207, v207
	v_mul_f32_e32 v206, v206, v154
	s_waitcnt vmcnt(10)
	s_barrier
	s_waitcnt lgkmcnt(4)
	v_mfma_f32_32x32x16_f16 v[0:15], a[48:51], v[160:163], v[0:15]
	ds_read_b128 v[160:163], v192 offset:32768
	v_rcp_f32_e32 v208, v208
	v_mul_f32_e32 v207, v207, v155
	v_mfma_f32_32x32x16_f16 v[16:31], a[48:51], v[164:167], v[16:31]
	ds_read_b128 v[164:167], v192 offset:33792
	v_rcp_f32_e32 v209, v209
	v_fmamk_f32 v208, v208, 0xc0b8aa3b, v198
	v_mfma_f32_32x32x16_f16 v[0:15], a[52:55], v[168:171], v[0:15]
	ds_read_b128 v[168:171], v192 offset:34816
	v_rcp_f32_e32 v210, v210
	v_fmamk_f32 v209, v209, 0xc0b8aa3b, v198
	v_fma_f32 v152, v200, v208, v204
	v_mfma_f32_32x32x16_f16 v[16:31], a[52:55], v[172:175], v[16:31]
	ds_read_b128 v[172:175], v192 offset:35840
	global_load_lds_dwordx4 v192, s[44:45] offset:3072 sc1
	v_rcp_f32_e32 v211, v211
	v_fmamk_f32 v210, v210, 0xc0b8aa3b, v198
	v_fma_f32 v153, v201, v209, v205
	s_waitcnt lgkmcnt(4)
	v_mfma_f32_32x32x16_f16 v[0:15], a[56:59], v[176:179], v[0:15]
	ds_read_b128 v[176:179], v192 offset:36864
	v_rcp_f32_e32 v212, v212
	v_fmamk_f32 v211, v211, 0xc0b8aa3b, v198
	v_fma_f32 v154, v202, v210, v206
	v_mfma_f32_32x32x16_f16 v[16:31], a[56:59], v[180:183], v[16:31]
	ds_read_b128 v[180:183], v192 offset:37888
	v_rcp_f32_e32 v213, v213
	v_fma_f32 v155, v203, v211, v207
	v_mfma_f32_32x32x16_f16 v[0:15], a[60:63], v[184:187], v[0:15]
	ds_read_b128 v[184:187], v192 offset:38912
	v_rcp_f32_e32 v214, v214
	v_mfma_f32_32x32x16_f16 v[16:31], a[60:63], v[188:191], v[16:31]
	ds_read_b128 v[188:191], v192 offset:39936
	s_add_u32 s44, s34, 0x18000
	s_addc_u32 s45, s35, 0
	s_mov_b32 m0, s58
	s_nop 0
	global_load_lds_dwordx4 v192, s[44:45] sc1
	v_rcp_f32_e32 v215, v215
	s_waitcnt lgkmcnt(4)
	v_mfma_f32_32x32x16_f16 v[0:15], a[64:67], v[160:163], v[0:15]
	ds_read_b128 v[160:163], v192 offset:40960
	v_exp_f32_e32 v200, v152
	v_mfma_f32_32x32x16_f16 v[16:31], a[64:67], v[164:167], v[16:31]
	ds_read_b128 v[164:167], v192 offset:41984
	v_exp_f32_e32 v201, v153
	v_add_f32_e32 v200, 1.0, v200
	v_mfma_f32_32x32x16_f16 v[0:15], a[68:71], v[168:171], v[0:15]
	ds_read_b128 v[168:171], v192 offset:43008
	v_exp_f32_e32 v202, v154
	v_add_f32_e32 v201, 1.0, v201
	v_mfma_f32_32x32x16_f16 v[16:31], a[68:71], v[172:175], v[16:31]
	ds_read_b128 v[172:175], v192 offset:44032
	global_load_lds_dwordx4 v192, s[44:45] offset:1024 sc1
	v_exp_f32_e32 v203, v155
	v_add_f32_e32 v202, 1.0, v202
	s_waitcnt lgkmcnt(4)
	v_mfma_f32_32x32x16_f16 v[0:15], a[72:75], v[176:179], v[0:15]
	ds_read_b128 v[176:179], v192 offset:45056
	v_add_f32_e32 v203, 1.0, v203
	v_rcp_f32_e32 v200, v200
	v_mfma_f32_32x32x16_f16 v[16:31], a[72:75], v[180:183], v[16:31]
	ds_read_b128 v[180:183], v192 offset:46080
	v_rcp_f32_e32 v201, v201
	v_fma_f32 v200, v200, 2.0, -1.0
	v_mfma_f32_32x32x16_f16 v[0:15], a[76:79], v[184:187], v[0:15]
	ds_read_b128 v[184:187], v192 offset:47104
	v_rcp_f32_e32 v202, v202
	v_fma_f32 v201, v201, 2.0, -1.0
	v_mul_f32_e32 v216, v212, v200
	v_mfma_f32_32x32x16_f16 v[16:31], a[76:79], v[188:191], v[16:31]
	ds_read_b128 v[188:191], v192 offset:48128
	global_load_lds_dwordx4 v192, s[44:45] offset:2048 sc1
	v_rcp_f32_e32 v203, v203
	v_fma_f32 v202, v202, 2.0, -1.0
	v_mul_f32_e32 v217, v213, v201
	s_waitcnt lgkmcnt(4)
	v_mfma_f32_32x32x16_f16 v[0:15], a[80:83], v[160:163], v[0:15]
	ds_read_b128 v[160:163], v192 offset:49152
	v_fma_f32 v203, v203, 2.0, -1.0
	v_mul_f32_e32 v218, v214, v202
	v_exp_f32_e32 v200, v112
	v_mfma_f32_32x32x16_f16 v[16:31], a[80:83], v[164:167], v[16:31]
	ds_read_b128 v[164:167], v192 offset:50176
	v_mul_f32_e32 v219, v215, v203
	v_cvt_pk_f16_f32 v220, v216, v217
	v_exp_f32_e32 v201, v113
	v_mfma_f32_32x32x16_f16 v[0:15], a[84:87], v[168:171], v[0:15]
	ds_read_b128 v[168:171], v192 offset:51200
	v_cvt_pk_f16_f32 v221, v218, v219
	v_exp_f32_e32 v202, v114
	v_add_f32_e32 v200, 1.0, v200
	v_mfma_f32_32x32x16_f16 v[16:31], a[84:87], v[172:175], v[16:31]
	ds_read_b128 v[172:175], v192 offset:52224
	global_load_lds_dwordx4 v192, s[44:45] offset:3072 sc1
	v_exp_f32_e32 v203, v115
	v_add_f32_e32 v201, 1.0, v201
	v_add_f32_e32 v202, 1.0, v202
	s_waitcnt lgkmcnt(4)
	v_mfma_f32_32x32x16_f16 v[0:15], a[88:91], v[176:179], v[0:15]
	ds_read_b128 v[176:179], v192 offset:53248
	v_exp_f32_e32 v204, v116
	v_add_f32_e32 v203, 1.0, v203
	v_mfma_f32_32x32x16_f16 v[16:31], a[88:91], v[180:183], v[16:31]
	ds_read_b128 v[180:183], v192 offset:54272
	v_exp_f32_e32 v205, v117
	v_add_f32_e32 v204, 1.0, v204
	v_mfma_f32_32x32x16_f16 v[0:15], a[92:95], v[184:187], v[0:15]
	ds_read_b128 v[184:187], v192 offset:55296
	v_exp_f32_e32 v206, v118
	v_add_f32_e32 v205, 1.0, v205
	v_mfma_f32_32x32x16_f16 v[16:31], a[92:95], v[188:191], v[16:31]
	ds_read_b128 v[188:191], v192 offset:56320
	s_add_u32 s44, s34, 0x19000
	s_addc_u32 s45, s35, 0
	s_mov_b32 m0, s59
	s_nop 0
	global_load_lds_dwordx4 v192, s[44:45] sc1
	v_exp_f32_e32 v207, v119
	v_add_f32_e32 v206, 1.0, v206
	s_waitcnt lgkmcnt(4)
	v_mfma_f32_32x32x16_f16 v[0:15], a[96:99], v[160:163], v[0:15]
	ds_read_b128 v[160:163], v192 offset:57344
	v_exp_f32_e32 v208, v120
	v_add_f32_e32 v207, 1.0, v207
	v_mfma_f32_32x32x16_f16 v[16:31], a[96:99], v[164:167], v[16:31]
	ds_read_b128 v[164:167], v192 offset:58368
	v_exp_f32_e32 v209, v121
	v_add_f32_e32 v208, 1.0, v208
	v_mfma_f32_32x32x16_f16 v[0:15], a[100:103], v[168:171], v[0:15]
	ds_read_b128 v[168:171], v192 offset:59392
	v_exp_f32_e32 v210, v122
	v_add_f32_e32 v209, 1.0, v209
	v_mfma_f32_32x32x16_f16 v[16:31], a[100:103], v[172:175], v[16:31]
	ds_read_b128 v[172:175], v192 offset:60416
	global_load_lds_dwordx4 v192, s[44:45] offset:1024 sc1
	v_exp_f32_e32 v211, v123
	v_add_f32_e32 v210, 1.0, v210
	s_waitcnt lgkmcnt(4)
	v_mfma_f32_32x32x16_f16 v[0:15], a[104:107], v[176:179], v[0:15]
	ds_read_b128 v[176:179], v192 offset:61440
	v_exp_f32_e32 v212, v124
	v_add_f32_e32 v211, 1.0, v211
	v_mfma_f32_32x32x16_f16 v[16:31], a[104:107], v[180:183], v[16:31]
	ds_read_b128 v[180:183], v192 offset:62464
	v_exp_f32_e32 v213, v125
	v_add_f32_e32 v212, 1.0, v212
	v_mfma_f32_32x32x16_f16 v[0:15], a[108:111], v[184:187], v[0:15]
	ds_read_b128 v[184:187], v192 offset:63488
	v_exp_f32_e32 v214, v126
	v_add_f32_e32 v213, 1.0, v213
	v_mfma_f32_32x32x16_f16 v[16:31], a[108:111], v[188:191], v[16:31]
	ds_read_b128 v[188:191], v192 offset:64512
	global_load_lds_dwordx4 v192, s[44:45] offset:2048 sc1
	v_exp_f32_e32 v215, v127
	v_add_f32_e32 v214, 1.0, v214
	s_waitcnt vmcnt(7)
	s_barrier
	s_waitcnt lgkmcnt(4)
	v_mfma_f32_32x32x16_f16 v[0:15], a[112:115], v[160:163], v[0:15]
	ds_read_b128 v[160:163], v193 offset:0
	v_add_f32_e32 v215, 1.0, v215
	v_rcp_f32_e32 v200, v200
	v_mfma_f32_32x32x16_f16 v[16:31], a[112:115], v[164:167], v[16:31]
	ds_read_b128 v[164:167], v193 offset:1024
	v_rcp_f32_e32 v201, v201
	v_mfma_f32_32x32x16_f16 v[0:15], a[116:119], v[168:171], v[0:15]
	ds_read_b128 v[168:171], v193 offset:2048
	v_rcp_f32_e32 v202, v202
	v_mfma_f32_32x32x16_f16 v[16:31], a[116:119], v[172:175], v[16:31]
	ds_read_b128 v[172:175], v193 offset:3072
	global_load_lds_dwordx4 v192, s[44:45] offset:3072 sc1
	v_rcp_f32_e32 v203, v203
	s_waitcnt lgkmcnt(4)
	v_mfma_f32_32x32x16_f16 v[0:15], a[120:123], v[176:179], v[0:15]
	ds_read_b128 v[176:179], v193 offset:4096
	v_rcp_f32_e32 v204, v204
	v_mfma_f32_32x32x16_f16 v[16:31], a[120:123], v[180:183], v[16:31]
	ds_read_b128 v[180:183], v193 offset:5120
	v_rcp_f32_e32 v205, v205
	v_mul_f32_e32 v204, v204, v156
	v_mfma_f32_32x32x2_f32 v[64:79], v248, v228, v[232:247]
	v_mfma_f32_32x32x16_f16 v[0:15], a[124:127], v[184:187], v[0:15]
	ds_read_b128 v[184:187], v193 offset:6144
	v_rcp_f32_e32 v206, v206
	v_mul_f32_e32 v205, v205, v157
	v_mfma_f32_32x32x2_f32 v[80:95], v248, v229, v[232:247]
	v_mfma_f32_32x32x16_f16 v[16:31], a[124:127], v[188:191], v[16:31]
	ds_read_b128 v[188:191], v193 offset:7168
	v_cmp_gt_u32_e32 vcc, 2, v251
	s_cbranch_vccnz .LE_tpoll21
.LE_tok20:
	s_and_b32 s64, s71, 1
	s_lshl_b32 s64, s64, 22
	s_add_u32 s64, s64, s49
	s_add_u32 s64, s64, 0x20000
	s_add_u32 s34, s6, s64
	s_addc_u32 s35, s7, 0
	s_add_u32 s44, s34, 0x0
	s_addc_u32 s45, s35, 0
	s_mov_b32 m0, s52
	s_nop 0
	global_load_lds_dwordx4 v192, s[44:45] sc1
	v_rcp_f32_e32 v207, v207
	v_mul_f32_e32 v206, v206, v158
	s_waitcnt lgkmcnt(4)
	v_mfma_f32_32x32x16_f16 v[0:15], a[128:131], v[160:163], v[0:15]
	ds_read_b128 v[160:163], v193 offset:8192
	v_rcp_f32_e32 v208, v208
	v_mul_f32_e32 v207, v207, v159
	v_mfma_f32_32x32x16_f16 v[16:31], a[128:131], v[164:167], v[16:31]
	ds_read_b128 v[164:167], v193 offset:9216
	v_rcp_f32_e32 v209, v209
	v_fmamk_f32 v208, v208, 0xc0b8aa3b, v198
	v_mfma_f32_32x32x16_f16 v[0:15], a[132:135], v[168:171], v[0:15]
	ds_read_b128 v[168:171], v193 offset:10240
	v_rcp_f32_e32 v210, v210
	v_fmamk_f32 v209, v209, 0xc0b8aa3b, v198
	v_fma_f32 v156, v200, v208, v204
	v_mfma_f32_32x32x16_f16 v[16:31], a[132:135], v[172:175], v[16:31]
	ds_read_b128 v[172:175], v193 offset:11264
	global_load_lds_dwordx4 v192, s[44:45] offset:1024 sc1
	v_rcp_f32_e32 v211, v211
	v_fmamk_f32 v210, v210, 0xc0b8aa3b, v198
	v_fma_f32 v157, v201, v209, v205
	s_waitcnt lgkmcnt(4)
	v_mfma_f32_32x32x16_f16 v[0:15], a[136:139], v[176:179], v[0:15]
	ds_read_b128 v[176:179], v193 offset:12288
	v_rcp_f32_e32 v212, v212
	v_fmamk_f32 v211, v211, 0xc0b8aa3b, v198
	v_fma_f32 v158, v202, v210, v206
	v_mfma_f32_32x32x16_f16 v[16:31], a[136:139], v[180:183], v[16:31]
	ds_read_b128 v[180:183], v193 offset:13312
	v_rcp_f32_e32 v213, v213
	v_fma_f32 v159, v203, v211, v207
	v_mfma_f32_32x32x16_f16 v[0:15], a[140:143], v[184:187], v[0:15]
	ds_read_b128 v[184:187], v193 offset:14336
	v_rcp_f32_e32 v214, v214
	v_mfma_f32_32x32x16_f16 v[16:31], a[140:143], v[188:191], v[16:31]
	ds_read_b128 v[188:191], v193 offset:15360
	global_load_lds_dwordx4 v192, s[44:45] offset:2048 sc1
	v_rcp_f32_e32 v215, v215
	s_waitcnt lgkmcnt(4)
	v_mfma_f32_32x32x16_f16 v[0:15], a[144:147], v[160:163], v[0:15]
	ds_read_b128 v[160:163], v193 offset:16384
	v_exp_f32_e32 v200, v156
	v_mfma_f32_32x32x16_f16 v[16:31], a[144:147], v[164:167], v[16:31]
	ds_read_b128 v[164:167], v193 offset:17408
	v_exp_f32_e32 v201, v157
	v_add_f32_e32 v200, 1.0, v200
	v_mfma_f32_32x32x16_f16 v[0:15], a[148:151], v[168:171], v[0:15]
	ds_read_b128 v[168:171], v193 offset:18432
	v_exp_f32_e32 v202, v158
	v_add_f32_e32 v201, 1.0, v201
	v_mfma_f32_32x32x16_f16 v[16:31], a[148:151], v[172:175], v[16:31]
	ds_read_b128 v[172:175], v193 offset:19456
	global_load_lds_dwordx4 v192, s[44:45] offset:3072 sc1
	v_exp_f32_e32 v203, v159
	v_add_f32_e32 v202, 1.0, v202
	s_waitcnt lgkmcnt(4)
	v_mfma_f32_32x32x16_f16 v[0:15], a[152:155], v[176:179], v[0:15]
	ds_read_b128 v[176:179], v193 offset:20480
	v_add_f32_e32 v203, 1.0, v203
	v_rcp_f32_e32 v200, v200
	v_mfma_f32_32x32x16_f16 v[16:31], a[152:155], v[180:183], v[16:31]
	ds_read_b128 v[180:183], v193 offset:21504
	v_rcp_f32_e32 v201, v201
	v_fma_f32 v200, v200, 2.0, -1.0
	v_mfma_f32_32x32x16_f16 v[0:15], a[156:159], v[184:187], v[0:15]
	ds_read_b128 v[184:187], v193 offset:22528
	v_rcp_f32_e32 v202, v202
	v_fma_f32 v201, v201, 2.0, -1.0
	v_mul_f32_e32 v216, v212, v200
	v_mfma_f32_32x32x16_f16 v[16:31], a[156:159], v[188:191], v[16:31]
	ds_read_b128 v[188:191], v193 offset:23552
	s_add_u32 s44, s34, 0x1000
	s_addc_u32 s45, s35, 0
	s_mov_b32 m0, s53
	s_nop 0
	global_load_lds_dwordx4 v192, s[44:45] sc1
	v_rcp_f32_e32 v203, v203
	v_fma_f32 v202, v202, 2.0, -1.0
	v_mul_f32_e32 v217, v213, v201
	s_waitcnt lgkmcnt(4)
	v_mfma_f32_32x32x16_f16 v[0:15], a[160:163], v[160:163], v[0:15]
	ds_read_b128 v[160:163], v193 offset:24576
	v_fma_f32 v203, v203, 2.0, -1.0
	v_mul_f32_e32 v218, v214, v202
	v_mfma_f32_32x32x16_f16 v[16:31], a[160:163], v[164:167], v[16:31]
	ds_read_b128 v[164:167], v193 offset:25600
	v_mul_f32_e32 v219, v215, v203
	v_cvt_pk_f16_f32 v222, v216, v217
	v_mfma_f32_32x32x16_f16 v[0:15], a[164:167], v[168:171], v[0:15]
	ds_read_b128 v[168:171], v193 offset:26624
	v_cvt_pk_f16_f32 v223, v218, v219
	v_mfma_f32_32x32x16_f16 v[16:31], a[164:167], v[172:175], v[16:31]
	ds_read_b128 v[172:175], v193 offset:27648
	global_load_lds_dwordx4 v192, s[44:45] offset:1024 sc1
	s_nop 1
	v_permlane32_swap_b32_e32 v220, v222
	v_permlane32_swap_b32_e32 v221, v223
	s_cmp_eq_u32 s31, 0
	s_cbranch_scc1 .LE_slow22
	global_store_dwordx4 v195, v[220:223], s[36:37] offset:0
.LE_join23:
	s_waitcnt lgkmcnt(4)
	v_mfma_f32_32x32x16_f16 v[0:15], a[168:171], v[176:179], v[0:15]
	ds_read_b128 v[176:179], v193 offset:28672
	v_mfma_f32_32x32x16_f16 v[16:31], a[168:171], v[180:183], v[16:31]
	ds_read_b128 v[180:183], v193 offset:29696
	v_mfma_f32_32x32x16_f16 v[0:15], a[172:175], v[184:187], v[0:15]
	ds_read_b128 v[184:187], v193 offset:30720
	v_mfma_f32_32x32x16_f16 v[16:31], a[172:175], v[188:191], v[16:31]
	ds_read_b128 v[188:191], v193 offset:31744
	global_load_lds_dwordx4 v192, s[44:45] offset:2048 sc1
	s_waitcnt vmcnt(8)
	s_barrier
	s_waitcnt lgkmcnt(4)
	v_mfma_f32_32x32x16_f16 v[0:15], a[176:179], v[160:163], v[0:15]
	ds_read_b128 v[160:163], v193 offset:32768
	v_mfma_f32_32x32x16_f16 v[16:31], a[176:179], v[164:167], v[16:31]
	ds_read_b128 v[164:167], v193 offset:33792
	v_mfma_f32_32x32x16_f16 v[0:15], a[180:183], v[168:171], v[0:15]
	ds_read_b128 v[168:171], v193 offset:34816
	v_mfma_f32_32x32x16_f16 v[16:31], a[180:183], v[172:175], v[16:31]
	ds_read_b128 v[172:175], v193 offset:35840
	global_load_lds_dwordx4 v192, s[44:45] offset:3072 sc1
	s_waitcnt lgkmcnt(4)
	v_mfma_f32_32x32x16_f16 v[0:15], a[184:187], v[176:179], v[0:15]
	ds_read_b128 v[176:179], v193 offset:36864
	v_mfma_f32_32x32x16_f16 v[16:31], a[184:187], v[180:183], v[16:31]
	ds_read_b128 v[180:183], v193 offset:37888
	v_mfma_f32_32x32x16_f16 v[0:15], a[188:191], v[184:187], v[0:15]
	ds_read_b128 v[184:187], v193 offset:38912
	v_mfma_f32_32x32x16_f16 v[16:31], a[188:191], v[188:191], v[16:31]
	ds_read_b128 v[188:191], v193 offset:39936
	s_add_u32 s44, s34, 0x8000
	s_addc_u32 s45, s35, 0
	s_mov_b32 m0, s54
	s_nop 0
	global_load_lds_dwordx4 v192, s[44:45] sc1
	s_waitcnt lgkmcnt(4)
	v_mfma_f32_32x32x16_f16 v[0:15], a[192:195], v[160:163], v[0:15]
	ds_read_b128 v[160:163], v193 offset:40960
	s_waitcnt vmcnt(3)
	s_barrier
	v_mov_b32_e32 v199, 4
	s_cmp_eq_u32 s31, 0
	s_cbranch_scc1 .LE_slow24
	global_store_dword v197, v199, s[40:41]
.LE_join25:
	v_mfma_f32_32x32x16_f16 v[16:31], a[192:195], v[164:167], v[16:31]
	ds_read_b128 v[164:167], v193 offset:41984
	v_mfma_f32_32x32x16_f16 v[0:15], a[196:199], v[168:171], v[0:15]
	ds_read_b128 v[168:171], v193 offset:43008
	v_mfma_f32_32x32x16_f16 v[16:31], a[196:199], v[172:175], v[16:31]
	ds_read_b128 v[172:175], v193 offset:44032
	global_load_lds_dwordx4 v192, s[44:45] offset:1024 sc1
	s_waitcnt lgkmcnt(4)
	v_mfma_f32_32x32x16_f16 v[0:15], a[200:203], v[176:179], v[0:15]
	ds_read_b128 v[176:179], v193 offset:45056
	s_and_b32 s64, s33, 1
	s_lshl_b32 s64, s64, 22
	s_add_u32 s64, s64, s50
	s_add_u32 s36, s6, s64
	s_addc_u32 s37, s7, 0
	s_lshl_b32 s64, s33, 3
	s_add_u32 s64, s64, s29
	s_lshl_b32 s64, s64, 5
	s_add_u32 s64, s64, s30
	s_lshl_b32 s64, s64, 2
	s_add_u32 s40, s8, s64
	s_addc_u32 s41, s9, 0
	s_lshl_b32 s64, s33, 11
	s_lshl_b32 s65, s29, 8
	s_add_u32 s64, s64, s65
	s_add_u32 s64, s64, 192
	s_lshl_b32 s64, s64, 3
	s_add_u32 s42, s12, s64
	s_addc_u32 s43, s13, 0
	v_mfma_f32_32x32x16_f16 v[16:31], a[200:203], v[180:183], v[16:31]
	ds_read_b128 v[180:183], v193 offset:46080
	v_mfma_f32_32x32x16_f16 v[0:15], a[204:207], v[184:187], v[0:15]
	ds_read_b128 v[184:187], v193 offset:47104
	v_mfma_f32_32x32x16_f16 v[16:31], a[204:207], v[188:191], v[16:31]
	ds_read_b128 v[188:191], v193 offset:48128
	global_load_lds_dwordx4 v192, s[44:45] offset:2048 sc1
	s_waitcnt lgkmcnt(4)
	v_mfma_f32_32x32x16_f16 v[0:15], a[208:211], v[160:163], v[0:15]
	ds_read_b128 v[160:163], v193 offset:49152
	v_mfma_f32_32x32x16_f16 v[16:31], a[208:211], v[164:167], v[16:31]
	ds_read_b128 v[164:167], v193 offset:50176
	v_mfma_f32_32x32x16_f16 v[0:15], a[212:215], v[168:171], v[0:15]
	ds_read_b128 v[168:171], v193 offset:51200
	v_mfma_f32_32x32x16_f16 v[16:31], a[212:215], v[172:175], v[16:31]
	ds_read_b128 v[172:175], v193 offset:52224
	global_load_lds_dwordx4 v192, s[44:45] offset:3072 sc1
	s_waitcnt lgkmcnt(4)
	v_mfma_f32_32x32x16_f16 v[0:15], a[216:219], v[176:179], v[0:15]
	ds_read_b128 v[176:179], v193 offset:53248
	v_mfma_f32_32x32x16_f16 v[16:31], a[216:219], v[180:183], v[16:31]
	ds_read_b128 v[180:183], v193 offset:54272
	v_mfma_f32_32x32x16_f16 v[0:15], a[220:223], v[184:187], v[0:15]
	ds_read_b128 v[184:187], v193 offset:55296
	v_mfma_f32_32x32x16_f16 v[16:31], a[220:223], v[188:191], v[16:31]
	ds_read_b128 v[188:191], v193 offset:56320
	s_add_u32 s44, s34, 0x9000
	s_addc_u32 s45, s35, 0
	s_mov_b32 m0, s55
	s_nop 0
	global_load_lds_dwordx4 v192, s[44:45] sc1
	s_waitcnt lgkmcnt(4)
	v_mfma_f32_32x32x16_f16 v[0:15], a[224:227], v[160:163], v[0:15]
	ds_read_b128 v[160:163], v193 offset:57344
	v_mfma_f32_32x32x16_f16 v[16:31], a[224:227], v[164:167], v[16:31]
	ds_read_b128 v[164:167], v193 offset:58368
	v_mfma_f32_32x32x16_f16 v[0:15], a[228:231], v[168:171], v[0:15]
	ds_read_b128 v[168:171], v193 offset:59392
	v_mfma_f32_32x32x16_f16 v[16:31], a[228:231], v[172:175], v[16:31]
	ds_read_b128 v[172:175], v193 offset:60416
	global_load_lds_dwordx4 v192, s[44:45] offset:1024 sc1
	s_waitcnt lgkmcnt(4)
	v_mfma_f32_32x32x16_f16 v[0:15], a[232:235], v[176:179], v[0:15]
	ds_read_b128 v[176:179], v193 offset:61440
	v_mfma_f32_32x32x16_f16 v[16:31], a[232:235], v[180:183], v[16:31]
	ds_read_b128 v[180:183], v193 offset:62464
	v_mfma_f32_32x32x16_f16 v[0:15], a[236:239], v[184:187], v[0:15]
	ds_read_b128 v[184:187], v193 offset:63488
	v_mfma_f32_32x32x16_f16 v[16:31], a[236:239], v[188:191], v[16:31]
	ds_read_b128 v[188:191], v193 offset:64512
	global_load_lds_dwordx4 v192, s[44:45] offset:2048 sc1
	s_waitcnt vmcnt(8)
	s_barrier
	s_waitcnt lgkmcnt(4)
	v_mfma_f32_32x32x16_f16 v[0:15], a[240:243], v[160:163], v[0:15]
	ds_read_b128 v[160:163], v192 offset:0
	v_mfma_f32_32x32x16_f16 v[16:31], a[240:243], v[164:167], v[16:31]
	ds_read_b128 v[164:167], v192 offset:1024
	v_mfma_f32_32x32x16_f16 v[0:15], a[244:247], v[168:171], v[0:15]
	ds_read_b128 v[168:171], v192 offset:2048
	v_mfma_f32_32x32x16_f16 v[16:31], a[244:247], v[172:175], v[16:31]
	ds_read_b128 v[172:175], v192 offset:3072
	global_load_lds_dwordx4 v192, s[44:45] offset:3072 sc1
	s_waitcnt lgkmcnt(4)
	v_mfma_f32_32x32x16_f16 v[0:15], a[248:251], v[176:179], v[0:15]
	ds_read_b128 v[176:179], v192 offset:4096
	v_mfma_f32_32x32x16_f16 v[16:31], a[248:251], v[180:183], v[16:31]
	ds_read_b128 v[180:183], v192 offset:5120
	v_mfma_f32_32x32x16_f16 v[0:15], a[252:255], v[184:187], v[0:15]
	ds_read_b128 v[184:187], v192 offset:6144
	v_mfma_f32_32x32x16_f16 v[16:31], a[252:255], v[188:191], v[16:31]
	ds_read_b128 v[188:191], v192 offset:7168
	s_add_u32 s44, s34, 0x10000
	s_addc_u32 s45, s35, 0
	s_mov_b32 m0, s56
	s_nop 0
	global_load_lds_dwordx4 v192, s[44:45] sc1
	s_nop 3
	global_load_dword v228, v249, s[42:43] offset:0
	global_load_dword v229, v249, s[42:43] offset:256
	s_waitcnt lgkmcnt(4)
	v_mfma_f32_32x32x16_f16 v[32:47], a[0:3], v[160:163], v[32:47]
	ds_read_b128 v[160:163], v192 offset:8192
	v_exp_f32_e32 v200, v0
	v_mfma_f32_32x32x16_f16 v[48:63], a[0:3], v[164:167], v[48:63]
	ds_read_b128 v[164:167], v192 offset:9216
	s_lshl_b32 s64, s71, 3
	s_add_u32 s64, s64, s29
	s_lshl_b32 s64, s64, 7
	s_add_u32 s38, s8, s64
	s_addc_u32 s39, s9, 0
	global_load_dword v251, v196, s[38:39] sc1
	v_exp_f32_e32 v201, v1
	v_add_f32_e32 v200, 1.0, v200
	v_mfma_f32_32x32x16_f16 v[32:47], a[4:7], v[168:171], v[32:47]
	ds_read_b128 v[168:171], v192 offset:10240
	v_exp_f32_e32 v202, v2
	v_add_f32_e32 v201, 1.0, v201
	v_mfma_f32_32x32x16_f16 v[48:63], a[4:7], v[172:175], v[48:63]
	ds_read_b128 v[172:175], v192 offset:11264
	global_load_lds_dwordx4 v192, s[44:45] offset:1024 sc1
	v_exp_f32_e32 v203, v3
	v_add_f32_e32 v202, 1.0, v202
	s_waitcnt lgkmcnt(4)
	v_mfma_f32_32x32x16_f16 v[32:47], a[8:11], v[176:179], v[32:47]
	ds_read_b128 v[176:179], v192 offset:12288
	v_exp_f32_e32 v204, v4
	v_add_f32_e32 v203, 1.0, v203
	v_mfma_f32_32x32x16_f16 v[48:63], a[8:11], v[180:183], v[48:63]
	ds_read_b128 v[180:183], v192 offset:13312
	v_exp_f32_e32 v205, v5
	v_add_f32_e32 v204, 1.0, v204
	v_mfma_f32_32x32x16_f16 v[32:47], a[12:15], v[184:187], v[32:47]
	ds_read_b128 v[184:187], v192 offset:14336
	v_exp_f32_e32 v206, v6
	v_add_f32_e32 v205, 1.0, v205
	v_mfma_f32_32x32x16_f16 v[48:63], a[12:15], v[188:191], v[48:63]
	ds_read_b128 v[188:191], v192 offset:15360
	global_load_lds_dwordx4 v192, s[44:45] offset:2048 sc1
	v_exp_f32_e32 v207, v7
	v_add_f32_e32 v206, 1.0, v206
	s_waitcnt lgkmcnt(4)
	v_mfma_f32_32x32x16_f16 v[32:47], a[16:19], v[160:163], v[32:47]
	ds_read_b128 v[160:163], v192 offset:16384
	v_exp_f32_e32 v208, v8
	v_add_f32_e32 v207, 1.0, v207
	v_mfma_f32_32x32x16_f16 v[48:63], a[16:19], v[164:167], v[48:63]
	ds_read_b128 v[164:167], v192 offset:17408
	v_exp_f32_e32 v209, v9
	v_add_f32_e32 v208, 1.0, v208
	v_mfma_f32_32x32x16_f16 v[32:47], a[20:23], v[168:171], v[32:47]
	ds_read_b128 v[168:171], v192 offset:18432
	v_exp_f32_e32 v210, v10
	v_add_f32_e32 v209, 1.0, v209
	v_mfma_f32_32x32x16_f16 v[48:63], a[20:23], v[172:175], v[48:63]
	ds_read_b128 v[172:175], v192 offset:19456
	global_load_lds_dwordx4 v192, s[44:45] offset:3072 sc1
	v_exp_f32_e32 v211, v11
	v_add_f32_e32 v210, 1.0, v210
	s_waitcnt lgkmcnt(4)
	v_mfma_f32_32x32x16_f16 v[32:47], a[24:27], v[176:179], v[32:47]
	ds_read_b128 v[176:179], v192 offset:20480
	v_exp_f32_e32 v212, v12
	v_add_f32_e32 v211, 1.0, v211
	v_mfma_f32_32x32x16_f16 v[48:63], a[24:27], v[180:183], v[48:63]
	ds_read_b128 v[180:183], v192 offset:21504
	v_exp_f32_e32 v213, v13
	v_add_f32_e32 v212, 1.0, v212
	v_mfma_f32_32x32x16_f16 v[32:47], a[28:31], v[184:187], v[32:47]
	ds_read_b128 v[184:187], v192 offset:22528
	v_exp_f32_e32 v214, v14
	v_add_f32_e32 v213, 1.0, v213
	v_mfma_f32_32x32x16_f16 v[48:63], a[28:31], v[188:191], v[48:63]
	ds_read_b128 v[188:191], v192 offset:23552
	s_add_u32 s44, s34, 0x11000
	s_addc_u32 s45, s35, 0
	s_mov_b32 m0, s57
	s_nop 0
	global_load_lds_dwordx4 v192, s[44:45] sc1
	v_exp_f32_e32 v215, v15
	v_add_f32_e32 v214, 1.0, v214
	s_waitcnt lgkmcnt(4)
	v_mfma_f32_32x32x16_f16 v[32:47], a[32:35], v[160:163], v[32:47]
	ds_read_b128 v[160:163], v192 offset:24576
	v_add_f32_e32 v215, 1.0, v215
	v_rcp_f32_e32 v200, v200
	v_mfma_f32_32x32x16_f16 v[48:63], a[32:35], v[164:167], v[48:63]
	ds_read_b128 v[164:167], v192 offset:25600
	v_rcp_f32_e32 v201, v201
	v_mfma_f32_32x32x16_f16 v[32:47], a[36:39], v[168:171], v[32:47]
	ds_read_b128 v[168:171], v192 offset:26624
	v_rcp_f32_e32 v202, v202
	v_mfma_f32_32x32x16_f16 v[48:63], a[36:39], v[172:175], v[48:63]
	ds_read_b128 v[172:175], v192 offset:27648
	global_load_lds_dwordx4 v192, s[44:45] offset:1024 sc1
	v_rcp_f32_e32 v203, v203
	s_waitcnt lgkmcnt(4)
	v_mfma_f32_32x32x16_f16 v[32:47], a[40:43], v[176:179], v[32:47]
	ds_read_b128 v[176:179], v192 offset:28672
	v_rcp_f32_e32 v204, v204
	v_mfma_f32_32x32x16_f16 v[48:63], a[40:43], v[180:183], v[48:63]
	ds_read_b128 v[180:183], v192 offset:29696
	v_rcp_f32_e32 v205, v205
	v_mul_f32_e32 v204, v204, v128
	v_mfma_f32_32x32x16_f16 v[32:47], a[44:47], v[184:187], v[32:47]
	ds_read_b128 v[184:187], v192 offset:30720
	v_rcp_f32_e32 v206, v206
	v_mul_f32_e32 v205, v205, v129
	v_mfma_f32_32x32x16_f16 v[48:63], a[44:47], v[188:191], v[48:63]
	ds_read_b128 v[188:191], v192 offset:31744
	global_load_lds_dwordx4 v192, s[44:45] offset:2048 sc1
	v_rcp_f32_e32 v207, v207
	v_mul_f32_e32 v206, v206, v130
	s_waitcnt vmcnt(10)
	s_barrier
	s_waitcnt lgkmcnt(4)
	v_mfma_f32_32x32x16_f16 v[32:47], a[48:51], v[160:163], v[32:47]
	ds_read_b128 v[160:163], v192 offset:32768
	v_rcp_f32_e32 v208, v208
	v_mul_f32_e32 v207, v207, v131
	v_mfma_f32_32x32x16_f16 v[48:63], a[48:51], v[164:167], v[48:63]
	ds_read_b128 v[164:167], v192 offset:33792
	v_rcp_f32_e32 v209, v209
	v_fmamk_f32 v208, v208, 0xc0b8aa3b, v198
	v_mfma_f32_32x32x16_f16 v[32:47], a[52:55], v[168:171], v[32:47]
	ds_read_b128 v[168:171], v192 offset:34816
	v_rcp_f32_e32 v210, v210
	v_fmamk_f32 v209, v209, 0xc0b8aa3b, v198
	v_fma_f32 v128, v200, v208, v204
	v_mfma_f32_32x32x16_f16 v[48:63], a[52:55], v[172:175], v[48:63]
	ds_read_b128 v[172:175], v192 offset:35840
	global_load_lds_dwordx4 v192, s[44:45] offset:3072 sc1
	v_rcp_f32_e32 v211, v211
	v_fmamk_f32 v210, v210, 0xc0b8aa3b, v198
	v_fma_f32 v129, v201, v209, v205
	s_waitcnt lgkmcnt(4)
	v_mfma_f32_32x32x16_f16 v[32:47], a[56:59], v[176:179], v[32:47]
	ds_read_b128 v[176:179], v192 offset:36864
	v_rcp_f32_e32 v212, v212
	v_fmamk_f32 v211, v211, 0xc0b8aa3b, v198
	v_fma_f32 v130, v202, v210, v206
	v_mfma_f32_32x32x16_f16 v[48:63], a[56:59], v[180:183], v[48:63]
	ds_read_b128 v[180:183], v192 offset:37888
	v_rcp_f32_e32 v213, v213
	v_fma_f32 v131, v203, v211, v207
	v_mfma_f32_32x32x16_f16 v[32:47], a[60:63], v[184:187], v[32:47]
	ds_read_b128 v[184:187], v192 offset:38912
	v_rcp_f32_e32 v214, v214
	v_mfma_f32_32x32x16_f16 v[48:63], a[60:63], v[188:191], v[48:63]
	ds_read_b128 v[188:191], v192 offset:39936
	s_add_u32 s44, s34, 0x18000
	s_addc_u32 s45, s35, 0
	s_mov_b32 m0, s58
	s_nop 0
	global_load_lds_dwordx4 v192, s[44:45] sc1
	v_rcp_f32_e32 v215, v215
	s_waitcnt lgkmcnt(4)
	v_mfma_f32_32x32x16_f16 v[32:47], a[64:67], v[160:163], v[32:47]
	ds_read_b128 v[160:163], v192 offset:40960
	v_exp_f32_e32 v200, v128
	v_mfma_f32_32x32x16_f16 v[48:63], a[64:67], v[164:167], v[48:63]
	ds_read_b128 v[164:167], v192 offset:41984
	v_exp_f32_e32 v201, v129
	v_add_f32_e32 v200, 1.0, v200
	v_mfma_f32_32x32x16_f16 v[32:47], a[68:71], v[168:171], v[32:47]
	ds_read_b128 v[168:171], v192 offset:43008
	v_exp_f32_e32 v202, v130
	v_add_f32_e32 v201, 1.0, v201
	v_mfma_f32_32x32x16_f16 v[48:63], a[68:71], v[172:175], v[48:63]
	ds_read_b128 v[172:175], v192 offset:44032
	global_load_lds_dwordx4 v192, s[44:45] offset:1024 sc1
	v_exp_f32_e32 v203, v131
	v_add_f32_e32 v202, 1.0, v202
	s_waitcnt lgkmcnt(4)
	v_mfma_f32_32x32x16_f16 v[32:47], a[72:75], v[176:179], v[32:47]
	ds_read_b128 v[176:179], v192 offset:45056
	v_add_f32_e32 v203, 1.0, v203
	v_rcp_f32_e32 v200, v200
	v_mfma_f32_32x32x16_f16 v[48:63], a[72:75], v[180:183], v[48:63]
	ds_read_b128 v[180:183], v192 offset:46080
	v_rcp_f32_e32 v201, v201
	v_fma_f32 v200, v200, 2.0, -1.0
	v_mfma_f32_32x32x16_f16 v[32:47], a[76:79], v[184:187], v[32:47]
	ds_read_b128 v[184:187], v192 offset:47104
	v_rcp_f32_e32 v202, v202
	v_fma_f32 v201, v201, 2.0, -1.0
	v_mul_f32_e32 v216, v212, v200
	v_mfma_f32_32x32x16_f16 v[48:63], a[76:79], v[188:191], v[48:63]
	ds_read_b128 v[188:191], v192 offset:48128
	global_load_lds_dwordx4 v192, s[44:45] offset:2048 sc1
	v_rcp_f32_e32 v203, v203
	v_fma_f32 v202, v202, 2.0, -1.0
	v_mul_f32_e32 v217, v213, v201
	s_waitcnt lgkmcnt(4)
	v_mfma_f32_32x32x16_f16 v[32:47], a[80:83], v[160:163], v[32:47]
	ds_read_b128 v[160:163], v192 offset:49152
	v_fma_f32 v203, v203, 2.0, -1.0
	v_mul_f32_e32 v218, v214, v202
	v_exp_f32_e32 v200, v16
	v_mfma_f32_32x32x16_f16 v[48:63], a[80:83], v[164:167], v[48:63]
	ds_read_b128 v[164:167], v192 offset:50176
	v_mul_f32_e32 v219, v215, v203
	v_cvt_pk_f16_f32 v220, v216, v217
	v_exp_f32_e32 v201, v17
	v_mfma_f32_32x32x16_f16 v[32:47], a[84:87], v[168:171], v[32:47]
	ds_read_b128 v[168:171], v192 offset:51200
	v_cvt_pk_f16_f32 v221, v218, v219
	v_exp_f32_e32 v202, v18
	v_add_f32_e32 v200, 1.0, v200
	v_mfma_f32_32x32x16_f16 v[48:63], a[84:87], v[172:175], v[48:63]
	ds_read_b128 v[172:175], v192 offset:52224
	global_load_lds_dwordx4 v192, s[44:45] offset:3072 sc1
	s_cmp_eq_u32 s33, s60
	s_cbranch_scc1 .LE_ht26
.LE_htb27:
	v_exp_f32_e32 v203, v19
	s_waitcnt lgkmcnt(4)
	v_mfma_f32_32x32x16_f16 v[32:47], a[88:91], v[176:179], v[32:47]
	ds_read_b128 v[176:179], v192 offset:53248
	v_exp_f32_e32 v204, v20
	v_add_f32_e32 v201, 1.0, v201
	v_add_f32_e32 v202, 1.0, v202
	v_mfma_f32_32x32x16_f16 v[48:63], a[88:91], v[180:183], v[48:63]
	ds_read_b128 v[180:183], v192 offset:54272
	v_exp_f32_e32 v205, v21
	v_add_f32_e32 v203, 1.0, v203
	v_add_f32_e32 v204, 1.0, v204
	v_mfma_f32_32x32x16_f16 v[32:47], a[92:95], v[184:187], v[32:47]
	ds_read_b128 v[184:187], v192 offset:55296
	v_exp_f32_e32 v206, v22
	v_add_f32_e32 v205, 1.0, v205
	v_mfma_f32_32x32x16_f16 v[48:63], a[92:95], v[188:191], v[48:63]
	ds_read_b128 v[188:191], v192 offset:56320
	s_add_u32 s44, s34, 0x19000
	s_addc_u32 s45, s35, 0
	s_mov_b32 m0, s59
	s_nop 0
	global_load_lds_dwordx4 v192, s[44:45] sc1
	v_exp_f32_e32 v207, v23
	v_add_f32_e32 v206, 1.0, v206
	s_waitcnt lgkmcnt(4)
	v_mfma_f32_32x32x16_f16 v[32:47], a[96:99], v[160:163], v[32:47]
	ds_read_b128 v[160:163], v192 offset:57344
	v_exp_f32_e32 v208, v24
	v_add_f32_e32 v207, 1.0, v207
	v_mfma_f32_32x32x16_f16 v[48:63], a[96:99], v[164:167], v[48:63]
	ds_read_b128 v[164:167], v192 offset:58368
	v_exp_f32_e32 v209, v25
	v_add_f32_e32 v208, 1.0, v208
	v_mfma_f32_32x32x16_f16 v[32:47], a[100:103], v[168:171], v[32:47]
	ds_read_b128 v[168:171], v192 offset:59392
	v_exp_f32_e32 v210, v26
	v_add_f32_e32 v209, 1.0, v209
	v_mfma_f32_32x32x16_f16 v[48:63], a[100:103], v[172:175], v[48:63]
	ds_read_b128 v[172:175], v192 offset:60416
	global_load_lds_dwordx4 v192, s[44:45] offset:1024 sc1
	v_exp_f32_e32 v211, v27
	v_add_f32_e32 v210, 1.0, v210
	s_waitcnt lgkmcnt(4)
	v_mfma_f32_32x32x16_f16 v[32:47], a[104:107], v[176:179], v[32:47]
	ds_read_b128 v[176:179], v192 offset:61440
	v_exp_f32_e32 v212, v28
	v_add_f32_e32 v211, 1.0, v211
	v_mfma_f32_32x32x16_f16 v[48:63], a[104:107], v[180:183], v[48:63]
	ds_read_b128 v[180:183], v192 offset:62464
	v_exp_f32_e32 v213, v29
	v_add_f32_e32 v212, 1.0, v212
	v_mfma_f32_32x32x16_f16 v[32:47], a[108:111], v[184:187], v[32:47]
	ds_read_b128 v[184:187], v192 offset:63488
	v_exp_f32_e32 v214, v30
	v_add_f32_e32 v213, 1.0, v213
	v_mfma_f32_32x32x16_f16 v[48:63], a[108:111], v[188:191], v[48:63]
	ds_read_b128 v[188:191], v192 offset:64512
	global_load_lds_dwordx4 v192, s[44:45] offset:2048 sc1
	v_exp_f32_e32 v215, v31
	v_add_f32_e32 v214, 1.0, v214
	s_waitcnt vmcnt(7)
	s_barrier
	s_waitcnt lgkmcnt(4)
	v_mfma_f32_32x32x16_f16 v[32:47], a[112:115], v[160:163], v[32:47]
	ds_read_b128 v[160:163], v193 offset:0
	v_add_f32_e32 v215, 1.0, v215
	v_rcp_f32_e32 v200, v200
	v_mfma_f32_32x32x16_f16 v[48:63], a[112:115], v[164:167], v[48:63]
	ds_read_b128 v[164:167], v193 offset:1024
	v_rcp_f32_e32 v201, v201
	v_mfma_f32_32x32x16_f16 v[32:47], a[116:119], v[168:171], v[32:47]
	ds_read_b128 v[168:171], v193 offset:2048
	v_rcp_f32_e32 v202, v202
	v_mfma_f32_32x32x16_f16 v[48:63], a[116:119], v[172:175], v[48:63]
	ds_read_b128 v[172:175], v193 offset:3072
	global_load_lds_dwordx4 v192, s[44:45] offset:3072 sc1
	v_rcp_f32_e32 v203, v203
	s_waitcnt lgkmcnt(4)
	v_mfma_f32_32x32x16_f16 v[32:47], a[120:123], v[176:179], v[32:47]
	ds_read_b128 v[176:179], v193 offset:4096
	v_rcp_f32_e32 v204, v204
	v_mfma_f32_32x32x16_f16 v[48:63], a[120:123], v[180:183], v[48:63]
	ds_read_b128 v[180:183], v193 offset:5120
	v_rcp_f32_e32 v205, v205
	v_mul_f32_e32 v204, v204, v132
	v_mfma_f32_32x32x2_f32 v[96:111], v248, v228, v[232:247]
	v_mfma_f32_32x32x16_f16 v[32:47], a[124:127], v[184:187], v[32:47]
	ds_read_b128 v[184:187], v193 offset:6144
	v_rcp_f32_e32 v206, v206
	v_mul_f32_e32 v205, v205, v133
	v_mfma_f32_32x32x2_f32 v[112:127], v248, v229, v[232:247]
	v_mfma_f32_32x32x16_f16 v[48:63], a[124:127], v[188:191], v[48:63]
	ds_read_b128 v[188:191], v193 offset:7168
	v_cmp_gt_u32_e32 vcc, 3, v251
	s_cbranch_vccnz .LE_tpoll29
.LE_tok28:
	s_and_b32 s64, s71, 1
	s_lshl_b32 s64, s64, 22
	s_add_u32 s64, s64, s49
	s_add_u32 s64, s64, 0x40000
	s_add_u32 s34, s6, s64
	s_addc_u32 s35, s7, 0
	s_add_u32 s44, s34, 0x0
	s_addc_u32 s45, s35, 0
	s_mov_b32 m0, s52
	s_nop 0
	global_load_lds_dwordx4 v192, s[44:45] sc1
	v_rcp_f32_e32 v207, v207
	v_mul_f32_e32 v206, v206, v134
	s_waitcnt lgkmcnt(4)
	v_mfma_f32_32x32x16_f16 v[32:47], a[128:131], v[160:163], v[32:47]
	ds_read_b128 v[160:163], v193 offset:8192
	v_rcp_f32_e32 v208, v208
	v_mul_f32_e32 v207, v207, v135
	v_mfma_f32_32x32x16_f16 v[48:63], a[128:131], v[164:167], v[48:63]
	ds_read_b128 v[164:167], v193 offset:9216
	v_rcp_f32_e32 v209, v209
	v_fmamk_f32 v208, v208, 0xc0b8aa3b, v198
	v_mfma_f32_32x32x16_f16 v[32:47], a[132:135], v[168:171], v[32:47]
	ds_read_b128 v[168:171], v193 offset:10240
	v_rcp_f32_e32 v210, v210
	v_fmamk_f32 v209, v209, 0xc0b8aa3b, v198
	v_fma_f32 v132, v200, v208, v204
	v_mfma_f32_32x32x16_f16 v[48:63], a[132:135], v[172:175], v[48:63]
	ds_read_b128 v[172:175], v193 offset:11264
	global_load_lds_dwordx4 v192, s[44:45] offset:1024 sc1
	v_rcp_f32_e32 v211, v211
	v_fmamk_f32 v210, v210, 0xc0b8aa3b, v198
	v_fma_f32 v133, v201, v209, v205
	s_waitcnt lgkmcnt(4)
	v_mfma_f32_32x32x16_f16 v[32:47], a[136:139], v[176:179], v[32:47]
	ds_read_b128 v[176:179], v193 offset:12288
	v_rcp_f32_e32 v212, v212
	v_fmamk_f32 v211, v211, 0xc0b8aa3b, v198
	v_fma_f32 v134, v202, v210, v206
	v_mfma_f32_32x32x16_f16 v[48:63], a[136:139], v[180:183], v[48:63]
	ds_read_b128 v[180:183], v193 offset:13312
	v_rcp_f32_e32 v213, v213
	v_fma_f32 v135, v203, v211, v207
	v_mfma_f32_32x32x16_f16 v[32:47], a[140:143], v[184:187], v[32:47]
	ds_read_b128 v[184:187], v193 offset:14336
	v_rcp_f32_e32 v214, v214
	v_mfma_f32_32x32x16_f16 v[48:63], a[140:143], v[188:191], v[48:63]
	ds_read_b128 v[188:191], v193 offset:15360
	global_load_lds_dwordx4 v192, s[44:45] offset:2048 sc1
	v_rcp_f32_e32 v215, v215
	s_waitcnt lgkmcnt(4)
	v_mfma_f32_32x32x16_f16 v[32:47], a[144:147], v[160:163], v[32:47]
	ds_read_b128 v[160:163], v193 offset:16384
	v_exp_f32_e32 v200, v132
	v_mfma_f32_32x32x16_f16 v[48:63], a[144:147], v[164:167], v[48:63]
	ds_read_b128 v[164:167], v193 offset:17408
	v_exp_f32_e32 v201, v133
	v_add_f32_e32 v200, 1.0, v200
	v_mfma_f32_32x32x16_f16 v[32:47], a[148:151], v[168:171], v[32:47]
	ds_read_b128 v[168:171], v193 offset:18432
	v_exp_f32_e32 v202, v134
	v_add_f32_e32 v201, 1.0, v201
	v_mfma_f32_32x32x16_f16 v[48:63], a[148:151], v[172:175], v[48:63]
	ds_read_b128 v[172:175], v193 offset:19456
	global_load_lds_dwordx4 v192, s[44:45] offset:3072 sc1
	v_exp_f32_e32 v203, v135
	v_add_f32_e32 v202, 1.0, v202
	s_waitcnt lgkmcnt(4)
	v_mfma_f32_32x32x16_f16 v[32:47], a[152:155], v[176:179], v[32:47]
	ds_read_b128 v[176:179], v193 offset:20480
	v_add_f32_e32 v203, 1.0, v203
	v_rcp_f32_e32 v200, v200
	v_mfma_f32_32x32x16_f16 v[48:63], a[152:155], v[180:183], v[48:63]
	ds_read_b128 v[180:183], v193 offset:21504
	v_rcp_f32_e32 v201, v201
	v_fma_f32 v200, v200, 2.0, -1.0
	v_mfma_f32_32x32x16_f16 v[32:47], a[156:159], v[184:187], v[32:47]
	ds_read_b128 v[184:187], v193 offset:22528
	v_rcp_f32_e32 v202, v202
	v_fma_f32 v201, v201, 2.0, -1.0
	v_mul_f32_e32 v216, v212, v200
	v_mfma_f32_32x32x16_f16 v[48:63], a[156:159], v[188:191], v[48:63]
	ds_read_b128 v[188:191], v193 offset:23552
	s_add_u32 s44, s34, 0x1000
	s_addc_u32 s45, s35, 0
	s_mov_b32 m0, s53
	s_nop 0
	global_load_lds_dwordx4 v192, s[44:45] sc1
	v_rcp_f32_e32 v203, v203
	v_fma_f32 v202, v202, 2.0, -1.0
	v_mul_f32_e32 v217, v213, v201
	s_waitcnt lgkmcnt(4)
	v_mfma_f32_32x32x16_f16 v[32:47], a[160:163], v[160:163], v[32:47]
	ds_read_b128 v[160:163], v193 offset:24576
	v_fma_f32 v203, v203, 2.0, -1.0
	v_mul_f32_e32 v218, v214, v202
	v_mfma_f32_32x32x16_f16 v[48:63], a[160:163], v[164:167], v[48:63]
	ds_read_b128 v[164:167], v193 offset:25600
	v_mul_f32_e32 v219, v215, v203
	v_cvt_pk_f16_f32 v222, v216, v217
	v_mfma_f32_32x32x16_f16 v[32:47], a[164:167], v[168:171], v[32:47]
	ds_read_b128 v[168:171], v193 offset:26624
	v_cvt_pk_f16_f32 v223, v218, v219
	v_mfma_f32_32x32x16_f16 v[48:63], a[164:167], v[172:175], v[48:63]
	ds_read_b128 v[172:175], v193 offset:27648
	global_load_lds_dwordx4 v192, s[44:45] offset:1024 sc1
	s_cmp_eq_u32 s33, s60
	s_cbranch_scc1 .LE_ht30
.LE_htb31:
	s_waitcnt lgkmcnt(4)
	v_mfma_f32_32x32x16_f16 v[32:47], a[168:171], v[176:179], v[32:47]
	ds_read_b128 v[176:179], v193 offset:28672
	s_nop 1
	v_permlane32_swap_b32_e32 v220, v222
	v_permlane32_swap_b32_e32 v221, v223
	s_cmp_eq_u32 s31, 0
	s_cbranch_scc1 .LE_slow32
	global_store_dwordx4 v195, v[220:223], s[36:37] offset:0
.LE_join33:
	v_mfma_f32_32x32x16_f16 v[48:63], a[168:171], v[180:183], v[48:63]
	ds_read_b128 v[180:183], v193 offset:29696
	v_mfma_f32_32x32x16_f16 v[32:47], a[172:175], v[184:187], v[32:47]
	ds_read_b128 v[184:187], v193 offset:30720
	v_mfma_f32_32x32x16_f16 v[48:63], a[172:175], v[188:191], v[48:63]
	ds_read_b128 v[188:191], v193 offset:31744
	global_load_lds_dwordx4 v192, s[44:45] offset:2048 sc1
	s_waitcnt vmcnt(8)
	s_barrier
	s_waitcnt lgkmcnt(4)
	v_mfma_f32_32x32x16_f16 v[32:47], a[176:179], v[160:163], v[32:47]
	ds_read_b128 v[160:163], v193 offset:32768
	v_mfma_f32_32x32x16_f16 v[48:63], a[176:179], v[164:167], v[48:63]
	ds_read_b128 v[164:167], v193 offset:33792
	v_mfma_f32_32x32x16_f16 v[32:47], a[180:183], v[168:171], v[32:47]
	ds_read_b128 v[168:171], v193 offset:34816
	v_mfma_f32_32x32x16_f16 v[48:63], a[180:183], v[172:175], v[48:63]
	ds_read_b128 v[172:175], v193 offset:35840
	global_load_lds_dwordx4 v192, s[44:45] offset:3072 sc1
	s_waitcnt lgkmcnt(4)
	v_mfma_f32_32x32x16_f16 v[32:47], a[184:187], v[176:179], v[32:47]
	ds_read_b128 v[176:179], v193 offset:36864
	v_mfma_f32_32x32x16_f16 v[48:63], a[184:187], v[180:183], v[48:63]
	ds_read_b128 v[180:183], v193 offset:37888
	v_mfma_f32_32x32x16_f16 v[32:47], a[188:191], v[184:187], v[32:47]
	ds_read_b128 v[184:187], v193 offset:38912
	v_mfma_f32_32x32x16_f16 v[48:63], a[188:191], v[188:191], v[48:63]
	ds_read_b128 v[188:191], v193 offset:39936
	s_add_u32 s44, s34, 0x8000
	s_addc_u32 s45, s35, 0
	s_mov_b32 m0, s54
	s_nop 0
	global_load_lds_dwordx4 v192, s[44:45] sc1
	s_waitcnt lgkmcnt(4)
	v_mfma_f32_32x32x16_f16 v[32:47], a[192:195], v[160:163], v[32:47]
	ds_read_b128 v[160:163], v193 offset:40960
	v_mfma_f32_32x32x16_f16 v[48:63], a[192:195], v[164:167], v[48:63]
	ds_read_b128 v[164:167], v193 offset:41984
	s_waitcnt vmcnt(3)
	s_barrier
	v_mov_b32_e32 v199, 1
	s_cmp_eq_u32 s31, 0
	s_cbranch_scc1 .LE_slow34
	global_store_dword v197, v199, s[40:41]
.LE_join35:
	v_mfma_f32_32x32x16_f16 v[32:47], a[196:199], v[168:171], v[32:47]
	ds_read_b128 v[168:171], v193 offset:43008
	v_mfma_f32_32x32x16_f16 v[48:63], a[196:199], v[172:175], v[48:63]
	ds_read_b128 v[172:175], v193 offset:44032
	global_load_lds_dwordx4 v192, s[44:45] offset:1024 sc1
	s_waitcnt lgkmcnt(4)
	v_mfma_f32_32x32x16_f16 v[32:47], a[200:203], v[176:179], v[32:47]
	ds_read_b128 v[176:179], v193 offset:45056
	v_mfma_f32_32x32x16_f16 v[48:63], a[200:203], v[180:183], v[48:63]
	ds_read_b128 v[180:183], v193 offset:46080
	s_and_b32 s64, s33, 1
	s_lshl_b32 s64, s64, 22
	s_add_u32 s64, s64, s50
	s_add_u32 s64, s64, 0x20000
	s_add_u32 s36, s6, s64
	s_addc_u32 s37, s7, 0
	s_lshl_b32 s64, s33, 3
	s_add_u32 s64, s64, s29
	s_lshl_b32 s64, s64, 5
	s_add_u32 s64, s64, s30
	s_lshl_b32 s64, s64, 2
	s_add_u32 s40, s8, s64
	s_addc_u32 s41, s9, 0
	s_lshl_b32 s64, s61, 11
	s_lshl_b32 s65, s29, 8
	s_add_u32 s64, s64, s65
	s_lshl_b32 s64, s64, 3
	s_add_u32 s42, s12, s64
	s_addc_u32 s43, s13, 0
	v_mfma_f32_32x32x16_f16 v[32:47], a[204:207], v[184:187], v[32:47]
	ds_read_b128 v[184:187], v193 offset:47104
	v_mfma_f32_32x32x16_f16 v[48:63], a[204:207], v[188:191], v[48:63]
	ds_read_b128 v[188:191], v193 offset:48128
	global_load_lds_dwordx4 v192, s[44:45] offset:2048 sc1
	s_waitcnt lgkmcnt(4)
	v_mfma_f32_32x32x16_f16 v[32:47], a[208:211], v[160:163], v[32:47]
	ds_read_b128 v[160:163], v193 offset:49152
	v_mfma_f32_32x32x16_f16 v[48:63], a[208:211], v[164:167], v[48:63]
	ds_read_b128 v[164:167], v193 offset:50176
	v_mfma_f32_32x32x16_f16 v[32:47], a[212:215], v[168:171], v[32:47]
	ds_read_b128 v[168:171], v193 offset:51200
	v_mfma_f32_32x32x16_f16 v[48:63], a[212:215], v[172:175], v[48:63]
	ds_read_b128 v[172:175], v193 offset:52224
	global_load_lds_dwordx4 v192, s[44:45] offset:3072 sc1
	s_waitcnt lgkmcnt(4)
	v_mfma_f32_32x32x16_f16 v[32:47], a[216:219], v[176:179], v[32:47]
	ds_read_b128 v[176:179], v193 offset:53248
	v_mfma_f32_32x32x16_f16 v[48:63], a[216:219], v[180:183], v[48:63]
	ds_read_b128 v[180:183], v193 offset:54272
	v_mfma_f32_32x32x16_f16 v[32:47], a[220:223], v[184:187], v[32:47]
	ds_read_b128 v[184:187], v193 offset:55296
	v_mfma_f32_32x32x16_f16 v[48:63], a[220:223], v[188:191], v[48:63]
	ds_read_b128 v[188:191], v193 offset:56320
	s_add_u32 s44, s34, 0x9000
	s_addc_u32 s45, s35, 0
	s_mov_b32 m0, s55
	s_nop 0
	global_load_lds_dwordx4 v192, s[44:45] sc1
	s_waitcnt lgkmcnt(4)
	v_mfma_f32_32x32x16_f16 v[32:47], a[224:227], v[160:163], v[32:47]
	ds_read_b128 v[160:163], v193 offset:57344
	v_mfma_f32_32x32x16_f16 v[48:63], a[224:227], v[164:167], v[48:63]
	ds_read_b128 v[164:167], v193 offset:58368
	v_mfma_f32_32x32x16_f16 v[32:47], a[228:231], v[168:171], v[32:47]
	ds_read_b128 v[168:171], v193 offset:59392
	v_mfma_f32_32x32x16_f16 v[48:63], a[228:231], v[172:175], v[48:63]
	ds_read_b128 v[172:175], v193 offset:60416
	global_load_lds_dwordx4 v192, s[44:45] offset:1024 sc1
	s_waitcnt lgkmcnt(4)
	v_mfma_f32_32x32x16_f16 v[32:47], a[232:235], v[176:179], v[32:47]
	ds_read_b128 v[176:179], v193 offset:61440
	v_mfma_f32_32x32x16_f16 v[48:63], a[232:235], v[180:183], v[48:63]
	ds_read_b128 v[180:183], v193 offset:62464
	v_mfma_f32_32x32x16_f16 v[32:47], a[236:239], v[184:187], v[32:47]
	ds_read_b128 v[184:187], v193 offset:63488
	v_mfma_f32_32x32x16_f16 v[48:63], a[236:239], v[188:191], v[48:63]
	ds_read_b128 v[188:191], v193 offset:64512
	global_load_lds_dwordx4 v192, s[44:45] offset:2048 sc1
	s_waitcnt vmcnt(8)
	s_barrier
	s_waitcnt lgkmcnt(4)
	v_mfma_f32_32x32x16_f16 v[32:47], a[240:243], v[160:163], v[32:47]
	ds_read_b128 v[160:163], v192 offset:0
	v_mfma_f32_32x32x16_f16 v[48:63], a[240:243], v[164:167], v[48:63]
	ds_read_b128 v[164:167], v192 offset:1024
	v_mfma_f32_32x32x16_f16 v[32:47], a[244:247], v[168:171], v[32:47]
	ds_read_b128 v[168:171], v192 offset:2048
	v_mfma_f32_32x32x16_f16 v[48:63], a[244:247], v[172:175], v[48:63]
	ds_read_b128 v[172:175], v192 offset:3072
	global_load_lds_dwordx4 v192, s[44:45] offset:3072 sc1
	s_waitcnt lgkmcnt(4)
	v_mfma_f32_32x32x16_f16 v[32:47], a[248:251], v[176:179], v[32:47]
	ds_read_b128 v[176:179], v192 offset:4096
	v_mfma_f32_32x32x16_f16 v[48:63], a[248:251], v[180:183], v[48:63]
	ds_read_b128 v[180:183], v192 offset:5120
	v_mfma_f32_32x32x16_f16 v[32:47], a[252:255], v[184:187], v[32:47]
	ds_read_b128 v[184:187], v192 offset:6144
	v_mfma_f32_32x32x16_f16 v[48:63], a[252:255], v[188:191], v[48:63]
	ds_read_b128 v[188:191], v192 offset:7168
	s_add_u32 s44, s34, 0x10000
	s_addc_u32 s45, s35, 0
	s_mov_b32 m0, s56
	s_nop 0
	global_load_lds_dwordx4 v192, s[44:45] sc1
	s_nop 3
	global_load_dword v228, v249, s[42:43] offset:0
	global_load_dword v229, v249, s[42:43] offset:256
	s_waitcnt lgkmcnt(4)
	v_mfma_f32_32x32x16_f16 v[64:79], a[0:3], v[160:163], v[64:79]
	ds_read_b128 v[160:163], v192 offset:8192
	v_exp_f32_e32 v200, v32
	v_mfma_f32_32x32x16_f16 v[80:95], a[0:3], v[164:167], v[80:95]
	ds_read_b128 v[164:167], v192 offset:9216
	s_lshl_b32 s64, s71, 3
	s_add_u32 s64, s64, s29
	s_lshl_b32 s64, s64, 7
	s_add_u32 s38, s8, s64
	s_addc_u32 s39, s9, 0
	global_load_dword v251, v196, s[38:39] sc1
	v_exp_f32_e32 v201, v33
	v_add_f32_e32 v200, 1.0, v200
	v_mfma_f32_32x32x16_f16 v[64:79], a[4:7], v[168:171], v[64:79]
	ds_read_b128 v[168:171], v192 offset:10240
	v_exp_f32_e32 v202, v34
	v_add_f32_e32 v201, 1.0, v201
	v_mfma_f32_32x32x16_f16 v[80:95], a[4:7], v[172:175], v[80:95]
	ds_read_b128 v[172:175], v192 offset:11264
	global_load_lds_dwordx4 v192, s[44:45] offset:1024 sc1
	v_exp_f32_e32 v203, v35
	v_add_f32_e32 v202, 1.0, v202
	s_waitcnt lgkmcnt(4)
	v_mfma_f32_32x32x16_f16 v[64:79], a[8:11], v[176:179], v[64:79]
	ds_read_b128 v[176:179], v192 offset:12288
	v_exp_f32_e32 v204, v36
	v_add_f32_e32 v203, 1.0, v203
	v_mfma_f32_32x32x16_f16 v[80:95], a[8:11], v[180:183], v[80:95]
	ds_read_b128 v[180:183], v192 offset:13312
	v_exp_f32_e32 v205, v37
	v_add_f32_e32 v204, 1.0, v204
	v_mfma_f32_32x32x16_f16 v[64:79], a[12:15], v[184:187], v[64:79]
	ds_read_b128 v[184:187], v192 offset:14336
	v_exp_f32_e32 v206, v38
	v_add_f32_e32 v205, 1.0, v205
	v_mfma_f32_32x32x16_f16 v[80:95], a[12:15], v[188:191], v[80:95]
	ds_read_b128 v[188:191], v192 offset:15360
	global_load_lds_dwordx4 v192, s[44:45] offset:2048 sc1
	v_exp_f32_e32 v207, v39
	v_add_f32_e32 v206, 1.0, v206
	s_waitcnt lgkmcnt(4)
	v_mfma_f32_32x32x16_f16 v[64:79], a[16:19], v[160:163], v[64:79]
	ds_read_b128 v[160:163], v192 offset:16384
	v_exp_f32_e32 v208, v40
	v_add_f32_e32 v207, 1.0, v207
	v_mfma_f32_32x32x16_f16 v[80:95], a[16:19], v[164:167], v[80:95]
	ds_read_b128 v[164:167], v192 offset:17408
	v_exp_f32_e32 v209, v41
	v_add_f32_e32 v208, 1.0, v208
	v_mfma_f32_32x32x16_f16 v[64:79], a[20:23], v[168:171], v[64:79]
	ds_read_b128 v[168:171], v192 offset:18432
	v_exp_f32_e32 v210, v42
	v_add_f32_e32 v209, 1.0, v209
	v_mfma_f32_32x32x16_f16 v[80:95], a[20:23], v[172:175], v[80:95]
	ds_read_b128 v[172:175], v192 offset:19456
	global_load_lds_dwordx4 v192, s[44:45] offset:3072 sc1
	v_exp_f32_e32 v211, v43
	v_add_f32_e32 v210, 1.0, v210
	s_waitcnt lgkmcnt(4)
	v_mfma_f32_32x32x16_f16 v[64:79], a[24:27], v[176:179], v[64:79]
	ds_read_b128 v[176:179], v192 offset:20480
	v_exp_f32_e32 v212, v44
	v_add_f32_e32 v211, 1.0, v211
	v_mfma_f32_32x32x16_f16 v[80:95], a[24:27], v[180:183], v[80:95]
	ds_read_b128 v[180:183], v192 offset:21504
	v_exp_f32_e32 v213, v45
	v_add_f32_e32 v212, 1.0, v212
	v_mfma_f32_32x32x16_f16 v[64:79], a[28:31], v[184:187], v[64:79]
	ds_read_b128 v[184:187], v192 offset:22528
	v_exp_f32_e32 v214, v46
	v_add_f32_e32 v213, 1.0, v213
	v_mfma_f32_32x32x16_f16 v[80:95], a[28:31], v[188:191], v[80:95]
	ds_read_b128 v[188:191], v192 offset:23552
	s_add_u32 s44, s34, 0x11000
	s_addc_u32 s45, s35, 0
	s_mov_b32 m0, s57
	s_nop 0
	global_load_lds_dwordx4 v192, s[44:45] sc1
	v_exp_f32_e32 v215, v47
	v_add_f32_e32 v214, 1.0, v214
	s_waitcnt lgkmcnt(4)
	v_mfma_f32_32x32x16_f16 v[64:79], a[32:35], v[160:163], v[64:79]
	ds_read_b128 v[160:163], v192 offset:24576
	v_add_f32_e32 v215, 1.0, v215
	v_rcp_f32_e32 v200, v200
	v_mfma_f32_32x32x16_f16 v[80:95], a[32:35], v[164:167], v[80:95]
	ds_read_b128 v[164:167], v192 offset:25600
	v_rcp_f32_e32 v201, v201
	v_mfma_f32_32x32x16_f16 v[64:79], a[36:39], v[168:171], v[64:79]
	ds_read_b128 v[168:171], v192 offset:26624
	v_rcp_f32_e32 v202, v202
	v_mfma_f32_32x32x16_f16 v[80:95], a[36:39], v[172:175], v[80:95]
	ds_read_b128 v[172:175], v192 offset:27648
	global_load_lds_dwordx4 v192, s[44:45] offset:1024 sc1
	v_rcp_f32_e32 v203, v203
	s_waitcnt lgkmcnt(4)
	v_mfma_f32_32x32x16_f16 v[64:79], a[40:43], v[176:179], v[64:79]
	ds_read_b128 v[176:179], v192 offset:28672
	v_rcp_f32_e32 v204, v204
	v_mfma_f32_32x32x16_f16 v[80:95], a[40:43], v[180:183], v[80:95]
	ds_read_b128 v[180:183], v192 offset:29696
	v_rcp_f32_e32 v205, v205
	v_mul_f32_e32 v204, v204, v136
	v_mfma_f32_32x32x16_f16 v[64:79], a[44:47], v[184:187], v[64:79]
	ds_read_b128 v[184:187], v192 offset:30720
	v_rcp_f32_e32 v206, v206
	v_mul_f32_e32 v205, v205, v137
	v_mfma_f32_32x32x16_f16 v[80:95], a[44:47], v[188:191], v[80:95]
	ds_read_b128 v[188:191], v192 offset:31744
	global_load_lds_dwordx4 v192, s[44:45] offset:2048 sc1
	v_rcp_f32_e32 v207, v207
	v_mul_f32_e32 v206, v206, v138
	s_waitcnt vmcnt(10)
	s_barrier
	s_waitcnt lgkmcnt(4)
	v_mfma_f32_32x32x16_f16 v[64:79], a[48:51], v[160:163], v[64:79]
	ds_read_b128 v[160:163], v192 offset:32768
	v_rcp_f32_e32 v208, v208
	v_mul_f32_e32 v207, v207, v139
	v_mfma_f32_32x32x16_f16 v[80:95], a[48:51], v[164:167], v[80:95]
	ds_read_b128 v[164:167], v192 offset:33792
	v_rcp_f32_e32 v209, v209
	v_fmamk_f32 v208, v208, 0xc0b8aa3b, v198
	v_mfma_f32_32x32x16_f16 v[64:79], a[52:55], v[168:171], v[64:79]
	ds_read_b128 v[168:171], v192 offset:34816
	v_rcp_f32_e32 v210, v210
	v_fmamk_f32 v209, v209, 0xc0b8aa3b, v198
	v_fma_f32 v136, v200, v208, v204
	v_mfma_f32_32x32x16_f16 v[80:95], a[52:55], v[172:175], v[80:95]
	ds_read_b128 v[172:175], v192 offset:35840
	global_load_lds_dwordx4 v192, s[44:45] offset:3072 sc1
	v_rcp_f32_e32 v211, v211
	v_fmamk_f32 v210, v210, 0xc0b8aa3b, v198
	v_fma_f32 v137, v201, v209, v205
	s_waitcnt lgkmcnt(4)
	v_mfma_f32_32x32x16_f16 v[64:79], a[56:59], v[176:179], v[64:79]
	ds_read_b128 v[176:179], v192 offset:36864
	v_rcp_f32_e32 v212, v212
	v_fmamk_f32 v211, v211, 0xc0b8aa3b, v198
	v_fma_f32 v138, v202, v210, v206
	v_mfma_f32_32x32x16_f16 v[80:95], a[56:59], v[180:183], v[80:95]
	ds_read_b128 v[180:183], v192 offset:37888
	v_rcp_f32_e32 v213, v213
	v_fma_f32 v139, v203, v211, v207
	v_mfma_f32_32x32x16_f16 v[64:79], a[60:63], v[184:187], v[64:79]
	ds_read_b128 v[184:187], v192 offset:38912
	v_rcp_f32_e32 v214, v214
	v_mfma_f32_32x32x16_f16 v[80:95], a[60:63], v[188:191], v[80:95]
	ds_read_b128 v[188:191], v192 offset:39936
	s_add_u32 s44, s34, 0x18000
	s_addc_u32 s45, s35, 0
	s_mov_b32 m0, s58
	s_nop 0
	global_load_lds_dwordx4 v192, s[44:45] sc1
	v_rcp_f32_e32 v215, v215
	s_waitcnt lgkmcnt(4)
	v_mfma_f32_32x32x16_f16 v[64:79], a[64:67], v[160:163], v[64:79]
	ds_read_b128 v[160:163], v192 offset:40960
	v_exp_f32_e32 v200, v136
	v_mfma_f32_32x32x16_f16 v[80:95], a[64:67], v[164:167], v[80:95]
	ds_read_b128 v[164:167], v192 offset:41984
	v_exp_f32_e32 v201, v137
	v_add_f32_e32 v200, 1.0, v200
	v_mfma_f32_32x32x16_f16 v[64:79], a[68:71], v[168:171], v[64:79]
	ds_read_b128 v[168:171], v192 offset:43008
	v_exp_f32_e32 v202, v138
	v_add_f32_e32 v201, 1.0, v201
	v_mfma_f32_32x32x16_f16 v[80:95], a[68:71], v[172:175], v[80:95]
	ds_read_b128 v[172:175], v192 offset:44032
	global_load_lds_dwordx4 v192, s[44:45] offset:1024 sc1
	v_exp_f32_e32 v203, v139
	v_add_f32_e32 v202, 1.0, v202
	s_waitcnt lgkmcnt(4)
	v_mfma_f32_32x32x16_f16 v[64:79], a[72:75], v[176:179], v[64:79]
	ds_read_b128 v[176:179], v192 offset:45056
	v_add_f32_e32 v203, 1.0, v203
	v_rcp_f32_e32 v200, v200
	v_mfma_f32_32x32x16_f16 v[80:95], a[72:75], v[180:183], v[80:95]
	ds_read_b128 v[180:183], v192 offset:46080
	v_rcp_f32_e32 v201, v201
	v_fma_f32 v200, v200, 2.0, -1.0
	v_mfma_f32_32x32x16_f16 v[64:79], a[76:79], v[184:187], v[64:79]
	ds_read_b128 v[184:187], v192 offset:47104
	v_rcp_f32_e32 v202, v202
	v_fma_f32 v201, v201, 2.0, -1.0
	v_mul_f32_e32 v216, v212, v200
	v_mfma_f32_32x32x16_f16 v[80:95], a[76:79], v[188:191], v[80:95]
	ds_read_b128 v[188:191], v192 offset:48128
	global_load_lds_dwordx4 v192, s[44:45] offset:2048 sc1
	v_rcp_f32_e32 v203, v203
	v_fma_f32 v202, v202, 2.0, -1.0
	v_mul_f32_e32 v217, v213, v201
	s_waitcnt lgkmcnt(4)
	v_mfma_f32_32x32x16_f16 v[64:79], a[80:83], v[160:163], v[64:79]
	ds_read_b128 v[160:163], v192 offset:49152
	v_fma_f32 v203, v203, 2.0, -1.0
	v_mul_f32_e32 v218, v214, v202
	v_exp_f32_e32 v200, v48
	v_mfma_f32_32x32x16_f16 v[80:95], a[80:83], v[164:167], v[80:95]
	ds_read_b128 v[164:167], v192 offset:50176
	v_mul_f32_e32 v219, v215, v203
	v_cvt_pk_f16_f32 v220, v216, v217
	v_exp_f32_e32 v201, v49
	v_mfma_f32_32x32x16_f16 v[64:79], a[84:87], v[168:171], v[64:79]
	ds_read_b128 v[168:171], v192 offset:51200
	v_cvt_pk_f16_f32 v221, v218, v219
	v_exp_f32_e32 v202, v50
	v_add_f32_e32 v200, 1.0, v200
	v_mfma_f32_32x32x16_f16 v[80:95], a[84:87], v[172:175], v[80:95]
	ds_read_b128 v[172:175], v192 offset:52224
	global_load_lds_dwordx4 v192, s[44:45] offset:3072 sc1
	s_cmp_eq_u32 s33, s60
	s_cbranch_scc1 .LE_ht36
.LE_htb37:
	v_exp_f32_e32 v203, v51
	s_waitcnt lgkmcnt(4)
	v_mfma_f32_32x32x16_f16 v[64:79], a[88:91], v[176:179], v[64:79]
	ds_read_b128 v[176:179], v192 offset:53248
	v_exp_f32_e32 v204, v52
	v_add_f32_e32 v201, 1.0, v201
	v_add_f32_e32 v202, 1.0, v202
	v_mfma_f32_32x32x16_f16 v[80:95], a[88:91], v[180:183], v[80:95]
	ds_read_b128 v[180:183], v192 offset:54272
	v_exp_f32_e32 v205, v53
	v_add_f32_e32 v203, 1.0, v203
	v_add_f32_e32 v204, 1.0, v204
	v_mfma_f32_32x32x16_f16 v[64:79], a[92:95], v[184:187], v[64:79]
	ds_read_b128 v[184:187], v192 offset:55296
	v_exp_f32_e32 v206, v54
	v_add_f32_e32 v205, 1.0, v205
	v_mfma_f32_32x32x16_f16 v[80:95], a[92:95], v[188:191], v[80:95]
	ds_read_b128 v[188:191], v192 offset:56320
	s_add_u32 s44, s34, 0x19000
	s_addc_u32 s45, s35, 0
	s_mov_b32 m0, s59
	s_nop 0
	global_load_lds_dwordx4 v192, s[44:45] sc1
	v_exp_f32_e32 v207, v55
	v_add_f32_e32 v206, 1.0, v206
	s_waitcnt lgkmcnt(4)
	v_mfma_f32_32x32x16_f16 v[64:79], a[96:99], v[160:163], v[64:79]
	ds_read_b128 v[160:163], v192 offset:57344
	v_exp_f32_e32 v208, v56
	v_add_f32_e32 v207, 1.0, v207
	v_mfma_f32_32x32x16_f16 v[80:95], a[96:99], v[164:167], v[80:95]
	ds_read_b128 v[164:167], v192 offset:58368
	v_exp_f32_e32 v209, v57
	v_add_f32_e32 v208, 1.0, v208
	v_mfma_f32_32x32x16_f16 v[64:79], a[100:103], v[168:171], v[64:79]
	ds_read_b128 v[168:171], v192 offset:59392
	v_exp_f32_e32 v210, v58
	v_add_f32_e32 v209, 1.0, v209
	v_mfma_f32_32x32x16_f16 v[80:95], a[100:103], v[172:175], v[80:95]
	ds_read_b128 v[172:175], v192 offset:60416
	global_load_lds_dwordx4 v192, s[44:45] offset:1024 sc1
	v_exp_f32_e32 v211, v59
	v_add_f32_e32 v210, 1.0, v210
	s_waitcnt lgkmcnt(4)
	v_mfma_f32_32x32x16_f16 v[64:79], a[104:107], v[176:179], v[64:79]
	ds_read_b128 v[176:179], v192 offset:61440
	v_exp_f32_e32 v212, v60
	v_add_f32_e32 v211, 1.0, v211
	v_mfma_f32_32x32x16_f16 v[80:95], a[104:107], v[180:183], v[80:95]
	ds_read_b128 v[180:183], v192 offset:62464
	v_exp_f32_e32 v213, v61
	v_add_f32_e32 v212, 1.0, v212
	v_mfma_f32_32x32x16_f16 v[64:79], a[108:111], v[184:187], v[64:79]
	ds_read_b128 v[184:187], v192 offset:63488
	v_exp_f32_e32 v214, v62
	v_add_f32_e32 v213, 1.0, v213
	v_mfma_f32_32x32x16_f16 v[80:95], a[108:111], v[188:191], v[80:95]
	ds_read_b128 v[188:191], v192 offset:64512
	global_load_lds_dwordx4 v192, s[44:45] offset:2048 sc1
	v_exp_f32_e32 v215, v63
	v_add_f32_e32 v214, 1.0, v214
	s_waitcnt vmcnt(7)
	s_barrier
	s_waitcnt lgkmcnt(4)
	v_mfma_f32_32x32x16_f16 v[64:79], a[112:115], v[160:163], v[64:79]
	ds_read_b128 v[160:163], v193 offset:0
	v_add_f32_e32 v215, 1.0, v215
	v_rcp_f32_e32 v200, v200
	v_mfma_f32_32x32x16_f16 v[80:95], a[112:115], v[164:167], v[80:95]
	ds_read_b128 v[164:167], v193 offset:1024
	v_rcp_f32_e32 v201, v201
	v_mfma_f32_32x32x16_f16 v[64:79], a[116:119], v[168:171], v[64:79]
	ds_read_b128 v[168:171], v193 offset:2048
	v_rcp_f32_e32 v202, v202
	v_mfma_f32_32x32x16_f16 v[80:95], a[116:119], v[172:175], v[80:95]
	ds_read_b128 v[172:175], v193 offset:3072
	global_load_lds_dwordx4 v192, s[44:45] offset:3072 sc1
	v_rcp_f32_e32 v203, v203
	s_waitcnt lgkmcnt(4)
	v_mfma_f32_32x32x16_f16 v[64:79], a[120:123], v[176:179], v[64:79]
	ds_read_b128 v[176:179], v193 offset:4096
	v_rcp_f32_e32 v204, v204
	v_mfma_f32_32x32x16_f16 v[80:95], a[120:123], v[180:183], v[80:95]
	ds_read_b128 v[180:183], v193 offset:5120
	v_rcp_f32_e32 v205, v205
	v_mul_f32_e32 v204, v204, v140
	v_mfma_f32_32x32x2_f32 v[0:15], v248, v228, v[232:247]
	v_mfma_f32_32x32x16_f16 v[64:79], a[124:127], v[184:187], v[64:79]
	ds_read_b128 v[184:187], v193 offset:6144
	v_rcp_f32_e32 v206, v206
	v_mul_f32_e32 v205, v205, v141
	v_mfma_f32_32x32x2_f32 v[16:31], v248, v229, v[232:247]
	v_mfma_f32_32x32x16_f16 v[80:95], a[124:127], v[188:191], v[80:95]
	ds_read_b128 v[188:191], v193 offset:7168
	v_cmp_gt_u32_e32 vcc, 4, v251
	s_cbranch_vccnz .LE_tpoll39
.LE_tok38:
	s_and_b32 s64, s71, 1
	s_lshl_b32 s64, s64, 22
	s_add_u32 s64, s64, s49
	s_add_u32 s64, s64, 0x60000
	s_add_u32 s34, s6, s64
	s_addc_u32 s35, s7, 0
	s_add_u32 s44, s34, 0x0
	s_addc_u32 s45, s35, 0
	s_mov_b32 m0, s52
	s_nop 0
	global_load_lds_dwordx4 v192, s[44:45] sc1
	v_rcp_f32_e32 v207, v207
	v_mul_f32_e32 v206, v206, v142
	s_waitcnt lgkmcnt(4)
	v_mfma_f32_32x32x16_f16 v[64:79], a[128:131], v[160:163], v[64:79]
	ds_read_b128 v[160:163], v193 offset:8192
	v_rcp_f32_e32 v208, v208
	v_mul_f32_e32 v207, v207, v143
	v_mfma_f32_32x32x16_f16 v[80:95], a[128:131], v[164:167], v[80:95]
	ds_read_b128 v[164:167], v193 offset:9216
	v_rcp_f32_e32 v209, v209
	v_fmamk_f32 v208, v208, 0xc0b8aa3b, v198
	v_mfma_f32_32x32x16_f16 v[64:79], a[132:135], v[168:171], v[64:79]
	ds_read_b128 v[168:171], v193 offset:10240
	v_rcp_f32_e32 v210, v210
	v_fmamk_f32 v209, v209, 0xc0b8aa3b, v198
	v_fma_f32 v140, v200, v208, v204
	v_mfma_f32_32x32x16_f16 v[80:95], a[132:135], v[172:175], v[80:95]
	ds_read_b128 v[172:175], v193 offset:11264
	global_load_lds_dwordx4 v192, s[44:45] offset:1024 sc1
	v_rcp_f32_e32 v211, v211
	v_fmamk_f32 v210, v210, 0xc0b8aa3b, v198
	v_fma_f32 v141, v201, v209, v205
	s_waitcnt lgkmcnt(4)
	v_mfma_f32_32x32x16_f16 v[64:79], a[136:139], v[176:179], v[64:79]
	ds_read_b128 v[176:179], v193 offset:12288
	v_rcp_f32_e32 v212, v212
	v_fmamk_f32 v211, v211, 0xc0b8aa3b, v198
	v_fma_f32 v142, v202, v210, v206
	v_mfma_f32_32x32x16_f16 v[80:95], a[136:139], v[180:183], v[80:95]
	ds_read_b128 v[180:183], v193 offset:13312
	v_rcp_f32_e32 v213, v213
	v_fma_f32 v143, v203, v211, v207
	v_mfma_f32_32x32x16_f16 v[64:79], a[140:143], v[184:187], v[64:79]
	ds_read_b128 v[184:187], v193 offset:14336
	v_rcp_f32_e32 v214, v214
	v_mfma_f32_32x32x16_f16 v[80:95], a[140:143], v[188:191], v[80:95]
	ds_read_b128 v[188:191], v193 offset:15360
	global_load_lds_dwordx4 v192, s[44:45] offset:2048 sc1
	v_rcp_f32_e32 v215, v215
	s_waitcnt lgkmcnt(4)
	v_mfma_f32_32x32x16_f16 v[64:79], a[144:147], v[160:163], v[64:79]
	ds_read_b128 v[160:163], v193 offset:16384
	v_exp_f32_e32 v200, v140
	v_mfma_f32_32x32x16_f16 v[80:95], a[144:147], v[164:167], v[80:95]
	ds_read_b128 v[164:167], v193 offset:17408
	v_exp_f32_e32 v201, v141
	v_add_f32_e32 v200, 1.0, v200
	v_mfma_f32_32x32x16_f16 v[64:79], a[148:151], v[168:171], v[64:79]
	ds_read_b128 v[168:171], v193 offset:18432
	v_exp_f32_e32 v202, v142
	v_add_f32_e32 v201, 1.0, v201
	v_mfma_f32_32x32x16_f16 v[80:95], a[148:151], v[172:175], v[80:95]
	ds_read_b128 v[172:175], v193 offset:19456
	global_load_lds_dwordx4 v192, s[44:45] offset:3072 sc1
	v_exp_f32_e32 v203, v143
	v_add_f32_e32 v202, 1.0, v202
	s_waitcnt lgkmcnt(4)
	v_mfma_f32_32x32x16_f16 v[64:79], a[152:155], v[176:179], v[64:79]
	ds_read_b128 v[176:179], v193 offset:20480
	v_add_f32_e32 v203, 1.0, v203
	v_rcp_f32_e32 v200, v200
	v_mfma_f32_32x32x16_f16 v[80:95], a[152:155], v[180:183], v[80:95]
	ds_read_b128 v[180:183], v193 offset:21504
	v_rcp_f32_e32 v201, v201
	v_fma_f32 v200, v200, 2.0, -1.0
	v_mfma_f32_32x32x16_f16 v[64:79], a[156:159], v[184:187], v[64:79]
	ds_read_b128 v[184:187], v193 offset:22528
	v_rcp_f32_e32 v202, v202
	v_fma_f32 v201, v201, 2.0, -1.0
	v_mul_f32_e32 v216, v212, v200
	v_mfma_f32_32x32x16_f16 v[80:95], a[156:159], v[188:191], v[80:95]
	ds_read_b128 v[188:191], v193 offset:23552
	s_add_u32 s44, s34, 0x1000
	s_addc_u32 s45, s35, 0
	s_mov_b32 m0, s53
	s_nop 0
	global_load_lds_dwordx4 v192, s[44:45] sc1
	v_rcp_f32_e32 v203, v203
	v_fma_f32 v202, v202, 2.0, -1.0
	v_mul_f32_e32 v217, v213, v201
	s_waitcnt lgkmcnt(4)
	v_mfma_f32_32x32x16_f16 v[64:79], a[160:163], v[160:163], v[64:79]
	ds_read_b128 v[160:163], v193 offset:24576
	v_fma_f32 v203, v203, 2.0, -1.0
	v_mul_f32_e32 v218, v214, v202
	v_mfma_f32_32x32x16_f16 v[80:95], a[160:163], v[164:167], v[80:95]
	ds_read_b128 v[164:167], v193 offset:25600
	v_mul_f32_e32 v219, v215, v203
	v_cvt_pk_f16_f32 v222, v216, v217
	v_mfma_f32_32x32x16_f16 v[64:79], a[164:167], v[168:171], v[64:79]
	ds_read_b128 v[168:171], v193 offset:26624
	v_cvt_pk_f16_f32 v223, v218, v219
	v_mfma_f32_32x32x16_f16 v[80:95], a[164:167], v[172:175], v[80:95]
	ds_read_b128 v[172:175], v193 offset:27648
	global_load_lds_dwordx4 v192, s[44:45] offset:1024 sc1
	s_cmp_eq_u32 s33, s60
	s_cbranch_scc1 .LE_ht40
.LE_htb41:
	s_waitcnt lgkmcnt(4)
	v_mfma_f32_32x32x16_f16 v[64:79], a[168:171], v[176:179], v[64:79]
	ds_read_b128 v[176:179], v193 offset:28672
	s_nop 1
	v_permlane32_swap_b32_e32 v220, v222
	v_permlane32_swap_b32_e32 v221, v223
	s_cmp_eq_u32 s31, 0
	s_cbranch_scc1 .LE_slow42
	global_store_dwordx4 v195, v[220:223], s[36:37] offset:0
.LE_join43:
	v_mfma_f32_32x32x16_f16 v[80:95], a[168:171], v[180:183], v[80:95]
	ds_read_b128 v[180:183], v193 offset:29696
	v_mfma_f32_32x32x16_f16 v[64:79], a[172:175], v[184:187], v[64:79]
	ds_read_b128 v[184:187], v193 offset:30720
	v_mfma_f32_32x32x16_f16 v[80:95], a[172:175], v[188:191], v[80:95]
	ds_read_b128 v[188:191], v193 offset:31744
	global_load_lds_dwordx4 v192, s[44:45] offset:2048 sc1
	s_waitcnt vmcnt(8)
	s_barrier
	s_waitcnt lgkmcnt(4)
	v_mfma_f32_32x32x16_f16 v[64:79], a[176:179], v[160:163], v[64:79]
	ds_read_b128 v[160:163], v193 offset:32768
	v_mfma_f32_32x32x16_f16 v[80:95], a[176:179], v[164:167], v[80:95]
	ds_read_b128 v[164:167], v193 offset:33792
	v_mfma_f32_32x32x16_f16 v[64:79], a[180:183], v[168:171], v[64:79]
	ds_read_b128 v[168:171], v193 offset:34816
	v_mfma_f32_32x32x16_f16 v[80:95], a[180:183], v[172:175], v[80:95]
	ds_read_b128 v[172:175], v193 offset:35840
	global_load_lds_dwordx4 v192, s[44:45] offset:3072 sc1
	s_waitcnt lgkmcnt(4)
	v_mfma_f32_32x32x16_f16 v[64:79], a[184:187], v[176:179], v[64:79]
	ds_read_b128 v[176:179], v193 offset:36864
	v_mfma_f32_32x32x16_f16 v[80:95], a[184:187], v[180:183], v[80:95]
	ds_read_b128 v[180:183], v193 offset:37888
	v_mfma_f32_32x32x16_f16 v[64:79], a[188:191], v[184:187], v[64:79]
	ds_read_b128 v[184:187], v193 offset:38912
	v_mfma_f32_32x32x16_f16 v[80:95], a[188:191], v[188:191], v[80:95]
	ds_read_b128 v[188:191], v193 offset:39936
	s_add_u32 s44, s34, 0x8000
	s_addc_u32 s45, s35, 0
	s_mov_b32 m0, s54
	s_nop 0
	global_load_lds_dwordx4 v192, s[44:45] sc1
	s_waitcnt lgkmcnt(4)
	v_mfma_f32_32x32x16_f16 v[64:79], a[192:195], v[160:163], v[64:79]
	ds_read_b128 v[160:163], v193 offset:40960
	v_mfma_f32_32x32x16_f16 v[80:95], a[192:195], v[164:167], v[80:95]
	ds_read_b128 v[164:167], v193 offset:41984
	s_waitcnt vmcnt(3)
	s_barrier
	v_mov_b32_e32 v199, 2
	s_cmp_eq_u32 s31, 0
	s_cbranch_scc1 .LE_slow44
	global_store_dword v197, v199, s[40:41]
.LE_join45:
	v_mfma_f32_32x32x16_f16 v[64:79], a[196:199], v[168:171], v[64:79]
	ds_read_b128 v[168:171], v193 offset:43008
	v_mfma_f32_32x32x16_f16 v[80:95], a[196:199], v[172:175], v[80:95]
	ds_read_b128 v[172:175], v193 offset:44032
	global_load_lds_dwordx4 v192, s[44:45] offset:1024 sc1
	s_waitcnt lgkmcnt(4)
	v_mfma_f32_32x32x16_f16 v[64:79], a[200:203], v[176:179], v[64:79]
	ds_read_b128 v[176:179], v193 offset:45056
	v_mfma_f32_32x32x16_f16 v[80:95], a[200:203], v[180:183], v[80:95]
	ds_read_b128 v[180:183], v193 offset:46080
	s_and_b32 s64, s33, 1
	s_lshl_b32 s64, s64, 22
	s_add_u32 s64, s64, s50
	s_add_u32 s64, s64, 0x40000
	s_add_u32 s36, s6, s64
	s_addc_u32 s37, s7, 0
	s_lshl_b32 s64, s33, 3
	s_add_u32 s64, s64, s29
	s_lshl_b32 s64, s64, 5
	s_add_u32 s64, s64, s30
	s_lshl_b32 s64, s64, 2
	s_add_u32 s40, s8, s64
	s_addc_u32 s41, s9, 0
	s_lshl_b32 s64, s61, 11
	s_lshl_b32 s65, s29, 8
	s_add_u32 s64, s64, s65
	s_add_u32 s64, s64, 64
	s_lshl_b32 s64, s64, 3
	s_add_u32 s42, s12, s64
	s_addc_u32 s43, s13, 0
	v_mfma_f32_32x32x16_f16 v[64:79], a[204:207], v[184:187], v[64:79]
	ds_read_b128 v[184:187], v193 offset:47104
	v_mfma_f32_32x32x16_f16 v[80:95], a[204:207], v[188:191], v[80:95]
	ds_read_b128 v[188:191], v193 offset:48128
	global_load_lds_dwordx4 v192, s[44:45] offset:2048 sc1
	s_waitcnt lgkmcnt(4)
	v_mfma_f32_32x32x16_f16 v[64:79], a[208:211], v[160:163], v[64:79]
	ds_read_b128 v[160:163], v193 offset:49152
	v_mfma_f32_32x32x16_f16 v[80:95], a[208:211], v[164:167], v[80:95]
	ds_read_b128 v[164:167], v193 offset:50176
	v_mfma_f32_32x32x16_f16 v[64:79], a[212:215], v[168:171], v[64:79]
	ds_read_b128 v[168:171], v193 offset:51200
	v_mfma_f32_32x32x16_f16 v[80:95], a[212:215], v[172:175], v[80:95]
	ds_read_b128 v[172:175], v193 offset:52224
	global_load_lds_dwordx4 v192, s[44:45] offset:3072 sc1
	s_waitcnt lgkmcnt(4)
	v_mfma_f32_32x32x16_f16 v[64:79], a[216:219], v[176:179], v[64:79]
	ds_read_b128 v[176:179], v193 offset:53248
	v_mfma_f32_32x32x16_f16 v[80:95], a[216:219], v[180:183], v[80:95]
	ds_read_b128 v[180:183], v193 offset:54272
	v_mfma_f32_32x32x16_f16 v[64:79], a[220:223], v[184:187], v[64:79]
	ds_read_b128 v[184:187], v193 offset:55296
	v_mfma_f32_32x32x16_f16 v[80:95], a[220:223], v[188:191], v[80:95]
	ds_read_b128 v[188:191], v193 offset:56320
	s_add_u32 s44, s34, 0x9000
	s_addc_u32 s45, s35, 0
	s_mov_b32 m0, s55
	s_nop 0
	global_load_lds_dwordx4 v192, s[44:45] sc1
	s_waitcnt lgkmcnt(4)
	v_mfma_f32_32x32x16_f16 v[64:79], a[224:227], v[160:163], v[64:79]
	ds_read_b128 v[160:163], v193 offset:57344
	v_mfma_f32_32x32x16_f16 v[80:95], a[224:227], v[164:167], v[80:95]
	ds_read_b128 v[164:167], v193 offset:58368
	v_mfma_f32_32x32x16_f16 v[64:79], a[228:231], v[168:171], v[64:79]
	ds_read_b128 v[168:171], v193 offset:59392
	v_mfma_f32_32x32x16_f16 v[80:95], a[228:231], v[172:175], v[80:95]
	ds_read_b128 v[172:175], v193 offset:60416
	global_load_lds_dwordx4 v192, s[44:45] offset:1024 sc1
	s_waitcnt lgkmcnt(4)
	v_mfma_f32_32x32x16_f16 v[64:79], a[232:235], v[176:179], v[64:79]
	ds_read_b128 v[176:179], v193 offset:61440
	v_mfma_f32_32x32x16_f16 v[80:95], a[232:235], v[180:183], v[80:95]
	ds_read_b128 v[180:183], v193 offset:62464
	v_mfma_f32_32x32x16_f16 v[64:79], a[236:239], v[184:187], v[64:79]
	ds_read_b128 v[184:187], v193 offset:63488
	v_mfma_f32_32x32x16_f16 v[80:95], a[236:239], v[188:191], v[80:95]
	ds_read_b128 v[188:191], v193 offset:64512
	global_load_lds_dwordx4 v192, s[44:45] offset:2048 sc1
	s_waitcnt vmcnt(8)
	s_barrier
	s_waitcnt lgkmcnt(4)
	v_mfma_f32_32x32x16_f16 v[64:79], a[240:243], v[160:163], v[64:79]
	ds_read_b128 v[160:163], v192 offset:0
	v_mfma_f32_32x32x16_f16 v[80:95], a[240:243], v[164:167], v[80:95]
	ds_read_b128 v[164:167], v192 offset:1024
	v_mfma_f32_32x32x16_f16 v[64:79], a[244:247], v[168:171], v[64:79]
	ds_read_b128 v[168:171], v192 offset:2048
	v_mfma_f32_32x32x16_f16 v[80:95], a[244:247], v[172:175], v[80:95]
	ds_read_b128 v[172:175], v192 offset:3072
	global_load_lds_dwordx4 v192, s[44:45] offset:3072 sc1
	s_waitcnt lgkmcnt(4)
	v_mfma_f32_32x32x16_f16 v[64:79], a[248:251], v[176:179], v[64:79]
	ds_read_b128 v[176:179], v192 offset:4096
	v_mfma_f32_32x32x16_f16 v[80:95], a[248:251], v[180:183], v[80:95]
	ds_read_b128 v[180:183], v192 offset:5120
	v_mfma_f32_32x32x16_f16 v[64:79], a[252:255], v[184:187], v[64:79]
	ds_read_b128 v[184:187], v192 offset:6144
	v_mfma_f32_32x32x16_f16 v[80:95], a[252:255], v[188:191], v[80:95]
	ds_read_b128 v[188:191], v192 offset:7168
	s_add_u32 s44, s34, 0x10000
	s_addc_u32 s45, s35, 0
	s_mov_b32 m0, s56
	s_nop 0
	global_load_lds_dwordx4 v192, s[44:45] sc1
	s_nop 3
	global_load_dword v228, v249, s[42:43] offset:0
	global_load_dword v229, v249, s[42:43] offset:256
	s_waitcnt lgkmcnt(4)
	v_mfma_f32_32x32x16_f16 v[96:111], a[0:3], v[160:163], v[96:111]
	ds_read_b128 v[160:163], v192 offset:8192
	v_exp_f32_e32 v200, v64
	v_mfma_f32_32x32x16_f16 v[112:127], a[0:3], v[164:167], v[112:127]
	ds_read_b128 v[164:167], v192 offset:9216
	s_lshl_b32 s64, s33, 3
	s_add_u32 s64, s64, s29
	s_lshl_b32 s64, s64, 7
	s_add_u32 s38, s8, s64
	s_addc_u32 s39, s9, 0
	global_load_dword v251, v196, s[38:39] sc1
	v_exp_f32_e32 v201, v65
	v_add_f32_e32 v200, 1.0, v200
	v_mfma_f32_32x32x16_f16 v[96:111], a[4:7], v[168:171], v[96:111]
	ds_read_b128 v[168:171], v192 offset:10240
	v_exp_f32_e32 v202, v66
	v_add_f32_e32 v201, 1.0, v201
	v_mfma_f32_32x32x16_f16 v[112:127], a[4:7], v[172:175], v[112:127]
	ds_read_b128 v[172:175], v192 offset:11264
	global_load_lds_dwordx4 v192, s[44:45] offset:1024 sc1
	v_exp_f32_e32 v203, v67
	v_add_f32_e32 v202, 1.0, v202
	s_waitcnt lgkmcnt(4)
	v_mfma_f32_32x32x16_f16 v[96:111], a[8:11], v[176:179], v[96:111]
	ds_read_b128 v[176:179], v192 offset:12288
	v_exp_f32_e32 v204, v68
	v_add_f32_e32 v203, 1.0, v203
	v_mfma_f32_32x32x16_f16 v[112:127], a[8:11], v[180:183], v[112:127]
	ds_read_b128 v[180:183], v192 offset:13312
	v_exp_f32_e32 v205, v69
	v_add_f32_e32 v204, 1.0, v204
	v_mfma_f32_32x32x16_f16 v[96:111], a[12:15], v[184:187], v[96:111]
	ds_read_b128 v[184:187], v192 offset:14336
	v_exp_f32_e32 v206, v70
	v_add_f32_e32 v205, 1.0, v205
	v_mfma_f32_32x32x16_f16 v[112:127], a[12:15], v[188:191], v[112:127]
	ds_read_b128 v[188:191], v192 offset:15360
	global_load_lds_dwordx4 v192, s[44:45] offset:2048 sc1
	v_exp_f32_e32 v207, v71
	v_add_f32_e32 v206, 1.0, v206
	s_waitcnt lgkmcnt(4)
	v_mfma_f32_32x32x16_f16 v[96:111], a[16:19], v[160:163], v[96:111]
	ds_read_b128 v[160:163], v192 offset:16384
	v_exp_f32_e32 v208, v72
	v_add_f32_e32 v207, 1.0, v207
	v_mfma_f32_32x32x16_f16 v[112:127], a[16:19], v[164:167], v[112:127]
	ds_read_b128 v[164:167], v192 offset:17408
	v_exp_f32_e32 v209, v73
	v_add_f32_e32 v208, 1.0, v208
	v_mfma_f32_32x32x16_f16 v[96:111], a[20:23], v[168:171], v[96:111]
	ds_read_b128 v[168:171], v192 offset:18432
	v_exp_f32_e32 v210, v74
	v_add_f32_e32 v209, 1.0, v209
	v_mfma_f32_32x32x16_f16 v[112:127], a[20:23], v[172:175], v[112:127]
	ds_read_b128 v[172:175], v192 offset:19456
	global_load_lds_dwordx4 v192, s[44:45] offset:3072 sc1
	v_exp_f32_e32 v211, v75
	v_add_f32_e32 v210, 1.0, v210
	s_waitcnt lgkmcnt(4)
	v_mfma_f32_32x32x16_f16 v[96:111], a[24:27], v[176:179], v[96:111]
	ds_read_b128 v[176:179], v192 offset:20480
	v_exp_f32_e32 v212, v76
	v_add_f32_e32 v211, 1.0, v211
	v_mfma_f32_32x32x16_f16 v[112:127], a[24:27], v[180:183], v[112:127]
	ds_read_b128 v[180:183], v192 offset:21504
	v_exp_f32_e32 v213, v77
	v_add_f32_e32 v212, 1.0, v212
	v_mfma_f32_32x32x16_f16 v[96:111], a[28:31], v[184:187], v[96:111]
	ds_read_b128 v[184:187], v192 offset:22528
	v_exp_f32_e32 v214, v78
	v_add_f32_e32 v213, 1.0, v213
	v_mfma_f32_32x32x16_f16 v[112:127], a[28:31], v[188:191], v[112:127]
	ds_read_b128 v[188:191], v192 offset:23552
	s_add_u32 s44, s34, 0x11000
	s_addc_u32 s45, s35, 0
	s_mov_b32 m0, s57
	s_nop 0
	global_load_lds_dwordx4 v192, s[44:45] sc1
	v_exp_f32_e32 v215, v79
	v_add_f32_e32 v214, 1.0, v214
	s_waitcnt lgkmcnt(4)
	v_mfma_f32_32x32x16_f16 v[96:111], a[32:35], v[160:163], v[96:111]
	ds_read_b128 v[160:163], v192 offset:24576
	v_add_f32_e32 v215, 1.0, v215
	v_rcp_f32_e32 v200, v200
	v_mfma_f32_32x32x16_f16 v[112:127], a[32:35], v[164:167], v[112:127]
	ds_read_b128 v[164:167], v192 offset:25600
	v_rcp_f32_e32 v201, v201
	v_mfma_f32_32x32x16_f16 v[96:111], a[36:39], v[168:171], v[96:111]
	ds_read_b128 v[168:171], v192 offset:26624
	v_rcp_f32_e32 v202, v202
	v_mfma_f32_32x32x16_f16 v[112:127], a[36:39], v[172:175], v[112:127]
	ds_read_b128 v[172:175], v192 offset:27648
	global_load_lds_dwordx4 v192, s[44:45] offset:1024 sc1
	v_rcp_f32_e32 v203, v203
	s_waitcnt lgkmcnt(4)
	v_mfma_f32_32x32x16_f16 v[96:111], a[40:43], v[176:179], v[96:111]
	ds_read_b128 v[176:179], v192 offset:28672
	v_rcp_f32_e32 v204, v204
	v_mfma_f32_32x32x16_f16 v[112:127], a[40:43], v[180:183], v[112:127]
	ds_read_b128 v[180:183], v192 offset:29696
	v_rcp_f32_e32 v205, v205
	v_mul_f32_e32 v204, v204, v144
	v_mfma_f32_32x32x16_f16 v[96:111], a[44:47], v[184:187], v[96:111]
	ds_read_b128 v[184:187], v192 offset:30720
	v_rcp_f32_e32 v206, v206
	v_mul_f32_e32 v205, v205, v145
	v_mfma_f32_32x32x16_f16 v[112:127], a[44:47], v[188:191], v[112:127]
	ds_read_b128 v[188:191], v192 offset:31744
	global_load_lds_dwordx4 v192, s[44:45] offset:2048 sc1
	v_rcp_f32_e32 v207, v207
	v_mul_f32_e32 v206, v206, v146
	s_waitcnt vmcnt(10)
	s_barrier
	s_waitcnt lgkmcnt(4)
	v_mfma_f32_32x32x16_f16 v[96:111], a[48:51], v[160:163], v[96:111]
	ds_read_b128 v[160:163], v192 offset:32768
	v_rcp_f32_e32 v208, v208
	v_mul_f32_e32 v207, v207, v147
	v_mfma_f32_32x32x16_f16 v[112:127], a[48:51], v[164:167], v[112:127]
	ds_read_b128 v[164:167], v192 offset:33792
	v_rcp_f32_e32 v209, v209
	v_fmamk_f32 v208, v208, 0xc0b8aa3b, v198
	v_mfma_f32_32x32x16_f16 v[96:111], a[52:55], v[168:171], v[96:111]
	ds_read_b128 v[168:171], v192 offset:34816
	v_rcp_f32_e32 v210, v210
	v_fmamk_f32 v209, v209, 0xc0b8aa3b, v198
	v_fma_f32 v144, v200, v208, v204
	v_mfma_f32_32x32x16_f16 v[112:127], a[52:55], v[172:175], v[112:127]
	ds_read_b128 v[172:175], v192 offset:35840
	global_load_lds_dwordx4 v192, s[44:45] offset:3072 sc1
	v_rcp_f32_e32 v211, v211
	v_fmamk_f32 v210, v210, 0xc0b8aa3b, v198
	v_fma_f32 v145, v201, v209, v205
	s_waitcnt lgkmcnt(4)
	v_mfma_f32_32x32x16_f16 v[96:111], a[56:59], v[176:179], v[96:111]
	ds_read_b128 v[176:179], v192 offset:36864
	v_rcp_f32_e32 v212, v212
	v_fmamk_f32 v211, v211, 0xc0b8aa3b, v198
	v_fma_f32 v146, v202, v210, v206
	v_mfma_f32_32x32x16_f16 v[112:127], a[56:59], v[180:183], v[112:127]
	ds_read_b128 v[180:183], v192 offset:37888
	v_rcp_f32_e32 v213, v213
	v_fma_f32 v147, v203, v211, v207
	v_mfma_f32_32x32x16_f16 v[96:111], a[60:63], v[184:187], v[96:111]
	ds_read_b128 v[184:187], v192 offset:38912
	v_rcp_f32_e32 v214, v214
	v_mfma_f32_32x32x16_f16 v[112:127], a[60:63], v[188:191], v[112:127]
	ds_read_b128 v[188:191], v192 offset:39936
	s_add_u32 s44, s34, 0x18000
	s_addc_u32 s45, s35, 0
	s_mov_b32 m0, s58
	s_nop 0
	global_load_lds_dwordx4 v192, s[44:45] sc1
	v_rcp_f32_e32 v215, v215
	s_waitcnt lgkmcnt(4)
	v_mfma_f32_32x32x16_f16 v[96:111], a[64:67], v[160:163], v[96:111]
	ds_read_b128 v[160:163], v192 offset:40960
	v_exp_f32_e32 v200, v144
	v_mfma_f32_32x32x16_f16 v[112:127], a[64:67], v[164:167], v[112:127]
	ds_read_b128 v[164:167], v192 offset:41984
	v_exp_f32_e32 v201, v145
	v_add_f32_e32 v200, 1.0, v200
	v_mfma_f32_32x32x16_f16 v[96:111], a[68:71], v[168:171], v[96:111]
	ds_read_b128 v[168:171], v192 offset:43008
	v_exp_f32_e32 v202, v146
	v_add_f32_e32 v201, 1.0, v201
	v_mfma_f32_32x32x16_f16 v[112:127], a[68:71], v[172:175], v[112:127]
	ds_read_b128 v[172:175], v192 offset:44032
	global_load_lds_dwordx4 v192, s[44:45] offset:1024 sc1
	v_exp_f32_e32 v203, v147
	v_add_f32_e32 v202, 1.0, v202
	s_waitcnt lgkmcnt(4)
	v_mfma_f32_32x32x16_f16 v[96:111], a[72:75], v[176:179], v[96:111]
	ds_read_b128 v[176:179], v192 offset:45056
	v_add_f32_e32 v203, 1.0, v203
	v_rcp_f32_e32 v200, v200
	v_mfma_f32_32x32x16_f16 v[112:127], a[72:75], v[180:183], v[112:127]
	ds_read_b128 v[180:183], v192 offset:46080
	v_rcp_f32_e32 v201, v201
	v_fma_f32 v200, v200, 2.0, -1.0
	v_mfma_f32_32x32x16_f16 v[96:111], a[76:79], v[184:187], v[96:111]
	ds_read_b128 v[184:187], v192 offset:47104
	v_rcp_f32_e32 v202, v202
	v_fma_f32 v201, v201, 2.0, -1.0
	v_mul_f32_e32 v216, v212, v200
	v_mfma_f32_32x32x16_f16 v[112:127], a[76:79], v[188:191], v[112:127]
	ds_read_b128 v[188:191], v192 offset:48128
	global_load_lds_dwordx4 v192, s[44:45] offset:2048 sc1
	v_rcp_f32_e32 v203, v203
	v_fma_f32 v202, v202, 2.0, -1.0
	v_mul_f32_e32 v217, v213, v201
	s_waitcnt lgkmcnt(4)
	v_mfma_f32_32x32x16_f16 v[96:111], a[80:83], v[160:163], v[96:111]
	ds_read_b128 v[160:163], v192 offset:49152
	v_fma_f32 v203, v203, 2.0, -1.0
	v_mul_f32_e32 v218, v214, v202
	v_exp_f32_e32 v200, v80
	v_mfma_f32_32x32x16_f16 v[112:127], a[80:83], v[164:167], v[112:127]
	ds_read_b128 v[164:167], v192 offset:50176
	v_mul_f32_e32 v219, v215, v203
	v_cvt_pk_f16_f32 v220, v216, v217
	v_exp_f32_e32 v201, v81
	v_mfma_f32_32x32x16_f16 v[96:111], a[84:87], v[168:171], v[96:111]
	ds_read_b128 v[168:171], v192 offset:51200
	v_cvt_pk_f16_f32 v221, v218, v219
	v_exp_f32_e32 v202, v82
	v_add_f32_e32 v200, 1.0, v200
	v_mfma_f32_32x32x16_f16 v[112:127], a[84:87], v[172:175], v[112:127]
	ds_read_b128 v[172:175], v192 offset:52224
	global_load_lds_dwordx4 v192, s[44:45] offset:3072 sc1
	s_cmp_eq_u32 s33, s60
	s_cbranch_scc1 .LE_ht46
.LE_htb47:
	v_exp_f32_e32 v203, v83
	s_waitcnt lgkmcnt(4)
	v_mfma_f32_32x32x16_f16 v[96:111], a[88:91], v[176:179], v[96:111]
	ds_read_b128 v[176:179], v192 offset:53248
	v_exp_f32_e32 v204, v84
	v_add_f32_e32 v201, 1.0, v201
	v_add_f32_e32 v202, 1.0, v202
	v_mfma_f32_32x32x16_f16 v[112:127], a[88:91], v[180:183], v[112:127]
	ds_read_b128 v[180:183], v192 offset:54272
	v_exp_f32_e32 v205, v85
	v_add_f32_e32 v203, 1.0, v203
	v_add_f32_e32 v204, 1.0, v204
	v_mfma_f32_32x32x16_f16 v[96:111], a[92:95], v[184:187], v[96:111]
	ds_read_b128 v[184:187], v192 offset:55296
	v_exp_f32_e32 v206, v86
	v_add_f32_e32 v205, 1.0, v205
	v_mfma_f32_32x32x16_f16 v[112:127], a[92:95], v[188:191], v[112:127]
	ds_read_b128 v[188:191], v192 offset:56320
	s_add_u32 s44, s34, 0x19000
	s_addc_u32 s45, s35, 0
	s_mov_b32 m0, s59
	s_nop 0
	global_load_lds_dwordx4 v192, s[44:45] sc1
	v_exp_f32_e32 v207, v87
	v_add_f32_e32 v206, 1.0, v206
	s_waitcnt lgkmcnt(4)
	v_mfma_f32_32x32x16_f16 v[96:111], a[96:99], v[160:163], v[96:111]
	ds_read_b128 v[160:163], v192 offset:57344
	v_exp_f32_e32 v208, v88
	v_add_f32_e32 v207, 1.0, v207
	v_mfma_f32_32x32x16_f16 v[112:127], a[96:99], v[164:167], v[112:127]
	ds_read_b128 v[164:167], v192 offset:58368
	v_exp_f32_e32 v209, v89
	v_add_f32_e32 v208, 1.0, v208
	v_mfma_f32_32x32x16_f16 v[96:111], a[100:103], v[168:171], v[96:111]
	ds_read_b128 v[168:171], v192 offset:59392
	v_exp_f32_e32 v210, v90
	v_add_f32_e32 v209, 1.0, v209
	v_mfma_f32_32x32x16_f16 v[112:127], a[100:103], v[172:175], v[112:127]
	ds_read_b128 v[172:175], v192 offset:60416
	global_load_lds_dwordx4 v192, s[44:45] offset:1024 sc1
	v_exp_f32_e32 v211, v91
	v_add_f32_e32 v210, 1.0, v210
	s_waitcnt lgkmcnt(4)
	v_mfma_f32_32x32x16_f16 v[96:111], a[104:107], v[176:179], v[96:111]
	ds_read_b128 v[176:179], v192 offset:61440
	v_exp_f32_e32 v212, v92
	v_add_f32_e32 v211, 1.0, v211
	v_mfma_f32_32x32x16_f16 v[112:127], a[104:107], v[180:183], v[112:127]
	ds_read_b128 v[180:183], v192 offset:62464
	v_exp_f32_e32 v213, v93
	v_add_f32_e32 v212, 1.0, v212
	v_mfma_f32_32x32x16_f16 v[96:111], a[108:111], v[184:187], v[96:111]
	ds_read_b128 v[184:187], v192 offset:63488
	v_exp_f32_e32 v214, v94
	v_add_f32_e32 v213, 1.0, v213
	v_mfma_f32_32x32x16_f16 v[112:127], a[108:111], v[188:191], v[112:127]
	ds_read_b128 v[188:191], v192 offset:64512
	global_load_lds_dwordx4 v192, s[44:45] offset:2048 sc1
	v_exp_f32_e32 v215, v95
	v_add_f32_e32 v214, 1.0, v214
	s_waitcnt vmcnt(7)
	s_barrier
	s_waitcnt lgkmcnt(4)
	v_mfma_f32_32x32x16_f16 v[96:111], a[112:115], v[160:163], v[96:111]
	ds_read_b128 v[160:163], v193 offset:0
	v_add_f32_e32 v215, 1.0, v215
	v_rcp_f32_e32 v200, v200
	v_mfma_f32_32x32x16_f16 v[112:127], a[112:115], v[164:167], v[112:127]
	ds_read_b128 v[164:167], v193 offset:1024
	v_rcp_f32_e32 v201, v201
	v_mfma_f32_32x32x16_f16 v[96:111], a[116:119], v[168:171], v[96:111]
	ds_read_b128 v[168:171], v193 offset:2048
	v_rcp_f32_e32 v202, v202
	v_mfma_f32_32x32x16_f16 v[112:127], a[116:119], v[172:175], v[112:127]
	ds_read_b128 v[172:175], v193 offset:3072
	global_load_lds_dwordx4 v192, s[44:45] offset:3072 sc1
	v_rcp_f32_e32 v203, v203
	s_waitcnt lgkmcnt(4)
	v_mfma_f32_32x32x16_f16 v[96:111], a[120:123], v[176:179], v[96:111]
	ds_read_b128 v[176:179], v193 offset:4096
	v_rcp_f32_e32 v204, v204
	v_mfma_f32_32x32x16_f16 v[112:127], a[120:123], v[180:183], v[112:127]
	ds_read_b128 v[180:183], v193 offset:5120
	v_rcp_f32_e32 v205, v205
	v_mul_f32_e32 v204, v204, v148
	v_mfma_f32_32x32x2_f32 v[32:47], v248, v228, v[232:247]
	v_mfma_f32_32x32x16_f16 v[96:111], a[124:127], v[184:187], v[96:111]
	ds_read_b128 v[184:187], v193 offset:6144
	v_rcp_f32_e32 v206, v206
	v_mul_f32_e32 v205, v205, v149
	v_mfma_f32_32x32x2_f32 v[48:63], v248, v229, v[232:247]
	v_mfma_f32_32x32x16_f16 v[112:127], a[124:127], v[188:191], v[112:127]
	ds_read_b128 v[188:191], v193 offset:7168
	v_cmp_gt_u32_e32 vcc, 1, v251
	s_cbranch_vccnz .LE_tpoll49
.LE_tok48:
	s_and_b32 s64, s33, 1
	s_lshl_b32 s64, s64, 22
	s_add_u32 s64, s64, s49
	s_add_u32 s34, s6, s64
	s_addc_u32 s35, s7, 0
	s_add_u32 s44, s34, 0x0
	s_addc_u32 s45, s35, 0
	s_mov_b32 m0, s52
	s_nop 0
	global_load_lds_dwordx4 v192, s[44:45] sc1
	v_rcp_f32_e32 v207, v207
	v_mul_f32_e32 v206, v206, v150
	s_waitcnt lgkmcnt(4)
	v_mfma_f32_32x32x16_f16 v[96:111], a[128:131], v[160:163], v[96:111]
	ds_read_b128 v[160:163], v193 offset:8192
	v_rcp_f32_e32 v208, v208
	v_mul_f32_e32 v207, v207, v151
	v_mfma_f32_32x32x16_f16 v[112:127], a[128:131], v[164:167], v[112:127]
	ds_read_b128 v[164:167], v193 offset:9216
	v_rcp_f32_e32 v209, v209
	v_fmamk_f32 v208, v208, 0xc0b8aa3b, v198
	v_mfma_f32_32x32x16_f16 v[96:111], a[132:135], v[168:171], v[96:111]
	ds_read_b128 v[168:171], v193 offset:10240
	v_rcp_f32_e32 v210, v210
	v_fmamk_f32 v209, v209, 0xc0b8aa3b, v198
	v_fma_f32 v148, v200, v208, v204
	v_mfma_f32_32x32x16_f16 v[112:127], a[132:135], v[172:175], v[112:127]
	ds_read_b128 v[172:175], v193 offset:11264
	global_load_lds_dwordx4 v192, s[44:45] offset:1024 sc1
	v_rcp_f32_e32 v211, v211
	v_fmamk_f32 v210, v210, 0xc0b8aa3b, v198
	v_fma_f32 v149, v201, v209, v205
	s_waitcnt lgkmcnt(4)
	v_mfma_f32_32x32x16_f16 v[96:111], a[136:139], v[176:179], v[96:111]
	ds_read_b128 v[176:179], v193 offset:12288
	v_rcp_f32_e32 v212, v212
	v_fmamk_f32 v211, v211, 0xc0b8aa3b, v198
	v_fma_f32 v150, v202, v210, v206
	v_mfma_f32_32x32x16_f16 v[112:127], a[136:139], v[180:183], v[112:127]
	ds_read_b128 v[180:183], v193 offset:13312
	v_rcp_f32_e32 v213, v213
	v_fma_f32 v151, v203, v211, v207
	v_mfma_f32_32x32x16_f16 v[96:111], a[140:143], v[184:187], v[96:111]
	ds_read_b128 v[184:187], v193 offset:14336
	v_rcp_f32_e32 v214, v214
	v_mfma_f32_32x32x16_f16 v[112:127], a[140:143], v[188:191], v[112:127]
	ds_read_b128 v[188:191], v193 offset:15360
	global_load_lds_dwordx4 v192, s[44:45] offset:2048 sc1
	v_rcp_f32_e32 v215, v215
	s_waitcnt lgkmcnt(4)
	v_mfma_f32_32x32x16_f16 v[96:111], a[144:147], v[160:163], v[96:111]
	ds_read_b128 v[160:163], v193 offset:16384
	v_exp_f32_e32 v200, v148
	v_mfma_f32_32x32x16_f16 v[112:127], a[144:147], v[164:167], v[112:127]
	ds_read_b128 v[164:167], v193 offset:17408
	v_exp_f32_e32 v201, v149
	v_add_f32_e32 v200, 1.0, v200
	v_mfma_f32_32x32x16_f16 v[96:111], a[148:151], v[168:171], v[96:111]
	ds_read_b128 v[168:171], v193 offset:18432
	v_exp_f32_e32 v202, v150
	v_add_f32_e32 v201, 1.0, v201
	v_mfma_f32_32x32x16_f16 v[112:127], a[148:151], v[172:175], v[112:127]
	ds_read_b128 v[172:175], v193 offset:19456
	global_load_lds_dwordx4 v192, s[44:45] offset:3072 sc1
	v_exp_f32_e32 v203, v151
	v_add_f32_e32 v202, 1.0, v202
	s_waitcnt lgkmcnt(4)
	v_mfma_f32_32x32x16_f16 v[96:111], a[152:155], v[176:179], v[96:111]
	ds_read_b128 v[176:179], v193 offset:20480
	v_add_f32_e32 v203, 1.0, v203
	v_rcp_f32_e32 v200, v200
	v_mfma_f32_32x32x16_f16 v[112:127], a[152:155], v[180:183], v[112:127]
	ds_read_b128 v[180:183], v193 offset:21504
	v_rcp_f32_e32 v201, v201
	v_fma_f32 v200, v200, 2.0, -1.0
	v_mfma_f32_32x32x16_f16 v[96:111], a[156:159], v[184:187], v[96:111]
	ds_read_b128 v[184:187], v193 offset:22528
	v_rcp_f32_e32 v202, v202
	v_fma_f32 v201, v201, 2.0, -1.0
	v_mul_f32_e32 v216, v212, v200
	v_mfma_f32_32x32x16_f16 v[112:127], a[156:159], v[188:191], v[112:127]
	ds_read_b128 v[188:191], v193 offset:23552
	s_add_u32 s44, s34, 0x1000
	s_addc_u32 s45, s35, 0
	s_mov_b32 m0, s53
	s_nop 0
	global_load_lds_dwordx4 v192, s[44:45] sc1
	v_rcp_f32_e32 v203, v203
	v_fma_f32 v202, v202, 2.0, -1.0
	v_mul_f32_e32 v217, v213, v201
	s_waitcnt lgkmcnt(4)
	v_mfma_f32_32x32x16_f16 v[96:111], a[160:163], v[160:163], v[96:111]
	ds_read_b128 v[160:163], v193 offset:24576
	v_fma_f32 v203, v203, 2.0, -1.0
	v_mul_f32_e32 v218, v214, v202
	v_mfma_f32_32x32x16_f16 v[112:127], a[160:163], v[164:167], v[112:127]
	ds_read_b128 v[164:167], v193 offset:25600
	v_mul_f32_e32 v219, v215, v203
	v_cvt_pk_f16_f32 v222, v216, v217
	v_mfma_f32_32x32x16_f16 v[96:111], a[164:167], v[168:171], v[96:111]
	ds_read_b128 v[168:171], v193 offset:26624
	v_cvt_pk_f16_f32 v223, v218, v219
	v_mfma_f32_32x32x16_f16 v[112:127], a[164:167], v[172:175], v[112:127]
	ds_read_b128 v[172:175], v193 offset:27648
	global_load_lds_dwordx4 v192, s[44:45] offset:1024 sc1
	s_cmp_eq_u32 s33, s60
	s_cbranch_scc1 .LE_ht50
.LE_htb51:
	s_waitcnt lgkmcnt(4)
	v_mfma_f32_32x32x16_f16 v[96:111], a[168:171], v[176:179], v[96:111]
	ds_read_b128 v[176:179], v193 offset:28672
	s_nop 1
	v_permlane32_swap_b32_e32 v220, v222
	v_permlane32_swap_b32_e32 v221, v223
	s_cmp_eq_u32 s31, 0
	s_cbranch_scc1 .LE_slow52
	global_store_dwordx4 v195, v[220:223], s[36:37] offset:0
.LE_join53:
	v_mfma_f32_32x32x16_f16 v[112:127], a[168:171], v[180:183], v[112:127]
	ds_read_b128 v[180:183], v193 offset:29696
	v_mfma_f32_32x32x16_f16 v[96:111], a[172:175], v[184:187], v[96:111]
	ds_read_b128 v[184:187], v193 offset:30720
	v_mfma_f32_32x32x16_f16 v[112:127], a[172:175], v[188:191], v[112:127]
	ds_read_b128 v[188:191], v193 offset:31744
	global_load_lds_dwordx4 v192, s[44:45] offset:2048 sc1
	s_waitcnt vmcnt(8)
	s_barrier
	s_waitcnt lgkmcnt(4)
	v_mfma_f32_32x32x16_f16 v[96:111], a[176:179], v[160:163], v[96:111]
	ds_read_b128 v[160:163], v193 offset:32768
	v_mfma_f32_32x32x16_f16 v[112:127], a[176:179], v[164:167], v[112:127]
	ds_read_b128 v[164:167], v193 offset:33792
	v_mfma_f32_32x32x16_f16 v[96:111], a[180:183], v[168:171], v[96:111]
	ds_read_b128 v[168:171], v193 offset:34816
	v_mfma_f32_32x32x16_f16 v[112:127], a[180:183], v[172:175], v[112:127]
	ds_read_b128 v[172:175], v193 offset:35840
	global_load_lds_dwordx4 v192, s[44:45] offset:3072 sc1
	s_waitcnt lgkmcnt(4)
	v_mfma_f32_32x32x16_f16 v[96:111], a[184:187], v[176:179], v[96:111]
	ds_read_b128 v[176:179], v193 offset:36864
	v_mfma_f32_32x32x16_f16 v[112:127], a[184:187], v[180:183], v[112:127]
	ds_read_b128 v[180:183], v193 offset:37888
	v_mfma_f32_32x32x16_f16 v[96:111], a[188:191], v[184:187], v[96:111]
	ds_read_b128 v[184:187], v193 offset:38912
	v_mfma_f32_32x32x16_f16 v[112:127], a[188:191], v[188:191], v[112:127]
	ds_read_b128 v[188:191], v193 offset:39936
	s_add_u32 s44, s34, 0x8000
	s_addc_u32 s45, s35, 0
	s_mov_b32 m0, s54
	s_nop 0
	global_load_lds_dwordx4 v192, s[44:45] sc1
	s_waitcnt lgkmcnt(4)
	v_mfma_f32_32x32x16_f16 v[96:111], a[192:195], v[160:163], v[96:111]
	ds_read_b128 v[160:163], v193 offset:40960
	v_mfma_f32_32x32x16_f16 v[112:127], a[192:195], v[164:167], v[112:127]
	ds_read_b128 v[164:167], v193 offset:41984
	s_waitcnt vmcnt(3)
	s_barrier
	v_mov_b32_e32 v199, 3
	s_cmp_eq_u32 s31, 0
	s_cbranch_scc1 .LE_slow54
	global_store_dword v197, v199, s[40:41]
.LE_join55:
	v_mfma_f32_32x32x16_f16 v[96:111], a[196:199], v[168:171], v[96:111]
	ds_read_b128 v[168:171], v193 offset:43008
	v_mfma_f32_32x32x16_f16 v[112:127], a[196:199], v[172:175], v[112:127]
	ds_read_b128 v[172:175], v193 offset:44032
	global_load_lds_dwordx4 v192, s[44:45] offset:1024 sc1
	s_waitcnt lgkmcnt(4)
	v_mfma_f32_32x32x16_f16 v[96:111], a[200:203], v[176:179], v[96:111]
	ds_read_b128 v[176:179], v193 offset:45056
	v_mfma_f32_32x32x16_f16 v[112:127], a[200:203], v[180:183], v[112:127]
	ds_read_b128 v[180:183], v193 offset:46080
	v_mfma_f32_32x32x16_f16 v[96:111], a[204:207], v[184:187], v[96:111]
	ds_read_b128 v[184:187], v193 offset:47104
	v_mfma_f32_32x32x16_f16 v[112:127], a[204:207], v[188:191], v[112:127]
	ds_read_b128 v[188:191], v193 offset:48128
	global_load_lds_dwordx4 v192, s[44:45] offset:2048 sc1
	s_waitcnt lgkmcnt(4)
	v_mfma_f32_32x32x16_f16 v[96:111], a[208:211], v[160:163], v[96:111]
	ds_read_b128 v[160:163], v193 offset:49152
	v_mfma_f32_32x32x16_f16 v[112:127], a[208:211], v[164:167], v[112:127]
	ds_read_b128 v[164:167], v193 offset:50176
	v_mfma_f32_32x32x16_f16 v[96:111], a[212:215], v[168:171], v[96:111]
	ds_read_b128 v[168:171], v193 offset:51200
	v_mfma_f32_32x32x16_f16 v[112:127], a[212:215], v[172:175], v[112:127]
	ds_read_b128 v[172:175], v193 offset:52224
	global_load_lds_dwordx4 v192, s[44:45] offset:3072 sc1
	s_waitcnt lgkmcnt(4)
	v_mfma_f32_32x32x16_f16 v[96:111], a[216:219], v[176:179], v[96:111]
	ds_read_b128 v[176:179], v193 offset:53248
	v_mfma_f32_32x32x16_f16 v[112:127], a[216:219], v[180:183], v[112:127]
	ds_read_b128 v[180:183], v193 offset:54272
	v_mfma_f32_32x32x16_f16 v[96:111], a[220:223], v[184:187], v[96:111]
	ds_read_b128 v[184:187], v193 offset:55296
	v_mfma_f32_32x32x16_f16 v[112:127], a[220:223], v[188:191], v[112:127]
	ds_read_b128 v[188:191], v193 offset:56320
	s_add_u32 s44, s34, 0x9000
	s_addc_u32 s45, s35, 0
	s_mov_b32 m0, s55
	s_nop 0
	global_load_lds_dwordx4 v192, s[44:45] sc1
	s_waitcnt lgkmcnt(4)
	v_mfma_f32_32x32x16_f16 v[96:111], a[224:227], v[160:163], v[96:111]
	ds_read_b128 v[160:163], v193 offset:57344
	v_mfma_f32_32x32x16_f16 v[112:127], a[224:227], v[164:167], v[112:127]
	ds_read_b128 v[164:167], v193 offset:58368
	v_mfma_f32_32x32x16_f16 v[96:111], a[228:231], v[168:171], v[96:111]
	ds_read_b128 v[168:171], v193 offset:59392
	v_mfma_f32_32x32x16_f16 v[112:127], a[228:231], v[172:175], v[112:127]
	ds_read_b128 v[172:175], v193 offset:60416
	global_load_lds_dwordx4 v192, s[44:45] offset:1024 sc1
	s_waitcnt lgkmcnt(4)
	v_mfma_f32_32x32x16_f16 v[96:111], a[232:235], v[176:179], v[96:111]
	ds_read_b128 v[176:179], v193 offset:61440
	v_mfma_f32_32x32x16_f16 v[112:127], a[232:235], v[180:183], v[112:127]
	ds_read_b128 v[180:183], v193 offset:62464
	v_mfma_f32_32x32x16_f16 v[96:111], a[236:239], v[184:187], v[96:111]
	ds_read_b128 v[184:187], v193 offset:63488
	v_mfma_f32_32x32x16_f16 v[112:127], a[236:239], v[188:191], v[112:127]
	ds_read_b128 v[188:191], v193 offset:64512
	global_load_lds_dwordx4 v192, s[44:45] offset:2048 sc1
	s_waitcnt vmcnt(8)
	s_barrier
	s_waitcnt lgkmcnt(4)
	v_mfma_f32_32x32x16_f16 v[96:111], a[240:243], v[160:163], v[96:111]
	ds_read_b128 v[160:163], v192 offset:0
	v_mfma_f32_32x32x16_f16 v[112:127], a[240:243], v[164:167], v[112:127]
	ds_read_b128 v[164:167], v192 offset:1024
	v_mfma_f32_32x32x16_f16 v[96:111], a[244:247], v[168:171], v[96:111]
	ds_read_b128 v[168:171], v192 offset:2048
	v_mfma_f32_32x32x16_f16 v[112:127], a[244:247], v[172:175], v[112:127]
	ds_read_b128 v[172:175], v192 offset:3072
	global_load_lds_dwordx4 v192, s[44:45] offset:3072 sc1
	s_waitcnt lgkmcnt(4)
	v_mfma_f32_32x32x16_f16 v[96:111], a[248:251], v[176:179], v[96:111]
	ds_read_b128 v[176:179], v192 offset:4096
	v_mfma_f32_32x32x16_f16 v[112:127], a[248:251], v[180:183], v[112:127]
	ds_read_b128 v[180:183], v192 offset:5120
	v_mfma_f32_32x32x16_f16 v[96:111], a[252:255], v[184:187], v[96:111]
	ds_read_b128 v[184:187], v192 offset:6144
	v_mfma_f32_32x32x16_f16 v[112:127], a[252:255], v[188:191], v[112:127]
	ds_read_b128 v[188:191], v192 offset:7168
	s_add_u32 s44, s34, 0x10000
	s_addc_u32 s45, s35, 0
	s_mov_b32 m0, s56
	s_nop 0
	global_load_lds_dwordx4 v192, s[44:45] sc1
	s_add_u32 s33, s33, 1
	s_cmp_lt_u32 s33, s28
	s_cbranch_scc1 .LE_loop16

.LE_slow4:
	global_store_dwordx4 v195, v[220:223], s[36:37] offset:0 sc1
	s_branch .LE_join5
.LE_slow6:
	global_store_dword v197, v199, s[40:41] sc1
	s_branch .LE_join7

.LE_tpoll21:
	s_cmp_eq_u32 s48, 0
	s_cbranch_scc1 .LE_tok20
	s_sub_u32 s48, s48, 1
	s_sleep 1
	global_load_dword v251, v196, s[38:39] sc1
	s_waitcnt vmcnt(0)
	v_cmp_gt_u32_e32 vcc, 2, v251
	s_cbranch_vccnz .LE_tpoll21
	s_branch .LE_tok20

.LE_ht26:
	s_add_u32 s46, s62, 0x0
	s_addc_u32 s47, s63, 0
	global_store_dwordx4 v250, v[216:219], s[46:47]
	s_waitcnt vmcnt(0)
	s_branch .LE_htb27
.LE_tpoll29:
	s_cmp_eq_u32 s48, 0
	s_cbranch_scc1 .LE_tok28
	s_sub_u32 s48, s48, 1
	s_sleep 1
	global_load_dword v251, v196, s[38:39] sc1
	s_waitcnt vmcnt(0)
	v_cmp_gt_u32_e32 vcc, 3, v251
	s_cbranch_vccnz .LE_tpoll29
	s_branch .LE_tok28
.LE_ht30:
	s_add_u32 s46, s62, 0x20000
	s_addc_u32 s47, s63, 0
	global_store_dwordx4 v250, v[216:219], s[46:47]
	s_waitcnt vmcnt(0)
	s_branch .LE_htb31

.LE_ht36:
	s_add_u32 s46, s62, 0x40000
	s_addc_u32 s47, s63, 0
	global_store_dwordx4 v250, v[216:219], s[46:47]
	s_waitcnt vmcnt(0)
	s_branch .LE_htb37
.LE_tpoll39:
	s_cmp_eq_u32 s48, 0
	s_cbranch_scc1 .LE_tok38
	s_sub_u32 s48, s48, 1
	s_sleep 1
	global_load_dword v251, v196, s[38:39] sc1
	s_waitcnt vmcnt(0)
	v_cmp_gt_u32_e32 vcc, 4, v251
	s_cbranch_vccnz .LE_tpoll39
	s_branch .LE_tok38
.LE_ht40:
	s_add_u32 s46, s62, 0x60000
	s_addc_u32 s47, s63, 0
	global_store_dwordx4 v250, v[216:219], s[46:47]
	s_waitcnt vmcnt(0)
	s_branch .LE_htb41

.LE_ht46:
	s_add_u32 s46, s62, 0x80000
	s_addc_u32 s47, s63, 0
	global_store_dwordx4 v250, v[216:219], s[46:47]
	s_waitcnt vmcnt(0)
	s_branch .LE_htb47
.LE_tpoll49:
	s_cmp_eq_u32 s48, 0
	s_cbranch_scc1 .LE_tok48
	s_sub_u32 s48, s48, 1
	s_sleep 1
	global_load_dword v251, v196, s[38:39] sc1
	s_waitcnt vmcnt(0)
	v_cmp_gt_u32_e32 vcc, 1, v251
	s_cbranch_vccnz .LE_tpoll49
	s_branch .LE_tok48
.LE_ht50:
	s_add_u32 s46, s62, 0xa0000
	s_addc_u32 s47, s63, 0
	global_store_dwordx4 v250, v[216:219], s[46:47]
	s_waitcnt vmcnt(0)
	s_branch .LE_htb51

.LE_slow54:
	global_store_dword v197, v199, s[40:41] sc1
	s_branch .LE_join55
	.p2align 8

.LD_cdone1:
	s_waitcnt lgkmcnt(0)
	s_barrier
	v_mov_b32_e32 v252, 0x22000
	ds_read_b32 v200, v252
	ds_read_b32 v201, v252 offset:4
	ds_read_b32 v202, v252 offset:8
	s_waitcnt lgkmcnt(0)
	s_nop 1
	v_readfirstlane_b32 s31, v200
	v_readfirstlane_b32 s29, v201
	v_readfirstlane_b32 s30, v202
	s_nop 3
	s_barrier
	s_lshl_b32 s49, s29, 19
	s_lshl_b32 s64, s32, 13
	s_add_u32 s49, s49, s64
	s_mov_b32 s51, s64
	s_add_u32 s52, s51, 0x0
	s_add_u32 s53, s51, 0x1000
	s_add_u32 s54, s51, 0x8000
	s_add_u32 s55, s51, 0x9000
	s_add_u32 s56, s51, 0x10000
	s_add_u32 s57, s51, 0x11000
	s_add_u32 s58, s51, 0x18000
	s_add_u32 s59, s51, 0x19000
	s_lshl_b32 s64, s29, 8
	s_lshl_b32 s65, s30, 1
	s_add_u32 s64, s64, s65
	s_lshr_b32 s65, s32, 1
	s_add_u32 s64, s64, s65
	s_lshl_b32 s64, s64, 11
	s_and_b32 s65, s32, 1
	s_lshl_b32 s65, s65, 9
	s_add_u32 s50, s64, s65
	s_sub_u32 s60, s28, 1
	s_lshl_b32 s64, s30, 2
	s_add_u32 s64, s64, s32
	s_lshl_b32 s64, s64, 16
	s_add_u32 s44, s4, s64
	s_addc_u32 s45, s5, 0
	global_load_dwordx4 a[0:3], v192, s[44:45] offset:0
	global_load_dwordx4 a[4:7], v192, s[44:45] offset:1024
	global_load_dwordx4 a[8:11], v192, s[44:45] offset:2048
	global_load_dwordx4 a[12:15], v192, s[44:45] offset:3072
	s_add_u32 s44, s44, 0x1000
	s_addc_u32 s45, s45, 0
	global_load_dwordx4 a[16:19], v192, s[44:45] offset:0
	global_load_dwordx4 a[20:23], v192, s[44:45] offset:1024
	global_load_dwordx4 a[24:27], v192, s[44:45] offset:2048
	global_load_dwordx4 a[28:31], v192, s[44:45] offset:3072
	s_add_u32 s44, s44, 0x1000
	s_addc_u32 s45, s45, 0
	global_load_dwordx4 a[32:35], v192, s[44:45] offset:0
	global_load_dwordx4 a[36:39], v192, s[44:45] offset:1024
	global_load_dwordx4 a[40:43], v192, s[44:45] offset:2048
	global_load_dwordx4 a[44:47], v192, s[44:45] offset:3072
	s_add_u32 s44, s44, 0x1000
	s_addc_u32 s45, s45, 0
	global_load_dwordx4 a[48:51], v192, s[44:45] offset:0
	global_load_dwordx4 a[52:55], v192, s[44:45] offset:1024
	global_load_dwordx4 a[56:59], v192, s[44:45] offset:2048
	global_load_dwordx4 a[60:63], v192, s[44:45] offset:3072
	s_add_u32 s44, s44, 0x1000
	s_addc_u32 s45, s45, 0
	global_load_dwordx4 a[64:67], v192, s[44:45] offset:0
	global_load_dwordx4 a[68:71], v192, s[44:45] offset:1024
	global_load_dwordx4 a[72:75], v192, s[44:45] offset:2048
	global_load_dwordx4 a[76:79], v192, s[44:45] offset:3072
	s_add_u32 s44, s44, 0x1000
	s_addc_u32 s45, s45, 0
	global_load_dwordx4 a[80:83], v192, s[44:45] offset:0
	global_load_dwordx4 a[84:87], v192, s[44:45] offset:1024
	global_load_dwordx4 a[88:91], v192, s[44:45] offset:2048
	global_load_dwordx4 a[92:95], v192, s[44:45] offset:3072
	s_add_u32 s44, s44, 0x1000
	s_addc_u32 s45, s45, 0
	global_load_dwordx4 a[96:99], v192, s[44:45] offset:0
	global_load_dwordx4 a[100:103], v192, s[44:45] offset:1024
	global_load_dwordx4 a[104:107], v192, s[44:45] offset:2048
	global_load_dwordx4 a[108:111], v192, s[44:45] offset:3072
	s_add_u32 s44, s44, 0x1000
	s_addc_u32 s45, s45, 0
	global_load_dwordx4 a[112:115], v192, s[44:45] offset:0
	global_load_dwordx4 a[116:119], v192, s[44:45] offset:1024
	global_load_dwordx4 a[120:123], v192, s[44:45] offset:2048
	global_load_dwordx4 a[124:127], v192, s[44:45] offset:3072
	s_add_u32 s44, s44, 0x1000
	s_addc_u32 s45, s45, 0
	s_waitcnt vmcnt(16)
	global_load_dwordx4 a[128:131], v192, s[44:45] offset:0
	global_load_dwordx4 a[132:135], v192, s[44:45] offset:1024
	global_load_dwordx4 a[136:139], v192, s[44:45] offset:2048
	global_load_dwordx4 a[140:143], v192, s[44:45] offset:3072
	s_add_u32 s44, s44, 0x1000
	s_addc_u32 s45, s45, 0
	global_load_dwordx4 a[144:147], v192, s[44:45] offset:0
	global_load_dwordx4 a[148:151], v192, s[44:45] offset:1024
	global_load_dwordx4 a[152:155], v192, s[44:45] offset:2048
	global_load_dwordx4 a[156:159], v192, s[44:45] offset:3072
	s_add_u32 s44, s44, 0x1000
	s_addc_u32 s45, s45, 0
	global_load_dwordx4 a[160:163], v192, s[44:45] offset:0
	global_load_dwordx4 a[164:167], v192, s[44:45] offset:1024
	global_load_dwordx4 a[168:171], v192, s[44:45] offset:2048
	global_load_dwordx4 a[172:175], v192, s[44:45] offset:3072
	s_add_u32 s44, s44, 0x1000
	s_addc_u32 s45, s45, 0
	global_load_dwordx4 a[176:179], v192, s[44:45] offset:0
	global_load_dwordx4 a[180:183], v192, s[44:45] offset:1024
	global_load_dwordx4 a[184:187], v192, s[44:45] offset:2048
	global_load_dwordx4 a[188:191], v192, s[44:45] offset:3072
	s_add_u32 s44, s44, 0x1000
	s_addc_u32 s45, s45, 0
	global_load_dwordx4 a[192:195], v192, s[44:45] offset:0
	global_load_dwordx4 a[196:199], v192, s[44:45] offset:1024
	global_load_dwordx4 a[200:203], v192, s[44:45] offset:2048
	global_load_dwordx4 a[204:207], v192, s[44:45] offset:3072
	s_add_u32 s44, s44, 0x1000
	s_addc_u32 s45, s45, 0
	global_load_dwordx4 a[208:211], v192, s[44:45] offset:0
	global_load_dwordx4 a[212:215], v192, s[44:45] offset:1024
	global_load_dwordx4 a[216:219], v192, s[44:45] offset:2048
	global_load_dwordx4 a[220:223], v192, s[44:45] offset:3072
	s_add_u32 s44, s44, 0x1000
	s_addc_u32 s45, s45, 0
	global_load_dwordx4 a[224:227], v192, s[44:45] offset:0
	global_load_dwordx4 a[228:231], v192, s[44:45] offset:1024
	global_load_dwordx4 a[232:235], v192, s[44:45] offset:2048
	global_load_dwordx4 a[236:239], v192, s[44:45] offset:3072
	s_add_u32 s44, s44, 0x1000
	s_addc_u32 s45, s45, 0
	global_load_dwordx4 a[240:243], v192, s[44:45] offset:0
	global_load_dwordx4 a[244:247], v192, s[44:45] offset:1024
	global_load_dwordx4 a[248:251], v192, s[44:45] offset:2048
	global_load_dwordx4 a[252:255], v192, s[44:45] offset:3072
	s_add_u32 s44, s44, 0x1000
	s_addc_u32 s45, s45, 0
	v_mov_b32_e32 v128, 0
	v_mov_b32_e32 v129, 0
	v_mov_b32_e32 v130, 0
	v_mov_b32_e32 v131, 0
	v_mov_b32_e32 v132, 0
	v_mov_b32_e32 v133, 0
	v_mov_b32_e32 v134, 0
	v_mov_b32_e32 v135, 0
	v_mov_b32_e32 v136, 0
	v_mov_b32_e32 v137, 0
	v_mov_b32_e32 v138, 0
	v_mov_b32_e32 v139, 0
	v_mov_b32_e32 v140, 0
	v_mov_b32_e32 v141, 0
	v_mov_b32_e32 v142, 0
	v_mov_b32_e32 v143, 0
	v_mov_b32_e32 v144, 0
	v_mov_b32_e32 v145, 0
	v_mov_b32_e32 v146, 0
	v_mov_b32_e32 v147, 0
	v_mov_b32_e32 v148, 0
	v_mov_b32_e32 v149, 0
	v_mov_b32_e32 v150, 0
	v_mov_b32_e32 v151, 0
	v_mov_b32_e32 v152, 0
	v_mov_b32_e32 v153, 0
	v_mov_b32_e32 v154, 0
	v_mov_b32_e32 v155, 0
	v_mov_b32_e32 v156, 0
	v_mov_b32_e32 v157, 0
	v_mov_b32_e32 v158, 0
	v_mov_b32_e32 v159, 0
	s_lshl_b32 s64, s30, 5
	s_lshl_b32 s65, s32, 3
	s_add_u32 s64, s64, s65
	v_lshlrev_b32_e32 v255, 2, v254
	v_add_u32_e32 v255, s64, v255
	v_lshlrev_b32_e32 v200, 2, v255
	global_load_dwordx4 v[228:231], v200, s[22:23]
	v_add_u32_e32 v201, 0x1000, v200
	global_load_dwordx4 v[232:235], v201, s[22:23]
	s_lshl_b32 s65, s32, 11
	v_lshl_add_u32 v248, v253, 3, s65
	v_add_u32_e32 v248, 0x20000, v248
	v_and_b32_e32 v250, 15, v194
	s_mul_i32 s65, s32, 128
	v_lshl_add_u32 v249, v250, 3, s65
	v_add_u32_e32 v249, 0x20000, v249
	v_lshlrev_b32_e32 v250, 3, v250
	s_lshl_b32 s65, s30, 11
	s_lshl_b32 s66, s29, 8
	s_add_u32 s65, s65, s66
	s_mul_i32 s66, s32, 16
	s_add_u32 s65, s65, s66
	s_lshl_b32 s65, s65, 3
	s_add_u32 s62, s24, s65
	s_addc_u32 s63, s25, 0
	s_lshl_b32 s65, s29, 5
	s_add_u32 s65, s65, s30
	s_lshl_b32 s65, s65, 2
	s_add_u32 s65, s65, s32
	s_lshl_b32 s65, s65, 15
	s_add_u32 s42, s18, s65
	s_addc_u32 s43, s19, 0
	s_waitcnt vmcnt(0)
	s_waitcnt vmcnt(0)
	s_mov_b32 s33, 0
	s_add_u32 s46, s42, 0x0
	s_addc_u32 s47, s43, 0
	global_load_dwordx4 v[0:3], v192, s[46:47] offset:0
	global_load_dwordx4 v[4:7], v192, s[46:47] offset:1024
	global_load_dwordx4 v[8:11], v192, s[46:47] offset:2048
	global_load_dwordx4 v[12:15], v192, s[46:47] offset:3072
	s_add_u32 s46, s42, 0x1000
	s_addc_u32 s47, s43, 0
	global_load_dwordx4 v[16:19], v192, s[46:47] offset:0
	global_load_dwordx4 v[20:23], v192, s[46:47] offset:1024
	global_load_dwordx4 v[24:27], v192, s[46:47] offset:2048
	global_load_dwordx4 v[28:31], v192, s[46:47] offset:3072
	s_add_u32 s46, s42, 0x2000
	s_addc_u32 s47, s43, 0
	global_load_dwordx4 v[32:35], v192, s[46:47] offset:0
	global_load_dwordx4 v[36:39], v192, s[46:47] offset:1024
	global_load_dwordx4 v[40:43], v192, s[46:47] offset:2048
	global_load_dwordx4 v[44:47], v192, s[46:47] offset:3072
	s_add_u32 s46, s42, 0x3000
	s_addc_u32 s47, s43, 0
	global_load_dwordx4 v[48:51], v192, s[46:47] offset:0
	global_load_dwordx4 v[52:55], v192, s[46:47] offset:1024
	global_load_dwordx4 v[56:59], v192, s[46:47] offset:2048
	global_load_dwordx4 v[60:63], v192, s[46:47] offset:3072
	s_add_u32 s46, s42, 0x4000
	s_addc_u32 s47, s43, 0
	global_load_dwordx4 v[64:67], v192, s[46:47] offset:0
	global_load_dwordx4 v[68:71], v192, s[46:47] offset:1024
	global_load_dwordx4 v[72:75], v192, s[46:47] offset:2048
	global_load_dwordx4 v[76:79], v192, s[46:47] offset:3072
	s_add_u32 s46, s42, 0x5000
	s_addc_u32 s47, s43, 0
	global_load_dwordx4 v[80:83], v192, s[46:47] offset:0
	global_load_dwordx4 v[84:87], v192, s[46:47] offset:1024
	global_load_dwordx4 v[88:91], v192, s[46:47] offset:2048
	global_load_dwordx4 v[92:95], v192, s[46:47] offset:3072
	s_add_u32 s46, s42, 0x6000
	s_addc_u32 s47, s43, 0
	global_load_dwordx4 v[96:99], v192, s[46:47] offset:0
	global_load_dwordx4 v[100:103], v192, s[46:47] offset:1024
	global_load_dwordx4 v[104:107], v192, s[46:47] offset:2048
	global_load_dwordx4 v[108:111], v192, s[46:47] offset:3072
	s_add_u32 s46, s42, 0x7000
	s_addc_u32 s47, s43, 0
	global_load_dwordx4 v[112:115], v192, s[46:47] offset:0
	global_load_dwordx4 v[116:119], v192, s[46:47] offset:1024
	global_load_dwordx4 v[120:123], v192, s[46:47] offset:2048
	global_load_dwordx4 v[124:127], v192, s[46:47] offset:3072
	s_waitcnt vmcnt(0)
	s_waitcnt lgkmcnt(0)
	s_lshl_b32 s64, s33, 3
	s_add_u32 s64, s64, s29
	s_lshl_b32 s64, s64, 5
	s_add_u32 s64, s64, s30
	s_lshl_b32 s64, s64, 2
	s_add_u32 s40, s8, s64
	s_addc_u32 s41, s9, 0
	s_and_b32 s64, s33, 1
	s_lshl_b32 s64, s64, 22
	s_add_u32 s64, s64, s50
	s_add_u32 s36, s6, s64
	s_addc_u32 s37, s7, 0
	s_lshl_b32 s64, s33, 19
	s_add_u32 s72, s62, s64
	s_addc_u32 s73, s63, 0
	v_exp_f32_e32 v200, v0
	v_exp_f32_e32 v201, v1
	v_exp_f32_e32 v202, v2
	v_exp_f32_e32 v203, v3
	v_exp_f32_e32 v204, v4
	v_exp_f32_e32 v205, v5
	v_exp_f32_e32 v206, v6
	v_exp_f32_e32 v207, v7
	v_exp_f32_e32 v208, v8
	v_exp_f32_e32 v209, v9
	v_exp_f32_e32 v210, v10
	v_exp_f32_e32 v211, v11
	v_exp_f32_e32 v212, v12
	v_exp_f32_e32 v213, v13
	v_exp_f32_e32 v214, v14
	v_exp_f32_e32 v215, v15
	v_add_f32_e32 v200, 1.0, v200
	v_add_f32_e32 v201, 1.0, v201
	v_add_f32_e32 v202, 1.0, v202
	v_add_f32_e32 v203, 1.0, v203
	v_add_f32_e32 v204, 1.0, v204
	v_add_f32_e32 v205, 1.0, v205
	v_add_f32_e32 v206, 1.0, v206
	v_add_f32_e32 v207, 1.0, v207
	v_add_f32_e32 v208, 1.0, v208
	v_add_f32_e32 v209, 1.0, v209
	v_add_f32_e32 v210, 1.0, v210
	v_add_f32_e32 v211, 1.0, v211
	v_add_f32_e32 v212, 1.0, v212
	v_add_f32_e32 v213, 1.0, v213
	v_add_f32_e32 v214, 1.0, v214
	v_add_f32_e32 v215, 1.0, v215
	v_rcp_f32_e32 v200, v200
	v_rcp_f32_e32 v201, v201
	v_rcp_f32_e32 v202, v202
	v_rcp_f32_e32 v203, v203
	v_rcp_f32_e32 v204, v204
	v_rcp_f32_e32 v205, v205
	v_rcp_f32_e32 v206, v206
	v_rcp_f32_e32 v207, v207
	v_rcp_f32_e32 v208, v208
	v_rcp_f32_e32 v209, v209
	v_rcp_f32_e32 v210, v210
	v_rcp_f32_e32 v211, v211
	v_rcp_f32_e32 v212, v212
	v_rcp_f32_e32 v213, v213
	v_rcp_f32_e32 v214, v214
	v_rcp_f32_e32 v215, v215
	v_fmamk_f32 v208, v208, 0xc0b8aa3b, v198
	v_fmamk_f32 v209, v209, 0xc0b8aa3b, v198
	v_fmamk_f32 v210, v210, 0xc0b8aa3b, v198
	v_fmamk_f32 v211, v211, 0xc0b8aa3b, v198
	v_mul_f32_e32 v204, v204, v128
	v_mul_f32_e32 v205, v205, v129
	v_mul_f32_e32 v206, v206, v130
	v_mul_f32_e32 v207, v207, v131
	v_fma_f32 v128, v200, v208, v204
	v_fma_f32 v129, v201, v209, v205
	v_fma_f32 v130, v202, v210, v206
	v_fma_f32 v131, v203, v211, v207
	v_exp_f32_e32 v200, v128
	v_exp_f32_e32 v201, v129
	v_exp_f32_e32 v202, v130
	v_exp_f32_e32 v203, v131
	v_add_f32_e32 v200, 1.0, v200
	v_add_f32_e32 v201, 1.0, v201
	v_add_f32_e32 v202, 1.0, v202
	v_add_f32_e32 v203, 1.0, v203
	v_rcp_f32_e32 v200, v200
	v_rcp_f32_e32 v201, v201
	v_rcp_f32_e32 v202, v202
	v_rcp_f32_e32 v203, v203
	v_fma_f32 v200, v200, 2.0, -1.0
	v_fma_f32 v201, v201, 2.0, -1.0
	v_fma_f32 v202, v202, 2.0, -1.0
	v_fma_f32 v203, v203, 2.0, -1.0
	v_mul_f32_e32 v216, v212, v200
	v_mul_f32_e32 v217, v213, v201
	v_mul_f32_e32 v218, v214, v202
	v_mul_f32_e32 v219, v215, v203
	v_mul_f32_e32 v236, v216, v228
	v_mul_f32_e32 v237, v216, v232
	v_fmac_f32_e32 v236, v217, v229
	v_fmac_f32_e32 v237, v217, v233
	v_fmac_f32_e32 v236, v218, v230
	v_fmac_f32_e32 v237, v218, v234
	v_fmac_f32_e32 v236, v219, v231
	v_fmac_f32_e32 v237, v219, v235
	v_mov_b32_e32 v238, v236
	v_mov_b32_e32 v239, v236
	v_mov_b32_e32 v240, v237
	v_mov_b32_e32 v241, v237
	s_nop 1
	v_permlane32_swap_b32_e32 v238, v239
	v_permlane32_swap_b32_e32 v240, v241
	v_add_f32_e32 v238, v238, v239
	v_add_f32_e32 v239, v240, v241
	ds_write_b64 v248, v[238:239] offset:0
	v_cvt_pk_f16_f32 v220, v216, v217
	v_cvt_pk_f16_f32 v221, v218, v219
	v_exp_f32_e32 v200, v16
	v_exp_f32_e32 v201, v17
	v_exp_f32_e32 v202, v18
	v_exp_f32_e32 v203, v19
	v_exp_f32_e32 v204, v20
	v_exp_f32_e32 v205, v21
	v_exp_f32_e32 v206, v22
	v_exp_f32_e32 v207, v23
	v_exp_f32_e32 v208, v24
	v_exp_f32_e32 v209, v25
	v_exp_f32_e32 v210, v26
	v_exp_f32_e32 v211, v27
	v_exp_f32_e32 v212, v28
	v_exp_f32_e32 v213, v29
	v_exp_f32_e32 v214, v30
	v_exp_f32_e32 v215, v31
	v_add_f32_e32 v200, 1.0, v200
	v_add_f32_e32 v201, 1.0, v201
	v_add_f32_e32 v202, 1.0, v202
	v_add_f32_e32 v203, 1.0, v203
	v_add_f32_e32 v204, 1.0, v204
	v_add_f32_e32 v205, 1.0, v205
	v_add_f32_e32 v206, 1.0, v206
	v_add_f32_e32 v207, 1.0, v207
	v_add_f32_e32 v208, 1.0, v208
	v_add_f32_e32 v209, 1.0, v209
	v_add_f32_e32 v210, 1.0, v210
	v_add_f32_e32 v211, 1.0, v211
	v_add_f32_e32 v212, 1.0, v212
	v_add_f32_e32 v213, 1.0, v213
	v_add_f32_e32 v214, 1.0, v214
	v_add_f32_e32 v215, 1.0, v215
	v_rcp_f32_e32 v200, v200
	v_rcp_f32_e32 v201, v201
	v_rcp_f32_e32 v202, v202
	v_rcp_f32_e32 v203, v203
	v_rcp_f32_e32 v204, v204
	v_rcp_f32_e32 v205, v205
	v_rcp_f32_e32 v206, v206
	v_rcp_f32_e32 v207, v207
	v_rcp_f32_e32 v208, v208
	v_rcp_f32_e32 v209, v209
	v_rcp_f32_e32 v210, v210
	v_rcp_f32_e32 v211, v211
	v_rcp_f32_e32 v212, v212
	v_rcp_f32_e32 v213, v213
	v_rcp_f32_e32 v214, v214
	v_rcp_f32_e32 v215, v215
	v_fmamk_f32 v208, v208, 0xc0b8aa3b, v198
	v_fmamk_f32 v209, v209, 0xc0b8aa3b, v198
	v_fmamk_f32 v210, v210, 0xc0b8aa3b, v198
	v_fmamk_f32 v211, v211, 0xc0b8aa3b, v198
	v_mul_f32_e32 v204, v204, v132
	v_mul_f32_e32 v205, v205, v133
	v_mul_f32_e32 v206, v206, v134
	v_mul_f32_e32 v207, v207, v135
	v_fma_f32 v132, v200, v208, v204
	v_fma_f32 v133, v201, v209, v205
	v_fma_f32 v134, v202, v210, v206
	v_fma_f32 v135, v203, v211, v207
	v_exp_f32_e32 v200, v132
	v_exp_f32_e32 v201, v133
	v_exp_f32_e32 v202, v134
	v_exp_f32_e32 v203, v135
	v_add_f32_e32 v200, 1.0, v200
	v_add_f32_e32 v201, 1.0, v201
	v_add_f32_e32 v202, 1.0, v202
	v_add_f32_e32 v203, 1.0, v203
	v_rcp_f32_e32 v200, v200
	v_rcp_f32_e32 v201, v201
	v_rcp_f32_e32 v202, v202
	v_rcp_f32_e32 v203, v203
	v_fma_f32 v200, v200, 2.0, -1.0
	v_fma_f32 v201, v201, 2.0, -1.0
	v_fma_f32 v202, v202, 2.0, -1.0
	v_fma_f32 v203, v203, 2.0, -1.0
	v_mul_f32_e32 v216, v212, v200
	v_mul_f32_e32 v217, v213, v201
	v_mul_f32_e32 v218, v214, v202
	v_mul_f32_e32 v219, v215, v203
	v_mul_f32_e32 v236, v216, v228
	v_mul_f32_e32 v237, v216, v232
	v_fmac_f32_e32 v236, v217, v229
	v_fmac_f32_e32 v237, v217, v233
	v_fmac_f32_e32 v236, v218, v230
	v_fmac_f32_e32 v237, v218, v234
	v_fmac_f32_e32 v236, v219, v231
	v_fmac_f32_e32 v237, v219, v235
	v_mov_b32_e32 v238, v236
	v_mov_b32_e32 v239, v236
	v_mov_b32_e32 v240, v237
	v_mov_b32_e32 v241, v237
	s_nop 1
	v_permlane32_swap_b32_e32 v238, v239
	v_permlane32_swap_b32_e32 v240, v241
	v_add_f32_e32 v238, v238, v239
	v_add_f32_e32 v239, v240, v241
	ds_write_b64 v248, v[238:239] offset:256
	v_cvt_pk_f16_f32 v222, v216, v217
	v_cvt_pk_f16_f32 v223, v218, v219
	s_nop 1
	v_permlane32_swap_b32_e32 v220, v222
	v_permlane32_swap_b32_e32 v221, v223
	s_cmp_eq_u32 s31, 0
	s_cbranch_scc1 .LD_slow4
	global_store_dwordx4 v195, v[220:223], s[36:37] offset:0
.LD_join5:
	s_waitcnt vmcnt(0)
	s_waitcnt lgkmcnt(0)
	s_barrier
	v_mov_b32_e32 v199, 1
	s_cmp_eq_u32 s31, 0
	s_cbranch_scc1 .LD_slow6
	global_store_dword v197, v199, s[40:41]
.LD_join7:
	ds_read_b64 v[200:201], v249 offset:0
	ds_read_b64 v[202:203], v249 offset:2048
	ds_read_b64 v[204:205], v249 offset:4096
	ds_read_b64 v[206:207], v249 offset:6144
	s_waitcnt lgkmcnt(0)
	v_add_f32_e32 v200, v200, v202
	v_add_f32_e32 v201, v201, v203
	v_add_f32_e32 v200, v200, v204
	v_add_f32_e32 v201, v201, v205
	v_add_f32_e32 v200, v200, v206
	v_add_f32_e32 v201, v201, v207
	global_store_dwordx2 v250, v[200:201], s[72:73]
	s_and_b32 s64, s33, 1
	s_lshl_b32 s64, s64, 22
	s_add_u32 s64, s64, s50
	s_add_u32 s64, s64, 0x20000
	s_add_u32 s36, s6, s64
	s_addc_u32 s37, s7, 0
	s_lshl_b32 s64, s33, 19
	s_add_u32 s64, s64, 0x200
	s_add_u32 s72, s62, s64
	s_addc_u32 s73, s63, 0
	v_exp_f32_e32 v200, v32
	v_exp_f32_e32 v201, v33
	v_exp_f32_e32 v202, v34
	v_exp_f32_e32 v203, v35
	v_exp_f32_e32 v204, v36
	v_exp_f32_e32 v205, v37
	v_exp_f32_e32 v206, v38
	v_exp_f32_e32 v207, v39
	v_exp_f32_e32 v208, v40
	v_exp_f32_e32 v209, v41
	v_exp_f32_e32 v210, v42
	v_exp_f32_e32 v211, v43
	v_exp_f32_e32 v212, v44
	v_exp_f32_e32 v213, v45
	v_exp_f32_e32 v214, v46
	v_exp_f32_e32 v215, v47
	v_add_f32_e32 v200, 1.0, v200
	v_add_f32_e32 v201, 1.0, v201
	v_add_f32_e32 v202, 1.0, v202
	v_add_f32_e32 v203, 1.0, v203
	v_add_f32_e32 v204, 1.0, v204
	v_add_f32_e32 v205, 1.0, v205
	v_add_f32_e32 v206, 1.0, v206
	v_add_f32_e32 v207, 1.0, v207
	v_add_f32_e32 v208, 1.0, v208
	v_add_f32_e32 v209, 1.0, v209
	v_add_f32_e32 v210, 1.0, v210
	v_add_f32_e32 v211, 1.0, v211
	v_add_f32_e32 v212, 1.0, v212
	v_add_f32_e32 v213, 1.0, v213
	v_add_f32_e32 v214, 1.0, v214
	v_add_f32_e32 v215, 1.0, v215
	v_rcp_f32_e32 v200, v200
	v_rcp_f32_e32 v201, v201
	v_rcp_f32_e32 v202, v202
	v_rcp_f32_e32 v203, v203
	v_rcp_f32_e32 v204, v204
	v_rcp_f32_e32 v205, v205
	v_rcp_f32_e32 v206, v206
	v_rcp_f32_e32 v207, v207
	v_rcp_f32_e32 v208, v208
	v_rcp_f32_e32 v209, v209
	v_rcp_f32_e32 v210, v210
	v_rcp_f32_e32 v211, v211
	v_rcp_f32_e32 v212, v212
	v_rcp_f32_e32 v213, v213
	v_rcp_f32_e32 v214, v214
	v_rcp_f32_e32 v215, v215
	v_fmamk_f32 v208, v208, 0xc0b8aa3b, v198
	v_fmamk_f32 v209, v209, 0xc0b8aa3b, v198
	v_fmamk_f32 v210, v210, 0xc0b8aa3b, v198
	v_fmamk_f32 v211, v211, 0xc0b8aa3b, v198
	v_mul_f32_e32 v204, v204, v136
	v_mul_f32_e32 v205, v205, v137
	v_mul_f32_e32 v206, v206, v138
	v_mul_f32_e32 v207, v207, v139
	v_fma_f32 v136, v200, v208, v204
	v_fma_f32 v137, v201, v209, v205
	v_fma_f32 v138, v202, v210, v206
	v_fma_f32 v139, v203, v211, v207
	v_exp_f32_e32 v200, v136
	v_exp_f32_e32 v201, v137
	v_exp_f32_e32 v202, v138
	v_exp_f32_e32 v203, v139
	v_add_f32_e32 v200, 1.0, v200
	v_add_f32_e32 v201, 1.0, v201
	v_add_f32_e32 v202, 1.0, v202
	v_add_f32_e32 v203, 1.0, v203
	v_rcp_f32_e32 v200, v200
	v_rcp_f32_e32 v201, v201
	v_rcp_f32_e32 v202, v202
	v_rcp_f32_e32 v203, v203
	v_fma_f32 v200, v200, 2.0, -1.0
	v_fma_f32 v201, v201, 2.0, -1.0
	v_fma_f32 v202, v202, 2.0, -1.0
	v_fma_f32 v203, v203, 2.0, -1.0
	v_mul_f32_e32 v216, v212, v200
	v_mul_f32_e32 v217, v213, v201
	v_mul_f32_e32 v218, v214, v202
	v_mul_f32_e32 v219, v215, v203
	v_mul_f32_e32 v236, v216, v228
	v_mul_f32_e32 v237, v216, v232
	v_fmac_f32_e32 v236, v217, v229
	v_fmac_f32_e32 v237, v217, v233
	v_fmac_f32_e32 v236, v218, v230
	v_fmac_f32_e32 v237, v218, v234
	v_fmac_f32_e32 v236, v219, v231
	v_fmac_f32_e32 v237, v219, v235
	v_mov_b32_e32 v238, v236
	v_mov_b32_e32 v239, v236
	v_mov_b32_e32 v240, v237
	v_mov_b32_e32 v241, v237
	s_nop 1
	v_permlane32_swap_b32_e32 v238, v239
	v_permlane32_swap_b32_e32 v240, v241
	v_add_f32_e32 v238, v238, v239
	v_add_f32_e32 v239, v240, v241
	ds_write_b64 v248, v[238:239] offset:512
	v_cvt_pk_f16_f32 v220, v216, v217
	v_cvt_pk_f16_f32 v221, v218, v219
	v_exp_f32_e32 v200, v48
	v_exp_f32_e32 v201, v49
	v_exp_f32_e32 v202, v50
	v_exp_f32_e32 v203, v51
	v_exp_f32_e32 v204, v52
	v_exp_f32_e32 v205, v53
	v_exp_f32_e32 v206, v54
	v_exp_f32_e32 v207, v55
	v_exp_f32_e32 v208, v56
	v_exp_f32_e32 v209, v57
	v_exp_f32_e32 v210, v58
	v_exp_f32_e32 v211, v59
	v_exp_f32_e32 v212, v60
	v_exp_f32_e32 v213, v61
	v_exp_f32_e32 v214, v62
	v_exp_f32_e32 v215, v63
	v_add_f32_e32 v200, 1.0, v200
	v_add_f32_e32 v201, 1.0, v201
	v_add_f32_e32 v202, 1.0, v202
	v_add_f32_e32 v203, 1.0, v203
	v_add_f32_e32 v204, 1.0, v204
	v_add_f32_e32 v205, 1.0, v205
	v_add_f32_e32 v206, 1.0, v206
	v_add_f32_e32 v207, 1.0, v207
	v_add_f32_e32 v208, 1.0, v208
	v_add_f32_e32 v209, 1.0, v209
	v_add_f32_e32 v210, 1.0, v210
	v_add_f32_e32 v211, 1.0, v211
	v_add_f32_e32 v212, 1.0, v212
	v_add_f32_e32 v213, 1.0, v213
	v_add_f32_e32 v214, 1.0, v214
	v_add_f32_e32 v215, 1.0, v215
	v_rcp_f32_e32 v200, v200
	v_rcp_f32_e32 v201, v201
	v_rcp_f32_e32 v202, v202
	v_rcp_f32_e32 v203, v203
	v_rcp_f32_e32 v204, v204
	v_rcp_f32_e32 v205, v205
	v_rcp_f32_e32 v206, v206
	v_rcp_f32_e32 v207, v207
	v_rcp_f32_e32 v208, v208
	v_rcp_f32_e32 v209, v209
	v_rcp_f32_e32 v210, v210
	v_rcp_f32_e32 v211, v211
	v_rcp_f32_e32 v212, v212
	v_rcp_f32_e32 v213, v213
	v_rcp_f32_e32 v214, v214
	v_rcp_f32_e32 v215, v215
	v_fmamk_f32 v208, v208, 0xc0b8aa3b, v198
	v_fmamk_f32 v209, v209, 0xc0b8aa3b, v198
	v_fmamk_f32 v210, v210, 0xc0b8aa3b, v198
	v_fmamk_f32 v211, v211, 0xc0b8aa3b, v198
	v_mul_f32_e32 v204, v204, v140
	v_mul_f32_e32 v205, v205, v141
	v_mul_f32_e32 v206, v206, v142
	v_mul_f32_e32 v207, v207, v143
	v_fma_f32 v140, v200, v208, v204
	v_fma_f32 v141, v201, v209, v205
	v_fma_f32 v142, v202, v210, v206
	v_fma_f32 v143, v203, v211, v207
	v_exp_f32_e32 v200, v140
	v_exp_f32_e32 v201, v141
	v_exp_f32_e32 v202, v142
	v_exp_f32_e32 v203, v143
	v_add_f32_e32 v200, 1.0, v200
	v_add_f32_e32 v201, 1.0, v201
	v_add_f32_e32 v202, 1.0, v202
	v_add_f32_e32 v203, 1.0, v203
	v_rcp_f32_e32 v200, v200
	v_rcp_f32_e32 v201, v201
	v_rcp_f32_e32 v202, v202
	v_rcp_f32_e32 v203, v203
	v_fma_f32 v200, v200, 2.0, -1.0
	v_fma_f32 v201, v201, 2.0, -1.0
	v_fma_f32 v202, v202, 2.0, -1.0
	v_fma_f32 v203, v203, 2.0, -1.0
	v_mul_f32_e32 v216, v212, v200
	v_mul_f32_e32 v217, v213, v201
	v_mul_f32_e32 v218, v214, v202
	v_mul_f32_e32 v219, v215, v203
	v_mul_f32_e32 v236, v216, v228
	v_mul_f32_e32 v237, v216, v232
	v_fmac_f32_e32 v236, v217, v229
	v_fmac_f32_e32 v237, v217, v233
	v_fmac_f32_e32 v236, v218, v230
	v_fmac_f32_e32 v237, v218, v234
	v_fmac_f32_e32 v236, v219, v231
	v_fmac_f32_e32 v237, v219, v235
	v_mov_b32_e32 v238, v236
	v_mov_b32_e32 v239, v236
	v_mov_b32_e32 v240, v237
	v_mov_b32_e32 v241, v237
	s_nop 1
	v_permlane32_swap_b32_e32 v238, v239
	v_permlane32_swap_b32_e32 v240, v241
	v_add_f32_e32 v238, v238, v239
	v_add_f32_e32 v239, v240, v241
	ds_write_b64 v248, v[238:239] offset:768
	v_cvt_pk_f16_f32 v222, v216, v217
	v_cvt_pk_f16_f32 v223, v218, v219
	s_nop 1
	v_permlane32_swap_b32_e32 v220, v222
	v_permlane32_swap_b32_e32 v221, v223
	s_cmp_eq_u32 s31, 0
	s_cbranch_scc1 .LD_slow8
	global_store_dwordx4 v195, v[220:223], s[36:37] offset:0
.LD_join9:
	s_waitcnt vmcnt(0)
	s_waitcnt lgkmcnt(0)
	s_barrier
	v_mov_b32_e32 v199, 2
	s_cmp_eq_u32 s31, 0
	s_cbranch_scc1 .LD_slow10
	global_store_dword v197, v199, s[40:41]
.LD_join11:
	ds_read_b64 v[200:201], v249 offset:512
	ds_read_b64 v[202:203], v249 offset:2560
	ds_read_b64 v[204:205], v249 offset:4608
	ds_read_b64 v[206:207], v249 offset:6656
	s_waitcnt lgkmcnt(0)
	v_add_f32_e32 v200, v200, v202
	v_add_f32_e32 v201, v201, v203
	v_add_f32_e32 v200, v200, v204
	v_add_f32_e32 v201, v201, v205
	v_add_f32_e32 v200, v200, v206
	v_add_f32_e32 v201, v201, v207
	global_store_dwordx2 v250, v[200:201], s[72:73]
	s_and_b32 s64, s33, 1
	s_lshl_b32 s64, s64, 22
	s_add_u32 s64, s64, s50
	s_add_u32 s64, s64, 0x40000
	s_add_u32 s36, s6, s64
	s_addc_u32 s37, s7, 0
	s_lshl_b32 s64, s33, 19
	s_add_u32 s64, s64, 0x400
	s_add_u32 s72, s62, s64
	s_addc_u32 s73, s63, 0
	v_exp_f32_e32 v200, v64
	v_exp_f32_e32 v201, v65
	v_exp_f32_e32 v202, v66
	v_exp_f32_e32 v203, v67
	v_exp_f32_e32 v204, v68
	v_exp_f32_e32 v205, v69
	v_exp_f32_e32 v206, v70
	v_exp_f32_e32 v207, v71
	v_exp_f32_e32 v208, v72
	v_exp_f32_e32 v209, v73
	v_exp_f32_e32 v210, v74
	v_exp_f32_e32 v211, v75
	v_exp_f32_e32 v212, v76
	v_exp_f32_e32 v213, v77
	v_exp_f32_e32 v214, v78
	v_exp_f32_e32 v215, v79
	v_add_f32_e32 v200, 1.0, v200
	v_add_f32_e32 v201, 1.0, v201
	v_add_f32_e32 v202, 1.0, v202
	v_add_f32_e32 v203, 1.0, v203
	v_add_f32_e32 v204, 1.0, v204
	v_add_f32_e32 v205, 1.0, v205
	v_add_f32_e32 v206, 1.0, v206
	v_add_f32_e32 v207, 1.0, v207
	v_add_f32_e32 v208, 1.0, v208
	v_add_f32_e32 v209, 1.0, v209
	v_add_f32_e32 v210, 1.0, v210
	v_add_f32_e32 v211, 1.0, v211
	v_add_f32_e32 v212, 1.0, v212
	v_add_f32_e32 v213, 1.0, v213
	v_add_f32_e32 v214, 1.0, v214
	v_add_f32_e32 v215, 1.0, v215
	v_rcp_f32_e32 v200, v200
	v_rcp_f32_e32 v201, v201
	v_rcp_f32_e32 v202, v202
	v_rcp_f32_e32 v203, v203
	v_rcp_f32_e32 v204, v204
	v_rcp_f32_e32 v205, v205
	v_rcp_f32_e32 v206, v206
	v_rcp_f32_e32 v207, v207
	v_rcp_f32_e32 v208, v208
	v_rcp_f32_e32 v209, v209
	v_rcp_f32_e32 v210, v210
	v_rcp_f32_e32 v211, v211
	v_rcp_f32_e32 v212, v212
	v_rcp_f32_e32 v213, v213
	v_rcp_f32_e32 v214, v214
	v_rcp_f32_e32 v215, v215
	v_fmamk_f32 v208, v208, 0xc0b8aa3b, v198
	v_fmamk_f32 v209, v209, 0xc0b8aa3b, v198
	v_fmamk_f32 v210, v210, 0xc0b8aa3b, v198
	v_fmamk_f32 v211, v211, 0xc0b8aa3b, v198
	v_mul_f32_e32 v204, v204, v144
	v_mul_f32_e32 v205, v205, v145
	v_mul_f32_e32 v206, v206, v146
	v_mul_f32_e32 v207, v207, v147
	v_fma_f32 v144, v200, v208, v204
	v_fma_f32 v145, v201, v209, v205
	v_fma_f32 v146, v202, v210, v206
	v_fma_f32 v147, v203, v211, v207
	v_exp_f32_e32 v200, v144
	v_exp_f32_e32 v201, v145
	v_exp_f32_e32 v202, v146
	v_exp_f32_e32 v203, v147
	v_add_f32_e32 v200, 1.0, v200
	v_add_f32_e32 v201, 1.0, v201
	v_add_f32_e32 v202, 1.0, v202
	v_add_f32_e32 v203, 1.0, v203
	v_rcp_f32_e32 v200, v200
	v_rcp_f32_e32 v201, v201
	v_rcp_f32_e32 v202, v202
	v_rcp_f32_e32 v203, v203
	v_fma_f32 v200, v200, 2.0, -1.0
	v_fma_f32 v201, v201, 2.0, -1.0
	v_fma_f32 v202, v202, 2.0, -1.0
	v_fma_f32 v203, v203, 2.0, -1.0
	v_mul_f32_e32 v216, v212, v200
	v_mul_f32_e32 v217, v213, v201
	v_mul_f32_e32 v218, v214, v202
	v_mul_f32_e32 v219, v215, v203
	v_mul_f32_e32 v236, v216, v228
	v_mul_f32_e32 v237, v216, v232
	v_fmac_f32_e32 v236, v217, v229
	v_fmac_f32_e32 v237, v217, v233
	v_fmac_f32_e32 v236, v218, v230
	v_fmac_f32_e32 v237, v218, v234
	v_fmac_f32_e32 v236, v219, v231
	v_fmac_f32_e32 v237, v219, v235
	v_mov_b32_e32 v238, v236
	v_mov_b32_e32 v239, v236
	v_mov_b32_e32 v240, v237
	v_mov_b32_e32 v241, v237
	s_nop 1
	v_permlane32_swap_b32_e32 v238, v239
	v_permlane32_swap_b32_e32 v240, v241
	v_add_f32_e32 v238, v238, v239
	v_add_f32_e32 v239, v240, v241
	ds_write_b64 v248, v[238:239] offset:1024
	v_cvt_pk_f16_f32 v220, v216, v217
	v_cvt_pk_f16_f32 v221, v218, v219
	v_exp_f32_e32 v200, v80
	v_exp_f32_e32 v201, v81
	v_exp_f32_e32 v202, v82
	v_exp_f32_e32 v203, v83
	v_exp_f32_e32 v204, v84
	v_exp_f32_e32 v205, v85
	v_exp_f32_e32 v206, v86
	v_exp_f32_e32 v207, v87
	v_exp_f32_e32 v208, v88
	v_exp_f32_e32 v209, v89
	v_exp_f32_e32 v210, v90
	v_exp_f32_e32 v211, v91
	v_exp_f32_e32 v212, v92
	v_exp_f32_e32 v213, v93
	v_exp_f32_e32 v214, v94
	v_exp_f32_e32 v215, v95
	v_add_f32_e32 v200, 1.0, v200
	v_add_f32_e32 v201, 1.0, v201
	v_add_f32_e32 v202, 1.0, v202
	v_add_f32_e32 v203, 1.0, v203
	v_add_f32_e32 v204, 1.0, v204
	v_add_f32_e32 v205, 1.0, v205
	v_add_f32_e32 v206, 1.0, v206
	v_add_f32_e32 v207, 1.0, v207
	v_add_f32_e32 v208, 1.0, v208
	v_add_f32_e32 v209, 1.0, v209
	v_add_f32_e32 v210, 1.0, v210
	v_add_f32_e32 v211, 1.0, v211
	v_add_f32_e32 v212, 1.0, v212
	v_add_f32_e32 v213, 1.0, v213
	v_add_f32_e32 v214, 1.0, v214
	v_add_f32_e32 v215, 1.0, v215
	v_rcp_f32_e32 v200, v200
	v_rcp_f32_e32 v201, v201
	v_rcp_f32_e32 v202, v202
	v_rcp_f32_e32 v203, v203
	v_rcp_f32_e32 v204, v204
	v_rcp_f32_e32 v205, v205
	v_rcp_f32_e32 v206, v206
	v_rcp_f32_e32 v207, v207
	v_rcp_f32_e32 v208, v208
	v_rcp_f32_e32 v209, v209
	v_rcp_f32_e32 v210, v210
	v_rcp_f32_e32 v211, v211
	v_rcp_f32_e32 v212, v212
	v_rcp_f32_e32 v213, v213
	v_rcp_f32_e32 v214, v214
	v_rcp_f32_e32 v215, v215
	v_fmamk_f32 v208, v208, 0xc0b8aa3b, v198
	v_fmamk_f32 v209, v209, 0xc0b8aa3b, v198
	v_fmamk_f32 v210, v210, 0xc0b8aa3b, v198
	v_fmamk_f32 v211, v211, 0xc0b8aa3b, v198
	v_mul_f32_e32 v204, v204, v148
	v_mul_f32_e32 v205, v205, v149
	v_mul_f32_e32 v206, v206, v150
	v_mul_f32_e32 v207, v207, v151
	v_fma_f32 v148, v200, v208, v204
	v_fma_f32 v149, v201, v209, v205
	v_fma_f32 v150, v202, v210, v206
	v_fma_f32 v151, v203, v211, v207
	v_exp_f32_e32 v200, v148
	v_exp_f32_e32 v201, v149
	v_exp_f32_e32 v202, v150
	v_exp_f32_e32 v203, v151
	v_add_f32_e32 v200, 1.0, v200
	v_add_f32_e32 v201, 1.0, v201
	v_add_f32_e32 v202, 1.0, v202
	v_add_f32_e32 v203, 1.0, v203
	v_rcp_f32_e32 v200, v200
	v_rcp_f32_e32 v201, v201
	v_rcp_f32_e32 v202, v202
	v_rcp_f32_e32 v203, v203
	v_fma_f32 v200, v200, 2.0, -1.0
	v_fma_f32 v201, v201, 2.0, -1.0
	v_fma_f32 v202, v202, 2.0, -1.0
	v_fma_f32 v203, v203, 2.0, -1.0
	v_mul_f32_e32 v216, v212, v200
	v_mul_f32_e32 v217, v213, v201
	v_mul_f32_e32 v218, v214, v202
	v_mul_f32_e32 v219, v215, v203
	v_mul_f32_e32 v236, v216, v228
	v_mul_f32_e32 v237, v216, v232
	v_fmac_f32_e32 v236, v217, v229
	v_fmac_f32_e32 v237, v217, v233
	v_fmac_f32_e32 v236, v218, v230
	v_fmac_f32_e32 v237, v218, v234
	v_fmac_f32_e32 v236, v219, v231
	v_fmac_f32_e32 v237, v219, v235
	v_mov_b32_e32 v238, v236
	v_mov_b32_e32 v239, v236
	v_mov_b32_e32 v240, v237
	v_mov_b32_e32 v241, v237
	s_nop 1
	v_permlane32_swap_b32_e32 v238, v239
	v_permlane32_swap_b32_e32 v240, v241
	v_add_f32_e32 v238, v238, v239
	v_add_f32_e32 v239, v240, v241
	ds_write_b64 v248, v[238:239] offset:1280
	v_cvt_pk_f16_f32 v222, v216, v217
	v_cvt_pk_f16_f32 v223, v218, v219
	s_nop 1
	v_permlane32_swap_b32_e32 v220, v222
	v_permlane32_swap_b32_e32 v221, v223
	s_cmp_eq_u32 s31, 0
	s_cbranch_scc1 .LD_slow12
	global_store_dwordx4 v195, v[220:223], s[36:37] offset:0
.LD_join13:
	s_waitcnt vmcnt(0)
	s_waitcnt lgkmcnt(0)
	s_barrier
	v_mov_b32_e32 v199, 3
	s_cmp_eq_u32 s31, 0
	s_cbranch_scc1 .LD_slow14
	global_store_dword v197, v199, s[40:41]
.LD_join15:
	ds_read_b64 v[200:201], v249 offset:1024
	ds_read_b64 v[202:203], v249 offset:3072
	ds_read_b64 v[204:205], v249 offset:5120
	ds_read_b64 v[206:207], v249 offset:7168
	s_waitcnt lgkmcnt(0)
	v_add_f32_e32 v200, v200, v202
	v_add_f32_e32 v201, v201, v203
	v_add_f32_e32 v200, v200, v204
	v_add_f32_e32 v201, v201, v205
	v_add_f32_e32 v200, v200, v206
	v_add_f32_e32 v201, v201, v207
	global_store_dwordx2 v250, v[200:201], s[72:73]
	s_mov_b32 s33, 1
	s_add_u32 s46, s42, 0x0
	s_addc_u32 s47, s43, 0
	global_load_dwordx4 v[0:3], v192, s[46:47] offset:0
	global_load_dwordx4 v[4:7], v192, s[46:47] offset:1024
	global_load_dwordx4 v[8:11], v192, s[46:47] offset:2048
	global_load_dwordx4 v[12:15], v192, s[46:47] offset:3072
	s_add_u32 s46, s42, 0x1000
	s_addc_u32 s47, s43, 0
	global_load_dwordx4 v[16:19], v192, s[46:47] offset:0
	global_load_dwordx4 v[20:23], v192, s[46:47] offset:1024
	global_load_dwordx4 v[24:27], v192, s[46:47] offset:2048
	global_load_dwordx4 v[28:31], v192, s[46:47] offset:3072
	s_add_u32 s46, s42, 0x2000
	s_addc_u32 s47, s43, 0
	global_load_dwordx4 v[32:35], v192, s[46:47] offset:0
	global_load_dwordx4 v[36:39], v192, s[46:47] offset:1024
	global_load_dwordx4 v[40:43], v192, s[46:47] offset:2048
	global_load_dwordx4 v[44:47], v192, s[46:47] offset:3072
	s_add_u32 s46, s42, 0x3000
	s_addc_u32 s47, s43, 0
	global_load_dwordx4 v[48:51], v192, s[46:47] offset:0
	global_load_dwordx4 v[52:55], v192, s[46:47] offset:1024
	global_load_dwordx4 v[56:59], v192, s[46:47] offset:2048
	global_load_dwordx4 v[60:63], v192, s[46:47] offset:3072
	s_waitcnt vmcnt(0)
	s_waitcnt lgkmcnt(0)
	s_cmp_ge_u32 s33, s28
	s_cbranch_scc1 .LD_end17
	s_sub_u32 s71, s33, 1
	s_and_b32 s64, s71, 1
	s_lshl_b32 s64, s64, 22
	s_add_u32 s64, s64, s49
	s_add_u32 s34, s6, s64
	s_addc_u32 s35, s7, 0
	s_lshl_b32 s64, s71, 3
	s_add_u32 s64, s64, s29
	s_lshl_b32 s64, s64, 7
	s_add_u32 s38, s8, s64
	s_addc_u32 s39, s9, 0

.LD_loop16:
	s_sub_u32 s71, s33, 1
	s_add_u32 s61, s33, 1
	s_min_u32 s61, s61, s60
	s_and_b32 s64, s71, 1
	s_lshl_b32 s64, s64, 22
	s_add_u32 s64, s64, s50
	s_add_u32 s64, s64, 0x60000
	s_add_u32 s36, s6, s64
	s_addc_u32 s37, s7, 0
	s_lshl_b32 s64, s71, 3
	s_add_u32 s64, s64, s29
	s_lshl_b32 s64, s64, 5
	s_add_u32 s64, s64, s30
	s_lshl_b32 s64, s64, 2
	s_add_u32 s40, s8, s64
	s_addc_u32 s41, s9, 0
	s_lshl_b32 s64, s71, 19
	s_add_u32 s64, s64, 0x600
	s_add_u32 s72, s62, s64
	s_addc_u32 s73, s63, 0
	s_nop 3
	s_waitcnt lgkmcnt(4)
	v_mfma_f32_32x32x16_f16 v[0:15], a[0:3], v[160:163], v[0:15]
	ds_read_b128 v[160:163], v192 offset:8192
	v_exp_f32_e32 v200, v96
	v_mfma_f32_32x32x16_f16 v[16:31], a[0:3], v[164:167], v[16:31]
	ds_read_b128 v[164:167], v192 offset:9216
	s_lshl_b32 s64, s71, 3
	s_add_u32 s64, s64, s29
	s_lshl_b32 s64, s64, 7
	s_add_u32 s38, s8, s64
	s_addc_u32 s39, s9, 0
	global_load_dword v251, v196, s[38:39] sc1
	v_exp_f32_e32 v201, v97
	v_add_f32_e32 v200, 1.0, v200
	v_mfma_f32_32x32x16_f16 v[0:15], a[4:7], v[168:171], v[0:15]
	ds_read_b128 v[168:171], v192 offset:10240
	v_exp_f32_e32 v202, v98
	v_add_f32_e32 v201, 1.0, v201
	v_mfma_f32_32x32x16_f16 v[16:31], a[4:7], v[172:175], v[16:31]
	ds_read_b128 v[172:175], v192 offset:11264
	global_load_lds_dwordx4 v192, s[44:45] offset:1024 sc1
	v_exp_f32_e32 v203, v99
	v_add_f32_e32 v202, 1.0, v202
	s_waitcnt lgkmcnt(4)
	v_mfma_f32_32x32x16_f16 v[0:15], a[8:11], v[176:179], v[0:15]
	ds_read_b128 v[176:179], v192 offset:12288
	v_exp_f32_e32 v204, v100
	v_add_f32_e32 v203, 1.0, v203
	v_mfma_f32_32x32x16_f16 v[16:31], a[8:11], v[180:183], v[16:31]
	ds_read_b128 v[180:183], v192 offset:13312
	v_exp_f32_e32 v205, v101
	v_add_f32_e32 v204, 1.0, v204
	v_mfma_f32_32x32x16_f16 v[0:15], a[12:15], v[184:187], v[0:15]
	ds_read_b128 v[184:187], v192 offset:14336
	v_exp_f32_e32 v206, v102
	v_add_f32_e32 v205, 1.0, v205
	v_mfma_f32_32x32x16_f16 v[16:31], a[12:15], v[188:191], v[16:31]
	ds_read_b128 v[188:191], v192 offset:15360
	global_load_lds_dwordx4 v192, s[44:45] offset:2048 sc1
	v_exp_f32_e32 v207, v103
	v_add_f32_e32 v206, 1.0, v206
	s_waitcnt lgkmcnt(4)
	v_mfma_f32_32x32x16_f16 v[0:15], a[16:19], v[160:163], v[0:15]
	ds_read_b128 v[160:163], v192 offset:16384
	v_exp_f32_e32 v208, v104
	v_add_f32_e32 v207, 1.0, v207
	v_mfma_f32_32x32x16_f16 v[16:31], a[16:19], v[164:167], v[16:31]
	ds_read_b128 v[164:167], v192 offset:17408
	v_exp_f32_e32 v209, v105
	v_add_f32_e32 v208, 1.0, v208
	v_mfma_f32_32x32x16_f16 v[0:15], a[20:23], v[168:171], v[0:15]
	ds_read_b128 v[168:171], v192 offset:18432
	v_exp_f32_e32 v210, v106
	v_add_f32_e32 v209, 1.0, v209
	v_mfma_f32_32x32x16_f16 v[16:31], a[20:23], v[172:175], v[16:31]
	ds_read_b128 v[172:175], v192 offset:19456
	global_load_lds_dwordx4 v192, s[44:45] offset:3072 sc1
	v_exp_f32_e32 v211, v107
	v_add_f32_e32 v210, 1.0, v210
	s_waitcnt lgkmcnt(4)
	v_mfma_f32_32x32x16_f16 v[0:15], a[24:27], v[176:179], v[0:15]
	ds_read_b128 v[176:179], v192 offset:20480
	v_exp_f32_e32 v212, v108
	v_add_f32_e32 v211, 1.0, v211
	v_mfma_f32_32x32x16_f16 v[16:31], a[24:27], v[180:183], v[16:31]
	ds_read_b128 v[180:183], v192 offset:21504
	v_exp_f32_e32 v213, v109
	v_add_f32_e32 v212, 1.0, v212
	v_mfma_f32_32x32x16_f16 v[0:15], a[28:31], v[184:187], v[0:15]
	ds_read_b128 v[184:187], v192 offset:22528
	v_exp_f32_e32 v214, v110
	v_add_f32_e32 v213, 1.0, v213
	v_mfma_f32_32x32x16_f16 v[16:31], a[28:31], v[188:191], v[16:31]
	ds_read_b128 v[188:191], v192 offset:23552
	s_add_u32 s44, s34, 0x11000
	s_addc_u32 s45, s35, 0
	s_mov_b32 m0, s57
	s_nop 0
	global_load_lds_dwordx4 v192, s[44:45] sc1
	v_exp_f32_e32 v215, v111
	v_add_f32_e32 v214, 1.0, v214
	s_waitcnt lgkmcnt(4)
	v_mfma_f32_32x32x16_f16 v[0:15], a[32:35], v[160:163], v[0:15]
	ds_read_b128 v[160:163], v192 offset:24576
	v_add_f32_e32 v215, 1.0, v215
	v_rcp_f32_e32 v200, v200
	v_mfma_f32_32x32x16_f16 v[16:31], a[32:35], v[164:167], v[16:31]
	ds_read_b128 v[164:167], v192 offset:25600
	v_rcp_f32_e32 v201, v201
	v_mfma_f32_32x32x16_f16 v[0:15], a[36:39], v[168:171], v[0:15]
	ds_read_b128 v[168:171], v192 offset:26624
	v_rcp_f32_e32 v202, v202
	v_mfma_f32_32x32x16_f16 v[16:31], a[36:39], v[172:175], v[16:31]
	ds_read_b128 v[172:175], v192 offset:27648
	global_load_lds_dwordx4 v192, s[44:45] offset:1024 sc1
	v_rcp_f32_e32 v203, v203
	s_waitcnt lgkmcnt(4)
	v_mfma_f32_32x32x16_f16 v[0:15], a[40:43], v[176:179], v[0:15]
	ds_read_b128 v[176:179], v192 offset:28672
	v_rcp_f32_e32 v204, v204
	v_mfma_f32_32x32x16_f16 v[16:31], a[40:43], v[180:183], v[16:31]
	ds_read_b128 v[180:183], v192 offset:29696
	v_rcp_f32_e32 v205, v205
	v_mul_f32_e32 v204, v204, v152
	v_mfma_f32_32x32x16_f16 v[0:15], a[44:47], v[184:187], v[0:15]
	ds_read_b128 v[184:187], v192 offset:30720
	v_rcp_f32_e32 v206, v206
	v_mul_f32_e32 v205, v205, v153
	v_mfma_f32_32x32x16_f16 v[16:31], a[44:47], v[188:191], v[16:31]
	ds_read_b128 v[188:191], v192 offset:31744
	global_load_lds_dwordx4 v192, s[44:45] offset:2048 sc1
	v_rcp_f32_e32 v207, v207
	v_mul_f32_e32 v206, v206, v154
	s_waitcnt vmcnt(8)
	s_barrier
	s_waitcnt lgkmcnt(4)
	v_mfma_f32_32x32x16_f16 v[0:15], a[48:51], v[160:163], v[0:15]
	ds_read_b128 v[160:163], v192 offset:32768
	v_rcp_f32_e32 v208, v208
	v_mul_f32_e32 v207, v207, v155
	v_mfma_f32_32x32x16_f16 v[16:31], a[48:51], v[164:167], v[16:31]
	ds_read_b128 v[164:167], v192 offset:33792
	v_rcp_f32_e32 v209, v209
	v_fmamk_f32 v208, v208, 0xc0b8aa3b, v198
	v_mfma_f32_32x32x16_f16 v[0:15], a[52:55], v[168:171], v[0:15]
	ds_read_b128 v[168:171], v192 offset:34816
	v_rcp_f32_e32 v210, v210
	v_fmamk_f32 v209, v209, 0xc0b8aa3b, v198
	v_fma_f32 v152, v200, v208, v204
	v_mfma_f32_32x32x16_f16 v[16:31], a[52:55], v[172:175], v[16:31]
	ds_read_b128 v[172:175], v192 offset:35840
	global_load_lds_dwordx4 v192, s[44:45] offset:3072 sc1
	v_rcp_f32_e32 v211, v211
	v_fmamk_f32 v210, v210, 0xc0b8aa3b, v198
	v_fma_f32 v153, v201, v209, v205
	s_waitcnt lgkmcnt(4)
	v_mfma_f32_32x32x16_f16 v[0:15], a[56:59], v[176:179], v[0:15]
	ds_read_b128 v[176:179], v192 offset:36864
	v_rcp_f32_e32 v212, v212
	v_fmamk_f32 v211, v211, 0xc0b8aa3b, v198
	v_fma_f32 v154, v202, v210, v206
	v_mfma_f32_32x32x16_f16 v[16:31], a[56:59], v[180:183], v[16:31]
	ds_read_b128 v[180:183], v192 offset:37888
	v_rcp_f32_e32 v213, v213
	v_fma_f32 v155, v203, v211, v207
	v_mfma_f32_32x32x16_f16 v[0:15], a[60:63], v[184:187], v[0:15]
	ds_read_b128 v[184:187], v192 offset:38912
	v_rcp_f32_e32 v214, v214
	v_mfma_f32_32x32x16_f16 v[16:31], a[60:63], v[188:191], v[16:31]
	ds_read_b128 v[188:191], v192 offset:39936
	s_add_u32 s44, s34, 0x18000
	s_addc_u32 s45, s35, 0
	s_mov_b32 m0, s58
	s_nop 0
	global_load_lds_dwordx4 v192, s[44:45] sc1
	v_rcp_f32_e32 v215, v215
	s_waitcnt lgkmcnt(4)
	v_mfma_f32_32x32x16_f16 v[0:15], a[64:67], v[160:163], v[0:15]
	ds_read_b128 v[160:163], v192 offset:40960
	v_exp_f32_e32 v200, v152
	v_mfma_f32_32x32x16_f16 v[16:31], a[64:67], v[164:167], v[16:31]
	ds_read_b128 v[164:167], v192 offset:41984
	v_exp_f32_e32 v201, v153
	v_add_f32_e32 v200, 1.0, v200
	v_mfma_f32_32x32x16_f16 v[0:15], a[68:71], v[168:171], v[0:15]
	ds_read_b128 v[168:171], v192 offset:43008
	v_exp_f32_e32 v202, v154
	v_add_f32_e32 v201, 1.0, v201
	v_mfma_f32_32x32x16_f16 v[16:31], a[68:71], v[172:175], v[16:31]
	ds_read_b128 v[172:175], v192 offset:44032
	global_load_lds_dwordx4 v192, s[44:45] offset:1024 sc1
	v_exp_f32_e32 v203, v155
	v_add_f32_e32 v202, 1.0, v202
	s_waitcnt lgkmcnt(4)
	v_mfma_f32_32x32x16_f16 v[0:15], a[72:75], v[176:179], v[0:15]
	ds_read_b128 v[176:179], v192 offset:45056
	v_add_f32_e32 v203, 1.0, v203
	v_rcp_f32_e32 v200, v200
	v_mfma_f32_32x32x16_f16 v[16:31], a[72:75], v[180:183], v[16:31]
	ds_read_b128 v[180:183], v192 offset:46080
	v_rcp_f32_e32 v201, v201
	v_fma_f32 v200, v200, 2.0, -1.0
	v_mfma_f32_32x32x16_f16 v[0:15], a[76:79], v[184:187], v[0:15]
	ds_read_b128 v[184:187], v192 offset:47104
	v_rcp_f32_e32 v202, v202
	v_fma_f32 v201, v201, 2.0, -1.0
	v_mul_f32_e32 v216, v212, v200
	v_mfma_f32_32x32x16_f16 v[16:31], a[76:79], v[188:191], v[16:31]
	ds_read_b128 v[188:191], v192 offset:48128
	global_load_lds_dwordx4 v192, s[44:45] offset:2048 sc1
	v_rcp_f32_e32 v203, v203
	v_fma_f32 v202, v202, 2.0, -1.0
	v_mul_f32_e32 v217, v213, v201
	s_waitcnt lgkmcnt(4)
	v_mfma_f32_32x32x16_f16 v[0:15], a[80:83], v[160:163], v[0:15]
	ds_read_b128 v[160:163], v192 offset:49152
	v_fma_f32 v203, v203, 2.0, -1.0
	v_mul_f32_e32 v218, v214, v202
	v_exp_f32_e32 v200, v112
	v_mfma_f32_32x32x16_f16 v[16:31], a[80:83], v[164:167], v[16:31]
	ds_read_b128 v[164:167], v192 offset:50176
	v_mul_f32_e32 v219, v215, v203
	v_mul_f32_e32 v236, v216, v228
	v_exp_f32_e32 v201, v113
	v_mfma_f32_32x32x16_f16 v[0:15], a[84:87], v[168:171], v[0:15]
	ds_read_b128 v[168:171], v192 offset:51200
	v_mul_f32_e32 v237, v216, v232
	v_fmac_f32_e32 v236, v217, v229
	v_exp_f32_e32 v202, v114
	v_mfma_f32_32x32x16_f16 v[16:31], a[84:87], v[172:175], v[16:31]
	ds_read_b128 v[172:175], v192 offset:52224
	global_load_lds_dwordx4 v192, s[44:45] offset:3072 sc1
	v_fmac_f32_e32 v237, v217, v233
	v_fmac_f32_e32 v236, v218, v230
	v_exp_f32_e32 v203, v115
	s_waitcnt lgkmcnt(4)
	v_mfma_f32_32x32x16_f16 v[0:15], a[88:91], v[176:179], v[0:15]
	ds_read_b128 v[176:179], v192 offset:53248
	v_fmac_f32_e32 v237, v218, v234
	v_fmac_f32_e32 v236, v219, v231
	v_exp_f32_e32 v204, v116
	v_mfma_f32_32x32x16_f16 v[16:31], a[88:91], v[180:183], v[16:31]
	ds_read_b128 v[180:183], v192 offset:54272
	v_fmac_f32_e32 v237, v219, v235
	v_mov_b32_e32 v238, v236
	v_exp_f32_e32 v205, v117
	v_mfma_f32_32x32x16_f16 v[0:15], a[92:95], v[184:187], v[0:15]
	ds_read_b128 v[184:187], v192 offset:55296
	v_mov_b32_e32 v239, v236
	v_mov_b32_e32 v240, v237
	v_exp_f32_e32 v206, v118
	v_mfma_f32_32x32x16_f16 v[16:31], a[92:95], v[188:191], v[16:31]
	ds_read_b128 v[188:191], v192 offset:56320
	s_add_u32 s44, s34, 0x19000
	s_addc_u32 s45, s35, 0
	s_mov_b32 m0, s59
	s_nop 0
	global_load_lds_dwordx4 v192, s[44:45] sc1
	v_mov_b32_e32 v241, v237
	v_cvt_pk_f16_f32 v220, v216, v217
	v_exp_f32_e32 v207, v119
	s_waitcnt lgkmcnt(4)
	v_mfma_f32_32x32x16_f16 v[0:15], a[96:99], v[160:163], v[0:15]
	ds_read_b128 v[160:163], v192 offset:57344
	s_nop 1
	v_permlane32_swap_b32_e32 v238, v239
	v_permlane32_swap_b32_e32 v240, v241
	v_add_f32_e32 v238, v238, v239
	v_add_f32_e32 v239, v240, v241
	ds_write_b64 v248, v[238:239] offset:1536
	v_exp_f32_e32 v208, v120
	v_mfma_f32_32x32x16_f16 v[16:31], a[96:99], v[164:167], v[16:31]
	ds_read_b128 v[164:167], v192 offset:58368
	v_cvt_pk_f16_f32 v221, v218, v219
	v_exp_f32_e32 v209, v121
	v_add_f32_e32 v200, 1.0, v200
	v_mfma_f32_32x32x16_f16 v[0:15], a[100:103], v[168:171], v[0:15]
	ds_read_b128 v[168:171], v192 offset:59392
	v_exp_f32_e32 v210, v122
	v_add_f32_e32 v201, 1.0, v201
	v_add_f32_e32 v202, 1.0, v202
	v_mfma_f32_32x32x16_f16 v[16:31], a[100:103], v[172:175], v[16:31]
	ds_read_b128 v[172:175], v192 offset:60416
	global_load_lds_dwordx4 v192, s[44:45] offset:1024 sc1
	v_exp_f32_e32 v211, v123
	v_add_f32_e32 v203, 1.0, v203
	v_add_f32_e32 v204, 1.0, v204
	s_waitcnt lgkmcnt(5)
	v_mfma_f32_32x32x16_f16 v[0:15], a[104:107], v[176:179], v[0:15]
	ds_read_b128 v[176:179], v192 offset:61440
	v_exp_f32_e32 v212, v124
	v_add_f32_e32 v205, 1.0, v205
	v_add_f32_e32 v206, 1.0, v206
	v_mfma_f32_32x32x16_f16 v[16:31], a[104:107], v[180:183], v[16:31]
	ds_read_b128 v[180:183], v192 offset:62464
	v_exp_f32_e32 v213, v125
	v_add_f32_e32 v207, 1.0, v207
	v_add_f32_e32 v208, 1.0, v208
	v_mfma_f32_32x32x16_f16 v[0:15], a[108:111], v[184:187], v[0:15]
	ds_read_b128 v[184:187], v192 offset:63488
	v_exp_f32_e32 v214, v126
	v_add_f32_e32 v209, 1.0, v209
	v_add_f32_e32 v210, 1.0, v210
	v_mfma_f32_32x32x16_f16 v[16:31], a[108:111], v[188:191], v[16:31]
	ds_read_b128 v[188:191], v192 offset:64512
	global_load_lds_dwordx4 v192, s[44:45] offset:2048 sc1
	v_exp_f32_e32 v215, v127
	v_add_f32_e32 v211, 1.0, v211
	v_add_f32_e32 v212, 1.0, v212
	s_waitcnt vmcnt(7)
	s_barrier
	s_waitcnt lgkmcnt(4)
	v_mfma_f32_32x32x16_f16 v[0:15], a[112:115], v[160:163], v[0:15]
	ds_read_b128 v[160:163], v193 offset:0
	v_add_f32_e32 v213, 1.0, v213
	v_add_f32_e32 v214, 1.0, v214
	v_rcp_f32_e32 v200, v200
	v_mfma_f32_32x32x16_f16 v[16:31], a[112:115], v[164:167], v[16:31]
	ds_read_b128 v[164:167], v193 offset:1024
	v_add_f32_e32 v215, 1.0, v215
	v_rcp_f32_e32 v201, v201
	v_mfma_f32_32x32x16_f16 v[0:15], a[116:119], v[168:171], v[0:15]
	ds_read_b128 v[168:171], v193 offset:2048
	v_rcp_f32_e32 v202, v202
	v_mfma_f32_32x32x16_f16 v[16:31], a[116:119], v[172:175], v[16:31]
	ds_read_b128 v[172:175], v193 offset:3072
	global_load_lds_dwordx4 v192, s[44:45] offset:3072 sc1
	v_rcp_f32_e32 v203, v203
	s_waitcnt lgkmcnt(4)
	v_mfma_f32_32x32x16_f16 v[0:15], a[120:123], v[176:179], v[0:15]
	ds_read_b128 v[176:179], v193 offset:4096
	v_rcp_f32_e32 v204, v204
	s_add_u32 s46, s42, 0x4000
	s_addc_u32 s47, s43, 0
	global_load_dwordx4 v[64:67], v192, s[46:47] offset:0
	v_mfma_f32_32x32x16_f16 v[16:31], a[120:123], v[180:183], v[16:31]
	ds_read_b128 v[180:183], v193 offset:5120
	v_rcp_f32_e32 v205, v205
	v_mul_f32_e32 v204, v204, v156
	global_load_dwordx4 v[68:71], v192, s[46:47] offset:1024
	global_load_dwordx4 v[72:75], v192, s[46:47] offset:2048
	v_mfma_f32_32x32x16_f16 v[0:15], a[124:127], v[184:187], v[0:15]
	ds_read_b128 v[184:187], v193 offset:6144
	v_rcp_f32_e32 v206, v206
	v_mul_f32_e32 v205, v205, v157
	global_load_dwordx4 v[76:79], v192, s[46:47] offset:3072
	s_add_u32 s46, s42, 0x5000
	s_addc_u32 s47, s43, 0
	v_mfma_f32_32x32x16_f16 v[16:31], a[124:127], v[188:191], v[16:31]
	ds_read_b128 v[188:191], v193 offset:7168
	v_cmp_gt_u32_e32 vcc, 2, v251
	s_cbranch_vccnz .LD_tpoll21
.LD_tok20:
	s_and_b32 s64, s71, 1
	s_lshl_b32 s64, s64, 22
	s_add_u32 s64, s64, s49
	s_add_u32 s64, s64, 0x20000
	s_add_u32 s34, s6, s64
	s_addc_u32 s35, s7, 0
	s_add_u32 s44, s34, 0x0
	s_addc_u32 s45, s35, 0
	s_mov_b32 m0, s52
	s_nop 0
	global_load_lds_dwordx4 v192, s[44:45] sc1
	v_rcp_f32_e32 v207, v207
	v_mul_f32_e32 v206, v206, v158
	global_load_dwordx4 v[80:83], v192, s[46:47] offset:0
	global_load_dwordx4 v[84:87], v192, s[46:47] offset:1024
	s_waitcnt lgkmcnt(4)
	v_mfma_f32_32x32x16_f16 v[0:15], a[128:131], v[160:163], v[0:15]
	ds_read_b128 v[160:163], v193 offset:8192
	v_rcp_f32_e32 v208, v208
	v_mul_f32_e32 v207, v207, v159
	global_load_dwordx4 v[88:91], v192, s[46:47] offset:2048
	global_load_dwordx4 v[92:95], v192, s[46:47] offset:3072
	v_mfma_f32_32x32x16_f16 v[16:31], a[128:131], v[164:167], v[16:31]
	ds_read_b128 v[164:167], v193 offset:9216
	v_rcp_f32_e32 v209, v209
	v_fmamk_f32 v208, v208, 0xc0b8aa3b, v198
	v_mfma_f32_32x32x16_f16 v[0:15], a[132:135], v[168:171], v[0:15]
	ds_read_b128 v[168:171], v193 offset:10240
	v_rcp_f32_e32 v210, v210
	v_fmamk_f32 v209, v209, 0xc0b8aa3b, v198
	v_fma_f32 v156, v200, v208, v204
	v_mfma_f32_32x32x16_f16 v[16:31], a[132:135], v[172:175], v[16:31]
	ds_read_b128 v[172:175], v193 offset:11264
	global_load_lds_dwordx4 v192, s[44:45] offset:1024 sc1
	v_rcp_f32_e32 v211, v211
	v_fmamk_f32 v210, v210, 0xc0b8aa3b, v198
	v_fma_f32 v157, v201, v209, v205
	s_waitcnt lgkmcnt(4)
	v_mfma_f32_32x32x16_f16 v[0:15], a[136:139], v[176:179], v[0:15]
	ds_read_b128 v[176:179], v193 offset:12288
	v_rcp_f32_e32 v212, v212
	v_fmamk_f32 v211, v211, 0xc0b8aa3b, v198
	v_fma_f32 v158, v202, v210, v206
	v_mfma_f32_32x32x16_f16 v[16:31], a[136:139], v[180:183], v[16:31]
	ds_read_b128 v[180:183], v193 offset:13312
	v_rcp_f32_e32 v213, v213
	v_fma_f32 v159, v203, v211, v207
	v_mfma_f32_32x32x16_f16 v[0:15], a[140:143], v[184:187], v[0:15]
	ds_read_b128 v[184:187], v193 offset:14336
	v_rcp_f32_e32 v214, v214
	v_mfma_f32_32x32x16_f16 v[16:31], a[140:143], v[188:191], v[16:31]
	ds_read_b128 v[188:191], v193 offset:15360
	global_load_lds_dwordx4 v192, s[44:45] offset:2048 sc1
	v_rcp_f32_e32 v215, v215
	s_waitcnt lgkmcnt(4)
	v_mfma_f32_32x32x16_f16 v[0:15], a[144:147], v[160:163], v[0:15]
	ds_read_b128 v[160:163], v193 offset:16384
	v_exp_f32_e32 v200, v156
	v_mfma_f32_32x32x16_f16 v[16:31], a[144:147], v[164:167], v[16:31]
	ds_read_b128 v[164:167], v193 offset:17408
	v_exp_f32_e32 v201, v157
	v_add_f32_e32 v200, 1.0, v200
	v_mfma_f32_32x32x16_f16 v[0:15], a[148:151], v[168:171], v[0:15]
	ds_read_b128 v[168:171], v193 offset:18432
	v_exp_f32_e32 v202, v158
	v_add_f32_e32 v201, 1.0, v201
	v_mfma_f32_32x32x16_f16 v[16:31], a[148:151], v[172:175], v[16:31]
	ds_read_b128 v[172:175], v193 offset:19456
	global_load_lds_dwordx4 v192, s[44:45] offset:3072 sc1
	v_exp_f32_e32 v203, v159
	v_add_f32_e32 v202, 1.0, v202
	s_waitcnt lgkmcnt(4)
	v_mfma_f32_32x32x16_f16 v[0:15], a[152:155], v[176:179], v[0:15]
	ds_read_b128 v[176:179], v193 offset:20480
	v_add_f32_e32 v203, 1.0, v203
	v_rcp_f32_e32 v200, v200
	v_mfma_f32_32x32x16_f16 v[16:31], a[152:155], v[180:183], v[16:31]
	ds_read_b128 v[180:183], v193 offset:21504
	v_rcp_f32_e32 v201, v201
	v_fma_f32 v200, v200, 2.0, -1.0
	v_mfma_f32_32x32x16_f16 v[0:15], a[156:159], v[184:187], v[0:15]
	ds_read_b128 v[184:187], v193 offset:22528
	v_rcp_f32_e32 v202, v202
	v_fma_f32 v201, v201, 2.0, -1.0
	v_mul_f32_e32 v216, v212, v200
	v_mfma_f32_32x32x16_f16 v[16:31], a[156:159], v[188:191], v[16:31]
	ds_read_b128 v[188:191], v193 offset:23552
	s_add_u32 s44, s34, 0x1000
	s_addc_u32 s45, s35, 0
	s_mov_b32 m0, s53
	s_nop 0
	global_load_lds_dwordx4 v192, s[44:45] sc1
	v_rcp_f32_e32 v203, v203
	v_fma_f32 v202, v202, 2.0, -1.0
	v_mul_f32_e32 v217, v213, v201
	s_waitcnt lgkmcnt(4)
	v_mfma_f32_32x32x16_f16 v[0:15], a[160:163], v[160:163], v[0:15]
	ds_read_b128 v[160:163], v193 offset:24576
	v_fma_f32 v203, v203, 2.0, -1.0
	v_mul_f32_e32 v218, v214, v202
	v_mfma_f32_32x32x16_f16 v[16:31], a[160:163], v[164:167], v[16:31]
	ds_read_b128 v[164:167], v193 offset:25600
	v_mul_f32_e32 v219, v215, v203
	v_mul_f32_e32 v236, v216, v228
	v_mfma_f32_32x32x16_f16 v[0:15], a[164:167], v[168:171], v[0:15]
	ds_read_b128 v[168:171], v193 offset:26624
	v_mul_f32_e32 v237, v216, v232
	v_fmac_f32_e32 v236, v217, v229
	v_mfma_f32_32x32x16_f16 v[16:31], a[164:167], v[172:175], v[16:31]
	ds_read_b128 v[172:175], v193 offset:27648
	global_load_lds_dwordx4 v192, s[44:45] offset:1024 sc1
	v_fmac_f32_e32 v237, v217, v233
	v_fmac_f32_e32 v236, v218, v230
	s_waitcnt lgkmcnt(4)
	v_mfma_f32_32x32x16_f16 v[0:15], a[168:171], v[176:179], v[0:15]
	ds_read_b128 v[176:179], v193 offset:28672
	v_fmac_f32_e32 v237, v218, v234
	v_fmac_f32_e32 v236, v219, v231
	v_mfma_f32_32x32x16_f16 v[16:31], a[168:171], v[180:183], v[16:31]
	ds_read_b128 v[180:183], v193 offset:29696
	v_fmac_f32_e32 v237, v219, v235
	v_mov_b32_e32 v238, v236
	v_mfma_f32_32x32x16_f16 v[0:15], a[172:175], v[184:187], v[0:15]
	ds_read_b128 v[184:187], v193 offset:30720
	v_mov_b32_e32 v239, v236
	v_mov_b32_e32 v240, v237
	v_mfma_f32_32x32x16_f16 v[16:31], a[172:175], v[188:191], v[16:31]
	ds_read_b128 v[188:191], v193 offset:31744
	global_load_lds_dwordx4 v192, s[44:45] offset:2048 sc1
	v_mov_b32_e32 v241, v237
	v_cvt_pk_f16_f32 v222, v216, v217
	s_waitcnt vmcnt(15)
	s_barrier
	s_waitcnt lgkmcnt(4)
	v_mfma_f32_32x32x16_f16 v[0:15], a[176:179], v[160:163], v[0:15]
	ds_read_b128 v[160:163], v193 offset:32768
	s_nop 1
	v_permlane32_swap_b32_e32 v238, v239
	v_permlane32_swap_b32_e32 v240, v241
	v_add_f32_e32 v238, v238, v239
	v_add_f32_e32 v239, v240, v241
	ds_write_b64 v248, v[238:239] offset:1792
	v_mfma_f32_32x32x16_f16 v[16:31], a[176:179], v[164:167], v[16:31]
	ds_read_b128 v[164:167], v193 offset:33792
	v_cvt_pk_f16_f32 v223, v218, v219
	v_mfma_f32_32x32x16_f16 v[0:15], a[180:183], v[168:171], v[0:15]
	ds_read_b128 v[168:171], v193 offset:34816
	s_nop 1
	v_permlane32_swap_b32_e32 v220, v222
	v_permlane32_swap_b32_e32 v221, v223
	s_cmp_eq_u32 s31, 0
	s_cbranch_scc1 .LD_slow22
	global_store_dwordx4 v195, v[220:223], s[36:37] offset:0
.LD_join23:
	v_mfma_f32_32x32x16_f16 v[16:31], a[180:183], v[172:175], v[16:31]
	ds_read_b128 v[172:175], v193 offset:35840
	global_load_lds_dwordx4 v192, s[44:45] offset:3072 sc1
	s_waitcnt lgkmcnt(5)
	v_mfma_f32_32x32x16_f16 v[0:15], a[184:187], v[176:179], v[0:15]
	ds_read_b128 v[176:179], v193 offset:36864
	v_mfma_f32_32x32x16_f16 v[16:31], a[184:187], v[180:183], v[16:31]
	ds_read_b128 v[180:183], v193 offset:37888
	v_mfma_f32_32x32x16_f16 v[0:15], a[188:191], v[184:187], v[0:15]
	ds_read_b128 v[184:187], v193 offset:38912
	v_mfma_f32_32x32x16_f16 v[16:31], a[188:191], v[188:191], v[16:31]
	ds_read_b128 v[188:191], v193 offset:39936
	s_add_u32 s44, s34, 0x8000
	s_addc_u32 s45, s35, 0
	s_mov_b32 m0, s54
	s_nop 0
	global_load_lds_dwordx4 v192, s[44:45] sc1
	s_waitcnt lgkmcnt(4)
	v_mfma_f32_32x32x16_f16 v[0:15], a[192:195], v[160:163], v[0:15]
	ds_read_b128 v[160:163], v193 offset:40960
	v_mfma_f32_32x32x16_f16 v[16:31], a[192:195], v[164:167], v[16:31]
	ds_read_b128 v[164:167], v193 offset:41984
	v_mfma_f32_32x32x16_f16 v[0:15], a[196:199], v[168:171], v[0:15]
	ds_read_b128 v[168:171], v193 offset:43008
	v_mfma_f32_32x32x16_f16 v[16:31], a[196:199], v[172:175], v[16:31]
	ds_read_b128 v[172:175], v193 offset:44032
	global_load_lds_dwordx4 v192, s[44:45] offset:1024 sc1
	s_waitcnt lgkmcnt(4)
	v_mfma_f32_32x32x16_f16 v[0:15], a[200:203], v[176:179], v[0:15]
	ds_read_b128 v[176:179], v193 offset:45056
	v_mfma_f32_32x32x16_f16 v[16:31], a[200:203], v[180:183], v[16:31]
	ds_read_b128 v[180:183], v193 offset:46080
	v_mfma_f32_32x32x16_f16 v[0:15], a[204:207], v[184:187], v[0:15]
	ds_read_b128 v[184:187], v193 offset:47104
	v_mfma_f32_32x32x16_f16 v[16:31], a[204:207], v[188:191], v[16:31]
	ds_read_b128 v[188:191], v193 offset:48128
	global_load_lds_dwordx4 v192, s[44:45] offset:2048 sc1
	s_waitcnt vmcnt(4)
	s_barrier
	v_mov_b32_e32 v199, 4
	s_cmp_eq_u32 s31, 0
	s_cbranch_scc1 .LD_slow24
	global_store_dword v197, v199, s[40:41]
.LD_join25:
	ds_read_b64 v[200:201], v249 offset:1536
	ds_read_b64 v[202:203], v249 offset:3584
	ds_read_b64 v[204:205], v249 offset:5632
	ds_read_b64 v[206:207], v249 offset:7680
	s_waitcnt lgkmcnt(8)
	v_mfma_f32_32x32x16_f16 v[0:15], a[208:211], v[160:163], v[0:15]
	ds_read_b128 v[160:163], v193 offset:49152
	v_mfma_f32_32x32x16_f16 v[16:31], a[208:211], v[164:167], v[16:31]
	ds_read_b128 v[164:167], v193 offset:50176
	v_mfma_f32_32x32x16_f16 v[0:15], a[212:215], v[168:171], v[0:15]
	ds_read_b128 v[168:171], v193 offset:51200
	v_mfma_f32_32x32x16_f16 v[16:31], a[212:215], v[172:175], v[16:31]
	ds_read_b128 v[172:175], v193 offset:52224
	global_load_lds_dwordx4 v192, s[44:45] offset:3072 sc1
	s_waitcnt lgkmcnt(8)
	v_mfma_f32_32x32x16_f16 v[0:15], a[216:219], v[176:179], v[0:15]
	ds_read_b128 v[176:179], v193 offset:53248
	v_mfma_f32_32x32x16_f16 v[16:31], a[216:219], v[180:183], v[16:31]
	ds_read_b128 v[180:183], v193 offset:54272
	v_mfma_f32_32x32x16_f16 v[0:15], a[220:223], v[184:187], v[0:15]
	ds_read_b128 v[184:187], v193 offset:55296
	v_mfma_f32_32x32x16_f16 v[16:31], a[220:223], v[188:191], v[16:31]
	ds_read_b128 v[188:191], v193 offset:56320
	s_add_u32 s44, s34, 0x9000
	s_addc_u32 s45, s35, 0
	s_mov_b32 m0, s55
	s_nop 0
	global_load_lds_dwordx4 v192, s[44:45] sc1
	s_waitcnt lgkmcnt(4)
	v_mfma_f32_32x32x16_f16 v[0:15], a[224:227], v[160:163], v[0:15]
	ds_read_b128 v[160:163], v193 offset:57344
	v_mfma_f32_32x32x16_f16 v[16:31], a[224:227], v[164:167], v[16:31]
	ds_read_b128 v[164:167], v193 offset:58368
	v_mfma_f32_32x32x16_f16 v[0:15], a[228:231], v[168:171], v[0:15]
	ds_read_b128 v[168:171], v193 offset:59392
	v_mfma_f32_32x32x16_f16 v[16:31], a[228:231], v[172:175], v[16:31]
	ds_read_b128 v[172:175], v193 offset:60416
	global_load_lds_dwordx4 v192, s[44:45] offset:1024 sc1
	v_add_f32_e32 v200, v200, v202
	v_add_f32_e32 v201, v201, v203
	v_add_f32_e32 v200, v200, v204
	v_add_f32_e32 v201, v201, v205
	v_add_f32_e32 v200, v200, v206
	v_add_f32_e32 v201, v201, v207
	global_store_dwordx2 v250, v[200:201], s[72:73]
	s_waitcnt lgkmcnt(4)
	v_mfma_f32_32x32x16_f16 v[0:15], a[232:235], v[176:179], v[0:15]
	ds_read_b128 v[176:179], v193 offset:61440
	v_mfma_f32_32x32x16_f16 v[16:31], a[232:235], v[180:183], v[16:31]
	ds_read_b128 v[180:183], v193 offset:62464
	v_mfma_f32_32x32x16_f16 v[0:15], a[236:239], v[184:187], v[0:15]
	ds_read_b128 v[184:187], v193 offset:63488
	v_mfma_f32_32x32x16_f16 v[16:31], a[236:239], v[188:191], v[16:31]
	ds_read_b128 v[188:191], v193 offset:64512
	global_load_lds_dwordx4 v192, s[44:45] offset:2048 sc1
	s_and_b32 s64, s33, 1
	s_lshl_b32 s64, s64, 22
	s_add_u32 s64, s64, s50
	s_add_u32 s36, s6, s64
	s_addc_u32 s37, s7, 0
	s_lshl_b32 s64, s33, 3
	s_add_u32 s64, s64, s29
	s_lshl_b32 s64, s64, 5
	s_add_u32 s64, s64, s30
	s_lshl_b32 s64, s64, 2
	s_add_u32 s40, s8, s64
	s_addc_u32 s41, s9, 0
	s_lshl_b32 s64, s33, 19
	s_add_u32 s72, s62, s64
	s_addc_u32 s73, s63, 0
	s_waitcnt vmcnt(9)
	s_barrier
	s_waitcnt lgkmcnt(4)
	v_mfma_f32_32x32x16_f16 v[0:15], a[240:243], v[160:163], v[0:15]
	ds_read_b128 v[160:163], v192 offset:0
	v_mfma_f32_32x32x16_f16 v[16:31], a[240:243], v[164:167], v[16:31]
	ds_read_b128 v[164:167], v192 offset:1024
	v_mfma_f32_32x32x16_f16 v[0:15], a[244:247], v[168:171], v[0:15]
	ds_read_b128 v[168:171], v192 offset:2048
	v_mfma_f32_32x32x16_f16 v[16:31], a[244:247], v[172:175], v[16:31]
	ds_read_b128 v[172:175], v192 offset:3072
	global_load_lds_dwordx4 v192, s[44:45] offset:3072 sc1
	s_waitcnt lgkmcnt(4)
	v_mfma_f32_32x32x16_f16 v[0:15], a[248:251], v[176:179], v[0:15]
	ds_read_b128 v[176:179], v192 offset:4096
	v_mfma_f32_32x32x16_f16 v[16:31], a[248:251], v[180:183], v[16:31]
	ds_read_b128 v[180:183], v192 offset:5120
	v_mfma_f32_32x32x16_f16 v[0:15], a[252:255], v[184:187], v[0:15]
	ds_read_b128 v[184:187], v192 offset:6144
	v_mfma_f32_32x32x16_f16 v[16:31], a[252:255], v[188:191], v[16:31]
	ds_read_b128 v[188:191], v192 offset:7168
	s_add_u32 s44, s34, 0x10000
	s_addc_u32 s45, s35, 0
	s_mov_b32 m0, s56
	s_nop 0
	global_load_lds_dwordx4 v192, s[44:45] sc1
	s_nop 3
	s_waitcnt lgkmcnt(4)
	v_mfma_f32_32x32x16_f16 v[32:47], a[0:3], v[160:163], v[32:47]
	ds_read_b128 v[160:163], v192 offset:8192
	v_exp_f32_e32 v200, v0
	v_mfma_f32_32x32x16_f16 v[48:63], a[0:3], v[164:167], v[48:63]
	ds_read_b128 v[164:167], v192 offset:9216
	s_lshl_b32 s64, s71, 3
	s_add_u32 s64, s64, s29
	s_lshl_b32 s64, s64, 7
	s_add_u32 s38, s8, s64
	s_addc_u32 s39, s9, 0
	global_load_dword v251, v196, s[38:39] sc1
	v_exp_f32_e32 v201, v1
	v_add_f32_e32 v200, 1.0, v200
	v_mfma_f32_32x32x16_f16 v[32:47], a[4:7], v[168:171], v[32:47]
	ds_read_b128 v[168:171], v192 offset:10240
	v_exp_f32_e32 v202, v2
	v_add_f32_e32 v201, 1.0, v201
	v_mfma_f32_32x32x16_f16 v[48:63], a[4:7], v[172:175], v[48:63]
	ds_read_b128 v[172:175], v192 offset:11264
	global_load_lds_dwordx4 v192, s[44:45] offset:1024 sc1
	v_exp_f32_e32 v203, v3
	v_add_f32_e32 v202, 1.0, v202
	s_waitcnt lgkmcnt(4)
	v_mfma_f32_32x32x16_f16 v[32:47], a[8:11], v[176:179], v[32:47]
	ds_read_b128 v[176:179], v192 offset:12288
	v_exp_f32_e32 v204, v4
	v_add_f32_e32 v203, 1.0, v203
	v_mfma_f32_32x32x16_f16 v[48:63], a[8:11], v[180:183], v[48:63]
	ds_read_b128 v[180:183], v192 offset:13312
	v_exp_f32_e32 v205, v5
	v_add_f32_e32 v204, 1.0, v204
	v_mfma_f32_32x32x16_f16 v[32:47], a[12:15], v[184:187], v[32:47]
	ds_read_b128 v[184:187], v192 offset:14336
	v_exp_f32_e32 v206, v6
	v_add_f32_e32 v205, 1.0, v205
	v_mfma_f32_32x32x16_f16 v[48:63], a[12:15], v[188:191], v[48:63]
	ds_read_b128 v[188:191], v192 offset:15360
	global_load_lds_dwordx4 v192, s[44:45] offset:2048 sc1
	v_exp_f32_e32 v207, v7
	v_add_f32_e32 v206, 1.0, v206
	s_waitcnt lgkmcnt(4)
	v_mfma_f32_32x32x16_f16 v[32:47], a[16:19], v[160:163], v[32:47]
	ds_read_b128 v[160:163], v192 offset:16384
	v_exp_f32_e32 v208, v8
	v_add_f32_e32 v207, 1.0, v207
	v_mfma_f32_32x32x16_f16 v[48:63], a[16:19], v[164:167], v[48:63]
	ds_read_b128 v[164:167], v192 offset:17408
	v_exp_f32_e32 v209, v9
	v_add_f32_e32 v208, 1.0, v208
	v_mfma_f32_32x32x16_f16 v[32:47], a[20:23], v[168:171], v[32:47]
	ds_read_b128 v[168:171], v192 offset:18432
	v_exp_f32_e32 v210, v10
	v_add_f32_e32 v209, 1.0, v209
	v_mfma_f32_32x32x16_f16 v[48:63], a[20:23], v[172:175], v[48:63]
	ds_read_b128 v[172:175], v192 offset:19456
	global_load_lds_dwordx4 v192, s[44:45] offset:3072 sc1
	v_exp_f32_e32 v211, v11
	v_add_f32_e32 v210, 1.0, v210
	s_waitcnt lgkmcnt(4)
	v_mfma_f32_32x32x16_f16 v[32:47], a[24:27], v[176:179], v[32:47]
	ds_read_b128 v[176:179], v192 offset:20480
	v_exp_f32_e32 v212, v12
	v_add_f32_e32 v211, 1.0, v211
	v_mfma_f32_32x32x16_f16 v[48:63], a[24:27], v[180:183], v[48:63]
	ds_read_b128 v[180:183], v192 offset:21504
	v_exp_f32_e32 v213, v13
	v_add_f32_e32 v212, 1.0, v212
	v_mfma_f32_32x32x16_f16 v[32:47], a[28:31], v[184:187], v[32:47]
	ds_read_b128 v[184:187], v192 offset:22528
	v_exp_f32_e32 v214, v14
	v_add_f32_e32 v213, 1.0, v213
	v_mfma_f32_32x32x16_f16 v[48:63], a[28:31], v[188:191], v[48:63]
	ds_read_b128 v[188:191], v192 offset:23552
	s_add_u32 s44, s34, 0x11000
	s_addc_u32 s45, s35, 0
	s_mov_b32 m0, s57
	s_nop 0
	global_load_lds_dwordx4 v192, s[44:45] sc1
	v_exp_f32_e32 v215, v15
	v_add_f32_e32 v214, 1.0, v214
	s_waitcnt lgkmcnt(4)
	v_mfma_f32_32x32x16_f16 v[32:47], a[32:35], v[160:163], v[32:47]
	ds_read_b128 v[160:163], v192 offset:24576
	v_add_f32_e32 v215, 1.0, v215
	v_rcp_f32_e32 v200, v200
	v_mfma_f32_32x32x16_f16 v[48:63], a[32:35], v[164:167], v[48:63]
	ds_read_b128 v[164:167], v192 offset:25600
	v_rcp_f32_e32 v201, v201
	v_mfma_f32_32x32x16_f16 v[32:47], a[36:39], v[168:171], v[32:47]
	ds_read_b128 v[168:171], v192 offset:26624
	v_rcp_f32_e32 v202, v202
	v_mfma_f32_32x32x16_f16 v[48:63], a[36:39], v[172:175], v[48:63]
	ds_read_b128 v[172:175], v192 offset:27648
	global_load_lds_dwordx4 v192, s[44:45] offset:1024 sc1
	v_rcp_f32_e32 v203, v203
	s_waitcnt lgkmcnt(4)
	v_mfma_f32_32x32x16_f16 v[32:47], a[40:43], v[176:179], v[32:47]
	ds_read_b128 v[176:179], v192 offset:28672
	v_rcp_f32_e32 v204, v204
	v_mfma_f32_32x32x16_f16 v[48:63], a[40:43], v[180:183], v[48:63]
	ds_read_b128 v[180:183], v192 offset:29696
	v_rcp_f32_e32 v205, v205
	v_mul_f32_e32 v204, v204, v128
	v_mfma_f32_32x32x16_f16 v[32:47], a[44:47], v[184:187], v[32:47]
	ds_read_b128 v[184:187], v192 offset:30720
	v_rcp_f32_e32 v206, v206
	v_mul_f32_e32 v205, v205, v129
	v_mfma_f32_32x32x16_f16 v[48:63], a[44:47], v[188:191], v[48:63]
	ds_read_b128 v[188:191], v192 offset:31744
	global_load_lds_dwordx4 v192, s[44:45] offset:2048 sc1
	v_rcp_f32_e32 v207, v207
	v_mul_f32_e32 v206, v206, v130
	s_waitcnt vmcnt(8)
	s_barrier
	s_waitcnt lgkmcnt(4)
	v_mfma_f32_32x32x16_f16 v[32:47], a[48:51], v[160:163], v[32:47]
	ds_read_b128 v[160:163], v192 offset:32768
	v_rcp_f32_e32 v208, v208
	v_mul_f32_e32 v207, v207, v131
	v_mfma_f32_32x32x16_f16 v[48:63], a[48:51], v[164:167], v[48:63]
	ds_read_b128 v[164:167], v192 offset:33792
	v_rcp_f32_e32 v209, v209
	v_fmamk_f32 v208, v208, 0xc0b8aa3b, v198
	v_mfma_f32_32x32x16_f16 v[32:47], a[52:55], v[168:171], v[32:47]
	ds_read_b128 v[168:171], v192 offset:34816
	v_rcp_f32_e32 v210, v210
	v_fmamk_f32 v209, v209, 0xc0b8aa3b, v198
	v_fma_f32 v128, v200, v208, v204
	v_mfma_f32_32x32x16_f16 v[48:63], a[52:55], v[172:175], v[48:63]
	ds_read_b128 v[172:175], v192 offset:35840
	global_load_lds_dwordx4 v192, s[44:45] offset:3072 sc1
	v_rcp_f32_e32 v211, v211
	v_fmamk_f32 v210, v210, 0xc0b8aa3b, v198
	v_fma_f32 v129, v201, v209, v205
	s_waitcnt lgkmcnt(4)
	v_mfma_f32_32x32x16_f16 v[32:47], a[56:59], v[176:179], v[32:47]
	ds_read_b128 v[176:179], v192 offset:36864
	v_rcp_f32_e32 v212, v212
	v_fmamk_f32 v211, v211, 0xc0b8aa3b, v198
	v_fma_f32 v130, v202, v210, v206
	v_mfma_f32_32x32x16_f16 v[48:63], a[56:59], v[180:183], v[48:63]
	ds_read_b128 v[180:183], v192 offset:37888
	v_rcp_f32_e32 v213, v213
	v_fma_f32 v131, v203, v211, v207
	v_mfma_f32_32x32x16_f16 v[32:47], a[60:63], v[184:187], v[32:47]
	ds_read_b128 v[184:187], v192 offset:38912
	v_rcp_f32_e32 v214, v214
	v_mfma_f32_32x32x16_f16 v[48:63], a[60:63], v[188:191], v[48:63]
	ds_read_b128 v[188:191], v192 offset:39936
	s_add_u32 s44, s34, 0x18000
	s_addc_u32 s45, s35, 0
	s_mov_b32 m0, s58
	s_nop 0
	global_load_lds_dwordx4 v192, s[44:45] sc1
	v_rcp_f32_e32 v215, v215
	s_waitcnt lgkmcnt(4)
	v_mfma_f32_32x32x16_f16 v[32:47], a[64:67], v[160:163], v[32:47]
	ds_read_b128 v[160:163], v192 offset:40960
	v_exp_f32_e32 v200, v128
	v_mfma_f32_32x32x16_f16 v[48:63], a[64:67], v[164:167], v[48:63]
	ds_read_b128 v[164:167], v192 offset:41984
	v_exp_f32_e32 v201, v129
	v_add_f32_e32 v200, 1.0, v200
	v_mfma_f32_32x32x16_f16 v[32:47], a[68:71], v[168:171], v[32:47]
	ds_read_b128 v[168:171], v192 offset:43008
	v_exp_f32_e32 v202, v130
	v_add_f32_e32 v201, 1.0, v201
	v_mfma_f32_32x32x16_f16 v[48:63], a[68:71], v[172:175], v[48:63]
	ds_read_b128 v[172:175], v192 offset:44032
	global_load_lds_dwordx4 v192, s[44:45] offset:1024 sc1
	v_exp_f32_e32 v203, v131
	v_add_f32_e32 v202, 1.0, v202
	s_waitcnt lgkmcnt(4)
	v_mfma_f32_32x32x16_f16 v[32:47], a[72:75], v[176:179], v[32:47]
	ds_read_b128 v[176:179], v192 offset:45056
	v_add_f32_e32 v203, 1.0, v203
	v_rcp_f32_e32 v200, v200
	v_mfma_f32_32x32x16_f16 v[48:63], a[72:75], v[180:183], v[48:63]
	ds_read_b128 v[180:183], v192 offset:46080
	v_rcp_f32_e32 v201, v201
	v_fma_f32 v200, v200, 2.0, -1.0
	v_mfma_f32_32x32x16_f16 v[32:47], a[76:79], v[184:187], v[32:47]
	ds_read_b128 v[184:187], v192 offset:47104
	v_rcp_f32_e32 v202, v202
	v_fma_f32 v201, v201, 2.0, -1.0
	v_mul_f32_e32 v216, v212, v200
	v_mfma_f32_32x32x16_f16 v[48:63], a[76:79], v[188:191], v[48:63]
	ds_read_b128 v[188:191], v192 offset:48128
	global_load_lds_dwordx4 v192, s[44:45] offset:2048 sc1
	v_rcp_f32_e32 v203, v203
	v_fma_f32 v202, v202, 2.0, -1.0
	v_mul_f32_e32 v217, v213, v201
	s_waitcnt lgkmcnt(4)
	v_mfma_f32_32x32x16_f16 v[32:47], a[80:83], v[160:163], v[32:47]
	ds_read_b128 v[160:163], v192 offset:49152
	v_fma_f32 v203, v203, 2.0, -1.0
	v_mul_f32_e32 v218, v214, v202
	v_exp_f32_e32 v200, v16
	v_mfma_f32_32x32x16_f16 v[48:63], a[80:83], v[164:167], v[48:63]
	ds_read_b128 v[164:167], v192 offset:50176
	v_mul_f32_e32 v219, v215, v203
	v_mul_f32_e32 v236, v216, v228
	v_exp_f32_e32 v201, v17
	v_mfma_f32_32x32x16_f16 v[32:47], a[84:87], v[168:171], v[32:47]
	ds_read_b128 v[168:171], v192 offset:51200
	v_mul_f32_e32 v237, v216, v232
	v_fmac_f32_e32 v236, v217, v229
	v_exp_f32_e32 v202, v18
	v_mfma_f32_32x32x16_f16 v[48:63], a[84:87], v[172:175], v[48:63]
	ds_read_b128 v[172:175], v192 offset:52224
	global_load_lds_dwordx4 v192, s[44:45] offset:3072 sc1
	v_fmac_f32_e32 v237, v217, v233
	v_fmac_f32_e32 v236, v218, v230
	v_exp_f32_e32 v203, v19
	s_waitcnt lgkmcnt(4)
	v_mfma_f32_32x32x16_f16 v[32:47], a[88:91], v[176:179], v[32:47]
	ds_read_b128 v[176:179], v192 offset:53248
	v_fmac_f32_e32 v237, v218, v234
	v_fmac_f32_e32 v236, v219, v231
	v_exp_f32_e32 v204, v20
	v_mfma_f32_32x32x16_f16 v[48:63], a[88:91], v[180:183], v[48:63]
	ds_read_b128 v[180:183], v192 offset:54272
	v_fmac_f32_e32 v237, v219, v235
	v_mov_b32_e32 v238, v236
	v_exp_f32_e32 v205, v21
	v_mfma_f32_32x32x16_f16 v[32:47], a[92:95], v[184:187], v[32:47]
	ds_read_b128 v[184:187], v192 offset:55296
	v_mov_b32_e32 v239, v236
	v_mov_b32_e32 v240, v237
	v_exp_f32_e32 v206, v22
	v_mfma_f32_32x32x16_f16 v[48:63], a[92:95], v[188:191], v[48:63]
	ds_read_b128 v[188:191], v192 offset:56320
	s_add_u32 s44, s34, 0x19000
	s_addc_u32 s45, s35, 0
	s_mov_b32 m0, s59
	s_nop 0
	global_load_lds_dwordx4 v192, s[44:45] sc1
	v_mov_b32_e32 v241, v237
	v_cvt_pk_f16_f32 v220, v216, v217
	v_exp_f32_e32 v207, v23
	s_waitcnt lgkmcnt(4)
	v_mfma_f32_32x32x16_f16 v[32:47], a[96:99], v[160:163], v[32:47]
	ds_read_b128 v[160:163], v192 offset:57344
	s_nop 1
	v_permlane32_swap_b32_e32 v238, v239
	v_permlane32_swap_b32_e32 v240, v241
	v_add_f32_e32 v238, v238, v239
	v_add_f32_e32 v239, v240, v241
	ds_write_b64 v248, v[238:239] offset:0
	v_exp_f32_e32 v208, v24
	v_mfma_f32_32x32x16_f16 v[48:63], a[96:99], v[164:167], v[48:63]
	ds_read_b128 v[164:167], v192 offset:58368
	v_cvt_pk_f16_f32 v221, v218, v219
	v_exp_f32_e32 v209, v25
	v_add_f32_e32 v200, 1.0, v200
	v_mfma_f32_32x32x16_f16 v[32:47], a[100:103], v[168:171], v[32:47]
	ds_read_b128 v[168:171], v192 offset:59392
	v_exp_f32_e32 v210, v26
	v_add_f32_e32 v201, 1.0, v201
	v_add_f32_e32 v202, 1.0, v202
	v_mfma_f32_32x32x16_f16 v[48:63], a[100:103], v[172:175], v[48:63]
	ds_read_b128 v[172:175], v192 offset:60416
	global_load_lds_dwordx4 v192, s[44:45] offset:1024 sc1
	v_exp_f32_e32 v211, v27
	v_add_f32_e32 v203, 1.0, v203
	v_add_f32_e32 v204, 1.0, v204
	s_waitcnt lgkmcnt(5)
	v_mfma_f32_32x32x16_f16 v[32:47], a[104:107], v[176:179], v[32:47]
	ds_read_b128 v[176:179], v192 offset:61440
	v_exp_f32_e32 v212, v28
	v_add_f32_e32 v205, 1.0, v205
	v_add_f32_e32 v206, 1.0, v206
	v_mfma_f32_32x32x16_f16 v[48:63], a[104:107], v[180:183], v[48:63]
	ds_read_b128 v[180:183], v192 offset:62464
	v_exp_f32_e32 v213, v29
	v_add_f32_e32 v207, 1.0, v207
	v_add_f32_e32 v208, 1.0, v208
	v_mfma_f32_32x32x16_f16 v[32:47], a[108:111], v[184:187], v[32:47]
	ds_read_b128 v[184:187], v192 offset:63488
	v_exp_f32_e32 v214, v30
	v_add_f32_e32 v209, 1.0, v209
	v_add_f32_e32 v210, 1.0, v210
	v_mfma_f32_32x32x16_f16 v[48:63], a[108:111], v[188:191], v[48:63]
	ds_read_b128 v[188:191], v192 offset:64512
	global_load_lds_dwordx4 v192, s[44:45] offset:2048 sc1
	v_exp_f32_e32 v215, v31
	v_add_f32_e32 v211, 1.0, v211
	v_add_f32_e32 v212, 1.0, v212
	s_waitcnt vmcnt(7)
	s_barrier
	s_waitcnt lgkmcnt(4)
	v_mfma_f32_32x32x16_f16 v[32:47], a[112:115], v[160:163], v[32:47]
	ds_read_b128 v[160:163], v193 offset:0
	v_add_f32_e32 v213, 1.0, v213
	v_add_f32_e32 v214, 1.0, v214
	v_rcp_f32_e32 v200, v200
	v_mfma_f32_32x32x16_f16 v[48:63], a[112:115], v[164:167], v[48:63]
	ds_read_b128 v[164:167], v193 offset:1024
	v_add_f32_e32 v215, 1.0, v215
	v_rcp_f32_e32 v201, v201
	v_mfma_f32_32x32x16_f16 v[32:47], a[116:119], v[168:171], v[32:47]
	ds_read_b128 v[168:171], v193 offset:2048
	v_rcp_f32_e32 v202, v202
	v_mfma_f32_32x32x16_f16 v[48:63], a[116:119], v[172:175], v[48:63]
	ds_read_b128 v[172:175], v193 offset:3072
	global_load_lds_dwordx4 v192, s[44:45] offset:3072 sc1
	v_rcp_f32_e32 v203, v203
	s_waitcnt lgkmcnt(4)
	v_mfma_f32_32x32x16_f16 v[32:47], a[120:123], v[176:179], v[32:47]
	ds_read_b128 v[176:179], v193 offset:4096
	v_rcp_f32_e32 v204, v204
	s_add_u32 s46, s42, 0x6000
	s_addc_u32 s47, s43, 0
	global_load_dwordx4 v[96:99], v192, s[46:47] offset:0
	v_mfma_f32_32x32x16_f16 v[48:63], a[120:123], v[180:183], v[48:63]
	ds_read_b128 v[180:183], v193 offset:5120
	v_rcp_f32_e32 v205, v205
	v_mul_f32_e32 v204, v204, v132
	global_load_dwordx4 v[100:103], v192, s[46:47] offset:1024
	global_load_dwordx4 v[104:107], v192, s[46:47] offset:2048
	v_mfma_f32_32x32x16_f16 v[32:47], a[124:127], v[184:187], v[32:47]
	ds_read_b128 v[184:187], v193 offset:6144
	v_rcp_f32_e32 v206, v206
	v_mul_f32_e32 v205, v205, v133
	global_load_dwordx4 v[108:111], v192, s[46:47] offset:3072
	s_add_u32 s46, s42, 0x7000
	s_addc_u32 s47, s43, 0
	v_mfma_f32_32x32x16_f16 v[48:63], a[124:127], v[188:191], v[48:63]
	ds_read_b128 v[188:191], v193 offset:7168
	v_cmp_gt_u32_e32 vcc, 3, v251
	s_cbranch_vccnz .LD_tpoll27
.LD_tok26:
	s_and_b32 s64, s71, 1
	s_lshl_b32 s64, s64, 22
	s_add_u32 s64, s64, s49
	s_add_u32 s64, s64, 0x40000
	s_add_u32 s34, s6, s64
	s_addc_u32 s35, s7, 0
	s_add_u32 s44, s34, 0x0
	s_addc_u32 s45, s35, 0
	s_mov_b32 m0, s52
	s_nop 0
	global_load_lds_dwordx4 v192, s[44:45] sc1
	v_rcp_f32_e32 v207, v207
	v_mul_f32_e32 v206, v206, v134
	global_load_dwordx4 v[112:115], v192, s[46:47] offset:0
	global_load_dwordx4 v[116:119], v192, s[46:47] offset:1024
	s_waitcnt lgkmcnt(4)
	v_mfma_f32_32x32x16_f16 v[32:47], a[128:131], v[160:163], v[32:47]
	ds_read_b128 v[160:163], v193 offset:8192
	v_rcp_f32_e32 v208, v208
	v_mul_f32_e32 v207, v207, v135
	global_load_dwordx4 v[120:123], v192, s[46:47] offset:2048
	global_load_dwordx4 v[124:127], v192, s[46:47] offset:3072
	v_mfma_f32_32x32x16_f16 v[48:63], a[128:131], v[164:167], v[48:63]
	ds_read_b128 v[164:167], v193 offset:9216
	v_rcp_f32_e32 v209, v209
	v_fmamk_f32 v208, v208, 0xc0b8aa3b, v198
	v_mfma_f32_32x32x16_f16 v[32:47], a[132:135], v[168:171], v[32:47]
	ds_read_b128 v[168:171], v193 offset:10240
	v_rcp_f32_e32 v210, v210
	v_fmamk_f32 v209, v209, 0xc0b8aa3b, v198
	v_fma_f32 v132, v200, v208, v204
	v_mfma_f32_32x32x16_f16 v[48:63], a[132:135], v[172:175], v[48:63]
	ds_read_b128 v[172:175], v193 offset:11264
	global_load_lds_dwordx4 v192, s[44:45] offset:1024 sc1
	v_rcp_f32_e32 v211, v211
	v_fmamk_f32 v210, v210, 0xc0b8aa3b, v198
	v_fma_f32 v133, v201, v209, v205
	s_waitcnt lgkmcnt(4)
	v_mfma_f32_32x32x16_f16 v[32:47], a[136:139], v[176:179], v[32:47]
	ds_read_b128 v[176:179], v193 offset:12288
	v_rcp_f32_e32 v212, v212
	v_fmamk_f32 v211, v211, 0xc0b8aa3b, v198
	v_fma_f32 v134, v202, v210, v206
	v_mfma_f32_32x32x16_f16 v[48:63], a[136:139], v[180:183], v[48:63]
	ds_read_b128 v[180:183], v193 offset:13312
	v_rcp_f32_e32 v213, v213
	v_fma_f32 v135, v203, v211, v207
	v_mfma_f32_32x32x16_f16 v[32:47], a[140:143], v[184:187], v[32:47]
	ds_read_b128 v[184:187], v193 offset:14336
	v_rcp_f32_e32 v214, v214
	v_mfma_f32_32x32x16_f16 v[48:63], a[140:143], v[188:191], v[48:63]
	ds_read_b128 v[188:191], v193 offset:15360
	global_load_lds_dwordx4 v192, s[44:45] offset:2048 sc1
	v_rcp_f32_e32 v215, v215
	s_waitcnt lgkmcnt(4)
	v_mfma_f32_32x32x16_f16 v[32:47], a[144:147], v[160:163], v[32:47]
	ds_read_b128 v[160:163], v193 offset:16384
	v_exp_f32_e32 v200, v132
	v_mfma_f32_32x32x16_f16 v[48:63], a[144:147], v[164:167], v[48:63]
	ds_read_b128 v[164:167], v193 offset:17408
	v_exp_f32_e32 v201, v133
	v_add_f32_e32 v200, 1.0, v200
	v_mfma_f32_32x32x16_f16 v[32:47], a[148:151], v[168:171], v[32:47]
	ds_read_b128 v[168:171], v193 offset:18432
	v_exp_f32_e32 v202, v134
	v_add_f32_e32 v201, 1.0, v201
	v_mfma_f32_32x32x16_f16 v[48:63], a[148:151], v[172:175], v[48:63]
	ds_read_b128 v[172:175], v193 offset:19456
	global_load_lds_dwordx4 v192, s[44:45] offset:3072 sc1
	v_exp_f32_e32 v203, v135
	v_add_f32_e32 v202, 1.0, v202
	s_waitcnt lgkmcnt(4)
	v_mfma_f32_32x32x16_f16 v[32:47], a[152:155], v[176:179], v[32:47]
	ds_read_b128 v[176:179], v193 offset:20480
	v_add_f32_e32 v203, 1.0, v203
	v_rcp_f32_e32 v200, v200
	v_mfma_f32_32x32x16_f16 v[48:63], a[152:155], v[180:183], v[48:63]
	ds_read_b128 v[180:183], v193 offset:21504
	v_rcp_f32_e32 v201, v201
	v_fma_f32 v200, v200, 2.0, -1.0
	v_mfma_f32_32x32x16_f16 v[32:47], a[156:159], v[184:187], v[32:47]
	ds_read_b128 v[184:187], v193 offset:22528
	v_rcp_f32_e32 v202, v202
	v_fma_f32 v201, v201, 2.0, -1.0
	v_mul_f32_e32 v216, v212, v200
	v_mfma_f32_32x32x16_f16 v[48:63], a[156:159], v[188:191], v[48:63]
	ds_read_b128 v[188:191], v193 offset:23552
	s_add_u32 s44, s34, 0x1000
	s_addc_u32 s45, s35, 0
	s_mov_b32 m0, s53
	s_nop 0
	global_load_lds_dwordx4 v192, s[44:45] sc1
	v_rcp_f32_e32 v203, v203
	v_fma_f32 v202, v202, 2.0, -1.0
	v_mul_f32_e32 v217, v213, v201
	s_waitcnt lgkmcnt(4)
	v_mfma_f32_32x32x16_f16 v[32:47], a[160:163], v[160:163], v[32:47]
	ds_read_b128 v[160:163], v193 offset:24576
	v_fma_f32 v203, v203, 2.0, -1.0
	v_mul_f32_e32 v218, v214, v202
	v_mfma_f32_32x32x16_f16 v[48:63], a[160:163], v[164:167], v[48:63]
	ds_read_b128 v[164:167], v193 offset:25600
	v_mul_f32_e32 v219, v215, v203
	v_mul_f32_e32 v236, v216, v228
	v_mfma_f32_32x32x16_f16 v[32:47], a[164:167], v[168:171], v[32:47]
	ds_read_b128 v[168:171], v193 offset:26624
	v_mul_f32_e32 v237, v216, v232
	v_fmac_f32_e32 v236, v217, v229
	v_mfma_f32_32x32x16_f16 v[48:63], a[164:167], v[172:175], v[48:63]
	ds_read_b128 v[172:175], v193 offset:27648
	global_load_lds_dwordx4 v192, s[44:45] offset:1024 sc1
	v_fmac_f32_e32 v237, v217, v233
	v_fmac_f32_e32 v236, v218, v230
	s_waitcnt lgkmcnt(4)
	v_mfma_f32_32x32x16_f16 v[32:47], a[168:171], v[176:179], v[32:47]
	ds_read_b128 v[176:179], v193 offset:28672
	v_fmac_f32_e32 v237, v218, v234
	v_fmac_f32_e32 v236, v219, v231
	v_mfma_f32_32x32x16_f16 v[48:63], a[168:171], v[180:183], v[48:63]
	ds_read_b128 v[180:183], v193 offset:29696
	v_fmac_f32_e32 v237, v219, v235
	v_mov_b32_e32 v238, v236
	v_mfma_f32_32x32x16_f16 v[32:47], a[172:175], v[184:187], v[32:47]
	ds_read_b128 v[184:187], v193 offset:30720
	v_mov_b32_e32 v239, v236
	v_mov_b32_e32 v240, v237
	v_mfma_f32_32x32x16_f16 v[48:63], a[172:175], v[188:191], v[48:63]
	ds_read_b128 v[188:191], v193 offset:31744
	global_load_lds_dwordx4 v192, s[44:45] offset:2048 sc1
	v_mov_b32_e32 v241, v237
	v_cvt_pk_f16_f32 v222, v216, v217
	s_waitcnt vmcnt(15)
	s_barrier
	s_waitcnt lgkmcnt(4)
	v_mfma_f32_32x32x16_f16 v[32:47], a[176:179], v[160:163], v[32:47]
	ds_read_b128 v[160:163], v193 offset:32768
	s_nop 1
	v_permlane32_swap_b32_e32 v238, v239
	v_permlane32_swap_b32_e32 v240, v241
	v_add_f32_e32 v238, v238, v239
	v_add_f32_e32 v239, v240, v241
	ds_write_b64 v248, v[238:239] offset:256
	v_mfma_f32_32x32x16_f16 v[48:63], a[176:179], v[164:167], v[48:63]
	ds_read_b128 v[164:167], v193 offset:33792
	v_cvt_pk_f16_f32 v223, v218, v219
	v_mfma_f32_32x32x16_f16 v[32:47], a[180:183], v[168:171], v[32:47]
	ds_read_b128 v[168:171], v193 offset:34816
	s_nop 1
	v_permlane32_swap_b32_e32 v220, v222
	v_permlane32_swap_b32_e32 v221, v223
	s_cmp_eq_u32 s31, 0
	s_cbranch_scc1 .LD_slow28
	global_store_dwordx4 v195, v[220:223], s[36:37] offset:0
.LD_join29:
	v_mfma_f32_32x32x16_f16 v[48:63], a[180:183], v[172:175], v[48:63]
	ds_read_b128 v[172:175], v193 offset:35840
	global_load_lds_dwordx4 v192, s[44:45] offset:3072 sc1
	s_waitcnt lgkmcnt(5)
	v_mfma_f32_32x32x16_f16 v[32:47], a[184:187], v[176:179], v[32:47]
	ds_read_b128 v[176:179], v193 offset:36864
	v_mfma_f32_32x32x16_f16 v[48:63], a[184:187], v[180:183], v[48:63]
	ds_read_b128 v[180:183], v193 offset:37888
	v_mfma_f32_32x32x16_f16 v[32:47], a[188:191], v[184:187], v[32:47]
	ds_read_b128 v[184:187], v193 offset:38912
	v_mfma_f32_32x32x16_f16 v[48:63], a[188:191], v[188:191], v[48:63]
	ds_read_b128 v[188:191], v193 offset:39936
	s_add_u32 s44, s34, 0x8000
	s_addc_u32 s45, s35, 0
	s_mov_b32 m0, s54
	s_nop 0
	global_load_lds_dwordx4 v192, s[44:45] sc1
	s_waitcnt lgkmcnt(4)
	v_mfma_f32_32x32x16_f16 v[32:47], a[192:195], v[160:163], v[32:47]
	ds_read_b128 v[160:163], v193 offset:40960
	v_mfma_f32_32x32x16_f16 v[48:63], a[192:195], v[164:167], v[48:63]
	ds_read_b128 v[164:167], v193 offset:41984
	v_mfma_f32_32x32x16_f16 v[32:47], a[196:199], v[168:171], v[32:47]
	ds_read_b128 v[168:171], v193 offset:43008
	v_mfma_f32_32x32x16_f16 v[48:63], a[196:199], v[172:175], v[48:63]
	ds_read_b128 v[172:175], v193 offset:44032
	global_load_lds_dwordx4 v192, s[44:45] offset:1024 sc1
	s_waitcnt lgkmcnt(4)
	v_mfma_f32_32x32x16_f16 v[32:47], a[200:203], v[176:179], v[32:47]
	ds_read_b128 v[176:179], v193 offset:45056
	v_mfma_f32_32x32x16_f16 v[48:63], a[200:203], v[180:183], v[48:63]
	ds_read_b128 v[180:183], v193 offset:46080
	v_mfma_f32_32x32x16_f16 v[32:47], a[204:207], v[184:187], v[32:47]
	ds_read_b128 v[184:187], v193 offset:47104
	v_mfma_f32_32x32x16_f16 v[48:63], a[204:207], v[188:191], v[48:63]
	ds_read_b128 v[188:191], v193 offset:48128
	global_load_lds_dwordx4 v192, s[44:45] offset:2048 sc1
	s_waitcnt vmcnt(4)
	s_barrier
	v_mov_b32_e32 v199, 1
	s_cmp_eq_u32 s31, 0
	s_cbranch_scc1 .LD_slow30
	global_store_dword v197, v199, s[40:41]
.LD_join31:
	ds_read_b64 v[200:201], v249 offset:0
	ds_read_b64 v[202:203], v249 offset:2048
	ds_read_b64 v[204:205], v249 offset:4096
	ds_read_b64 v[206:207], v249 offset:6144
	s_waitcnt lgkmcnt(8)
	v_mfma_f32_32x32x16_f16 v[32:47], a[208:211], v[160:163], v[32:47]
	ds_read_b128 v[160:163], v193 offset:49152
	v_mfma_f32_32x32x16_f16 v[48:63], a[208:211], v[164:167], v[48:63]
	ds_read_b128 v[164:167], v193 offset:50176
	v_mfma_f32_32x32x16_f16 v[32:47], a[212:215], v[168:171], v[32:47]
	ds_read_b128 v[168:171], v193 offset:51200
	v_mfma_f32_32x32x16_f16 v[48:63], a[212:215], v[172:175], v[48:63]
	ds_read_b128 v[172:175], v193 offset:52224
	global_load_lds_dwordx4 v192, s[44:45] offset:3072 sc1
	s_waitcnt lgkmcnt(8)
	v_mfma_f32_32x32x16_f16 v[32:47], a[216:219], v[176:179], v[32:47]
	ds_read_b128 v[176:179], v193 offset:53248
	v_mfma_f32_32x32x16_f16 v[48:63], a[216:219], v[180:183], v[48:63]
	ds_read_b128 v[180:183], v193 offset:54272
	v_mfma_f32_32x32x16_f16 v[32:47], a[220:223], v[184:187], v[32:47]
	ds_read_b128 v[184:187], v193 offset:55296
	v_mfma_f32_32x32x16_f16 v[48:63], a[220:223], v[188:191], v[48:63]
	ds_read_b128 v[188:191], v193 offset:56320
	s_add_u32 s44, s34, 0x9000
	s_addc_u32 s45, s35, 0
	s_mov_b32 m0, s55
	s_nop 0
	global_load_lds_dwordx4 v192, s[44:45] sc1
	s_waitcnt lgkmcnt(4)
	v_mfma_f32_32x32x16_f16 v[32:47], a[224:227], v[160:163], v[32:47]
	ds_read_b128 v[160:163], v193 offset:57344
	v_mfma_f32_32x32x16_f16 v[48:63], a[224:227], v[164:167], v[48:63]
	ds_read_b128 v[164:167], v193 offset:58368
	v_mfma_f32_32x32x16_f16 v[32:47], a[228:231], v[168:171], v[32:47]
	ds_read_b128 v[168:171], v193 offset:59392
	v_mfma_f32_32x32x16_f16 v[48:63], a[228:231], v[172:175], v[48:63]
	ds_read_b128 v[172:175], v193 offset:60416
	global_load_lds_dwordx4 v192, s[44:45] offset:1024 sc1
	v_add_f32_e32 v200, v200, v202
	v_add_f32_e32 v201, v201, v203
	v_add_f32_e32 v200, v200, v204
	v_add_f32_e32 v201, v201, v205
	v_add_f32_e32 v200, v200, v206
	v_add_f32_e32 v201, v201, v207
	global_store_dwordx2 v250, v[200:201], s[72:73]
	s_waitcnt lgkmcnt(4)
	v_mfma_f32_32x32x16_f16 v[32:47], a[232:235], v[176:179], v[32:47]
	ds_read_b128 v[176:179], v193 offset:61440
	v_mfma_f32_32x32x16_f16 v[48:63], a[232:235], v[180:183], v[48:63]
	ds_read_b128 v[180:183], v193 offset:62464
	v_mfma_f32_32x32x16_f16 v[32:47], a[236:239], v[184:187], v[32:47]
	ds_read_b128 v[184:187], v193 offset:63488
	v_mfma_f32_32x32x16_f16 v[48:63], a[236:239], v[188:191], v[48:63]
	ds_read_b128 v[188:191], v193 offset:64512
	global_load_lds_dwordx4 v192, s[44:45] offset:2048 sc1
	s_and_b32 s64, s33, 1
	s_lshl_b32 s64, s64, 22
	s_add_u32 s64, s64, s50
	s_add_u32 s64, s64, 0x20000
	s_add_u32 s36, s6, s64
	s_addc_u32 s37, s7, 0
	s_lshl_b32 s64, s33, 3
	s_add_u32 s64, s64, s29
	s_lshl_b32 s64, s64, 5
	s_add_u32 s64, s64, s30
	s_lshl_b32 s64, s64, 2
	s_add_u32 s40, s8, s64
	s_addc_u32 s41, s9, 0
	s_lshl_b32 s64, s33, 19
	s_add_u32 s64, s64, 0x200
	s_add_u32 s72, s62, s64
	s_addc_u32 s73, s63, 0
	s_waitcnt vmcnt(9)
	s_barrier
	s_waitcnt lgkmcnt(4)
	v_mfma_f32_32x32x16_f16 v[32:47], a[240:243], v[160:163], v[32:47]
	ds_read_b128 v[160:163], v192 offset:0
	v_mfma_f32_32x32x16_f16 v[48:63], a[240:243], v[164:167], v[48:63]
	ds_read_b128 v[164:167], v192 offset:1024
	v_mfma_f32_32x32x16_f16 v[32:47], a[244:247], v[168:171], v[32:47]
	ds_read_b128 v[168:171], v192 offset:2048
	v_mfma_f32_32x32x16_f16 v[48:63], a[244:247], v[172:175], v[48:63]
	ds_read_b128 v[172:175], v192 offset:3072
	global_load_lds_dwordx4 v192, s[44:45] offset:3072 sc1
	s_waitcnt lgkmcnt(4)
	v_mfma_f32_32x32x16_f16 v[32:47], a[248:251], v[176:179], v[32:47]
	ds_read_b128 v[176:179], v192 offset:4096
	v_mfma_f32_32x32x16_f16 v[48:63], a[248:251], v[180:183], v[48:63]
	ds_read_b128 v[180:183], v192 offset:5120
	v_mfma_f32_32x32x16_f16 v[32:47], a[252:255], v[184:187], v[32:47]
	ds_read_b128 v[184:187], v192 offset:6144
	v_mfma_f32_32x32x16_f16 v[48:63], a[252:255], v[188:191], v[48:63]
	ds_read_b128 v[188:191], v192 offset:7168
	s_add_u32 s44, s34, 0x10000
	s_addc_u32 s45, s35, 0
	s_mov_b32 m0, s56
	s_nop 0
	global_load_lds_dwordx4 v192, s[44:45] sc1
	s_nop 3
	s_waitcnt lgkmcnt(4)
	v_mfma_f32_32x32x16_f16 v[64:79], a[0:3], v[160:163], v[64:79]
	ds_read_b128 v[160:163], v192 offset:8192
	v_exp_f32_e32 v200, v32
	v_mfma_f32_32x32x16_f16 v[80:95], a[0:3], v[164:167], v[80:95]
	ds_read_b128 v[164:167], v192 offset:9216
	s_lshl_b32 s64, s71, 3
	s_add_u32 s64, s64, s29
	s_lshl_b32 s64, s64, 7
	s_add_u32 s38, s8, s64
	s_addc_u32 s39, s9, 0
	global_load_dword v251, v196, s[38:39] sc1
	v_exp_f32_e32 v201, v33
	v_add_f32_e32 v200, 1.0, v200
	v_mfma_f32_32x32x16_f16 v[64:79], a[4:7], v[168:171], v[64:79]
	ds_read_b128 v[168:171], v192 offset:10240
	v_exp_f32_e32 v202, v34
	v_add_f32_e32 v201, 1.0, v201
	v_mfma_f32_32x32x16_f16 v[80:95], a[4:7], v[172:175], v[80:95]
	ds_read_b128 v[172:175], v192 offset:11264
	global_load_lds_dwordx4 v192, s[44:45] offset:1024 sc1
	v_exp_f32_e32 v203, v35
	v_add_f32_e32 v202, 1.0, v202
	s_waitcnt lgkmcnt(4)
	v_mfma_f32_32x32x16_f16 v[64:79], a[8:11], v[176:179], v[64:79]
	ds_read_b128 v[176:179], v192 offset:12288
	v_exp_f32_e32 v204, v36
	v_add_f32_e32 v203, 1.0, v203
	v_mfma_f32_32x32x16_f16 v[80:95], a[8:11], v[180:183], v[80:95]
	ds_read_b128 v[180:183], v192 offset:13312
	v_exp_f32_e32 v205, v37
	v_add_f32_e32 v204, 1.0, v204
	v_mfma_f32_32x32x16_f16 v[64:79], a[12:15], v[184:187], v[64:79]
	ds_read_b128 v[184:187], v192 offset:14336
	v_exp_f32_e32 v206, v38
	v_add_f32_e32 v205, 1.0, v205
	v_mfma_f32_32x32x16_f16 v[80:95], a[12:15], v[188:191], v[80:95]
	ds_read_b128 v[188:191], v192 offset:15360
	global_load_lds_dwordx4 v192, s[44:45] offset:2048 sc1
	v_exp_f32_e32 v207, v39
	v_add_f32_e32 v206, 1.0, v206
	s_waitcnt lgkmcnt(4)
	v_mfma_f32_32x32x16_f16 v[64:79], a[16:19], v[160:163], v[64:79]
	ds_read_b128 v[160:163], v192 offset:16384
	v_exp_f32_e32 v208, v40
	v_add_f32_e32 v207, 1.0, v207
	v_mfma_f32_32x32x16_f16 v[80:95], a[16:19], v[164:167], v[80:95]
	ds_read_b128 v[164:167], v192 offset:17408
	v_exp_f32_e32 v209, v41
	v_add_f32_e32 v208, 1.0, v208
	v_mfma_f32_32x32x16_f16 v[64:79], a[20:23], v[168:171], v[64:79]
	ds_read_b128 v[168:171], v192 offset:18432
	v_exp_f32_e32 v210, v42
	v_add_f32_e32 v209, 1.0, v209
	v_mfma_f32_32x32x16_f16 v[80:95], a[20:23], v[172:175], v[80:95]
	ds_read_b128 v[172:175], v192 offset:19456
	global_load_lds_dwordx4 v192, s[44:45] offset:3072 sc1
	v_exp_f32_e32 v211, v43
	v_add_f32_e32 v210, 1.0, v210
	s_waitcnt lgkmcnt(4)
	v_mfma_f32_32x32x16_f16 v[64:79], a[24:27], v[176:179], v[64:79]
	ds_read_b128 v[176:179], v192 offset:20480
	v_exp_f32_e32 v212, v44
	v_add_f32_e32 v211, 1.0, v211
	v_mfma_f32_32x32x16_f16 v[80:95], a[24:27], v[180:183], v[80:95]
	ds_read_b128 v[180:183], v192 offset:21504
	v_exp_f32_e32 v213, v45
	v_add_f32_e32 v212, 1.0, v212
	v_mfma_f32_32x32x16_f16 v[64:79], a[28:31], v[184:187], v[64:79]
	ds_read_b128 v[184:187], v192 offset:22528
	v_exp_f32_e32 v214, v46
	v_add_f32_e32 v213, 1.0, v213
	v_mfma_f32_32x32x16_f16 v[80:95], a[28:31], v[188:191], v[80:95]
	ds_read_b128 v[188:191], v192 offset:23552
	s_add_u32 s44, s34, 0x11000
	s_addc_u32 s45, s35, 0
	s_mov_b32 m0, s57
	s_nop 0
	global_load_lds_dwordx4 v192, s[44:45] sc1
	v_exp_f32_e32 v215, v47
	v_add_f32_e32 v214, 1.0, v214
	s_waitcnt lgkmcnt(4)
	v_mfma_f32_32x32x16_f16 v[64:79], a[32:35], v[160:163], v[64:79]
	ds_read_b128 v[160:163], v192 offset:24576
	v_add_f32_e32 v215, 1.0, v215
	v_rcp_f32_e32 v200, v200
	v_mfma_f32_32x32x16_f16 v[80:95], a[32:35], v[164:167], v[80:95]
	ds_read_b128 v[164:167], v192 offset:25600
	v_rcp_f32_e32 v201, v201
	v_mfma_f32_32x32x16_f16 v[64:79], a[36:39], v[168:171], v[64:79]
	ds_read_b128 v[168:171], v192 offset:26624
	v_rcp_f32_e32 v202, v202
	v_mfma_f32_32x32x16_f16 v[80:95], a[36:39], v[172:175], v[80:95]
	ds_read_b128 v[172:175], v192 offset:27648
	global_load_lds_dwordx4 v192, s[44:45] offset:1024 sc1
	v_rcp_f32_e32 v203, v203
	s_waitcnt lgkmcnt(4)
	v_mfma_f32_32x32x16_f16 v[64:79], a[40:43], v[176:179], v[64:79]
	ds_read_b128 v[176:179], v192 offset:28672
	v_rcp_f32_e32 v204, v204
	v_mfma_f32_32x32x16_f16 v[80:95], a[40:43], v[180:183], v[80:95]
	ds_read_b128 v[180:183], v192 offset:29696
	v_rcp_f32_e32 v205, v205
	v_mul_f32_e32 v204, v204, v136
	v_mfma_f32_32x32x16_f16 v[64:79], a[44:47], v[184:187], v[64:79]
	ds_read_b128 v[184:187], v192 offset:30720
	v_rcp_f32_e32 v206, v206
	v_mul_f32_e32 v205, v205, v137
	v_mfma_f32_32x32x16_f16 v[80:95], a[44:47], v[188:191], v[80:95]
	ds_read_b128 v[188:191], v192 offset:31744
	global_load_lds_dwordx4 v192, s[44:45] offset:2048 sc1
	v_rcp_f32_e32 v207, v207
	v_mul_f32_e32 v206, v206, v138
	s_waitcnt vmcnt(8)
	s_barrier
	s_waitcnt lgkmcnt(4)
	v_mfma_f32_32x32x16_f16 v[64:79], a[48:51], v[160:163], v[64:79]
	ds_read_b128 v[160:163], v192 offset:32768
	v_rcp_f32_e32 v208, v208
	v_mul_f32_e32 v207, v207, v139
	v_mfma_f32_32x32x16_f16 v[80:95], a[48:51], v[164:167], v[80:95]
	ds_read_b128 v[164:167], v192 offset:33792
	v_rcp_f32_e32 v209, v209
	v_fmamk_f32 v208, v208, 0xc0b8aa3b, v198
	v_mfma_f32_32x32x16_f16 v[64:79], a[52:55], v[168:171], v[64:79]
	ds_read_b128 v[168:171], v192 offset:34816
	v_rcp_f32_e32 v210, v210
	v_fmamk_f32 v209, v209, 0xc0b8aa3b, v198
	v_fma_f32 v136, v200, v208, v204
	v_mfma_f32_32x32x16_f16 v[80:95], a[52:55], v[172:175], v[80:95]
	ds_read_b128 v[172:175], v192 offset:35840
	global_load_lds_dwordx4 v192, s[44:45] offset:3072 sc1
	v_rcp_f32_e32 v211, v211
	v_fmamk_f32 v210, v210, 0xc0b8aa3b, v198
	v_fma_f32 v137, v201, v209, v205
	s_waitcnt lgkmcnt(4)
	v_mfma_f32_32x32x16_f16 v[64:79], a[56:59], v[176:179], v[64:79]
	ds_read_b128 v[176:179], v192 offset:36864
	v_rcp_f32_e32 v212, v212
	v_fmamk_f32 v211, v211, 0xc0b8aa3b, v198
	v_fma_f32 v138, v202, v210, v206
	v_mfma_f32_32x32x16_f16 v[80:95], a[56:59], v[180:183], v[80:95]
	ds_read_b128 v[180:183], v192 offset:37888
	v_rcp_f32_e32 v213, v213
	v_fma_f32 v139, v203, v211, v207
	v_mfma_f32_32x32x16_f16 v[64:79], a[60:63], v[184:187], v[64:79]
	ds_read_b128 v[184:187], v192 offset:38912
	v_rcp_f32_e32 v214, v214
	v_mfma_f32_32x32x16_f16 v[80:95], a[60:63], v[188:191], v[80:95]
	ds_read_b128 v[188:191], v192 offset:39936
	s_add_u32 s44, s34, 0x18000
	s_addc_u32 s45, s35, 0
	s_mov_b32 m0, s58
	s_nop 0
	global_load_lds_dwordx4 v192, s[44:45] sc1
	v_rcp_f32_e32 v215, v215
	s_waitcnt lgkmcnt(4)
	v_mfma_f32_32x32x16_f16 v[64:79], a[64:67], v[160:163], v[64:79]
	ds_read_b128 v[160:163], v192 offset:40960
	v_exp_f32_e32 v200, v136
	v_mfma_f32_32x32x16_f16 v[80:95], a[64:67], v[164:167], v[80:95]
	ds_read_b128 v[164:167], v192 offset:41984
	v_exp_f32_e32 v201, v137
	v_add_f32_e32 v200, 1.0, v200
	v_mfma_f32_32x32x16_f16 v[64:79], a[68:71], v[168:171], v[64:79]
	ds_read_b128 v[168:171], v192 offset:43008
	v_exp_f32_e32 v202, v138
	v_add_f32_e32 v201, 1.0, v201
	v_mfma_f32_32x32x16_f16 v[80:95], a[68:71], v[172:175], v[80:95]
	ds_read_b128 v[172:175], v192 offset:44032
	global_load_lds_dwordx4 v192, s[44:45] offset:1024 sc1
	v_exp_f32_e32 v203, v139
	v_add_f32_e32 v202, 1.0, v202
	s_waitcnt lgkmcnt(4)
	v_mfma_f32_32x32x16_f16 v[64:79], a[72:75], v[176:179], v[64:79]
	ds_read_b128 v[176:179], v192 offset:45056
	v_add_f32_e32 v203, 1.0, v203
	v_rcp_f32_e32 v200, v200
	v_mfma_f32_32x32x16_f16 v[80:95], a[72:75], v[180:183], v[80:95]
	ds_read_b128 v[180:183], v192 offset:46080
	v_rcp_f32_e32 v201, v201
	v_fma_f32 v200, v200, 2.0, -1.0
	v_mfma_f32_32x32x16_f16 v[64:79], a[76:79], v[184:187], v[64:79]
	ds_read_b128 v[184:187], v192 offset:47104
	v_rcp_f32_e32 v202, v202
	v_fma_f32 v201, v201, 2.0, -1.0
	v_mul_f32_e32 v216, v212, v200
	v_mfma_f32_32x32x16_f16 v[80:95], a[76:79], v[188:191], v[80:95]
	ds_read_b128 v[188:191], v192 offset:48128
	global_load_lds_dwordx4 v192, s[44:45] offset:2048 sc1
	v_rcp_f32_e32 v203, v203
	v_fma_f32 v202, v202, 2.0, -1.0
	v_mul_f32_e32 v217, v213, v201
	s_waitcnt lgkmcnt(4)
	v_mfma_f32_32x32x16_f16 v[64:79], a[80:83], v[160:163], v[64:79]
	ds_read_b128 v[160:163], v192 offset:49152
	v_fma_f32 v203, v203, 2.0, -1.0
	v_mul_f32_e32 v218, v214, v202
	v_exp_f32_e32 v200, v48
	v_mfma_f32_32x32x16_f16 v[80:95], a[80:83], v[164:167], v[80:95]
	ds_read_b128 v[164:167], v192 offset:50176
	v_mul_f32_e32 v219, v215, v203
	v_mul_f32_e32 v236, v216, v228
	v_exp_f32_e32 v201, v49
	v_mfma_f32_32x32x16_f16 v[64:79], a[84:87], v[168:171], v[64:79]
	ds_read_b128 v[168:171], v192 offset:51200
	v_mul_f32_e32 v237, v216, v232
	v_fmac_f32_e32 v236, v217, v229
	v_exp_f32_e32 v202, v50
	v_mfma_f32_32x32x16_f16 v[80:95], a[84:87], v[172:175], v[80:95]
	ds_read_b128 v[172:175], v192 offset:52224
	global_load_lds_dwordx4 v192, s[44:45] offset:3072 sc1
	v_fmac_f32_e32 v237, v217, v233
	v_fmac_f32_e32 v236, v218, v230
	v_exp_f32_e32 v203, v51
	s_waitcnt lgkmcnt(4)
	v_mfma_f32_32x32x16_f16 v[64:79], a[88:91], v[176:179], v[64:79]
	ds_read_b128 v[176:179], v192 offset:53248
	v_fmac_f32_e32 v237, v218, v234
	v_fmac_f32_e32 v236, v219, v231
	v_exp_f32_e32 v204, v52
	v_mfma_f32_32x32x16_f16 v[80:95], a[88:91], v[180:183], v[80:95]
	ds_read_b128 v[180:183], v192 offset:54272
	v_fmac_f32_e32 v237, v219, v235
	v_mov_b32_e32 v238, v236
	v_exp_f32_e32 v205, v53
	v_mfma_f32_32x32x16_f16 v[64:79], a[92:95], v[184:187], v[64:79]
	ds_read_b128 v[184:187], v192 offset:55296
	v_mov_b32_e32 v239, v236
	v_mov_b32_e32 v240, v237
	v_exp_f32_e32 v206, v54
	v_mfma_f32_32x32x16_f16 v[80:95], a[92:95], v[188:191], v[80:95]
	ds_read_b128 v[188:191], v192 offset:56320
	s_add_u32 s44, s34, 0x19000
	s_addc_u32 s45, s35, 0
	s_mov_b32 m0, s59
	s_nop 0
	global_load_lds_dwordx4 v192, s[44:45] sc1
	v_mov_b32_e32 v241, v237
	v_cvt_pk_f16_f32 v220, v216, v217
	v_exp_f32_e32 v207, v55
	s_waitcnt lgkmcnt(4)
	v_mfma_f32_32x32x16_f16 v[64:79], a[96:99], v[160:163], v[64:79]
	ds_read_b128 v[160:163], v192 offset:57344
	s_nop 1
	v_permlane32_swap_b32_e32 v238, v239
	v_permlane32_swap_b32_e32 v240, v241
	v_add_f32_e32 v238, v238, v239
	v_add_f32_e32 v239, v240, v241
	ds_write_b64 v248, v[238:239] offset:512
	v_exp_f32_e32 v208, v56
	v_mfma_f32_32x32x16_f16 v[80:95], a[96:99], v[164:167], v[80:95]
	ds_read_b128 v[164:167], v192 offset:58368
	v_cvt_pk_f16_f32 v221, v218, v219
	v_exp_f32_e32 v209, v57
	v_add_f32_e32 v200, 1.0, v200
	v_mfma_f32_32x32x16_f16 v[64:79], a[100:103], v[168:171], v[64:79]
	ds_read_b128 v[168:171], v192 offset:59392
	v_exp_f32_e32 v210, v58
	v_add_f32_e32 v201, 1.0, v201
	v_add_f32_e32 v202, 1.0, v202
	v_mfma_f32_32x32x16_f16 v[80:95], a[100:103], v[172:175], v[80:95]
	ds_read_b128 v[172:175], v192 offset:60416
	global_load_lds_dwordx4 v192, s[44:45] offset:1024 sc1
	v_exp_f32_e32 v211, v59
	v_add_f32_e32 v203, 1.0, v203
	v_add_f32_e32 v204, 1.0, v204
	s_waitcnt lgkmcnt(5)
	v_mfma_f32_32x32x16_f16 v[64:79], a[104:107], v[176:179], v[64:79]
	ds_read_b128 v[176:179], v192 offset:61440
	v_exp_f32_e32 v212, v60
	v_add_f32_e32 v205, 1.0, v205
	v_add_f32_e32 v206, 1.0, v206
	v_mfma_f32_32x32x16_f16 v[80:95], a[104:107], v[180:183], v[80:95]
	ds_read_b128 v[180:183], v192 offset:62464
	v_exp_f32_e32 v213, v61
	v_add_f32_e32 v207, 1.0, v207
	v_add_f32_e32 v208, 1.0, v208
	v_mfma_f32_32x32x16_f16 v[64:79], a[108:111], v[184:187], v[64:79]
	ds_read_b128 v[184:187], v192 offset:63488
	v_exp_f32_e32 v214, v62
	v_add_f32_e32 v209, 1.0, v209
	v_add_f32_e32 v210, 1.0, v210
	v_mfma_f32_32x32x16_f16 v[80:95], a[108:111], v[188:191], v[80:95]
	ds_read_b128 v[188:191], v192 offset:64512
	global_load_lds_dwordx4 v192, s[44:45] offset:2048 sc1
	v_exp_f32_e32 v215, v63
	v_add_f32_e32 v211, 1.0, v211
	v_add_f32_e32 v212, 1.0, v212
	s_waitcnt vmcnt(7)
	s_barrier
	s_waitcnt lgkmcnt(4)
	v_mfma_f32_32x32x16_f16 v[64:79], a[112:115], v[160:163], v[64:79]
	ds_read_b128 v[160:163], v193 offset:0
	v_add_f32_e32 v213, 1.0, v213
	v_add_f32_e32 v214, 1.0, v214
	v_rcp_f32_e32 v200, v200
	v_mfma_f32_32x32x16_f16 v[80:95], a[112:115], v[164:167], v[80:95]
	ds_read_b128 v[164:167], v193 offset:1024
	v_add_f32_e32 v215, 1.0, v215
	v_rcp_f32_e32 v201, v201
	v_mfma_f32_32x32x16_f16 v[64:79], a[116:119], v[168:171], v[64:79]
	ds_read_b128 v[168:171], v193 offset:2048
	v_rcp_f32_e32 v202, v202
	v_mfma_f32_32x32x16_f16 v[80:95], a[116:119], v[172:175], v[80:95]
	ds_read_b128 v[172:175], v193 offset:3072
	global_load_lds_dwordx4 v192, s[44:45] offset:3072 sc1
	v_rcp_f32_e32 v203, v203
	s_waitcnt lgkmcnt(4)
	v_mfma_f32_32x32x16_f16 v[64:79], a[120:123], v[176:179], v[64:79]
	ds_read_b128 v[176:179], v193 offset:4096
	v_rcp_f32_e32 v204, v204
	s_add_u32 s46, s42, 0x0
	s_addc_u32 s47, s43, 0
	global_load_dwordx4 v[0:3], v192, s[46:47] offset:0
	v_mfma_f32_32x32x16_f16 v[80:95], a[120:123], v[180:183], v[80:95]
	ds_read_b128 v[180:183], v193 offset:5120
	v_rcp_f32_e32 v205, v205
	v_mul_f32_e32 v204, v204, v140
	global_load_dwordx4 v[4:7], v192, s[46:47] offset:1024
	global_load_dwordx4 v[8:11], v192, s[46:47] offset:2048
	v_mfma_f32_32x32x16_f16 v[64:79], a[124:127], v[184:187], v[64:79]
	ds_read_b128 v[184:187], v193 offset:6144
	v_rcp_f32_e32 v206, v206
	v_mul_f32_e32 v205, v205, v141
	global_load_dwordx4 v[12:15], v192, s[46:47] offset:3072
	s_add_u32 s46, s42, 0x1000
	s_addc_u32 s47, s43, 0
	v_mfma_f32_32x32x16_f16 v[80:95], a[124:127], v[188:191], v[80:95]
	ds_read_b128 v[188:191], v193 offset:7168
	v_cmp_gt_u32_e32 vcc, 4, v251
	s_cbranch_vccnz .LD_tpoll33
.LD_tok32:
	s_and_b32 s64, s71, 1
	s_lshl_b32 s64, s64, 22
	s_add_u32 s64, s64, s49
	s_add_u32 s64, s64, 0x60000
	s_add_u32 s34, s6, s64
	s_addc_u32 s35, s7, 0
	s_add_u32 s44, s34, 0x0
	s_addc_u32 s45, s35, 0
	s_mov_b32 m0, s52
	s_nop 0
	global_load_lds_dwordx4 v192, s[44:45] sc1
	v_rcp_f32_e32 v207, v207
	v_mul_f32_e32 v206, v206, v142
	global_load_dwordx4 v[16:19], v192, s[46:47] offset:0
	global_load_dwordx4 v[20:23], v192, s[46:47] offset:1024
	s_waitcnt lgkmcnt(4)
	v_mfma_f32_32x32x16_f16 v[64:79], a[128:131], v[160:163], v[64:79]
	ds_read_b128 v[160:163], v193 offset:8192
	v_rcp_f32_e32 v208, v208
	v_mul_f32_e32 v207, v207, v143
	global_load_dwordx4 v[24:27], v192, s[46:47] offset:2048
	global_load_dwordx4 v[28:31], v192, s[46:47] offset:3072
	v_mfma_f32_32x32x16_f16 v[80:95], a[128:131], v[164:167], v[80:95]
	ds_read_b128 v[164:167], v193 offset:9216
	v_rcp_f32_e32 v209, v209
	v_fmamk_f32 v208, v208, 0xc0b8aa3b, v198
	v_mfma_f32_32x32x16_f16 v[64:79], a[132:135], v[168:171], v[64:79]
	ds_read_b128 v[168:171], v193 offset:10240
	v_rcp_f32_e32 v210, v210
	v_fmamk_f32 v209, v209, 0xc0b8aa3b, v198
	v_fma_f32 v140, v200, v208, v204
	v_mfma_f32_32x32x16_f16 v[80:95], a[132:135], v[172:175], v[80:95]
	ds_read_b128 v[172:175], v193 offset:11264
	global_load_lds_dwordx4 v192, s[44:45] offset:1024 sc1
	v_rcp_f32_e32 v211, v211
	v_fmamk_f32 v210, v210, 0xc0b8aa3b, v198
	v_fma_f32 v141, v201, v209, v205
	s_waitcnt lgkmcnt(4)
	v_mfma_f32_32x32x16_f16 v[64:79], a[136:139], v[176:179], v[64:79]
	ds_read_b128 v[176:179], v193 offset:12288
	v_rcp_f32_e32 v212, v212
	v_fmamk_f32 v211, v211, 0xc0b8aa3b, v198
	v_fma_f32 v142, v202, v210, v206
	v_mfma_f32_32x32x16_f16 v[80:95], a[136:139], v[180:183], v[80:95]
	ds_read_b128 v[180:183], v193 offset:13312
	v_rcp_f32_e32 v213, v213
	v_fma_f32 v143, v203, v211, v207
	v_mfma_f32_32x32x16_f16 v[64:79], a[140:143], v[184:187], v[64:79]
	ds_read_b128 v[184:187], v193 offset:14336
	v_rcp_f32_e32 v214, v214
	v_mfma_f32_32x32x16_f16 v[80:95], a[140:143], v[188:191], v[80:95]
	ds_read_b128 v[188:191], v193 offset:15360
	global_load_lds_dwordx4 v192, s[44:45] offset:2048 sc1
	v_rcp_f32_e32 v215, v215
	s_waitcnt lgkmcnt(4)
	v_mfma_f32_32x32x16_f16 v[64:79], a[144:147], v[160:163], v[64:79]
	ds_read_b128 v[160:163], v193 offset:16384
	v_exp_f32_e32 v200, v140
	v_mfma_f32_32x32x16_f16 v[80:95], a[144:147], v[164:167], v[80:95]
	ds_read_b128 v[164:167], v193 offset:17408
	v_exp_f32_e32 v201, v141
	v_add_f32_e32 v200, 1.0, v200
	v_mfma_f32_32x32x16_f16 v[64:79], a[148:151], v[168:171], v[64:79]
	ds_read_b128 v[168:171], v193 offset:18432
	v_exp_f32_e32 v202, v142
	v_add_f32_e32 v201, 1.0, v201
	v_mfma_f32_32x32x16_f16 v[80:95], a[148:151], v[172:175], v[80:95]
	ds_read_b128 v[172:175], v193 offset:19456
	global_load_lds_dwordx4 v192, s[44:45] offset:3072 sc1
	v_exp_f32_e32 v203, v143
	v_add_f32_e32 v202, 1.0, v202
	s_waitcnt lgkmcnt(4)
	v_mfma_f32_32x32x16_f16 v[64:79], a[152:155], v[176:179], v[64:79]
	ds_read_b128 v[176:179], v193 offset:20480
	v_add_f32_e32 v203, 1.0, v203
	v_rcp_f32_e32 v200, v200
	v_mfma_f32_32x32x16_f16 v[80:95], a[152:155], v[180:183], v[80:95]
	ds_read_b128 v[180:183], v193 offset:21504
	v_rcp_f32_e32 v201, v201
	v_fma_f32 v200, v200, 2.0, -1.0
	v_mfma_f32_32x32x16_f16 v[64:79], a[156:159], v[184:187], v[64:79]
	ds_read_b128 v[184:187], v193 offset:22528
	v_rcp_f32_e32 v202, v202
	v_fma_f32 v201, v201, 2.0, -1.0
	v_mul_f32_e32 v216, v212, v200
	v_mfma_f32_32x32x16_f16 v[80:95], a[156:159], v[188:191], v[80:95]
	ds_read_b128 v[188:191], v193 offset:23552
	s_add_u32 s44, s34, 0x1000
	s_addc_u32 s45, s35, 0
	s_mov_b32 m0, s53
	s_nop 0
	global_load_lds_dwordx4 v192, s[44:45] sc1
	v_rcp_f32_e32 v203, v203
	v_fma_f32 v202, v202, 2.0, -1.0
	v_mul_f32_e32 v217, v213, v201
	s_waitcnt lgkmcnt(4)
	v_mfma_f32_32x32x16_f16 v[64:79], a[160:163], v[160:163], v[64:79]
	ds_read_b128 v[160:163], v193 offset:24576
	v_fma_f32 v203, v203, 2.0, -1.0
	v_mul_f32_e32 v218, v214, v202
	v_mfma_f32_32x32x16_f16 v[80:95], a[160:163], v[164:167], v[80:95]
	ds_read_b128 v[164:167], v193 offset:25600
	v_mul_f32_e32 v219, v215, v203
	v_mul_f32_e32 v236, v216, v228
	v_mfma_f32_32x32x16_f16 v[64:79], a[164:167], v[168:171], v[64:79]
	ds_read_b128 v[168:171], v193 offset:26624
	v_mul_f32_e32 v237, v216, v232
	v_fmac_f32_e32 v236, v217, v229
	v_mfma_f32_32x32x16_f16 v[80:95], a[164:167], v[172:175], v[80:95]
	ds_read_b128 v[172:175], v193 offset:27648
	global_load_lds_dwordx4 v192, s[44:45] offset:1024 sc1
	v_fmac_f32_e32 v237, v217, v233
	v_fmac_f32_e32 v236, v218, v230
	s_waitcnt lgkmcnt(4)
	v_mfma_f32_32x32x16_f16 v[64:79], a[168:171], v[176:179], v[64:79]
	ds_read_b128 v[176:179], v193 offset:28672
	v_fmac_f32_e32 v237, v218, v234
	v_fmac_f32_e32 v236, v219, v231
	v_mfma_f32_32x32x16_f16 v[80:95], a[168:171], v[180:183], v[80:95]
	ds_read_b128 v[180:183], v193 offset:29696
	v_fmac_f32_e32 v237, v219, v235
	v_mov_b32_e32 v238, v236
	v_mfma_f32_32x32x16_f16 v[64:79], a[172:175], v[184:187], v[64:79]
	ds_read_b128 v[184:187], v193 offset:30720
	v_mov_b32_e32 v239, v236
	v_mov_b32_e32 v240, v237
	v_mfma_f32_32x32x16_f16 v[80:95], a[172:175], v[188:191], v[80:95]
	ds_read_b128 v[188:191], v193 offset:31744
	global_load_lds_dwordx4 v192, s[44:45] offset:2048 sc1
	v_mov_b32_e32 v241, v237
	v_cvt_pk_f16_f32 v222, v216, v217
	s_waitcnt vmcnt(15)
	s_barrier
	s_waitcnt lgkmcnt(4)
	v_mfma_f32_32x32x16_f16 v[64:79], a[176:179], v[160:163], v[64:79]
	ds_read_b128 v[160:163], v193 offset:32768
	s_nop 1
	v_permlane32_swap_b32_e32 v238, v239
	v_permlane32_swap_b32_e32 v240, v241
	v_add_f32_e32 v238, v238, v239
	v_add_f32_e32 v239, v240, v241
	ds_write_b64 v248, v[238:239] offset:768
	v_mfma_f32_32x32x16_f16 v[80:95], a[176:179], v[164:167], v[80:95]
	ds_read_b128 v[164:167], v193 offset:33792
	v_cvt_pk_f16_f32 v223, v218, v219
	v_mfma_f32_32x32x16_f16 v[64:79], a[180:183], v[168:171], v[64:79]
	ds_read_b128 v[168:171], v193 offset:34816
	s_nop 1
	v_permlane32_swap_b32_e32 v220, v222
	v_permlane32_swap_b32_e32 v221, v223
	s_cmp_eq_u32 s31, 0
	s_cbranch_scc1 .LD_slow34
	global_store_dwordx4 v195, v[220:223], s[36:37] offset:0
.LD_join35:
	v_mfma_f32_32x32x16_f16 v[80:95], a[180:183], v[172:175], v[80:95]
	ds_read_b128 v[172:175], v193 offset:35840
	global_load_lds_dwordx4 v192, s[44:45] offset:3072 sc1
	s_waitcnt lgkmcnt(5)
	v_mfma_f32_32x32x16_f16 v[64:79], a[184:187], v[176:179], v[64:79]
	ds_read_b128 v[176:179], v193 offset:36864
	v_mfma_f32_32x32x16_f16 v[80:95], a[184:187], v[180:183], v[80:95]
	ds_read_b128 v[180:183], v193 offset:37888
	v_mfma_f32_32x32x16_f16 v[64:79], a[188:191], v[184:187], v[64:79]
	ds_read_b128 v[184:187], v193 offset:38912
	v_mfma_f32_32x32x16_f16 v[80:95], a[188:191], v[188:191], v[80:95]
	ds_read_b128 v[188:191], v193 offset:39936
	s_add_u32 s44, s34, 0x8000
	s_addc_u32 s45, s35, 0
	s_mov_b32 m0, s54
	s_nop 0
	global_load_lds_dwordx4 v192, s[44:45] sc1
	s_waitcnt lgkmcnt(4)
	v_mfma_f32_32x32x16_f16 v[64:79], a[192:195], v[160:163], v[64:79]
	ds_read_b128 v[160:163], v193 offset:40960
	v_mfma_f32_32x32x16_f16 v[80:95], a[192:195], v[164:167], v[80:95]
	ds_read_b128 v[164:167], v193 offset:41984
	v_mfma_f32_32x32x16_f16 v[64:79], a[196:199], v[168:171], v[64:79]
	ds_read_b128 v[168:171], v193 offset:43008
	v_mfma_f32_32x32x16_f16 v[80:95], a[196:199], v[172:175], v[80:95]
	ds_read_b128 v[172:175], v193 offset:44032
	global_load_lds_dwordx4 v192, s[44:45] offset:1024 sc1
	s_waitcnt lgkmcnt(4)
	v_mfma_f32_32x32x16_f16 v[64:79], a[200:203], v[176:179], v[64:79]
	ds_read_b128 v[176:179], v193 offset:45056
	v_mfma_f32_32x32x16_f16 v[80:95], a[200:203], v[180:183], v[80:95]
	ds_read_b128 v[180:183], v193 offset:46080
	v_mfma_f32_32x32x16_f16 v[64:79], a[204:207], v[184:187], v[64:79]
	ds_read_b128 v[184:187], v193 offset:47104
	v_mfma_f32_32x32x16_f16 v[80:95], a[204:207], v[188:191], v[80:95]
	ds_read_b128 v[188:191], v193 offset:48128
	global_load_lds_dwordx4 v192, s[44:45] offset:2048 sc1
	s_waitcnt vmcnt(4)
	s_barrier
	v_mov_b32_e32 v199, 2
	s_cmp_eq_u32 s31, 0
	s_cbranch_scc1 .LD_slow36
	global_store_dword v197, v199, s[40:41]
.LD_join37:
	ds_read_b64 v[200:201], v249 offset:512
	ds_read_b64 v[202:203], v249 offset:2560
	ds_read_b64 v[204:205], v249 offset:4608
	ds_read_b64 v[206:207], v249 offset:6656
	s_waitcnt lgkmcnt(8)
	v_mfma_f32_32x32x16_f16 v[64:79], a[208:211], v[160:163], v[64:79]
	ds_read_b128 v[160:163], v193 offset:49152
	v_mfma_f32_32x32x16_f16 v[80:95], a[208:211], v[164:167], v[80:95]
	ds_read_b128 v[164:167], v193 offset:50176
	v_mfma_f32_32x32x16_f16 v[64:79], a[212:215], v[168:171], v[64:79]
	ds_read_b128 v[168:171], v193 offset:51200
	v_mfma_f32_32x32x16_f16 v[80:95], a[212:215], v[172:175], v[80:95]
	ds_read_b128 v[172:175], v193 offset:52224
	global_load_lds_dwordx4 v192, s[44:45] offset:3072 sc1
	s_waitcnt lgkmcnt(8)
	v_mfma_f32_32x32x16_f16 v[64:79], a[216:219], v[176:179], v[64:79]
	ds_read_b128 v[176:179], v193 offset:53248
	v_mfma_f32_32x32x16_f16 v[80:95], a[216:219], v[180:183], v[80:95]
	ds_read_b128 v[180:183], v193 offset:54272
	v_mfma_f32_32x32x16_f16 v[64:79], a[220:223], v[184:187], v[64:79]
	ds_read_b128 v[184:187], v193 offset:55296
	v_mfma_f32_32x32x16_f16 v[80:95], a[220:223], v[188:191], v[80:95]
	ds_read_b128 v[188:191], v193 offset:56320
	s_add_u32 s44, s34, 0x9000
	s_addc_u32 s45, s35, 0
	s_mov_b32 m0, s55
	s_nop 0
	global_load_lds_dwordx4 v192, s[44:45] sc1
	s_waitcnt lgkmcnt(4)
	v_mfma_f32_32x32x16_f16 v[64:79], a[224:227], v[160:163], v[64:79]
	ds_read_b128 v[160:163], v193 offset:57344
	v_mfma_f32_32x32x16_f16 v[80:95], a[224:227], v[164:167], v[80:95]
	ds_read_b128 v[164:167], v193 offset:58368
	v_mfma_f32_32x32x16_f16 v[64:79], a[228:231], v[168:171], v[64:79]
	ds_read_b128 v[168:171], v193 offset:59392
	v_mfma_f32_32x32x16_f16 v[80:95], a[228:231], v[172:175], v[80:95]
	ds_read_b128 v[172:175], v193 offset:60416
	global_load_lds_dwordx4 v192, s[44:45] offset:1024 sc1
	v_add_f32_e32 v200, v200, v202
	v_add_f32_e32 v201, v201, v203
	v_add_f32_e32 v200, v200, v204
	v_add_f32_e32 v201, v201, v205
	v_add_f32_e32 v200, v200, v206
	v_add_f32_e32 v201, v201, v207
	global_store_dwordx2 v250, v[200:201], s[72:73]
	s_waitcnt lgkmcnt(4)
	v_mfma_f32_32x32x16_f16 v[64:79], a[232:235], v[176:179], v[64:79]
	ds_read_b128 v[176:179], v193 offset:61440
	v_mfma_f32_32x32x16_f16 v[80:95], a[232:235], v[180:183], v[80:95]
	ds_read_b128 v[180:183], v193 offset:62464
	v_mfma_f32_32x32x16_f16 v[64:79], a[236:239], v[184:187], v[64:79]
	ds_read_b128 v[184:187], v193 offset:63488
	v_mfma_f32_32x32x16_f16 v[80:95], a[236:239], v[188:191], v[80:95]
	ds_read_b128 v[188:191], v193 offset:64512
	global_load_lds_dwordx4 v192, s[44:45] offset:2048 sc1
	s_and_b32 s64, s33, 1
	s_lshl_b32 s64, s64, 22
	s_add_u32 s64, s64, s50
	s_add_u32 s64, s64, 0x40000
	s_add_u32 s36, s6, s64
	s_addc_u32 s37, s7, 0
	s_lshl_b32 s64, s33, 3
	s_add_u32 s64, s64, s29
	s_lshl_b32 s64, s64, 5
	s_add_u32 s64, s64, s30
	s_lshl_b32 s64, s64, 2
	s_add_u32 s40, s8, s64
	s_addc_u32 s41, s9, 0
	s_lshl_b32 s64, s33, 19
	s_add_u32 s64, s64, 0x400
	s_add_u32 s72, s62, s64
	s_addc_u32 s73, s63, 0
	s_waitcnt vmcnt(9)
	s_barrier
	s_waitcnt lgkmcnt(4)
	v_mfma_f32_32x32x16_f16 v[64:79], a[240:243], v[160:163], v[64:79]
	ds_read_b128 v[160:163], v192 offset:0
	v_mfma_f32_32x32x16_f16 v[80:95], a[240:243], v[164:167], v[80:95]
	ds_read_b128 v[164:167], v192 offset:1024
	v_mfma_f32_32x32x16_f16 v[64:79], a[244:247], v[168:171], v[64:79]
	ds_read_b128 v[168:171], v192 offset:2048
	v_mfma_f32_32x32x16_f16 v[80:95], a[244:247], v[172:175], v[80:95]
	ds_read_b128 v[172:175], v192 offset:3072
	global_load_lds_dwordx4 v192, s[44:45] offset:3072 sc1
	s_waitcnt lgkmcnt(4)
	v_mfma_f32_32x32x16_f16 v[64:79], a[248:251], v[176:179], v[64:79]
	ds_read_b128 v[176:179], v192 offset:4096
	v_mfma_f32_32x32x16_f16 v[80:95], a[248:251], v[180:183], v[80:95]
	ds_read_b128 v[180:183], v192 offset:5120
	v_mfma_f32_32x32x16_f16 v[64:79], a[252:255], v[184:187], v[64:79]
	ds_read_b128 v[184:187], v192 offset:6144
	v_mfma_f32_32x32x16_f16 v[80:95], a[252:255], v[188:191], v[80:95]
	ds_read_b128 v[188:191], v192 offset:7168
	s_add_u32 s44, s34, 0x10000
	s_addc_u32 s45, s35, 0
	s_mov_b32 m0, s56
	s_nop 0
	global_load_lds_dwordx4 v192, s[44:45] sc1
	s_nop 3
	s_waitcnt lgkmcnt(4)
	v_mfma_f32_32x32x16_f16 v[96:111], a[0:3], v[160:163], v[96:111]
	ds_read_b128 v[160:163], v192 offset:8192
	v_exp_f32_e32 v200, v64
	v_mfma_f32_32x32x16_f16 v[112:127], a[0:3], v[164:167], v[112:127]
	ds_read_b128 v[164:167], v192 offset:9216
	s_lshl_b32 s64, s33, 3
	s_add_u32 s64, s64, s29
	s_lshl_b32 s64, s64, 7
	s_add_u32 s38, s8, s64
	s_addc_u32 s39, s9, 0
	global_load_dword v251, v196, s[38:39] sc1
	v_exp_f32_e32 v201, v65
	v_add_f32_e32 v200, 1.0, v200
	v_mfma_f32_32x32x16_f16 v[96:111], a[4:7], v[168:171], v[96:111]
	ds_read_b128 v[168:171], v192 offset:10240
	v_exp_f32_e32 v202, v66
	v_add_f32_e32 v201, 1.0, v201
	v_mfma_f32_32x32x16_f16 v[112:127], a[4:7], v[172:175], v[112:127]
	ds_read_b128 v[172:175], v192 offset:11264
	global_load_lds_dwordx4 v192, s[44:45] offset:1024 sc1
	v_exp_f32_e32 v203, v67
	v_add_f32_e32 v202, 1.0, v202
	s_waitcnt lgkmcnt(4)
	v_mfma_f32_32x32x16_f16 v[96:111], a[8:11], v[176:179], v[96:111]
	ds_read_b128 v[176:179], v192 offset:12288
	v_exp_f32_e32 v204, v68
	v_add_f32_e32 v203, 1.0, v203
	v_mfma_f32_32x32x16_f16 v[112:127], a[8:11], v[180:183], v[112:127]
	ds_read_b128 v[180:183], v192 offset:13312
	v_exp_f32_e32 v205, v69
	v_add_f32_e32 v204, 1.0, v204
	v_mfma_f32_32x32x16_f16 v[96:111], a[12:15], v[184:187], v[96:111]
	ds_read_b128 v[184:187], v192 offset:14336
	v_exp_f32_e32 v206, v70
	v_add_f32_e32 v205, 1.0, v205
	v_mfma_f32_32x32x16_f16 v[112:127], a[12:15], v[188:191], v[112:127]
	ds_read_b128 v[188:191], v192 offset:15360
	global_load_lds_dwordx4 v192, s[44:45] offset:2048 sc1
	v_exp_f32_e32 v207, v71
	v_add_f32_e32 v206, 1.0, v206
	s_waitcnt lgkmcnt(4)
	v_mfma_f32_32x32x16_f16 v[96:111], a[16:19], v[160:163], v[96:111]
	ds_read_b128 v[160:163], v192 offset:16384
	v_exp_f32_e32 v208, v72
	v_add_f32_e32 v207, 1.0, v207
	v_mfma_f32_32x32x16_f16 v[112:127], a[16:19], v[164:167], v[112:127]
	ds_read_b128 v[164:167], v192 offset:17408
	v_exp_f32_e32 v209, v73
	v_add_f32_e32 v208, 1.0, v208
	v_mfma_f32_32x32x16_f16 v[96:111], a[20:23], v[168:171], v[96:111]
	ds_read_b128 v[168:171], v192 offset:18432
	v_exp_f32_e32 v210, v74
	v_add_f32_e32 v209, 1.0, v209
	v_mfma_f32_32x32x16_f16 v[112:127], a[20:23], v[172:175], v[112:127]
	ds_read_b128 v[172:175], v192 offset:19456
	global_load_lds_dwordx4 v192, s[44:45] offset:3072 sc1
	v_exp_f32_e32 v211, v75
	v_add_f32_e32 v210, 1.0, v210
	s_waitcnt lgkmcnt(4)
	v_mfma_f32_32x32x16_f16 v[96:111], a[24:27], v[176:179], v[96:111]
	ds_read_b128 v[176:179], v192 offset:20480
	v_exp_f32_e32 v212, v76
	v_add_f32_e32 v211, 1.0, v211
	v_mfma_f32_32x32x16_f16 v[112:127], a[24:27], v[180:183], v[112:127]
	ds_read_b128 v[180:183], v192 offset:21504
	v_exp_f32_e32 v213, v77
	v_add_f32_e32 v212, 1.0, v212
	v_mfma_f32_32x32x16_f16 v[96:111], a[28:31], v[184:187], v[96:111]
	ds_read_b128 v[184:187], v192 offset:22528
	v_exp_f32_e32 v214, v78
	v_add_f32_e32 v213, 1.0, v213
	v_mfma_f32_32x32x16_f16 v[112:127], a[28:31], v[188:191], v[112:127]
	ds_read_b128 v[188:191], v192 offset:23552
	s_add_u32 s44, s34, 0x11000
	s_addc_u32 s45, s35, 0
	s_mov_b32 m0, s57
	s_nop 0
	global_load_lds_dwordx4 v192, s[44:45] sc1
	v_exp_f32_e32 v215, v79
	v_add_f32_e32 v214, 1.0, v214
	s_waitcnt lgkmcnt(4)
	v_mfma_f32_32x32x16_f16 v[96:111], a[32:35], v[160:163], v[96:111]
	ds_read_b128 v[160:163], v192 offset:24576
	v_add_f32_e32 v215, 1.0, v215
	v_rcp_f32_e32 v200, v200
	v_mfma_f32_32x32x16_f16 v[112:127], a[32:35], v[164:167], v[112:127]
	ds_read_b128 v[164:167], v192 offset:25600
	v_rcp_f32_e32 v201, v201
	v_mfma_f32_32x32x16_f16 v[96:111], a[36:39], v[168:171], v[96:111]
	ds_read_b128 v[168:171], v192 offset:26624
	v_rcp_f32_e32 v202, v202
	v_mfma_f32_32x32x16_f16 v[112:127], a[36:39], v[172:175], v[112:127]
	ds_read_b128 v[172:175], v192 offset:27648
	global_load_lds_dwordx4 v192, s[44:45] offset:1024 sc1
	v_rcp_f32_e32 v203, v203
	s_waitcnt lgkmcnt(4)
	v_mfma_f32_32x32x16_f16 v[96:111], a[40:43], v[176:179], v[96:111]
	ds_read_b128 v[176:179], v192 offset:28672
	v_rcp_f32_e32 v204, v204
	v_mfma_f32_32x32x16_f16 v[112:127], a[40:43], v[180:183], v[112:127]
	ds_read_b128 v[180:183], v192 offset:29696
	v_rcp_f32_e32 v205, v205
	v_mul_f32_e32 v204, v204, v144
	v_mfma_f32_32x32x16_f16 v[96:111], a[44:47], v[184:187], v[96:111]
	ds_read_b128 v[184:187], v192 offset:30720
	v_rcp_f32_e32 v206, v206
	v_mul_f32_e32 v205, v205, v145
	v_mfma_f32_32x32x16_f16 v[112:127], a[44:47], v[188:191], v[112:127]
	ds_read_b128 v[188:191], v192 offset:31744
	global_load_lds_dwordx4 v192, s[44:45] offset:2048 sc1
	v_rcp_f32_e32 v207, v207
	v_mul_f32_e32 v206, v206, v146
	s_waitcnt vmcnt(8)
	s_barrier
	s_waitcnt lgkmcnt(4)
	v_mfma_f32_32x32x16_f16 v[96:111], a[48:51], v[160:163], v[96:111]
	ds_read_b128 v[160:163], v192 offset:32768
	v_rcp_f32_e32 v208, v208
	v_mul_f32_e32 v207, v207, v147
	v_mfma_f32_32x32x16_f16 v[112:127], a[48:51], v[164:167], v[112:127]
	ds_read_b128 v[164:167], v192 offset:33792
	v_rcp_f32_e32 v209, v209
	v_fmamk_f32 v208, v208, 0xc0b8aa3b, v198
	v_mfma_f32_32x32x16_f16 v[96:111], a[52:55], v[168:171], v[96:111]
	ds_read_b128 v[168:171], v192 offset:34816
	v_rcp_f32_e32 v210, v210
	v_fmamk_f32 v209, v209, 0xc0b8aa3b, v198
	v_fma_f32 v144, v200, v208, v204
	v_mfma_f32_32x32x16_f16 v[112:127], a[52:55], v[172:175], v[112:127]
	ds_read_b128 v[172:175], v192 offset:35840
	global_load_lds_dwordx4 v192, s[44:45] offset:3072 sc1
	v_rcp_f32_e32 v211, v211
	v_fmamk_f32 v210, v210, 0xc0b8aa3b, v198
	v_fma_f32 v145, v201, v209, v205
	s_waitcnt lgkmcnt(4)
	v_mfma_f32_32x32x16_f16 v[96:111], a[56:59], v[176:179], v[96:111]
	ds_read_b128 v[176:179], v192 offset:36864
	v_rcp_f32_e32 v212, v212
	v_fmamk_f32 v211, v211, 0xc0b8aa3b, v198
	v_fma_f32 v146, v202, v210, v206
	v_mfma_f32_32x32x16_f16 v[112:127], a[56:59], v[180:183], v[112:127]
	ds_read_b128 v[180:183], v192 offset:37888
	v_rcp_f32_e32 v213, v213
	v_fma_f32 v147, v203, v211, v207
	v_mfma_f32_32x32x16_f16 v[96:111], a[60:63], v[184:187], v[96:111]
	ds_read_b128 v[184:187], v192 offset:38912
	v_rcp_f32_e32 v214, v214
	v_mfma_f32_32x32x16_f16 v[112:127], a[60:63], v[188:191], v[112:127]
	ds_read_b128 v[188:191], v192 offset:39936
	s_add_u32 s44, s34, 0x18000
	s_addc_u32 s45, s35, 0
	s_mov_b32 m0, s58
	s_nop 0
	global_load_lds_dwordx4 v192, s[44:45] sc1
	v_rcp_f32_e32 v215, v215
	s_waitcnt lgkmcnt(4)
	v_mfma_f32_32x32x16_f16 v[96:111], a[64:67], v[160:163], v[96:111]
	ds_read_b128 v[160:163], v192 offset:40960
	v_exp_f32_e32 v200, v144
	v_mfma_f32_32x32x16_f16 v[112:127], a[64:67], v[164:167], v[112:127]
	ds_read_b128 v[164:167], v192 offset:41984
	v_exp_f32_e32 v201, v145
	v_add_f32_e32 v200, 1.0, v200
	v_mfma_f32_32x32x16_f16 v[96:111], a[68:71], v[168:171], v[96:111]
	ds_read_b128 v[168:171], v192 offset:43008
	v_exp_f32_e32 v202, v146
	v_add_f32_e32 v201, 1.0, v201
	v_mfma_f32_32x32x16_f16 v[112:127], a[68:71], v[172:175], v[112:127]
	ds_read_b128 v[172:175], v192 offset:44032
	global_load_lds_dwordx4 v192, s[44:45] offset:1024 sc1
	v_exp_f32_e32 v203, v147
	v_add_f32_e32 v202, 1.0, v202
	s_waitcnt lgkmcnt(4)
	v_mfma_f32_32x32x16_f16 v[96:111], a[72:75], v[176:179], v[96:111]
	ds_read_b128 v[176:179], v192 offset:45056
	v_add_f32_e32 v203, 1.0, v203
	v_rcp_f32_e32 v200, v200
	v_mfma_f32_32x32x16_f16 v[112:127], a[72:75], v[180:183], v[112:127]
	ds_read_b128 v[180:183], v192 offset:46080
	v_rcp_f32_e32 v201, v201
	v_fma_f32 v200, v200, 2.0, -1.0
	v_mfma_f32_32x32x16_f16 v[96:111], a[76:79], v[184:187], v[96:111]
	ds_read_b128 v[184:187], v192 offset:47104
	v_rcp_f32_e32 v202, v202
	v_fma_f32 v201, v201, 2.0, -1.0
	v_mul_f32_e32 v216, v212, v200
	v_mfma_f32_32x32x16_f16 v[112:127], a[76:79], v[188:191], v[112:127]
	ds_read_b128 v[188:191], v192 offset:48128
	global_load_lds_dwordx4 v192, s[44:45] offset:2048 sc1
	v_rcp_f32_e32 v203, v203
	v_fma_f32 v202, v202, 2.0, -1.0
	v_mul_f32_e32 v217, v213, v201
	s_waitcnt lgkmcnt(4)
	v_mfma_f32_32x32x16_f16 v[96:111], a[80:83], v[160:163], v[96:111]
	ds_read_b128 v[160:163], v192 offset:49152
	v_fma_f32 v203, v203, 2.0, -1.0
	v_mul_f32_e32 v218, v214, v202
	v_exp_f32_e32 v200, v80
	v_mfma_f32_32x32x16_f16 v[112:127], a[80:83], v[164:167], v[112:127]
	ds_read_b128 v[164:167], v192 offset:50176
	v_mul_f32_e32 v219, v215, v203
	v_mul_f32_e32 v236, v216, v228
	v_exp_f32_e32 v201, v81
	v_mfma_f32_32x32x16_f16 v[96:111], a[84:87], v[168:171], v[96:111]
	ds_read_b128 v[168:171], v192 offset:51200
	v_mul_f32_e32 v237, v216, v232
	v_fmac_f32_e32 v236, v217, v229
	v_exp_f32_e32 v202, v82
	v_mfma_f32_32x32x16_f16 v[112:127], a[84:87], v[172:175], v[112:127]
	ds_read_b128 v[172:175], v192 offset:52224
	global_load_lds_dwordx4 v192, s[44:45] offset:3072 sc1
	v_fmac_f32_e32 v237, v217, v233
	v_fmac_f32_e32 v236, v218, v230
	v_exp_f32_e32 v203, v83
	s_waitcnt lgkmcnt(4)
	v_mfma_f32_32x32x16_f16 v[96:111], a[88:91], v[176:179], v[96:111]
	ds_read_b128 v[176:179], v192 offset:53248
	v_fmac_f32_e32 v237, v218, v234
	v_fmac_f32_e32 v236, v219, v231
	v_exp_f32_e32 v204, v84
	v_mfma_f32_32x32x16_f16 v[112:127], a[88:91], v[180:183], v[112:127]
	ds_read_b128 v[180:183], v192 offset:54272
	v_fmac_f32_e32 v237, v219, v235
	v_mov_b32_e32 v238, v236
	v_exp_f32_e32 v205, v85
	v_mfma_f32_32x32x16_f16 v[96:111], a[92:95], v[184:187], v[96:111]
	ds_read_b128 v[184:187], v192 offset:55296
	v_mov_b32_e32 v239, v236
	v_mov_b32_e32 v240, v237
	v_exp_f32_e32 v206, v86
	v_mfma_f32_32x32x16_f16 v[112:127], a[92:95], v[188:191], v[112:127]
	ds_read_b128 v[188:191], v192 offset:56320
	s_add_u32 s44, s34, 0x19000
	s_addc_u32 s45, s35, 0
	s_mov_b32 m0, s59
	s_nop 0
	global_load_lds_dwordx4 v192, s[44:45] sc1
	v_mov_b32_e32 v241, v237
	v_cvt_pk_f16_f32 v220, v216, v217
	v_exp_f32_e32 v207, v87
	s_waitcnt lgkmcnt(4)
	v_mfma_f32_32x32x16_f16 v[96:111], a[96:99], v[160:163], v[96:111]
	ds_read_b128 v[160:163], v192 offset:57344
	s_nop 1
	v_permlane32_swap_b32_e32 v238, v239
	v_permlane32_swap_b32_e32 v240, v241
	v_add_f32_e32 v238, v238, v239
	v_add_f32_e32 v239, v240, v241
	ds_write_b64 v248, v[238:239] offset:1024
	v_exp_f32_e32 v208, v88
	v_mfma_f32_32x32x16_f16 v[112:127], a[96:99], v[164:167], v[112:127]
	ds_read_b128 v[164:167], v192 offset:58368
	v_cvt_pk_f16_f32 v221, v218, v219
	v_exp_f32_e32 v209, v89
	v_add_f32_e32 v200, 1.0, v200
	v_mfma_f32_32x32x16_f16 v[96:111], a[100:103], v[168:171], v[96:111]
	ds_read_b128 v[168:171], v192 offset:59392
	v_exp_f32_e32 v210, v90
	v_add_f32_e32 v201, 1.0, v201
	v_add_f32_e32 v202, 1.0, v202
	v_mfma_f32_32x32x16_f16 v[112:127], a[100:103], v[172:175], v[112:127]
	ds_read_b128 v[172:175], v192 offset:60416
	global_load_lds_dwordx4 v192, s[44:45] offset:1024 sc1
	v_exp_f32_e32 v211, v91
	v_add_f32_e32 v203, 1.0, v203
	v_add_f32_e32 v204, 1.0, v204
	s_waitcnt lgkmcnt(5)
	v_mfma_f32_32x32x16_f16 v[96:111], a[104:107], v[176:179], v[96:111]
	ds_read_b128 v[176:179], v192 offset:61440
	v_exp_f32_e32 v212, v92
	v_add_f32_e32 v205, 1.0, v205
	v_add_f32_e32 v206, 1.0, v206
	v_mfma_f32_32x32x16_f16 v[112:127], a[104:107], v[180:183], v[112:127]
	ds_read_b128 v[180:183], v192 offset:62464
	v_exp_f32_e32 v213, v93
	v_add_f32_e32 v207, 1.0, v207
	v_add_f32_e32 v208, 1.0, v208
	v_mfma_f32_32x32x16_f16 v[96:111], a[108:111], v[184:187], v[96:111]
	ds_read_b128 v[184:187], v192 offset:63488
	v_exp_f32_e32 v214, v94
	v_add_f32_e32 v209, 1.0, v209
	v_add_f32_e32 v210, 1.0, v210
	v_mfma_f32_32x32x16_f16 v[112:127], a[108:111], v[188:191], v[112:127]
	ds_read_b128 v[188:191], v192 offset:64512
	global_load_lds_dwordx4 v192, s[44:45] offset:2048 sc1
	v_exp_f32_e32 v215, v95
	v_add_f32_e32 v211, 1.0, v211
	v_add_f32_e32 v212, 1.0, v212
	s_waitcnt vmcnt(7)
	s_barrier
	s_waitcnt lgkmcnt(4)
	v_mfma_f32_32x32x16_f16 v[96:111], a[112:115], v[160:163], v[96:111]
	ds_read_b128 v[160:163], v193 offset:0
	v_add_f32_e32 v213, 1.0, v213
	v_add_f32_e32 v214, 1.0, v214
	v_rcp_f32_e32 v200, v200
	v_mfma_f32_32x32x16_f16 v[112:127], a[112:115], v[164:167], v[112:127]
	ds_read_b128 v[164:167], v193 offset:1024
	v_add_f32_e32 v215, 1.0, v215
	v_rcp_f32_e32 v201, v201
	v_mfma_f32_32x32x16_f16 v[96:111], a[116:119], v[168:171], v[96:111]
	ds_read_b128 v[168:171], v193 offset:2048
	v_rcp_f32_e32 v202, v202
	v_mfma_f32_32x32x16_f16 v[112:127], a[116:119], v[172:175], v[112:127]
	ds_read_b128 v[172:175], v193 offset:3072
	global_load_lds_dwordx4 v192, s[44:45] offset:3072 sc1
	v_rcp_f32_e32 v203, v203
	s_waitcnt lgkmcnt(4)
	v_mfma_f32_32x32x16_f16 v[96:111], a[120:123], v[176:179], v[96:111]
	ds_read_b128 v[176:179], v193 offset:4096
	v_rcp_f32_e32 v204, v204
	s_add_u32 s46, s42, 0x2000
	s_addc_u32 s47, s43, 0
	global_load_dwordx4 v[32:35], v192, s[46:47] offset:0
	v_mfma_f32_32x32x16_f16 v[112:127], a[120:123], v[180:183], v[112:127]
	ds_read_b128 v[180:183], v193 offset:5120
	v_rcp_f32_e32 v205, v205
	v_mul_f32_e32 v204, v204, v148
	global_load_dwordx4 v[36:39], v192, s[46:47] offset:1024
	global_load_dwordx4 v[40:43], v192, s[46:47] offset:2048
	v_mfma_f32_32x32x16_f16 v[96:111], a[124:127], v[184:187], v[96:111]
	ds_read_b128 v[184:187], v193 offset:6144
	v_rcp_f32_e32 v206, v206
	v_mul_f32_e32 v205, v205, v149
	global_load_dwordx4 v[44:47], v192, s[46:47] offset:3072
	s_add_u32 s46, s42, 0x3000
	s_addc_u32 s47, s43, 0
	v_mfma_f32_32x32x16_f16 v[112:127], a[124:127], v[188:191], v[112:127]
	ds_read_b128 v[188:191], v193 offset:7168
	v_cmp_gt_u32_e32 vcc, 1, v251
	s_cbranch_vccnz .LD_tpoll39
.LD_tok38:
	s_and_b32 s64, s33, 1
	s_lshl_b32 s64, s64, 22
	s_add_u32 s64, s64, s49
	s_add_u32 s34, s6, s64
	s_addc_u32 s35, s7, 0
	s_add_u32 s44, s34, 0x0
	s_addc_u32 s45, s35, 0
	s_mov_b32 m0, s52
	s_nop 0
	global_load_lds_dwordx4 v192, s[44:45] sc1
	v_rcp_f32_e32 v207, v207
	v_mul_f32_e32 v206, v206, v150
	global_load_dwordx4 v[48:51], v192, s[46:47] offset:0
	global_load_dwordx4 v[52:55], v192, s[46:47] offset:1024
	s_waitcnt lgkmcnt(4)
	v_mfma_f32_32x32x16_f16 v[96:111], a[128:131], v[160:163], v[96:111]
	ds_read_b128 v[160:163], v193 offset:8192
	v_rcp_f32_e32 v208, v208
	v_mul_f32_e32 v207, v207, v151
	global_load_dwordx4 v[56:59], v192, s[46:47] offset:2048
	global_load_dwordx4 v[60:63], v192, s[46:47] offset:3072
	v_mfma_f32_32x32x16_f16 v[112:127], a[128:131], v[164:167], v[112:127]
	ds_read_b128 v[164:167], v193 offset:9216
	v_rcp_f32_e32 v209, v209
	v_fmamk_f32 v208, v208, 0xc0b8aa3b, v198
	v_mfma_f32_32x32x16_f16 v[96:111], a[132:135], v[168:171], v[96:111]
	ds_read_b128 v[168:171], v193 offset:10240
	v_rcp_f32_e32 v210, v210
	v_fmamk_f32 v209, v209, 0xc0b8aa3b, v198
	v_fma_f32 v148, v200, v208, v204
	v_mfma_f32_32x32x16_f16 v[112:127], a[132:135], v[172:175], v[112:127]
	ds_read_b128 v[172:175], v193 offset:11264
	global_load_lds_dwordx4 v192, s[44:45] offset:1024 sc1
	v_rcp_f32_e32 v211, v211
	v_fmamk_f32 v210, v210, 0xc0b8aa3b, v198
	v_fma_f32 v149, v201, v209, v205
	s_waitcnt lgkmcnt(4)
	v_mfma_f32_32x32x16_f16 v[96:111], a[136:139], v[176:179], v[96:111]
	ds_read_b128 v[176:179], v193 offset:12288
	v_rcp_f32_e32 v212, v212
	v_fmamk_f32 v211, v211, 0xc0b8aa3b, v198
	v_fma_f32 v150, v202, v210, v206
	v_mfma_f32_32x32x16_f16 v[112:127], a[136:139], v[180:183], v[112:127]
	ds_read_b128 v[180:183], v193 offset:13312
	v_rcp_f32_e32 v213, v213
	v_fma_f32 v151, v203, v211, v207
	v_mfma_f32_32x32x16_f16 v[96:111], a[140:143], v[184:187], v[96:111]
	ds_read_b128 v[184:187], v193 offset:14336
	v_rcp_f32_e32 v214, v214
	v_mfma_f32_32x32x16_f16 v[112:127], a[140:143], v[188:191], v[112:127]
	ds_read_b128 v[188:191], v193 offset:15360
	global_load_lds_dwordx4 v192, s[44:45] offset:2048 sc1
	v_rcp_f32_e32 v215, v215
	s_waitcnt lgkmcnt(4)
	v_mfma_f32_32x32x16_f16 v[96:111], a[144:147], v[160:163], v[96:111]
	ds_read_b128 v[160:163], v193 offset:16384
	v_exp_f32_e32 v200, v148
	v_mfma_f32_32x32x16_f16 v[112:127], a[144:147], v[164:167], v[112:127]
	ds_read_b128 v[164:167], v193 offset:17408
	v_exp_f32_e32 v201, v149
	v_add_f32_e32 v200, 1.0, v200
	v_mfma_f32_32x32x16_f16 v[96:111], a[148:151], v[168:171], v[96:111]
	ds_read_b128 v[168:171], v193 offset:18432
	v_exp_f32_e32 v202, v150
	v_add_f32_e32 v201, 1.0, v201
	v_mfma_f32_32x32x16_f16 v[112:127], a[148:151], v[172:175], v[112:127]
	ds_read_b128 v[172:175], v193 offset:19456
	global_load_lds_dwordx4 v192, s[44:45] offset:3072 sc1
	v_exp_f32_e32 v203, v151
	v_add_f32_e32 v202, 1.0, v202
	s_waitcnt lgkmcnt(4)
	v_mfma_f32_32x32x16_f16 v[96:111], a[152:155], v[176:179], v[96:111]
	ds_read_b128 v[176:179], v193 offset:20480
	v_add_f32_e32 v203, 1.0, v203
	v_rcp_f32_e32 v200, v200
	v_mfma_f32_32x32x16_f16 v[112:127], a[152:155], v[180:183], v[112:127]
	ds_read_b128 v[180:183], v193 offset:21504
	v_rcp_f32_e32 v201, v201
	v_fma_f32 v200, v200, 2.0, -1.0
	v_mfma_f32_32x32x16_f16 v[96:111], a[156:159], v[184:187], v[96:111]
	ds_read_b128 v[184:187], v193 offset:22528
	v_rcp_f32_e32 v202, v202
	v_fma_f32 v201, v201, 2.0, -1.0
	v_mul_f32_e32 v216, v212, v200
	v_mfma_f32_32x32x16_f16 v[112:127], a[156:159], v[188:191], v[112:127]
	ds_read_b128 v[188:191], v193 offset:23552
	s_add_u32 s44, s34, 0x1000
	s_addc_u32 s45, s35, 0
	s_mov_b32 m0, s53
	s_nop 0
	global_load_lds_dwordx4 v192, s[44:45] sc1
	v_rcp_f32_e32 v203, v203
	v_fma_f32 v202, v202, 2.0, -1.0
	v_mul_f32_e32 v217, v213, v201
	s_waitcnt lgkmcnt(4)
	v_mfma_f32_32x32x16_f16 v[96:111], a[160:163], v[160:163], v[96:111]
	ds_read_b128 v[160:163], v193 offset:24576
	v_fma_f32 v203, v203, 2.0, -1.0
	v_mul_f32_e32 v218, v214, v202
	v_mfma_f32_32x32x16_f16 v[112:127], a[160:163], v[164:167], v[112:127]
	ds_read_b128 v[164:167], v193 offset:25600
	v_mul_f32_e32 v219, v215, v203
	v_mul_f32_e32 v236, v216, v228
	v_mfma_f32_32x32x16_f16 v[96:111], a[164:167], v[168:171], v[96:111]
	ds_read_b128 v[168:171], v193 offset:26624
	v_mul_f32_e32 v237, v216, v232
	v_fmac_f32_e32 v236, v217, v229
	v_mfma_f32_32x32x16_f16 v[112:127], a[164:167], v[172:175], v[112:127]
	ds_read_b128 v[172:175], v193 offset:27648
	global_load_lds_dwordx4 v192, s[44:45] offset:1024 sc1
	v_fmac_f32_e32 v237, v217, v233
	v_fmac_f32_e32 v236, v218, v230
	s_waitcnt lgkmcnt(4)
	v_mfma_f32_32x32x16_f16 v[96:111], a[168:171], v[176:179], v[96:111]
	ds_read_b128 v[176:179], v193 offset:28672
	v_fmac_f32_e32 v237, v218, v234
	v_fmac_f32_e32 v236, v219, v231
	v_mfma_f32_32x32x16_f16 v[112:127], a[168:171], v[180:183], v[112:127]
	ds_read_b128 v[180:183], v193 offset:29696
	v_fmac_f32_e32 v237, v219, v235
	v_mov_b32_e32 v238, v236
	v_mfma_f32_32x32x16_f16 v[96:111], a[172:175], v[184:187], v[96:111]
	ds_read_b128 v[184:187], v193 offset:30720
	v_mov_b32_e32 v239, v236
	v_mov_b32_e32 v240, v237
	v_mfma_f32_32x32x16_f16 v[112:127], a[172:175], v[188:191], v[112:127]
	ds_read_b128 v[188:191], v193 offset:31744
	global_load_lds_dwordx4 v192, s[44:45] offset:2048 sc1
	v_mov_b32_e32 v241, v237
	v_cvt_pk_f16_f32 v222, v216, v217
	s_waitcnt vmcnt(15)
	s_barrier
	s_waitcnt lgkmcnt(4)
	v_mfma_f32_32x32x16_f16 v[96:111], a[176:179], v[160:163], v[96:111]
	ds_read_b128 v[160:163], v193 offset:32768
	s_nop 1
	v_permlane32_swap_b32_e32 v238, v239
	v_permlane32_swap_b32_e32 v240, v241
	v_add_f32_e32 v238, v238, v239
	v_add_f32_e32 v239, v240, v241
	ds_write_b64 v248, v[238:239] offset:1280
	v_mfma_f32_32x32x16_f16 v[112:127], a[176:179], v[164:167], v[112:127]
	ds_read_b128 v[164:167], v193 offset:33792
	v_cvt_pk_f16_f32 v223, v218, v219
	v_mfma_f32_32x32x16_f16 v[96:111], a[180:183], v[168:171], v[96:111]
	ds_read_b128 v[168:171], v193 offset:34816
	s_nop 1
	v_permlane32_swap_b32_e32 v220, v222
	v_permlane32_swap_b32_e32 v221, v223
	s_cmp_eq_u32 s31, 0
	s_cbranch_scc1 .LD_slow40
	global_store_dwordx4 v195, v[220:223], s[36:37] offset:0
.LD_join41:
	v_mfma_f32_32x32x16_f16 v[112:127], a[180:183], v[172:175], v[112:127]
	ds_read_b128 v[172:175], v193 offset:35840
	global_load_lds_dwordx4 v192, s[44:45] offset:3072 sc1
	s_waitcnt lgkmcnt(5)
	v_mfma_f32_32x32x16_f16 v[96:111], a[184:187], v[176:179], v[96:111]
	ds_read_b128 v[176:179], v193 offset:36864
	v_mfma_f32_32x32x16_f16 v[112:127], a[184:187], v[180:183], v[112:127]
	ds_read_b128 v[180:183], v193 offset:37888
	v_mfma_f32_32x32x16_f16 v[96:111], a[188:191], v[184:187], v[96:111]
	ds_read_b128 v[184:187], v193 offset:38912
	v_mfma_f32_32x32x16_f16 v[112:127], a[188:191], v[188:191], v[112:127]
	ds_read_b128 v[188:191], v193 offset:39936
	s_add_u32 s44, s34, 0x8000
	s_addc_u32 s45, s35, 0
	s_mov_b32 m0, s54
	s_nop 0
	global_load_lds_dwordx4 v192, s[44:45] sc1
	s_waitcnt lgkmcnt(4)
	v_mfma_f32_32x32x16_f16 v[96:111], a[192:195], v[160:163], v[96:111]
	ds_read_b128 v[160:163], v193 offset:40960
	v_mfma_f32_32x32x16_f16 v[112:127], a[192:195], v[164:167], v[112:127]
	ds_read_b128 v[164:167], v193 offset:41984
	v_mfma_f32_32x32x16_f16 v[96:111], a[196:199], v[168:171], v[96:111]
	ds_read_b128 v[168:171], v193 offset:43008
	v_mfma_f32_32x32x16_f16 v[112:127], a[196:199], v[172:175], v[112:127]
	ds_read_b128 v[172:175], v193 offset:44032
	global_load_lds_dwordx4 v192, s[44:45] offset:1024 sc1
	s_waitcnt lgkmcnt(4)
	v_mfma_f32_32x32x16_f16 v[96:111], a[200:203], v[176:179], v[96:111]
	ds_read_b128 v[176:179], v193 offset:45056
	v_mfma_f32_32x32x16_f16 v[112:127], a[200:203], v[180:183], v[112:127]
	ds_read_b128 v[180:183], v193 offset:46080
	v_mfma_f32_32x32x16_f16 v[96:111], a[204:207], v[184:187], v[96:111]
	ds_read_b128 v[184:187], v193 offset:47104
	v_mfma_f32_32x32x16_f16 v[112:127], a[204:207], v[188:191], v[112:127]
	ds_read_b128 v[188:191], v193 offset:48128
	global_load_lds_dwordx4 v192, s[44:45] offset:2048 sc1
	s_waitcnt vmcnt(4)
	s_barrier
	v_mov_b32_e32 v199, 3
	s_cmp_eq_u32 s31, 0
	s_cbranch_scc1 .LD_slow42
	global_store_dword v197, v199, s[40:41]
.LD_join43:
	ds_read_b64 v[200:201], v249 offset:1024
	ds_read_b64 v[202:203], v249 offset:3072
	ds_read_b64 v[204:205], v249 offset:5120
	ds_read_b64 v[206:207], v249 offset:7168
	s_waitcnt lgkmcnt(8)
	v_mfma_f32_32x32x16_f16 v[96:111], a[208:211], v[160:163], v[96:111]
	ds_read_b128 v[160:163], v193 offset:49152
	v_mfma_f32_32x32x16_f16 v[112:127], a[208:211], v[164:167], v[112:127]
	ds_read_b128 v[164:167], v193 offset:50176
	v_mfma_f32_32x32x16_f16 v[96:111], a[212:215], v[168:171], v[96:111]
	ds_read_b128 v[168:171], v193 offset:51200
	v_mfma_f32_32x32x16_f16 v[112:127], a[212:215], v[172:175], v[112:127]
	ds_read_b128 v[172:175], v193 offset:52224
	global_load_lds_dwordx4 v192, s[44:45] offset:3072 sc1
	s_waitcnt lgkmcnt(8)
	v_mfma_f32_32x32x16_f16 v[96:111], a[216:219], v[176:179], v[96:111]
	ds_read_b128 v[176:179], v193 offset:53248
	v_mfma_f32_32x32x16_f16 v[112:127], a[216:219], v[180:183], v[112:127]
	ds_read_b128 v[180:183], v193 offset:54272
	v_mfma_f32_32x32x16_f16 v[96:111], a[220:223], v[184:187], v[96:111]
	ds_read_b128 v[184:187], v193 offset:55296
	v_mfma_f32_32x32x16_f16 v[112:127], a[220:223], v[188:191], v[112:127]
	ds_read_b128 v[188:191], v193 offset:56320
	s_add_u32 s44, s34, 0x9000
	s_addc_u32 s45, s35, 0
	s_mov_b32 m0, s55
	s_nop 0
	global_load_lds_dwordx4 v192, s[44:45] sc1
	s_waitcnt lgkmcnt(4)
	v_mfma_f32_32x32x16_f16 v[96:111], a[224:227], v[160:163], v[96:111]
	ds_read_b128 v[160:163], v193 offset:57344
	v_mfma_f32_32x32x16_f16 v[112:127], a[224:227], v[164:167], v[112:127]
	ds_read_b128 v[164:167], v193 offset:58368
	v_mfma_f32_32x32x16_f16 v[96:111], a[228:231], v[168:171], v[96:111]
	ds_read_b128 v[168:171], v193 offset:59392
	v_mfma_f32_32x32x16_f16 v[112:127], a[228:231], v[172:175], v[112:127]
	ds_read_b128 v[172:175], v193 offset:60416
	global_load_lds_dwordx4 v192, s[44:45] offset:1024 sc1
	v_add_f32_e32 v200, v200, v202
	v_add_f32_e32 v201, v201, v203
	v_add_f32_e32 v200, v200, v204
	v_add_f32_e32 v201, v201, v205
	v_add_f32_e32 v200, v200, v206
	v_add_f32_e32 v201, v201, v207
	global_store_dwordx2 v250, v[200:201], s[72:73]
	s_waitcnt lgkmcnt(4)
	v_mfma_f32_32x32x16_f16 v[96:111], a[232:235], v[176:179], v[96:111]
	ds_read_b128 v[176:179], v193 offset:61440
	v_mfma_f32_32x32x16_f16 v[112:127], a[232:235], v[180:183], v[112:127]
	ds_read_b128 v[180:183], v193 offset:62464
	v_mfma_f32_32x32x16_f16 v[96:111], a[236:239], v[184:187], v[96:111]
	ds_read_b128 v[184:187], v193 offset:63488
	v_mfma_f32_32x32x16_f16 v[112:127], a[236:239], v[188:191], v[112:127]
	ds_read_b128 v[188:191], v193 offset:64512
	global_load_lds_dwordx4 v192, s[44:45] offset:2048 sc1
	s_waitcnt vmcnt(9)
	s_barrier
	s_waitcnt lgkmcnt(4)
	v_mfma_f32_32x32x16_f16 v[96:111], a[240:243], v[160:163], v[96:111]
	ds_read_b128 v[160:163], v192 offset:0
	v_mfma_f32_32x32x16_f16 v[112:127], a[240:243], v[164:167], v[112:127]
	ds_read_b128 v[164:167], v192 offset:1024
	v_mfma_f32_32x32x16_f16 v[96:111], a[244:247], v[168:171], v[96:111]
	ds_read_b128 v[168:171], v192 offset:2048
	v_mfma_f32_32x32x16_f16 v[112:127], a[244:247], v[172:175], v[112:127]
	ds_read_b128 v[172:175], v192 offset:3072
	global_load_lds_dwordx4 v192, s[44:45] offset:3072 sc1
	s_waitcnt lgkmcnt(4)
	v_mfma_f32_32x32x16_f16 v[96:111], a[248:251], v[176:179], v[96:111]
	ds_read_b128 v[176:179], v192 offset:4096
	v_mfma_f32_32x32x16_f16 v[112:127], a[248:251], v[180:183], v[112:127]
	ds_read_b128 v[180:183], v192 offset:5120
	v_mfma_f32_32x32x16_f16 v[96:111], a[252:255], v[184:187], v[96:111]
	ds_read_b128 v[184:187], v192 offset:6144
	v_mfma_f32_32x32x16_f16 v[112:127], a[252:255], v[188:191], v[112:127]
	ds_read_b128 v[188:191], v192 offset:7168
	s_add_u32 s44, s34, 0x10000
	s_addc_u32 s45, s35, 0
	s_mov_b32 m0, s56
	s_nop 0
	global_load_lds_dwordx4 v192, s[44:45] sc1
	s_add_u32 s33, s33, 1
	s_cmp_lt_u32 s33, s28
	s_cbranch_scc1 .LD_loop16
.LD_end17:
	s_nop 15
	s_nop 3
	s_sub_u32 s71, s33, 1
	s_and_b32 s64, s71, 1
	s_lshl_b32 s64, s64, 22
	s_add_u32 s64, s64, s50
	s_add_u32 s64, s64, 0x60000
	s_add_u32 s36, s6, s64
	s_addc_u32 s37, s7, 0
	s_lshl_b32 s64, s71, 3
	s_add_u32 s64, s64, s29
	s_lshl_b32 s64, s64, 5
	s_add_u32 s64, s64, s30
	s_lshl_b32 s64, s64, 2
	s_add_u32 s40, s8, s64
	s_addc_u32 s41, s9, 0
	s_lshl_b32 s64, s71, 19
	s_add_u32 s64, s64, 0x600
	s_add_u32 s72, s62, s64
	s_addc_u32 s73, s63, 0
	v_exp_f32_e32 v200, v96
	v_exp_f32_e32 v201, v97
	v_exp_f32_e32 v202, v98
	v_exp_f32_e32 v203, v99
	v_exp_f32_e32 v204, v100
	v_exp_f32_e32 v205, v101
	v_exp_f32_e32 v206, v102
	v_exp_f32_e32 v207, v103
	v_exp_f32_e32 v208, v104
	v_exp_f32_e32 v209, v105
	v_exp_f32_e32 v210, v106
	v_exp_f32_e32 v211, v107
	v_exp_f32_e32 v212, v108
	v_exp_f32_e32 v213, v109
	v_exp_f32_e32 v214, v110
	v_exp_f32_e32 v215, v111
	v_add_f32_e32 v200, 1.0, v200
	v_add_f32_e32 v201, 1.0, v201
	v_add_f32_e32 v202, 1.0, v202
	v_add_f32_e32 v203, 1.0, v203
	v_add_f32_e32 v204, 1.0, v204
	v_add_f32_e32 v205, 1.0, v205
	v_add_f32_e32 v206, 1.0, v206
	v_add_f32_e32 v207, 1.0, v207
	v_add_f32_e32 v208, 1.0, v208
	v_add_f32_e32 v209, 1.0, v209
	v_add_f32_e32 v210, 1.0, v210
	v_add_f32_e32 v211, 1.0, v211
	v_add_f32_e32 v212, 1.0, v212
	v_add_f32_e32 v213, 1.0, v213
	v_add_f32_e32 v214, 1.0, v214
	v_add_f32_e32 v215, 1.0, v215
	v_rcp_f32_e32 v200, v200
	v_rcp_f32_e32 v201, v201
	v_rcp_f32_e32 v202, v202
	v_rcp_f32_e32 v203, v203
	v_rcp_f32_e32 v204, v204
	v_rcp_f32_e32 v205, v205
	v_rcp_f32_e32 v206, v206
	v_rcp_f32_e32 v207, v207
	v_rcp_f32_e32 v208, v208
	v_rcp_f32_e32 v209, v209
	v_rcp_f32_e32 v210, v210
	v_rcp_f32_e32 v211, v211
	v_rcp_f32_e32 v212, v212
	v_rcp_f32_e32 v213, v213
	v_rcp_f32_e32 v214, v214
	v_rcp_f32_e32 v215, v215
	v_fmamk_f32 v208, v208, 0xc0b8aa3b, v198
	v_fmamk_f32 v209, v209, 0xc0b8aa3b, v198
	v_fmamk_f32 v210, v210, 0xc0b8aa3b, v198
	v_fmamk_f32 v211, v211, 0xc0b8aa3b, v198
	v_mul_f32_e32 v204, v204, v152
	v_mul_f32_e32 v205, v205, v153
	v_mul_f32_e32 v206, v206, v154
	v_mul_f32_e32 v207, v207, v155
	v_fma_f32 v152, v200, v208, v204
	v_fma_f32 v153, v201, v209, v205
	v_fma_f32 v154, v202, v210, v206
	v_fma_f32 v155, v203, v211, v207
	v_exp_f32_e32 v200, v152
	v_exp_f32_e32 v201, v153
	v_exp_f32_e32 v202, v154
	v_exp_f32_e32 v203, v155
	v_add_f32_e32 v200, 1.0, v200
	v_add_f32_e32 v201, 1.0, v201
	v_add_f32_e32 v202, 1.0, v202
	v_add_f32_e32 v203, 1.0, v203
	v_rcp_f32_e32 v200, v200
	v_rcp_f32_e32 v201, v201
	v_rcp_f32_e32 v202, v202
	v_rcp_f32_e32 v203, v203
	v_fma_f32 v200, v200, 2.0, -1.0
	v_fma_f32 v201, v201, 2.0, -1.0
	v_fma_f32 v202, v202, 2.0, -1.0
	v_fma_f32 v203, v203, 2.0, -1.0
	v_mul_f32_e32 v216, v212, v200
	v_mul_f32_e32 v217, v213, v201
	v_mul_f32_e32 v218, v214, v202
	v_mul_f32_e32 v219, v215, v203
	v_mul_f32_e32 v236, v216, v228
	v_mul_f32_e32 v237, v216, v232
	v_fmac_f32_e32 v236, v217, v229
	v_fmac_f32_e32 v237, v217, v233
	v_fmac_f32_e32 v236, v218, v230
	v_fmac_f32_e32 v237, v218, v234
	v_fmac_f32_e32 v236, v219, v231
	v_fmac_f32_e32 v237, v219, v235
	v_mov_b32_e32 v238, v236
	v_mov_b32_e32 v239, v236
	v_mov_b32_e32 v240, v237
	v_mov_b32_e32 v241, v237
	s_nop 1
	v_permlane32_swap_b32_e32 v238, v239
	v_permlane32_swap_b32_e32 v240, v241
	v_add_f32_e32 v238, v238, v239
	v_add_f32_e32 v239, v240, v241
	ds_write_b64 v248, v[238:239] offset:1536
	v_cvt_pk_f16_f32 v220, v216, v217
	v_cvt_pk_f16_f32 v221, v218, v219
	v_exp_f32_e32 v200, v112
	v_exp_f32_e32 v201, v113
	v_exp_f32_e32 v202, v114
	v_exp_f32_e32 v203, v115
	v_exp_f32_e32 v204, v116
	v_exp_f32_e32 v205, v117
	v_exp_f32_e32 v206, v118
	v_exp_f32_e32 v207, v119
	v_exp_f32_e32 v208, v120
	v_exp_f32_e32 v209, v121
	v_exp_f32_e32 v210, v122
	v_exp_f32_e32 v211, v123
	v_exp_f32_e32 v212, v124
	v_exp_f32_e32 v213, v125
	v_exp_f32_e32 v214, v126
	v_exp_f32_e32 v215, v127
	v_add_f32_e32 v200, 1.0, v200
	v_add_f32_e32 v201, 1.0, v201
	v_add_f32_e32 v202, 1.0, v202
	v_add_f32_e32 v203, 1.0, v203
	v_add_f32_e32 v204, 1.0, v204
	v_add_f32_e32 v205, 1.0, v205
	v_add_f32_e32 v206, 1.0, v206
	v_add_f32_e32 v207, 1.0, v207
	v_add_f32_e32 v208, 1.0, v208
	v_add_f32_e32 v209, 1.0, v209
	v_add_f32_e32 v210, 1.0, v210
	v_add_f32_e32 v211, 1.0, v211
	v_add_f32_e32 v212, 1.0, v212
	v_add_f32_e32 v213, 1.0, v213
	v_add_f32_e32 v214, 1.0, v214
	v_add_f32_e32 v215, 1.0, v215
	v_rcp_f32_e32 v200, v200
	v_rcp_f32_e32 v201, v201
	v_rcp_f32_e32 v202, v202
	v_rcp_f32_e32 v203, v203
	v_rcp_f32_e32 v204, v204
	v_rcp_f32_e32 v205, v205
	v_rcp_f32_e32 v206, v206
	v_rcp_f32_e32 v207, v207
	v_rcp_f32_e32 v208, v208
	v_rcp_f32_e32 v209, v209
	v_rcp_f32_e32 v210, v210
	v_rcp_f32_e32 v211, v211
	v_rcp_f32_e32 v212, v212
	v_rcp_f32_e32 v213, v213
	v_rcp_f32_e32 v214, v214
	v_rcp_f32_e32 v215, v215
	v_fmamk_f32 v208, v208, 0xc0b8aa3b, v198
	v_fmamk_f32 v209, v209, 0xc0b8aa3b, v198
	v_fmamk_f32 v210, v210, 0xc0b8aa3b, v198
	v_fmamk_f32 v211, v211, 0xc0b8aa3b, v198
	v_mul_f32_e32 v204, v204, v156
	v_mul_f32_e32 v205, v205, v157
	v_mul_f32_e32 v206, v206, v158
	v_mul_f32_e32 v207, v207, v159
	v_fma_f32 v156, v200, v208, v204
	v_fma_f32 v157, v201, v209, v205
	v_fma_f32 v158, v202, v210, v206
	v_fma_f32 v159, v203, v211, v207
	v_exp_f32_e32 v200, v156
	v_exp_f32_e32 v201, v157
	v_exp_f32_e32 v202, v158
	v_exp_f32_e32 v203, v159
	v_add_f32_e32 v200, 1.0, v200
	v_add_f32_e32 v201, 1.0, v201
	v_add_f32_e32 v202, 1.0, v202
	v_add_f32_e32 v203, 1.0, v203
	v_rcp_f32_e32 v200, v200
	v_rcp_f32_e32 v201, v201
	v_rcp_f32_e32 v202, v202
	v_rcp_f32_e32 v203, v203
	v_fma_f32 v200, v200, 2.0, -1.0
	v_fma_f32 v201, v201, 2.0, -1.0
	v_fma_f32 v202, v202, 2.0, -1.0
	v_fma_f32 v203, v203, 2.0, -1.0
	v_mul_f32_e32 v216, v212, v200
	v_mul_f32_e32 v217, v213, v201
	v_mul_f32_e32 v218, v214, v202
	v_mul_f32_e32 v219, v215, v203
	v_mul_f32_e32 v236, v216, v228
	v_mul_f32_e32 v237, v216, v232
	v_fmac_f32_e32 v236, v217, v229
	v_fmac_f32_e32 v237, v217, v233
	v_fmac_f32_e32 v236, v218, v230
	v_fmac_f32_e32 v237, v218, v234
	v_fmac_f32_e32 v236, v219, v231
	v_fmac_f32_e32 v237, v219, v235
	v_mov_b32_e32 v238, v236
	v_mov_b32_e32 v239, v236
	v_mov_b32_e32 v240, v237
	v_mov_b32_e32 v241, v237
	s_nop 1
	v_permlane32_swap_b32_e32 v238, v239
	v_permlane32_swap_b32_e32 v240, v241
	v_add_f32_e32 v238, v238, v239
	v_add_f32_e32 v239, v240, v241
	ds_write_b64 v248, v[238:239] offset:1792
	v_cvt_pk_f16_f32 v222, v216, v217
	v_cvt_pk_f16_f32 v223, v218, v219
	s_nop 1
	v_permlane32_swap_b32_e32 v220, v222
	v_permlane32_swap_b32_e32 v221, v223
	s_cmp_eq_u32 s31, 0
	s_cbranch_scc1 .LD_slow44
	global_store_dwordx4 v195, v[220:223], s[36:37] offset:0
.LD_join45:
	s_waitcnt vmcnt(0)
	s_waitcnt lgkmcnt(0)
	s_barrier
	v_mov_b32_e32 v199, 4
	s_cmp_eq_u32 s31, 0
	s_cbranch_scc1 .LD_slow46
	global_store_dword v197, v199, s[40:41]
.LD_join47:
	ds_read_b64 v[200:201], v249 offset:1536
	ds_read_b64 v[202:203], v249 offset:3584
	ds_read_b64 v[204:205], v249 offset:5632
	ds_read_b64 v[206:207], v249 offset:7680
	s_waitcnt lgkmcnt(0)
	v_add_f32_e32 v200, v200, v202
	v_add_f32_e32 v201, v201, v203
	v_add_f32_e32 v200, v200, v204
	v_add_f32_e32 v201, v201, v205
	v_add_f32_e32 v200, v200, v206
	v_add_f32_e32 v201, v201, v207
	global_store_dwordx2 v250, v[200:201], s[72:73]
	s_waitcnt vmcnt(0) lgkmcnt(0)
	s_endpgm
